# v_AD without the 66 s_nop 0 XNACK-replay pads between back-to-back global memory instructions (process runs xnack-)
# baseline (speedup 1.0000x reference)
.LBB0_21:
	v_lshl_add_u64 v[32:33], v[6:7], 0, s[14:15]
	v_add_co_u32_e32 v12, vcc, 0x9000, v32
	s_mov_b64 s[0:1], vcc
	v_add_co_u32_e32 v16, vcc, 0x12000, v32
	v_addc_co_u32_e64 v13, s[0:1], 0, v33, s[0:1]
	s_mov_b64 s[0:1], vcc
	v_add_co_u32_e32 v20, vcc, 0x1b000, v32
	v_addc_co_u32_e64 v17, s[0:1], 0, v33, s[0:1]
	s_mov_b64 s[0:1], vcc
	v_add_co_u32_e32 v24, vcc, 0x24000, v32
	v_addc_co_u32_e64 v21, s[0:1], 0, v33, s[0:1]
	s_mov_b64 s[0:1], vcc
	v_add_co_u32_e32 v28, vcc, 0x2d000, v32
	v_addc_co_u32_e64 v25, s[0:1], 0, v33, s[0:1]
	s_mov_b64 s[0:1], vcc
	v_add_co_u32_e32 v48, vcc, 0x36000, v32
	v_addc_co_u32_e64 v29, s[0:1], 0, v33, s[0:1]
	s_mov_b64 s[0:1], vcc
	v_add_co_u32_e32 v52, vcc, 0x3f000, v32
	v_addc_co_u32_e64 v49, s[0:1], 0, v33, s[0:1]
	s_mov_b64 s[0:1], vcc
	v_add_co_u32_e32 v56, vcc, 0x48000, v32
	v_addc_co_u32_e64 v53, s[0:1], 0, v33, s[0:1]
	s_mov_b64 s[0:1], vcc
	v_add_co_u32_e32 v60, vcc, 0x51000, v32
	v_addc_co_u32_e64 v57, s[0:1], 0, v33, s[0:1]
	s_mov_b64 s[0:1], vcc
	v_add_co_u32_e32 v64, vcc, 0x5a000, v32
	v_addc_co_u32_e64 v61, s[0:1], 0, v33, s[0:1]
	s_mov_b64 s[0:1], vcc
	v_add_co_u32_e32 v68, vcc, 0x63000, v32
	v_addc_co_u32_e64 v65, s[0:1], 0, v33, s[0:1]
	s_mov_b64 s[0:1], vcc
	global_load_dwordx4 v[8:11], v[32:33], off
	v_add_co_u32_e32 v72, vcc, 0x6c000, v32
	global_load_dwordx4 v[12:15], v[12:13], off
	v_addc_co_u32_e64 v69, s[0:1], 0, v33, s[0:1]
	global_load_dwordx4 v[16:19], v[16:17], off
	s_mov_b64 s[0:1], vcc
	global_load_dwordx4 v[20:23], v[20:21], off
	v_add_co_u32_e32 v76, vcc, 0x75000, v32
	global_load_dwordx4 v[24:27], v[24:25], off
	v_addc_co_u32_e64 v73, s[0:1], 0, v33, s[0:1]
	global_load_dwordx4 v[28:31], v[28:29], off
	s_mov_b64 s[0:1], vcc
	global_load_dwordx4 v[48:51], v[48:49], off
	v_add_co_u32_e32 v80, vcc, 0x7e000, v32
	global_load_dwordx4 v[52:55], v[52:53], off
	v_addc_co_u32_e64 v77, s[0:1], 0, v33, s[0:1]
	global_load_dwordx4 v[56:59], v[56:57], off
	s_mov_b64 s[0:1], vcc
	global_load_dwordx4 v[60:63], v[60:61], off
	v_add_co_u32_e32 v32, vcc, 0x87000, v32
	global_load_dwordx4 v[64:67], v[64:65], off
	v_addc_co_u32_e64 v81, s[0:1], 0, v33, s[0:1]
	global_load_dwordx4 v[68:71], v[68:69], off
	v_addc_co_u32_e32 v33, vcc, 0, v33, vcc
	global_load_dwordx4 v[72:75], v[72:73], off
	s_add_u32 s14, s14, 0x90000
	global_load_dwordx4 v[76:79], v[76:77], off
	global_load_dwordx4 v[80:83], v[80:81], off
	global_load_dwordx4 v[84:87], v[32:33], off
	s_addc_u32 s15, s15, 0
	s_cmp_lg_u32 s14, 0x120000
	s_waitcnt vmcnt(14)
	v_max3_f32 v2, v2, |v8|, |v12|
	v_max3_f32 v3, v3, |v9|, |v13|
	v_max3_f32 v4, v4, |v10|, |v14|
	v_max3_f32 v5, v5, |v11|, |v15|
	s_waitcnt vmcnt(12)
	v_max3_f32 v2, v2, |v16|, |v20|
	v_max3_f32 v3, v3, |v17|, |v21|
	v_max3_f32 v4, v4, |v18|, |v22|
	v_max3_f32 v5, v5, |v19|, |v23|
	s_waitcnt vmcnt(10)
	v_max3_f32 v2, v2, |v24|, |v28|
	v_max3_f32 v3, v3, |v25|, |v29|
	v_max3_f32 v4, v4, |v26|, |v30|
	v_max3_f32 v5, v5, |v27|, |v31|
	s_waitcnt vmcnt(8)
	v_max3_f32 v2, v2, |v48|, |v52|
	v_max3_f32 v3, v3, |v49|, |v53|
	v_max3_f32 v4, v4, |v50|, |v54|
	v_max3_f32 v5, v5, |v51|, |v55|
	s_waitcnt vmcnt(6)
	v_max3_f32 v2, v2, |v56|, |v60|
	v_max3_f32 v3, v3, |v57|, |v61|
	v_max3_f32 v4, v4, |v58|, |v62|
	v_max3_f32 v5, v5, |v59|, |v63|
	s_waitcnt vmcnt(4)
	v_max3_f32 v2, v2, |v64|, |v68|
	v_max3_f32 v3, v3, |v65|, |v69|
	v_max3_f32 v4, v4, |v66|, |v70|
	v_max3_f32 v5, v5, |v67|, |v71|
	s_waitcnt vmcnt(2)
	v_max3_f32 v2, v2, |v72|, |v76|
	v_max3_f32 v3, v3, |v73|, |v77|
	v_max3_f32 v4, v4, |v74|, |v78|
	v_max3_f32 v5, v5, |v75|, |v79|
	s_waitcnt vmcnt(0)
	v_max3_f32 v2, v2, |v80|, |v84|
	v_max3_f32 v3, v3, |v81|, |v85|
	v_max3_f32 v4, v4, |v82|, |v86|
	v_max3_f32 v5, v5, |v83|, |v87|
	s_cbranch_scc1 .LBB0_21
	s_lshl_b32 s10, s10, 2
	v_lshl_add_u64 v[6:7], v[38:39], 0, s[10:11]
	s_mov_b64 s[0:1], 0

.LBB0_25:
	v_lshl_add_u64 v[50:51], v[48:49], 0, s[14:15]
	v_add_co_u32_e32 v10, vcc, 0x4000, v50
	s_mov_b64 s[0:1], vcc
	v_add_co_u32_e32 v14, vcc, 0x8000, v50
	v_addc_co_u32_e64 v11, s[0:1], 0, v51, s[0:1]
	s_mov_b64 s[0:1], vcc
	v_add_co_u32_e32 v18, vcc, 0xc000, v50
	v_addc_co_u32_e64 v15, s[0:1], 0, v51, s[0:1]
	s_mov_b64 s[0:1], vcc
	v_add_co_u32_e32 v22, vcc, 0x10000, v50
	v_addc_co_u32_e64 v19, s[0:1], 0, v51, s[0:1]
	s_mov_b64 s[0:1], vcc
	v_add_co_u32_e32 v26, vcc, 0x14000, v50
	v_addc_co_u32_e64 v23, s[0:1], 0, v51, s[0:1]
	s_mov_b64 s[0:1], vcc
	v_add_co_u32_e32 v30, vcc, 0x18000, v50
	v_addc_co_u32_e64 v27, s[0:1], 0, v51, s[0:1]
	s_mov_b64 s[0:1], vcc
	v_add_co_u32_e32 v52, vcc, 0x1c000, v50
	v_addc_co_u32_e64 v31, s[0:1], 0, v51, s[0:1]
	s_mov_b64 s[0:1], vcc
	v_add_co_u32_e32 v56, vcc, 0x20000, v50
	v_addc_co_u32_e64 v53, s[0:1], 0, v51, s[0:1]
	s_mov_b64 s[0:1], vcc
	s_mov_b32 s10, 0x24000
	v_add_co_u32_e32 v60, vcc, s10, v50
	v_addc_co_u32_e64 v57, s[0:1], 0, v51, s[0:1]
	s_mov_b64 s[0:1], vcc
	s_mov_b32 s10, 0x28000
	v_add_co_u32_e32 v64, vcc, s10, v50
	v_addc_co_u32_e64 v61, s[0:1], 0, v51, s[0:1]
	s_mov_b64 s[0:1], vcc
	s_mov_b32 s10, 0x2c000
	v_add_co_u32_e32 v68, vcc, s10, v50
	v_addc_co_u32_e64 v65, s[0:1], 0, v51, s[0:1]
	s_mov_b64 s[0:1], vcc
	s_mov_b32 s10, 0x30000
	global_load_dwordx4 v[6:9], v[50:51], off
	v_add_co_u32_e32 v72, vcc, s10, v50
	global_load_dwordx4 v[10:13], v[10:11], off
	v_addc_co_u32_e64 v69, s[0:1], 0, v51, s[0:1]
	global_load_dwordx4 v[14:17], v[14:15], off
	s_mov_b64 s[0:1], vcc
	global_load_dwordx4 v[18:21], v[18:19], off
	s_mov_b32 s10, 0x34000
	global_load_dwordx4 v[22:25], v[22:23], off
	v_add_co_u32_e32 v76, vcc, s10, v50
	global_load_dwordx4 v[26:29], v[26:27], off
	v_addc_co_u32_e64 v73, s[0:1], 0, v51, s[0:1]
	global_load_dwordx4 v[30:33], v[30:31], off
	s_mov_b64 s[0:1], vcc
	global_load_dwordx4 v[52:55], v[52:53], off
	s_mov_b32 s10, 0x38000
	global_load_dwordx4 v[56:59], v[56:57], off
	v_add_co_u32_e32 v80, vcc, s10, v50
	global_load_dwordx4 v[60:63], v[60:61], off
	v_addc_co_u32_e64 v77, s[0:1], 0, v51, s[0:1]
	global_load_dwordx4 v[64:67], v[64:65], off
	s_mov_b64 s[0:1], vcc
	global_load_dwordx4 v[68:71], v[68:69], off
	s_mov_b32 s10, 0x3c000
	global_load_dwordx4 v[72:75], v[72:73], off
	v_add_co_u32_e32 v50, vcc, s10, v50
	global_load_dwordx4 v[76:79], v[76:77], off
	v_addc_co_u32_e64 v81, s[0:1], 0, v51, s[0:1]
	v_addc_co_u32_e32 v51, vcc, 0, v51, vcc
	global_load_dwordx4 v[80:83], v[80:81], off
	global_load_dwordx4 v[84:87], v[50:51], off
	s_add_u32 s14, s14, 0x40000
	s_addc_u32 s15, s15, 0
	s_cmp_lg_u32 s14, 0x80000
	s_waitcnt vmcnt(14)
	v_max3_f32 v2, v2, |v6|, |v10|
	v_max3_f32 v3, v3, |v7|, |v11|
	v_max3_f32 v4, v4, |v8|, |v12|
	v_max3_f32 v5, v5, |v9|, |v13|
	s_waitcnt vmcnt(12)
	v_max3_f32 v2, v2, |v14|, |v18|
	v_max3_f32 v3, v3, |v15|, |v19|
	v_max3_f32 v4, v4, |v16|, |v20|
	v_max3_f32 v5, v5, |v17|, |v21|
	s_waitcnt vmcnt(10)
	v_max3_f32 v2, v2, |v22|, |v26|
	v_max3_f32 v3, v3, |v23|, |v27|
	v_max3_f32 v4, v4, |v24|, |v28|
	v_max3_f32 v5, v5, |v25|, |v29|
	s_waitcnt vmcnt(8)
	v_max3_f32 v2, v2, |v30|, |v52|
	v_max3_f32 v3, v3, |v31|, |v53|
	v_max3_f32 v4, v4, |v32|, |v54|
	v_max3_f32 v5, v5, |v33|, |v55|
	s_waitcnt vmcnt(6)
	v_max3_f32 v2, v2, |v56|, |v60|
	v_max3_f32 v3, v3, |v57|, |v61|
	v_max3_f32 v4, v4, |v58|, |v62|
	v_max3_f32 v5, v5, |v59|, |v63|
	s_waitcnt vmcnt(4)
	v_max3_f32 v2, v2, |v64|, |v68|
	v_max3_f32 v3, v3, |v65|, |v69|
	v_max3_f32 v4, v4, |v66|, |v70|
	v_max3_f32 v5, v5, |v67|, |v71|
	s_waitcnt vmcnt(2)
	v_max3_f32 v2, v2, |v72|, |v76|
	v_max3_f32 v3, v3, |v73|, |v77|
	v_max3_f32 v4, v4, |v74|, |v78|
	v_max3_f32 v5, v5, |v75|, |v79|
	s_waitcnt vmcnt(0)
	v_max3_f32 v2, v2, |v80|, |v84|
	v_max3_f32 v3, v3, |v81|, |v85|
	v_max3_f32 v4, v4, |v82|, |v86|
	v_max3_f32 v5, v5, |v83|, |v87|
	s_cbranch_scc1 .LBB0_25
	s_lshl_b32 s0, s59, 10
	s_and_b32 s10, s0, 0x3c00
	v_lshl_add_u64 v[6:7], v[40:41], 0, s[10:11]

.LBB0_30:
	v_lshl_add_u64 v[32:33], v[6:7], 0, s[14:15]
	v_add_co_u32_e32 v12, vcc, 0xa000, v32
	s_mov_b64 s[0:1], vcc
	v_add_co_u32_e32 v16, vcc, 0x15000, v32
	v_addc_co_u32_e64 v13, s[0:1], 0, v33, s[0:1]
	s_mov_b64 s[0:1], vcc
	v_add_co_u32_e32 v20, vcc, s20, v32
	v_addc_co_u32_e64 v17, s[0:1], 0, v33, s[0:1]
	s_mov_b64 s[0:1], vcc
	v_add_co_u32_e32 v24, vcc, s21, v32
	v_addc_co_u32_e64 v21, s[0:1], 0, v33, s[0:1]
	s_mov_b64 s[0:1], vcc
	v_add_co_u32_e32 v28, vcc, s30, v32
	v_addc_co_u32_e64 v25, s[0:1], 0, v33, s[0:1]
	s_mov_b64 s[0:1], vcc
	v_add_co_u32_e32 v48, vcc, s31, v32
	v_addc_co_u32_e64 v29, s[0:1], 0, v33, s[0:1]
	s_mov_b64 s[0:1], vcc
	v_add_co_u32_e32 v52, vcc, s34, v32
	v_addc_co_u32_e64 v49, s[0:1], 0, v33, s[0:1]
	s_mov_b64 s[0:1], vcc
	v_add_co_u32_e32 v56, vcc, s35, v32
	v_addc_co_u32_e64 v53, s[0:1], 0, v33, s[0:1]
	s_mov_b64 s[0:1], vcc
	v_add_co_u32_e32 v60, vcc, s36, v32
	v_addc_co_u32_e64 v57, s[0:1], 0, v33, s[0:1]
	s_mov_b64 s[0:1], vcc
	v_add_co_u32_e32 v64, vcc, s37, v32
	v_addc_co_u32_e64 v61, s[0:1], 0, v33, s[0:1]
	s_mov_b64 s[0:1], vcc
	v_add_co_u32_e32 v68, vcc, s38, v32
	v_addc_co_u32_e64 v65, s[0:1], 0, v33, s[0:1]
	s_mov_b64 s[0:1], vcc
	global_load_dwordx4 v[8:11], v[32:33], off
	v_add_co_u32_e32 v72, vcc, s39, v32
	global_load_dwordx4 v[12:15], v[12:13], off offset:3072
	v_addc_co_u32_e64 v69, s[0:1], 0, v33, s[0:1]
	global_load_dwordx4 v[16:19], v[16:17], off offset:2048
	s_mov_b64 s[0:1], vcc
	global_load_dwordx4 v[20:23], v[20:21], off offset:1024
	v_add_co_u32_e32 v76, vcc, s56, v32
	global_load_dwordx4 v[24:27], v[24:25], off
	v_addc_co_u32_e64 v73, s[0:1], 0, v33, s[0:1]
	global_load_dwordx4 v[28:31], v[28:29], off offset:3072
	s_mov_b64 s[0:1], vcc
	global_load_dwordx4 v[48:51], v[48:49], off offset:2048
	v_add_co_u32_e32 v80, vcc, s57, v32
	global_load_dwordx4 v[52:55], v[52:53], off offset:1024
	v_addc_co_u32_e64 v77, s[0:1], 0, v33, s[0:1]
	global_load_dwordx4 v[56:59], v[56:57], off
	s_mov_b64 s[0:1], vcc
	global_load_dwordx4 v[60:63], v[60:61], off offset:3072
	v_add_co_u32_e32 v32, vcc, s58, v32
	global_load_dwordx4 v[64:67], v[64:65], off offset:2048
	v_addc_co_u32_e64 v81, s[0:1], 0, v33, s[0:1]
	global_load_dwordx4 v[68:71], v[68:69], off offset:1024
	v_addc_co_u32_e32 v33, vcc, 0, v33, vcc
	global_load_dwordx4 v[72:75], v[72:73], off
	s_add_u32 s14, s14, 0xac000
	global_load_dwordx4 v[76:79], v[76:77], off offset:3072
	global_load_dwordx4 v[80:83], v[80:81], off offset:2048
	global_load_dwordx4 v[84:87], v[32:33], off offset:1024
	s_addc_u32 s15, s15, 0
	s_cmp_lg_u32 s14, 0x158000
	s_waitcnt vmcnt(14)
	v_max3_f32 v2, v2, |v8|, |v12|
	v_max3_f32 v3, v3, |v9|, |v13|
	v_max3_f32 v4, v4, |v10|, |v14|
	v_max3_f32 v5, v5, |v11|, |v15|
	s_waitcnt vmcnt(12)
	v_max3_f32 v2, v2, |v16|, |v20|
	v_max3_f32 v3, v3, |v17|, |v21|
	v_max3_f32 v4, v4, |v18|, |v22|
	v_max3_f32 v5, v5, |v19|, |v23|
	s_waitcnt vmcnt(10)
	v_max3_f32 v2, v2, |v24|, |v28|
	v_max3_f32 v3, v3, |v25|, |v29|
	v_max3_f32 v4, v4, |v26|, |v30|
	v_max3_f32 v5, v5, |v27|, |v31|
	s_waitcnt vmcnt(8)
	v_max3_f32 v2, v2, |v48|, |v52|
	v_max3_f32 v3, v3, |v49|, |v53|
	v_max3_f32 v4, v4, |v50|, |v54|
	v_max3_f32 v5, v5, |v51|, |v55|
	s_waitcnt vmcnt(6)
	v_max3_f32 v2, v2, |v56|, |v60|
	v_max3_f32 v3, v3, |v57|, |v61|
	v_max3_f32 v4, v4, |v58|, |v62|
	v_max3_f32 v5, v5, |v59|, |v63|
	s_waitcnt vmcnt(4)
	v_max3_f32 v2, v2, |v64|, |v68|
	v_max3_f32 v3, v3, |v65|, |v69|
	v_max3_f32 v4, v4, |v66|, |v70|
	v_max3_f32 v5, v5, |v67|, |v71|
	s_waitcnt vmcnt(2)
	v_max3_f32 v2, v2, |v72|, |v76|
	v_max3_f32 v3, v3, |v73|, |v77|
	v_max3_f32 v4, v4, |v74|, |v78|
	v_max3_f32 v5, v5, |v75|, |v79|
	s_waitcnt vmcnt(0)
	v_max3_f32 v2, v2, |v80|, |v84|
	v_max3_f32 v3, v3, |v81|, |v85|
	v_max3_f32 v4, v4, |v82|, |v86|
	v_max3_f32 v5, v5, |v83|, |v87|
	s_cbranch_scc1 .LBB0_30
	s_lshl_b32 s10, s10, 2
	v_lshl_add_u64 v[6:7], v[42:43], 0, s[10:11]
	s_mov_b64 s[52:53], s[86:87]

.LBB0_35:
	v_lshl_add_u64 v[32:33], v[6:7], 0, s[16:17]
	v_add_co_u32_e32 v12, vcc, 0xa000, v32
	s_mov_b64 s[0:1], vcc
	v_add_co_u32_e32 v16, vcc, 0x15000, v32
	v_addc_co_u32_e64 v13, s[0:1], 0, v33, s[0:1]
	s_mov_b64 s[0:1], vcc
	v_add_co_u32_e32 v20, vcc, s20, v32
	v_addc_co_u32_e64 v17, s[0:1], 0, v33, s[0:1]
	s_mov_b64 s[0:1], vcc
	v_add_co_u32_e32 v24, vcc, s21, v32
	v_addc_co_u32_e64 v21, s[0:1], 0, v33, s[0:1]
	s_mov_b64 s[0:1], vcc
	v_add_co_u32_e32 v28, vcc, s30, v32
	v_addc_co_u32_e64 v25, s[0:1], 0, v33, s[0:1]
	s_mov_b64 s[0:1], vcc
	v_add_co_u32_e32 v48, vcc, s31, v32
	v_addc_co_u32_e64 v29, s[0:1], 0, v33, s[0:1]
	s_mov_b64 s[0:1], vcc
	v_add_co_u32_e32 v52, vcc, s34, v32
	v_addc_co_u32_e64 v49, s[0:1], 0, v33, s[0:1]
	s_mov_b64 s[0:1], vcc
	v_add_co_u32_e32 v56, vcc, s35, v32
	v_addc_co_u32_e64 v53, s[0:1], 0, v33, s[0:1]
	s_mov_b64 s[0:1], vcc
	v_add_co_u32_e32 v60, vcc, s36, v32
	v_addc_co_u32_e64 v57, s[0:1], 0, v33, s[0:1]
	s_mov_b64 s[0:1], vcc
	v_add_co_u32_e32 v64, vcc, s37, v32
	v_addc_co_u32_e64 v61, s[0:1], 0, v33, s[0:1]
	s_mov_b64 s[0:1], vcc
	v_add_co_u32_e32 v68, vcc, s38, v32
	v_addc_co_u32_e64 v65, s[0:1], 0, v33, s[0:1]
	s_mov_b64 s[0:1], vcc
	global_load_dwordx4 v[8:11], v[32:33], off
	v_add_co_u32_e32 v72, vcc, s39, v32
	global_load_dwordx4 v[12:15], v[12:13], off offset:3072
	v_addc_co_u32_e64 v69, s[0:1], 0, v33, s[0:1]
	global_load_dwordx4 v[16:19], v[16:17], off offset:2048
	s_mov_b64 s[0:1], vcc
	global_load_dwordx4 v[20:23], v[20:21], off offset:1024
	v_add_co_u32_e32 v76, vcc, s56, v32
	global_load_dwordx4 v[24:27], v[24:25], off
	v_addc_co_u32_e64 v73, s[0:1], 0, v33, s[0:1]
	global_load_dwordx4 v[28:31], v[28:29], off offset:3072
	s_mov_b64 s[0:1], vcc
	global_load_dwordx4 v[48:51], v[48:49], off offset:2048
	v_add_co_u32_e32 v80, vcc, s57, v32
	global_load_dwordx4 v[52:55], v[52:53], off offset:1024
	v_addc_co_u32_e64 v77, s[0:1], 0, v33, s[0:1]
	global_load_dwordx4 v[56:59], v[56:57], off
	s_mov_b64 s[0:1], vcc
	global_load_dwordx4 v[60:63], v[60:61], off offset:3072
	v_add_co_u32_e32 v32, vcc, s58, v32
	global_load_dwordx4 v[64:67], v[64:65], off offset:2048
	v_addc_co_u32_e64 v81, s[0:1], 0, v33, s[0:1]
	global_load_dwordx4 v[68:71], v[68:69], off offset:1024
	v_addc_co_u32_e32 v33, vcc, 0, v33, vcc
	global_load_dwordx4 v[72:75], v[72:73], off
	s_add_u32 s16, s16, 0xac000
	global_load_dwordx4 v[76:79], v[76:77], off offset:3072
	global_load_dwordx4 v[80:83], v[80:81], off offset:2048
	global_load_dwordx4 v[84:87], v[32:33], off offset:1024
	s_addc_u32 s17, s17, 0
	s_cmp_lg_u32 s16, 0x158000
	s_waitcnt vmcnt(14)
	v_max3_f32 v2, v2, |v8|, |v12|
	v_max3_f32 v3, v3, |v9|, |v13|
	v_max3_f32 v4, v4, |v10|, |v14|
	v_max3_f32 v5, v5, |v11|, |v15|
	s_waitcnt vmcnt(12)
	v_max3_f32 v2, v2, |v16|, |v20|
	v_max3_f32 v3, v3, |v17|, |v21|
	v_max3_f32 v4, v4, |v18|, |v22|
	v_max3_f32 v5, v5, |v19|, |v23|
	s_waitcnt vmcnt(10)
	v_max3_f32 v2, v2, |v24|, |v28|
	v_max3_f32 v3, v3, |v25|, |v29|
	v_max3_f32 v4, v4, |v26|, |v30|
	v_max3_f32 v5, v5, |v27|, |v31|
	s_waitcnt vmcnt(8)
	v_max3_f32 v2, v2, |v48|, |v52|
	v_max3_f32 v3, v3, |v49|, |v53|
	v_max3_f32 v4, v4, |v50|, |v54|
	v_max3_f32 v5, v5, |v51|, |v55|
	s_waitcnt vmcnt(6)
	v_max3_f32 v2, v2, |v56|, |v60|
	v_max3_f32 v3, v3, |v57|, |v61|
	v_max3_f32 v4, v4, |v58|, |v62|
	v_max3_f32 v5, v5, |v59|, |v63|
	s_waitcnt vmcnt(4)
	v_max3_f32 v2, v2, |v64|, |v68|
	v_max3_f32 v3, v3, |v65|, |v69|
	v_max3_f32 v4, v4, |v66|, |v70|
	v_max3_f32 v5, v5, |v67|, |v71|
	s_waitcnt vmcnt(2)
	v_max3_f32 v2, v2, |v72|, |v76|
	v_max3_f32 v3, v3, |v73|, |v77|
	v_max3_f32 v4, v4, |v74|, |v78|
	v_max3_f32 v5, v5, |v75|, |v79|
	s_waitcnt vmcnt(0)
	v_max3_f32 v2, v2, |v80|, |v84|
	v_max3_f32 v3, v3, |v81|, |v85|
	v_max3_f32 v4, v4, |v82|, |v86|
	v_max3_f32 v5, v5, |v83|, |v87|
	s_cbranch_scc1 .LBB0_35
	v_lshl_add_u64 v[6:7], s[14:15], 2, v[44:45]
	s_mov_b64 s[52:53], s[86:87]
	s_branch .LBB0_16

.LBB0_142:
	v_add_co_u32_e32 v14, vcc, s3, v120
	s_nop 1
	v_addc_co_u32_e32 v15, vcc, -1, v121, vcc
	v_add_co_u32_e32 v26, vcc, s7, v120
	global_load_dwordx4 v[2:5], v[14:15], off offset:-3072
	global_load_dwordx4 v[6:9], v[14:15], off offset:-1024
	global_load_dwordx4 v[10:13], v[14:15], off offset:-2048
	global_load_dwordx4 v[14:17], v[14:15], off
	v_addc_co_u32_e32 v27, vcc, -1, v121, vcc
	global_load_dwordx4 v[18:21], v[26:27], off offset:-3072
	global_load_dwordx4 v[22:25], v[26:27], off offset:-2048
	v_add_co_u32_e32 v28, vcc, 0xffffd000, v120
	s_waitcnt vmcnt(5)
	v_pk_mul_f32 v[66:67], v[4:5], v[4:5]
	v_addc_co_u32_e32 v29, vcc, -1, v121, vcc
	global_load_dwordx4 v[62:65], v[28:29], off offset:-3072
	global_load_dwordx4 v[58:61], v[28:29], off offset:-2048
	global_load_dwordx4 v[34:37], v[28:29], off
	global_load_dwordx4 v[50:53], v[28:29], off offset:-1024
	global_load_dwordx4 v[30:33], v[26:27], off offset:-1024
	global_load_dwordx4 v[38:41], v[120:121], off offset:-3072
	global_load_dwordx4 v[42:45], v[120:121], off offset:-2048
	global_load_dwordx4 v[46:49], v[120:121], off offset:-1024
	global_load_dwordx4 v[26:29], v[120:121], off
	global_load_dwordx4 v[54:57], v[120:121], off offset:-4096
	v_pk_mul_f32 v[68:69], v[2:3], v[2:3]
	s_waitcnt vmcnt(13)
	v_mul_f32_e32 v70, v11, v11
	v_mul_f32_e32 v72, v13, v13
	s_waitcnt vmcnt(12)
	v_pk_mul_f32 v[74:75], v[16:17], v[16:17]
	v_pk_mul_f32 v[76:77], v[14:15], v[14:15]
	s_waitcnt vmcnt(11)
	v_mul_f32_e32 v78, v19, v19
	v_mul_f32_e32 v135, v8, v8
	v_mul_f32_e32 v138, v9, v9
	v_pk_mov_b32 v[136:137], v[68:69], v[66:67] op_sel:[1,0]
	v_mov_b32_e32 v69, v67
	v_pk_fma_f32 v[66:67], v[10:11], v[10:11], v[70:71] op_sel_hi:[1,1,0]
	v_pk_fma_f32 v[70:71], v[12:13], v[12:13], v[72:73] op_sel_hi:[1,1,0]
	v_pk_mov_b32 v[72:73], v[76:77], v[74:75] op_sel:[1,0]
	v_mov_b32_e32 v77, v75
	v_pk_fma_f32 v[74:75], v[18:19], v[18:19], v[78:79] op_sel_hi:[1,1,0]
	v_mov_b32_e32 v67, v135
	v_mov_b32_e32 v71, v138
	v_pk_add_f32 v[72:73], v[72:73], v[76:77]
	v_pk_add_f32 v[66:67], v[66:67], v[70:71]
	v_pk_add_f32 v[70:71], v[72:73], v[72:73] op_sel:[0,1] op_sel_hi:[1,0]
	v_pk_add_f32 v[68:69], v[136:137], v[68:69]
	v_mul_f32_e32 v81, v6, v6
	v_mul_f32_e32 v131, v7, v7
	v_pk_add_f32 v[68:69], v[68:69], v[68:69] op_sel:[0,1] op_sel_hi:[1,0]
	v_mul_f32_e32 v80, v21, v21
	v_mov_b32_e32 v69, v131
	s_waitcnt vmcnt(10)
	v_mul_f32_e32 v139, v22, v22
	v_mul_f32_e32 v140, v23, v23
	v_mul_f32_e32 v141, v24, v24
	v_mul_f32_e32 v142, v25, v25
	v_mov_b32_e32 v75, v141
	v_mov_b32_e32 v71, v140
	global_load_dwordx4 v[164:167], v[116:117], off
	global_load_dwordx4 v[160:163], v[114:115], off
	s_waitcnt vmcnt(11)
	v_pk_mul_f32 v[82:83], v[64:65], v[64:65]
	v_pk_mul_f32 v[84:85], v[62:63], v[62:63]
	s_waitcnt vmcnt(10)
	v_pk_mul_f32 v[86:87], v[60:61], v[60:61]
	v_pk_mul_f32 v[88:89], v[58:59], v[58:59]
	v_pk_mov_b32 v[78:79], v[84:85], v[82:83] op_sel:[1,0]
	v_mov_b32_e32 v85, v83
	v_pk_mov_b32 v[82:83], v[88:89], v[86:87] op_sel:[1,0]
	v_mov_b32_e32 v89, v87
	s_waitcnt vmcnt(8)
	v_mul_f32_e32 v132, v51, v51
	v_mul_f32_e32 v134, v53, v53
	v_pk_add_f32 v[76:77], v[78:79], v[84:85]
	v_pk_add_f32 v[78:79], v[82:83], v[88:89]
	v_mul_f32_e32 v143, v34, v34
	v_mul_f32_e32 v144, v35, v35
	v_mul_f32_e32 v145, v36, v36
	v_mul_f32_e32 v146, v37, v37
	v_pk_fma_f32 v[86:87], v[50:51], v[50:51], v[132:133] op_sel_hi:[1,1,0]
	v_pk_fma_f32 v[132:133], v[52:53], v[52:53], v[134:135] op_sel_hi:[1,1,0]
	v_pk_add_f32 v[72:73], v[76:77], v[76:77] op_sel:[0,1] op_sel_hi:[1,0]
	v_pk_add_f32 v[76:77], v[78:79], v[78:79] op_sel:[0,1] op_sel_hi:[1,0]
	v_mov_b32_e32 v87, v145
	v_mov_b32_e32 v133, v146
	v_mov_b32_e32 v73, v143
	v_mov_b32_e32 v77, v144
	v_pk_add_f32 v[78:79], v[86:87], v[132:133]
	v_pk_add_f32 v[72:73], v[72:73], v[76:77]
	global_load_dwordx4 v[82:85], v[94:95], off
	v_pk_add_f32 v[72:73], v[72:73], v[78:79]
	s_nop 0
	v_pk_add_f32 v[72:73], v[72:73], v[72:73] op_sel:[0,1] op_sel_hi:[1,0]
	s_nop 0
	v_mov_b32_e32 v73, v81
	v_pk_add_f32 v[68:69], v[72:73], v[68:69]
	s_nop 0
	v_pk_add_f32 v[66:67], v[68:69], v[66:67]
	v_pk_fma_f32 v[68:69], v[20:21], v[20:21], v[80:81] op_sel_hi:[1,1,0]
	v_pk_add_f32 v[66:67], v[66:67], v[66:67] op_sel:[0,1] op_sel_hi:[1,0]
	v_mov_b32_e32 v69, v142
	v_mov_b32_e32 v67, v139
	v_pk_add_f32 v[66:67], v[66:67], v[70:71]
	v_pk_add_f32 v[68:69], v[74:75], v[68:69]
	s_waitcnt vmcnt(8)
	v_pk_mul_f32 v[70:71], v[30:31], v[30:31]
	v_pk_add_f32 v[66:67], v[66:67], v[68:69]
	v_pk_mul_f32 v[68:69], v[32:33], v[32:33]
	v_pk_add_f32 v[66:67], v[66:67], v[66:67] op_sel:[0,1] op_sel_hi:[1,0]
	v_pk_mov_b32 v[72:73], v[70:71], v[68:69] op_sel:[1,0]
	v_mov_b32_e32 v71, v69
	v_pk_add_f32 v[68:69], v[72:73], v[70:71]
	s_waitcnt vmcnt(7)
	v_mul_f32_e32 v70, v38, v38
	v_mul_f32_e32 v71, v39, v39
	v_pk_add_f32 v[68:69], v[68:69], v[68:69] op_sel:[0,1] op_sel_hi:[1,0]
	v_mov_b32_e32 v67, v70
	v_mov_b32_e32 v69, v71
	v_pk_add_f32 v[66:67], v[66:67], v[68:69]
	s_waitcnt vmcnt(3)
	v_mul_f32_e32 v68, v55, v55
	v_mul_f32_e32 v70, v57, v57
	v_mul_f32_e32 v72, v40, v40
	v_mul_f32_e32 v73, v41, v41
	v_pk_fma_f32 v[68:69], v[54:55], v[54:55], v[68:69] op_sel_hi:[1,1,0]
	v_pk_fma_f32 v[70:71], v[56:57], v[56:57], v[70:71] op_sel_hi:[1,1,0]
	v_mov_b32_e32 v69, v72
	v_mov_b32_e32 v71, v73
	v_pk_add_f32 v[68:69], v[68:69], v[70:71]
	v_pk_mul_f32 v[70:71], v[42:43], v[42:43]
	v_pk_add_f32 v[66:67], v[66:67], v[68:69]
	v_pk_mul_f32 v[68:69], v[44:45], v[44:45]
	v_pk_add_f32 v[66:67], v[66:67], v[66:67] op_sel:[0,1] op_sel_hi:[1,0]
	v_pk_mov_b32 v[72:73], v[70:71], v[68:69] op_sel:[1,0]
	v_mov_b32_e32 v71, v69
	v_pk_add_f32 v[68:69], v[72:73], v[70:71]
	v_mul_f32_e32 v70, v26, v26
	v_mul_f32_e32 v71, v27, v27
	v_pk_add_f32 v[68:69], v[68:69], v[68:69] op_sel:[0,1] op_sel_hi:[1,0]
	v_mov_b32_e32 v67, v70
	v_mov_b32_e32 v69, v71
	v_pk_add_f32 v[66:67], v[66:67], v[68:69]
	v_mul_f32_e32 v68, v47, v47
	v_mul_f32_e32 v70, v49, v49
	v_mul_f32_e32 v72, v28, v28
	v_mul_f32_e32 v73, v29, v29
	v_pk_fma_f32 v[68:69], v[46:47], v[46:47], v[68:69] op_sel_hi:[1,1,0]
	v_pk_fma_f32 v[70:71], v[48:49], v[48:49], v[70:71] op_sel_hi:[1,1,0]
	v_mov_b32_e32 v69, v72
	v_mov_b32_e32 v71, v73
	v_pk_add_f32 v[68:69], v[68:69], v[70:71]
	global_load_dwordx4 v[74:77], v[94:95], off offset:1024
	global_load_dwordx4 v[70:73], v[94:95], off offset:2048
	v_pk_add_f32 v[66:67], v[66:67], v[68:69]
	s_nop 0
	v_add_f32_e32 v66, v66, v67
	ds_bpermute_b32 v67, v93, v66
	s_waitcnt lgkmcnt(0)
	v_add_f32_e32 v66, v66, v67
	ds_bpermute_b32 v67, v124, v66
	s_waitcnt lgkmcnt(0)
	v_add_f32_e32 v66, v66, v67
	ds_bpermute_b32 v67, v125, v66
	s_waitcnt lgkmcnt(0)
	v_add_f32_e32 v66, v66, v67
	ds_bpermute_b32 v67, v126, v66
	s_waitcnt lgkmcnt(0)
	v_add_f32_e32 v78, v66, v67
	ds_bpermute_b32 v79, v127, v78
	global_load_dwordx4 v[66:69], v[94:95], off offset:3072
	s_waitcnt lgkmcnt(0)
	v_add_f32_e32 v86, v78, v79
	ds_bpermute_b32 v87, v128, v86
	global_load_dwordx4 v[78:81], v[96:97], off
	s_waitcnt lgkmcnt(0)
	v_add_f32_e32 v131, v86, v87
	v_fmamk_f32 v131, v131, 0x39800000, v1
	v_mul_f32_e32 v132, 0x4f800000, v131
	v_cmp_gt_f32_e32 vcc, s18, v131
	global_load_dwordx4 v[86:89], v[98:99], off
	s_nop 0
	v_cndmask_b32_e32 v131, v131, v132, vcc
	v_sqrt_f32_e32 v140, v131
	global_load_dwordx4 v[132:135], v[100:101], off
	v_add_u32_e32 v136, -1, v140
	v_fma_f32 v137, -v136, v140, v131
	v_cmp_ge_f32_e64 s[4:5], 0, v137
	v_add_u32_e32 v142, 1, v140
	s_nop 0
	v_cndmask_b32_e64 v141, v140, v136, s[4:5]
	v_fma_f32 v140, -v142, v140, v131
	v_cmp_lt_f32_e64 s[4:5], 0, v140
	global_load_dwordx4 v[136:139], v[102:103], off
	s_nop 0
	v_cndmask_b32_e64 v140, v141, v142, s[4:5]
	v_mul_f32_e32 v141, 0x37800000, v140
	v_cndmask_b32_e32 v144, v140, v141, vcc
	v_cmp_class_f32_e32 vcc, v131, v129
	global_load_dwordx4 v[140:143], v[104:105], off
	s_nop 0
	v_cndmask_b32_e32 v131, v144, v131, vcc
	v_div_scale_f32 v152, s[4:5], v131, v131, 1.0
	v_rcp_f32_e32 v156, v152
	global_load_dwordx4 v[144:147], v[106:107], off
	v_div_scale_f32 v153, vcc, 1.0, v131, 1.0
	v_fma_f32 v148, -v152, v156, 1.0
	v_fmac_f32_e32 v156, v148, v156
	v_mul_f32_e32 v157, v153, v156
	global_load_dwordx4 v[148:151], v[108:109], off
	v_fma_f32 v154, -v152, v157, v153
	v_fmac_f32_e32 v157, v154, v156
	v_fma_f32 v158, -v152, v157, v153
	global_load_dwordx4 v[152:155], v[110:111], off
	v_div_fmas_f32 v156, v158, v156, v157
	v_div_fixup_f32 v168, v156, v131, 1.0
	global_load_dwordx4 v[156:159], v[112:113], off
	v_pk_mul_f32 v[58:59], v[58:59], v[168:169] op_sel_hi:[1,0]
	v_pk_mul_f32 v[52:53], v[52:53], v[168:169] op_sel_hi:[1,0]
	s_waitcnt vmcnt(11)
	v_pk_mul_f32 v[170:171], v[74:75], v[58:59]
	s_waitcnt vmcnt(10)
	v_pk_mul_f32 v[172:173], v[72:73], v[52:53]
	global_load_dwordx4 v[72:75], v[118:119], off
	v_pk_mul_f32 v[64:65], v[64:65], v[168:169] op_sel_hi:[1,0]
	v_pk_mul_f32 v[60:61], v[60:61], v[168:169] op_sel_hi:[1,0]
	v_pk_mul_f32 v[50:51], v[50:51], v[168:169] op_sel_hi:[1,0]
	v_pk_mul_f32 v[4:5], v[4:5], v[168:169] op_sel_hi:[1,0]
	v_pk_mul_f32 v[62:63], v[62:63], v[168:169] op_sel_hi:[1,0]
	v_pk_mul_f32 v[84:85], v[84:85], v[64:65]
	v_pk_mul_f32 v[76:77], v[76:77], v[60:61]
	v_pk_mul_f32 v[174:175], v[70:71], v[50:51]
	v_pk_mul_f32 v[36:37], v[36:37], v[168:169] op_sel_hi:[1,0]
	v_pk_mul_f32 v[2:3], v[2:3], v[168:169] op_sel_hi:[1,0]
	v_pk_mul_f32 v[82:83], v[82:83], v[62:63]
	v_max_f32_e64 v62, |v84|, |v85|
	v_max_f32_e64 v58, |v76|, |v77|
	v_pk_mul_f32 v[34:35], v[34:35], v[168:169] op_sel_hi:[1,0]
	v_max3_f32 v62, |v82|, |v83|, v62
	v_max3_f32 v58, |v170|, |v171|, v58
	v_max_f32_e64 v50, |v172|, |v173|
	v_max3_f32 v58, v62, 0, v58
	v_max3_f32 v50, |v174|, |v175|, v50
	s_waitcnt vmcnt(10)
	v_pk_mul_f32 v[176:177], v[68:69], v[36:37]
	v_pk_mul_f32 v[178:179], v[66:67], v[34:35]
	v_max_f32_e64 v34, |v176|, |v177|
	v_max3_f32 v34, |v178|, |v179|, v34
	v_max3_f32 v34, v58, v50, v34
	s_waitcnt vmcnt(9)
	v_pk_mul_f32 v[70:71], v[80:81], v[4:5]
	v_pk_mul_f32 v[78:79], v[78:79], v[2:3]
	v_max_f32_e64 v2, |v70|, |v71|
	v_pk_mul_f32 v[4:5], v[12:13], v[168:169] op_sel_hi:[1,0]
	v_max3_f32 v35, |v78|, |v79|, v2
	v_pk_mul_f32 v[2:3], v[10:11], v[168:169] op_sel_hi:[1,0]
	s_waitcnt vmcnt(8)
	v_pk_mul_f32 v[66:67], v[88:89], v[4:5]
	v_pk_mul_f32 v[68:69], v[86:87], v[2:3]
	v_max_f32_e64 v2, |v66|, |v67|
	v_max3_f32 v2, |v68|, |v69|, v2
	v_pk_mul_f32 v[4:5], v[8:9], v[168:169] op_sel_hi:[1,0]
	v_max3_f32 v10, v34, v35, v2
	v_pk_mul_f32 v[2:3], v[6:7], v[168:169] op_sel_hi:[1,0]
	s_waitcnt vmcnt(7)
	v_pk_mul_f32 v[62:63], v[134:135], v[4:5]
	v_pk_mul_f32 v[64:65], v[132:133], v[2:3]
	v_max_f32_e64 v2, |v62|, |v63|
	v_pk_mul_f32 v[4:5], v[16:17], v[168:169] op_sel_hi:[1,0]
	v_max3_f32 v6, |v64|, |v65|, v2
	v_pk_mul_f32 v[2:3], v[14:15], v[168:169] op_sel_hi:[1,0]
	v_pk_mul_f32 v[16:17], v[26:27], v[168:169] op_sel_hi:[1,0]
	s_waitcnt vmcnt(6)
	v_pk_mul_f32 v[58:59], v[138:139], v[4:5]
	v_pk_mul_f32 v[60:61], v[136:137], v[2:3]
	v_max_f32_e64 v2, |v58|, |v59|
	v_max3_f32 v2, |v60|, |v61|, v2
	v_pk_mul_f32 v[4:5], v[20:21], v[168:169] op_sel_hi:[1,0]
	v_max3_f32 v6, v10, v6, v2
	v_pk_mul_f32 v[2:3], v[18:19], v[168:169] op_sel_hi:[1,0]
	s_waitcnt vmcnt(5)
	v_pk_mul_f32 v[50:51], v[142:143], v[4:5]
	v_pk_mul_f32 v[52:53], v[140:141], v[2:3]
	v_max_f32_e64 v2, |v50|, |v51|
	v_pk_mul_f32 v[4:5], v[24:25], v[168:169] op_sel_hi:[1,0]
	v_max3_f32 v7, |v52|, |v53|, v2
	v_pk_mul_f32 v[2:3], v[22:23], v[168:169] op_sel_hi:[1,0]
	s_waitcnt vmcnt(4)
	v_pk_mul_f32 v[34:35], v[146:147], v[4:5]
	v_pk_mul_f32 v[36:37], v[144:145], v[2:3]
	v_max_f32_e64 v2, |v34|, |v35|
	v_max3_f32 v2, |v36|, |v37|, v2
	v_pk_mul_f32 v[4:5], v[32:33], v[168:169] op_sel_hi:[1,0]
	v_max3_f32 v6, v6, v7, v2
	v_pk_mul_f32 v[2:3], v[30:31], v[168:169] op_sel_hi:[1,0]
	s_waitcnt vmcnt(3)
	v_pk_mul_f32 v[22:23], v[4:5], v[150:151]
	v_pk_mul_f32 v[24:25], v[2:3], v[148:149]
	v_max_f32_e64 v2, |v22|, |v23|
	v_pk_mul_f32 v[4:5], v[56:57], v[168:169] op_sel_hi:[1,0]
	v_max3_f32 v7, |v24|, |v25|, v2
	v_pk_mul_f32 v[2:3], v[54:55], v[168:169] op_sel_hi:[1,0]
	s_waitcnt vmcnt(2)
	v_pk_mul_f32 v[18:19], v[4:5], v[154:155]
	v_pk_mul_f32 v[20:21], v[2:3], v[152:153]
	v_max_f32_e64 v2, |v18|, |v19|
	v_max3_f32 v2, |v20|, |v21|, v2
	v_pk_mul_f32 v[4:5], v[40:41], v[168:169] op_sel_hi:[1,0]
	v_max3_f32 v14, v6, v7, v2
	v_pk_mul_f32 v[2:3], v[38:39], v[168:169] op_sel_hi:[1,0]
	s_waitcnt vmcnt(1)
	v_pk_mul_f32 v[10:11], v[4:5], v[158:159]
	v_pk_mul_f32 v[12:13], v[2:3], v[156:157]
	v_max_f32_e64 v2, |v10|, |v11|
	v_pk_mul_f32 v[4:5], v[44:45], v[168:169] op_sel_hi:[1,0]
	v_max3_f32 v15, |v12|, |v13|, v2
	v_pk_mul_f32 v[2:3], v[42:43], v[168:169] op_sel_hi:[1,0]
	v_pk_mul_f32 v[6:7], v[4:5], v[162:163]
	v_pk_mul_f32 v[8:9], v[2:3], v[160:161]
	v_max_f32_e64 v2, |v6|, |v7|
	v_max3_f32 v2, |v8|, |v9|, v2
	v_max3_f32 v30, v14, v15, v2
	v_pk_mul_f32 v[2:3], v[48:49], v[168:169] op_sel_hi:[1,0]
	v_pk_mul_f32 v[4:5], v[46:47], v[168:169] op_sel_hi:[1,0]
	v_pk_mul_f32 v[2:3], v[2:3], v[166:167]
	v_pk_mul_f32 v[4:5], v[4:5], v[164:165]
	v_max_f32_e64 v14, |v2|, |v3|
	v_max3_f32 v31, |v4|, |v5|, v14
	v_pk_mul_f32 v[14:15], v[28:29], v[168:169] op_sel_hi:[1,0]
	s_waitcnt vmcnt(0)
	v_pk_mul_f32 v[16:17], v[16:17], v[72:73]
	v_pk_mul_f32 v[14:15], v[14:15], v[74:75]
	s_nop 0
	v_max_f32_e64 v26, |v14|, |v15|
	v_max3_f32 v26, |v16|, |v17|, v26
	v_max3_f32 v26, v30, v31, v26
	ds_bpermute_b32 v27, v93, v26
	s_waitcnt lgkmcnt(0)
	v_max_f32_e32 v27, v27, v27
	v_max_f32_e32 v26, v26, v27
	ds_bpermute_b32 v27, v124, v26
	s_waitcnt lgkmcnt(0)
	v_max_f32_e32 v27, v27, v27
	v_max_f32_e32 v26, v26, v27
	ds_bpermute_b32 v27, v125, v26
	s_waitcnt lgkmcnt(0)
	v_max_f32_e32 v27, v27, v27
	v_max_f32_e32 v26, v26, v27
	ds_bpermute_b32 v27, v126, v26
	s_waitcnt lgkmcnt(0)
	v_max_f32_e32 v27, v27, v27
	v_max_f32_e32 v26, v26, v27
	ds_bpermute_b32 v27, v127, v26
	s_waitcnt lgkmcnt(0)
	v_max_f32_e32 v27, v27, v27
	v_max_f32_e32 v26, v26, v27
	ds_bpermute_b32 v27, v128, v26
	s_waitcnt lgkmcnt(0)
	v_max_f32_e32 v27, v27, v27
	v_max_f32_e32 v26, v26, v27
	v_div_scale_f32 v27, s[4:5], v26, v26, s19
	v_rcp_f32_e32 v28, v27
	s_nop 0
	v_fma_f32 v29, -v27, v28, 1.0
	v_fmac_f32_e32 v28, v29, v28
	v_div_scale_f32 v29, vcc, s19, v26, s19
	v_mul_f32_e32 v30, v29, v28
	v_fma_f32 v31, -v27, v30, v29
	v_fmac_f32_e32 v30, v31, v28
	v_fma_f32 v27, -v27, v30, v29
	v_div_fmas_f32 v27, v27, v28, v30
	v_div_fixup_f32 v27, v27, v26, s19
	v_cmp_lt_f32_e32 vcc, 0, v26
	s_nop 1
	v_cndmask_b32_e32 v27, 0, v27, vcc
	v_mul_f32_e32 v29, v83, v27
	v_mul_f32_e32 v28, v82, v27
	v_mul_f32_e32 v30, v84, v27
	v_mul_f32_e32 v31, v85, v27
	v_med3_f32 v29, v29, s20, v130
	v_med3_f32 v28, v28, s20, v130
	v_rndne_f32_e32 v29, v29
	v_med3_f32 v30, v30, s20, v130
	v_med3_f32 v31, v31, s20, v130
	v_rndne_f32_e32 v28, v28
	v_cvt_i32_f32_e32 v29, v29
	v_rndne_f32_e32 v30, v30
	v_rndne_f32_e32 v31, v31
	v_cvt_i32_f32_e32 v28, v28
	v_cvt_i32_f32_sdwa v30, v30 dst_sel:WORD_1 dst_unused:UNUSED_PAD src0_sel:DWORD
	v_cvt_i32_f32_e32 v31, v31
	v_lshlrev_b32_e32 v29, 8, v29
	v_and_b32_e32 v29, 0xff00, v29
	v_and_b32_e32 v30, 0xff0000, v30
	v_perm_b32 v28, v31, v28, s21
	v_or3_b32 v28, v28, v29, v30
	v_mul_f32_e32 v29, v171, v27
	global_store_dword v[122:123], v28, off offset:-2048
	v_mul_f32_e32 v28, v170, v27
	v_mul_f32_e32 v30, v76, v27
	v_mul_f32_e32 v31, v77, v27
	v_med3_f32 v29, v29, s20, v130
	v_med3_f32 v28, v28, s20, v130
	v_rndne_f32_e32 v29, v29
	v_med3_f32 v30, v30, s20, v130
	v_med3_f32 v31, v31, s20, v130
	v_rndne_f32_e32 v28, v28
	v_cvt_i32_f32_e32 v29, v29
	v_rndne_f32_e32 v30, v30
	v_rndne_f32_e32 v31, v31
	v_cvt_i32_f32_e32 v28, v28
	v_cvt_i32_f32_sdwa v30, v30 dst_sel:WORD_1 dst_unused:UNUSED_PAD src0_sel:DWORD
	v_cvt_i32_f32_e32 v31, v31
	v_lshlrev_b32_e32 v29, 8, v29
	v_and_b32_e32 v29, 0xff00, v29
	v_and_b32_e32 v30, 0xff0000, v30
	v_perm_b32 v28, v31, v28, s21
	v_or3_b32 v28, v28, v29, v30
	v_mul_f32_e32 v29, v175, v27
	global_store_dword v[122:123], v28, off offset:-1792
	v_mul_f32_e32 v28, v174, v27
	v_mul_f32_e32 v30, v172, v27
	v_mul_f32_e32 v31, v173, v27
	v_med3_f32 v29, v29, s20, v130
	v_med3_f32 v28, v28, s20, v130
	v_rndne_f32_e32 v29, v29
	v_med3_f32 v30, v30, s20, v130
	v_med3_f32 v31, v31, s20, v130
	v_rndne_f32_e32 v28, v28
	v_cvt_i32_f32_e32 v29, v29
	v_rndne_f32_e32 v30, v30
	v_rndne_f32_e32 v31, v31
	v_cvt_i32_f32_e32 v28, v28
	v_cvt_i32_f32_sdwa v30, v30 dst_sel:WORD_1 dst_unused:UNUSED_PAD src0_sel:DWORD
	v_cvt_i32_f32_e32 v31, v31
	v_lshlrev_b32_e32 v29, 8, v29
	v_and_b32_e32 v29, 0xff00, v29
	v_and_b32_e32 v30, 0xff0000, v30
	v_perm_b32 v28, v31, v28, s21
	v_or3_b32 v28, v28, v29, v30
	v_mul_f32_e32 v29, v179, v27
	global_store_dword v[122:123], v28, off offset:-1536
	v_mul_f32_e32 v28, v178, v27
	v_mul_f32_e32 v30, v176, v27
	v_mul_f32_e32 v31, v177, v27
	v_med3_f32 v29, v29, s20, v130
	v_med3_f32 v28, v28, s20, v130
	v_rndne_f32_e32 v29, v29
	v_med3_f32 v30, v30, s20, v130
	v_med3_f32 v31, v31, s20, v130
	v_rndne_f32_e32 v28, v28
	v_cvt_i32_f32_e32 v29, v29
	v_rndne_f32_e32 v30, v30
	v_rndne_f32_e32 v31, v31
	v_cvt_i32_f32_e32 v28, v28
	v_cvt_i32_f32_sdwa v30, v30 dst_sel:WORD_1 dst_unused:UNUSED_PAD src0_sel:DWORD
	v_cvt_i32_f32_e32 v31, v31
	v_lshlrev_b32_e32 v29, 8, v29
	v_and_b32_e32 v29, 0xff00, v29
	v_and_b32_e32 v30, 0xff0000, v30
	v_perm_b32 v28, v31, v28, s21
	v_or3_b32 v28, v28, v29, v30
	v_mul_f32_e32 v29, v79, v27
	global_store_dword v[122:123], v28, off offset:-1280
	v_mul_f32_e32 v28, v78, v27
	v_mul_f32_e32 v30, v70, v27
	v_mul_f32_e32 v31, v71, v27
	v_med3_f32 v29, v29, s20, v130
	v_med3_f32 v28, v28, s20, v130
	v_rndne_f32_e32 v29, v29
	v_med3_f32 v30, v30, s20, v130
	v_med3_f32 v31, v31, s20, v130
	v_rndne_f32_e32 v28, v28
	v_cvt_i32_f32_e32 v29, v29
	v_rndne_f32_e32 v30, v30
	v_rndne_f32_e32 v31, v31
	v_cvt_i32_f32_e32 v28, v28
	v_cvt_i32_f32_sdwa v30, v30 dst_sel:WORD_1 dst_unused:UNUSED_PAD src0_sel:DWORD
	v_cvt_i32_f32_e32 v31, v31
	v_lshlrev_b32_e32 v29, 8, v29
	v_and_b32_e32 v29, 0xff00, v29
	v_and_b32_e32 v30, 0xff0000, v30
	v_perm_b32 v28, v31, v28, s21
	v_or3_b32 v28, v28, v29, v30
	v_mul_f32_e32 v29, v69, v27
	global_store_dword v[122:123], v28, off offset:-1024
	v_mul_f32_e32 v28, v68, v27
	v_mul_f32_e32 v30, v66, v27
	v_mul_f32_e32 v31, v67, v27
	v_med3_f32 v29, v29, s20, v130
	v_med3_f32 v28, v28, s20, v130
	v_rndne_f32_e32 v29, v29
	v_med3_f32 v30, v30, s20, v130
	v_med3_f32 v31, v31, s20, v130
	v_rndne_f32_e32 v28, v28
	v_cvt_i32_f32_e32 v29, v29
	v_rndne_f32_e32 v30, v30
	v_rndne_f32_e32 v31, v31
	v_cvt_i32_f32_e32 v28, v28
	v_cvt_i32_f32_sdwa v30, v30 dst_sel:WORD_1 dst_unused:UNUSED_PAD src0_sel:DWORD
	v_cvt_i32_f32_e32 v31, v31
	v_lshlrev_b32_e32 v29, 8, v29
	v_and_b32_e32 v29, 0xff00, v29
	v_and_b32_e32 v30, 0xff0000, v30
	v_perm_b32 v28, v31, v28, s21
	v_or3_b32 v28, v28, v29, v30
	v_mul_f32_e32 v29, v65, v27
	global_store_dword v[122:123], v28, off offset:-768
	v_mul_f32_e32 v28, v64, v27
	v_mul_f32_e32 v30, v62, v27
	v_mul_f32_e32 v31, v63, v27
	v_med3_f32 v29, v29, s20, v130
	v_med3_f32 v28, v28, s20, v130
	v_rndne_f32_e32 v29, v29
	v_med3_f32 v30, v30, s20, v130
	v_med3_f32 v31, v31, s20, v130
	v_rndne_f32_e32 v28, v28
	v_cvt_i32_f32_e32 v29, v29
	v_rndne_f32_e32 v30, v30
	v_rndne_f32_e32 v31, v31
	v_cvt_i32_f32_e32 v28, v28
	v_cvt_i32_f32_sdwa v30, v30 dst_sel:WORD_1 dst_unused:UNUSED_PAD src0_sel:DWORD
	v_cvt_i32_f32_e32 v31, v31
	v_lshlrev_b32_e32 v29, 8, v29
	v_and_b32_e32 v29, 0xff00, v29
	v_and_b32_e32 v30, 0xff0000, v30
	v_perm_b32 v28, v31, v28, s21
	v_or3_b32 v28, v28, v29, v30
	v_mul_f32_e32 v29, v61, v27
	global_store_dword v[122:123], v28, off offset:-512
	v_mul_f32_e32 v28, v60, v27
	v_mul_f32_e32 v30, v58, v27
	v_mul_f32_e32 v31, v59, v27
	v_med3_f32 v29, v29, s20, v130
	v_med3_f32 v28, v28, s20, v130
	v_rndne_f32_e32 v29, v29
	v_med3_f32 v30, v30, s20, v130
	v_med3_f32 v31, v31, s20, v130
	v_rndne_f32_e32 v28, v28
	v_cvt_i32_f32_e32 v29, v29
	v_rndne_f32_e32 v30, v30
	v_rndne_f32_e32 v31, v31
	v_cvt_i32_f32_e32 v28, v28
	v_cvt_i32_f32_sdwa v30, v30 dst_sel:WORD_1 dst_unused:UNUSED_PAD src0_sel:DWORD
	v_cvt_i32_f32_e32 v31, v31
	v_lshlrev_b32_e32 v29, 8, v29
	v_and_b32_e32 v29, 0xff00, v29
	v_and_b32_e32 v30, 0xff0000, v30
	v_perm_b32 v28, v31, v28, s21
	v_or3_b32 v28, v28, v29, v30
	v_mul_f32_e32 v29, v53, v27
	v_mul_f32_e32 v5, v5, v27
	global_store_dword v[122:123], v28, off offset:-256
	v_mul_f32_e32 v28, v52, v27
	v_mul_f32_e32 v30, v50, v27
	v_mul_f32_e32 v31, v51, v27
	v_med3_f32 v29, v29, s20, v130
	v_mul_f32_e32 v4, v4, v27
	v_mul_f32_e32 v2, v2, v27
	v_mul_f32_e32 v3, v3, v27
	v_med3_f32 v5, v5, s20, v130
	v_med3_f32 v28, v28, s20, v130
	v_rndne_f32_e32 v29, v29
	v_med3_f32 v30, v30, s20, v130
	v_med3_f32 v31, v31, s20, v130
	v_med3_f32 v4, v4, s20, v130
	v_rndne_f32_e32 v5, v5
	v_med3_f32 v2, v2, s20, v130
	v_med3_f32 v3, v3, s20, v130
	v_rndne_f32_e32 v28, v28
	v_cvt_i32_f32_e32 v29, v29
	v_rndne_f32_e32 v30, v30
	v_rndne_f32_e32 v31, v31
	v_rndne_f32_e32 v4, v4
	v_cvt_i32_f32_e32 v5, v5
	v_rndne_f32_e32 v2, v2
	v_rndne_f32_e32 v3, v3
	v_cvt_i32_f32_e32 v28, v28
	v_cvt_i32_f32_sdwa v30, v30 dst_sel:WORD_1 dst_unused:UNUSED_PAD src0_sel:DWORD
	v_cvt_i32_f32_e32 v31, v31
	v_cvt_i32_f32_e32 v4, v4
	v_cvt_i32_f32_sdwa v2, v2 dst_sel:WORD_1 dst_unused:UNUSED_PAD src0_sel:DWORD
	v_cvt_i32_f32_e32 v3, v3
	v_lshlrev_b32_e32 v29, 8, v29
	v_lshlrev_b32_e32 v5, 8, v5
	v_and_b32_e32 v29, 0xff00, v29
	v_and_b32_e32 v30, 0xff0000, v30
	v_perm_b32 v28, v31, v28, s21
	v_and_b32_e32 v5, 0xff00, v5
	v_and_b32_e32 v2, 0xff0000, v2
	v_perm_b32 v3, v3, v4, s21
	v_or3_b32 v28, v28, v29, v30
	v_mul_f32_e32 v29, v37, v27
	v_mul_f32_e32 v25, v25, v27
	v_mul_f32_e32 v21, v21, v27
	v_mul_f32_e32 v13, v13, v27
	v_mul_f32_e32 v9, v9, v27
	v_or3_b32 v2, v3, v5, v2
	v_mul_f32_e32 v3, v17, v27
	global_store_dword v[122:123], v28, off
	v_mul_f32_e32 v28, v36, v27
	v_mul_f32_e32 v30, v34, v27
	v_mul_f32_e32 v31, v35, v27
	v_med3_f32 v29, v29, s20, v130
	v_mul_f32_e32 v24, v24, v27
	v_mul_f32_e32 v22, v22, v27
	v_mul_f32_e32 v23, v23, v27
	v_med3_f32 v25, v25, s20, v130
	v_mul_f32_e32 v20, v20, v27
	v_mul_f32_e32 v18, v18, v27
	v_mul_f32_e32 v19, v19, v27
	v_med3_f32 v21, v21, s20, v130
	v_mul_f32_e32 v12, v12, v27
	v_mul_f32_e32 v10, v10, v27
	v_mul_f32_e32 v11, v11, v27
	v_med3_f32 v13, v13, s20, v130
	v_mul_f32_e32 v8, v8, v27
	v_mul_f32_e32 v6, v6, v27
	v_mul_f32_e32 v7, v7, v27
	v_med3_f32 v9, v9, s20, v130
	global_store_dword v[122:123], v2, off offset:1536
	v_mul_f32_e32 v2, v16, v27
	v_mul_f32_e32 v4, v14, v27
	v_mul_f32_e32 v5, v15, v27
	v_med3_f32 v3, v3, s20, v130
	v_med3_f32 v28, v28, s20, v130
	v_rndne_f32_e32 v29, v29
	v_med3_f32 v30, v30, s20, v130
	v_med3_f32 v31, v31, s20, v130
	v_med3_f32 v24, v24, s20, v130
	v_rndne_f32_e32 v25, v25
	v_med3_f32 v22, v22, s20, v130
	v_med3_f32 v23, v23, s20, v130
	v_med3_f32 v20, v20, s20, v130
	v_rndne_f32_e32 v21, v21
	v_med3_f32 v18, v18, s20, v130
	v_med3_f32 v19, v19, s20, v130
	v_med3_f32 v12, v12, s20, v130
	v_rndne_f32_e32 v13, v13
	v_med3_f32 v10, v10, s20, v130
	v_med3_f32 v11, v11, s20, v130
	v_med3_f32 v8, v8, s20, v130
	v_rndne_f32_e32 v9, v9
	v_med3_f32 v6, v6, s20, v130
	v_med3_f32 v7, v7, s20, v130
	v_med3_f32 v2, v2, s20, v130
	v_rndne_f32_e32 v3, v3
	v_med3_f32 v4, v4, s20, v130
	v_med3_f32 v5, v5, s20, v130
	v_rndne_f32_e32 v28, v28
	v_cvt_i32_f32_e32 v29, v29
	v_rndne_f32_e32 v30, v30
	v_rndne_f32_e32 v31, v31
	v_rndne_f32_e32 v24, v24
	v_cvt_i32_f32_e32 v25, v25
	v_rndne_f32_e32 v22, v22
	v_rndne_f32_e32 v23, v23
	v_rndne_f32_e32 v20, v20
	v_cvt_i32_f32_e32 v21, v21
	v_rndne_f32_e32 v18, v18
	v_rndne_f32_e32 v19, v19
	v_rndne_f32_e32 v12, v12
	v_cvt_i32_f32_e32 v13, v13
	v_rndne_f32_e32 v10, v10
	v_rndne_f32_e32 v11, v11
	v_rndne_f32_e32 v8, v8
	v_cvt_i32_f32_e32 v9, v9
	v_rndne_f32_e32 v6, v6
	v_rndne_f32_e32 v7, v7
	v_rndne_f32_e32 v2, v2
	v_cvt_i32_f32_e32 v3, v3
	v_rndne_f32_e32 v4, v4
	v_rndne_f32_e32 v5, v5
	v_cvt_i32_f32_e32 v28, v28
	v_cvt_i32_f32_sdwa v30, v30 dst_sel:WORD_1 dst_unused:UNUSED_PAD src0_sel:DWORD
	v_cvt_i32_f32_e32 v31, v31
	v_cvt_i32_f32_e32 v24, v24
	v_cvt_i32_f32_sdwa v22, v22 dst_sel:WORD_1 dst_unused:UNUSED_PAD src0_sel:DWORD
	v_cvt_i32_f32_e32 v23, v23
	v_cvt_i32_f32_e32 v20, v20
	v_cvt_i32_f32_sdwa v18, v18 dst_sel:WORD_1 dst_unused:UNUSED_PAD src0_sel:DWORD
	v_cvt_i32_f32_e32 v19, v19
	v_cvt_i32_f32_e32 v12, v12
	v_cvt_i32_f32_sdwa v10, v10 dst_sel:WORD_1 dst_unused:UNUSED_PAD src0_sel:DWORD
	v_cvt_i32_f32_e32 v11, v11
	v_cvt_i32_f32_e32 v8, v8
	v_cvt_i32_f32_sdwa v6, v6 dst_sel:WORD_1 dst_unused:UNUSED_PAD src0_sel:DWORD
	v_cvt_i32_f32_e32 v7, v7
	v_cvt_i32_f32_e32 v2, v2
	v_cvt_i32_f32_sdwa v4, v4 dst_sel:WORD_1 dst_unused:UNUSED_PAD src0_sel:DWORD
	v_cvt_i32_f32_e32 v5, v5
	v_lshlrev_b32_e32 v29, 8, v29
	v_lshlrev_b32_e32 v25, 8, v25
	v_lshlrev_b32_e32 v21, 8, v21
	v_lshlrev_b32_e32 v13, 8, v13
	v_lshlrev_b32_e32 v9, 8, v9
	v_lshlrev_b32_e32 v3, 8, v3
	v_and_b32_e32 v29, 0xff00, v29
	v_and_b32_e32 v30, 0xff0000, v30
	v_perm_b32 v28, v31, v28, s21
	v_and_b32_e32 v25, 0xff00, v25
	v_and_b32_e32 v22, 0xff0000, v22
	v_perm_b32 v23, v23, v24, s21
	v_and_b32_e32 v21, 0xff00, v21
	v_and_b32_e32 v18, 0xff0000, v18
	v_perm_b32 v19, v19, v20, s21
	v_and_b32_e32 v13, 0xff00, v13
	v_and_b32_e32 v10, 0xff0000, v10
	v_perm_b32 v11, v11, v12, s21
	v_and_b32_e32 v9, 0xff00, v9
	v_and_b32_e32 v6, 0xff0000, v6
	v_perm_b32 v7, v7, v8, s21
	v_and_b32_e32 v3, 0xff00, v3
	v_and_b32_e32 v4, 0xff0000, v4
	v_perm_b32 v2, v5, v2, s21
	v_or3_b32 v28, v28, v29, v30
	v_or3_b32 v22, v23, v25, v22
	v_or3_b32 v18, v19, v21, v18
	v_or3_b32 v10, v11, v13, v10
	v_or3_b32 v6, v7, v9, v6
	v_or3_b32 v2, v2, v3, v4
	global_store_dword v[122:123], v28, off offset:256
	global_store_dword v[122:123], v22, off offset:512
	global_store_dword v[122:123], v18, off offset:768
	global_store_dword v[122:123], v10, off offset:1024
	global_store_dword v[122:123], v6, off offset:1280
	global_store_dword v[122:123], v2, off offset:1792
	s_and_saveexec_b64 s[4:5], s[0:1]
	s_cbranch_execz .LBB0_141
	v_mul_f32_e32 v2, 0x3c010204, v26
	global_store_dword v91, v2, s[10:11]
	s_branch .LBB0_141

.LBB0_146:
	v_add_co_u32_e64 v18, s[0:1], s3, v100
	v_add_co_u32_e32 v62, vcc, 0xffffd000, v100
	s_nop 0
	v_addc_co_u32_e64 v19, s[0:1], -1, v101, s[0:1]
	v_add_co_u32_e64 v20, s[0:1], s7, v100
	v_addc_co_u32_e32 v63, vcc, -1, v101, vcc
	s_nop 0
	v_addc_co_u32_e64 v21, s[0:1], -1, v101, s[0:1]
	global_load_dwordx4 v[14:17], v[100:101], off offset:-3072
	global_load_dwordx4 v[10:13], v[100:101], off offset:-2048
	global_load_dwordx4 v[6:9], v[100:101], off offset:-1024
	global_load_dwordx4 v[2:5], v[100:101], off
	global_load_dwordx4 v[30:33], v[70:71], off
	global_load_dwordx4 v[46:49], v[18:19], off offset:-3072
	global_load_dwordx4 v[34:37], v[18:19], off offset:-1024
	global_load_dwordx4 v[50:53], v[18:19], off offset:-2048
	global_load_dwordx4 v[38:41], v[18:19], off
	global_load_dwordx4 v[26:29], v[20:21], off offset:-2048
	global_load_dwordx4 v[42:45], v[20:21], off offset:-3072
	global_load_dwordx4 v[22:25], v[20:21], off offset:-1024
	global_load_dwordx4 v[18:21], v[100:101], off offset:-4096
	global_load_dwordx4 v[66:69], v[62:63], off offset:-3072
	global_load_dwordx4 v[58:61], v[62:63], off offset:-2048
	global_load_dwordx4 v[54:57], v[62:63], off
	global_load_dwordx4 v[62:65], v[62:63], off offset:-1024
	v_add_co_u32_e64 v92, s[0:1], s7, v90
	s_add_i32 s6, s6, s92
	s_nop 0
	v_addc_co_u32_e64 v93, s[0:1], -1, v91, s[0:1]
	v_lshl_add_u64 v[100:101], v[100:101], 0, s[4:5]
	s_cmpk_gt_i32 s6, 0x3ff
	s_waitcnt vmcnt(11)
	v_pk_mul_f32 v[114:115], v[48:49], v[48:49]
	s_waitcnt vmcnt(10)
	v_mul_f32_e32 v143, v34, v34
	v_mul_f32_e32 v146, v35, v35
	s_waitcnt vmcnt(8)
	v_pk_mul_f32 v[116:117], v[40:41], v[40:41]
	v_pk_mul_f32 v[104:105], v[38:39], v[38:39]
	s_waitcnt vmcnt(7)
	v_mul_f32_e32 v145, v26, v26
	v_mul_f32_e32 v149, v27, v27
	v_mul_f32_e32 v152, v28, v28
	s_waitcnt vmcnt(6)
	v_mul_f32_e32 v124, v43, v43
	v_mul_f32_e32 v126, v45, v45
	v_mov_b32_e32 v156, v26
	v_mov_b32_e32 v157, v28
	v_mov_b32_e32 v28, v27
	s_waitcnt vmcnt(3)
	v_pk_mul_f32 v[26:27], v[68:69], v[68:69]
	v_pk_mul_f32 v[158:159], v[66:67], v[66:67]
	s_waitcnt vmcnt(2)
	v_pk_mul_f32 v[160:161], v[60:61], v[60:61]
	v_pk_mul_f32 v[162:163], v[58:59], v[58:59]
	v_pk_mul_f32 v[108:109], v[12:13], v[12:13]
	v_pk_mul_f32 v[110:111], v[10:11], v[10:11]
	v_mul_f32_e32 v112, v7, v7
	v_mul_f32_e32 v134, v9, v9
	v_mul_f32_e32 v150, v36, v36
	v_mov_b32_e32 v136, v34
	v_mov_b32_e32 v137, v36
	v_mov_b32_e32 v36, v35
	v_mov_b32_e32 v34, v38
	v_mov_b32_e32 v35, v40
	v_mov_b32_e32 v40, v39
	v_mov_b32_e32 v38, v42
	v_mov_b32_e32 v39, v44
	v_pk_mov_b32 v[172:173], v[104:105], v[116:117] op_sel:[1,0]
	v_mov_b32_e32 v105, v117
	v_pk_fma_f32 v[116:117], v[42:43], v[42:43], v[124:125] op_sel_hi:[1,1,0]
	v_pk_fma_f32 v[174:175], v[44:45], v[44:45], v[126:127] op_sel_hi:[1,1,0]
	v_mov_b32_e32 v44, v43
	v_pk_mov_b32 v[42:43], v[158:159], v[26:27] op_sel:[1,0]
	v_mov_b32_e32 v159, v27
	v_pk_mov_b32 v[26:27], v[162:163], v[160:161] op_sel:[1,0]
	v_mov_b32_e32 v163, v161
	v_mul_f32_e32 v154, v4, v4
	v_mul_f32_e32 v155, v5, v5
	v_mov_b32_e32 v102, v30
	v_mov_b32_e32 v103, v32
	v_mov_b32_e32 v32, v31
	v_pk_mul_f32 v[30:31], v[46:47], v[46:47]
	v_mul_f32_e32 v118, v51, v51
	v_mul_f32_e32 v120, v53, v53
	v_pk_mov_b32 v[132:133], v[110:111], v[108:109] op_sel:[1,0]
	v_mov_b32_e32 v111, v109
	v_pk_fma_f32 v[108:109], v[6:7], v[6:7], v[112:113] op_sel_hi:[1,1,0]
	v_pk_fma_f32 v[112:113], v[8:9], v[8:9], v[134:135] op_sel_hi:[1,1,0]
	s_waitcnt vmcnt(1)
	v_mul_f32_e32 v165, v54, v54
	v_mul_f32_e32 v167, v55, v55
	s_waitcnt vmcnt(0)
	v_mul_f32_e32 v164, v63, v63
	v_mul_f32_e32 v166, v65, v65
	v_pk_add_f32 v[42:43], v[42:43], v[158:159]
	v_pk_add_f32 v[26:27], v[26:27], v[162:163]
	v_mov_b32_e32 v134, v46
	v_mov_b32_e32 v135, v48
	v_mov_b32_e32 v48, v47
	v_mov_b32_e32 v46, v50
	v_mov_b32_e32 v47, v52
	v_mul_f32_e32 v180, v56, v56
	v_mul_f32_e32 v181, v57, v57
	v_pk_mov_b32 v[168:169], v[30:31], v[114:115] op_sel:[1,0]
	v_mov_b32_e32 v31, v115
	v_pk_fma_f32 v[114:115], v[50:51], v[50:51], v[118:119] op_sel_hi:[1,1,0]
	v_pk_fma_f32 v[170:171], v[52:53], v[52:53], v[120:121] op_sel_hi:[1,1,0]
	v_mov_b32_e32 v109, v154
	v_mov_b32_e32 v113, v155
	v_mov_b32_e32 v154, v54
	v_mov_b32_e32 v155, v56
	v_mov_b32_e32 v56, v55
	v_mov_b32_e32 v52, v51
	v_pk_fma_f32 v[50:51], v[62:63], v[62:63], v[164:165] op_sel_hi:[1,1,0]
	v_pk_fma_f32 v[54:55], v[64:65], v[64:65], v[166:167] op_sel_hi:[1,1,0]
	v_pk_add_f32 v[42:43], v[42:43], v[42:43] op_sel:[0,1] op_sel_hi:[1,0]
	v_pk_add_f32 v[26:27], v[26:27], v[26:27] op_sel:[0,1] op_sel_hi:[1,0]
	v_mov_b32_e32 v51, v180
	v_mov_b32_e32 v55, v181
	v_mov_b32_e32 v43, v165
	v_mov_b32_e32 v27, v167
	v_pk_add_f32 v[50:51], v[50:51], v[54:55]
	v_pk_add_f32 v[26:27], v[42:43], v[26:27]
	v_pk_add_f32 v[30:31], v[168:169], v[30:31]
	v_pk_add_f32 v[26:27], v[26:27], v[50:51]
	v_mul_f32_e32 v151, v37, v37
	v_pk_add_f32 v[30:31], v[30:31], v[30:31] op_sel:[0,1] op_sel_hi:[1,0]
	v_pk_add_f32 v[26:27], v[26:27], v[26:27] op_sel:[0,1] op_sel_hi:[1,0]
	v_mov_b32_e32 v115, v150
	v_mov_b32_e32 v171, v151
	v_mov_b32_e32 v31, v146
	v_mov_b32_e32 v27, v143
	v_pk_add_f32 v[110:111], v[132:133], v[110:111]
	v_mov_b32_e32 v132, v66
	v_mov_b32_e32 v133, v68
	v_mov_b32_e32 v68, v67
	v_mov_b32_e32 v66, v58
	v_mov_b32_e32 v67, v60
	v_mov_b32_e32 v60, v59
	v_mov_b32_e32 v58, v62
	v_mov_b32_e32 v59, v64
	v_mov_b32_e32 v64, v63
	v_pk_add_f32 v[62:63], v[114:115], v[170:171]
	v_pk_add_f32 v[26:27], v[26:27], v[30:31]
	v_pk_add_f32 v[104:105], v[172:173], v[104:105]
	v_pk_add_f32 v[26:27], v[26:27], v[62:63]
	v_mul_f32_e32 v153, v29, v29
	v_pk_add_f32 v[104:105], v[104:105], v[104:105] op_sel:[0,1] op_sel_hi:[1,0]
	v_pk_add_f32 v[26:27], v[26:27], v[26:27] op_sel:[0,1] op_sel_hi:[1,0]
	v_pk_mul_f32 v[122:123], v[24:25], v[24:25]
	v_pk_mul_f32 v[106:107], v[22:23], v[22:23]
	v_mov_b32_e32 v117, v152
	v_mov_b32_e32 v175, v153
	v_mov_b32_e32 v105, v149
	v_mov_b32_e32 v27, v145
	v_pk_mov_b32 v[176:177], v[106:107], v[122:123] op_sel:[1,0]
	v_mov_b32_e32 v107, v123
	v_pk_add_f32 v[108:109], v[108:109], v[112:113]
	v_pk_add_f32 v[112:113], v[116:117], v[174:175]
	v_pk_add_f32 v[26:27], v[26:27], v[104:105]
	v_mul_f32_e32 v128, v19, v19
	v_mul_f32_e32 v130, v21, v21
	v_pk_add_f32 v[106:107], v[176:177], v[106:107]
	v_pk_add_f32 v[26:27], v[26:27], v[112:113]
	v_mul_f32_e32 v140, v14, v14
	v_mul_f32_e32 v142, v15, v15
	v_mul_f32_e32 v147, v16, v16
	v_mul_f32_e32 v148, v17, v17
	v_pk_fma_f32 v[122:123], v[18:19], v[18:19], v[128:129] op_sel_hi:[1,1,0]
	v_pk_fma_f32 v[178:179], v[20:21], v[20:21], v[130:131] op_sel_hi:[1,1,0]
	v_pk_add_f32 v[106:107], v[106:107], v[106:107] op_sel:[0,1] op_sel_hi:[1,0]
	v_pk_add_f32 v[26:27], v[26:27], v[26:27] op_sel:[0,1] op_sel_hi:[1,0]
	v_mov_b32_e32 v123, v147
	v_mov_b32_e32 v179, v148
	v_mov_b32_e32 v107, v142
	v_mov_b32_e32 v27, v140
	v_pk_add_f32 v[114:115], v[122:123], v[178:179]
	v_pk_add_f32 v[26:27], v[26:27], v[106:107]
	v_mul_f32_e32 v141, v2, v2
	v_pk_add_f32 v[26:27], v[26:27], v[114:115]
	v_mul_f32_e32 v144, v3, v3
	v_pk_add_f32 v[110:111], v[110:111], v[110:111] op_sel:[0,1] op_sel_hi:[1,0]
	v_pk_add_f32 v[26:27], v[26:27], v[26:27] op_sel:[0,1] op_sel_hi:[1,0]
	v_mov_b32_e32 v111, v144
	v_mov_b32_e32 v27, v141
	v_pk_add_f32 v[26:27], v[26:27], v[110:111]
	s_nop 0
	v_pk_add_f32 v[26:27], v[26:27], v[108:109]
	s_nop 0
	v_add_f32_e32 v26, v26, v27
	ds_bpermute_b32 v27, v1, v26
	s_waitcnt lgkmcnt(0)
	v_add_f32_e32 v26, v26, v27
	ds_bpermute_b32 v27, v119, v26
	s_waitcnt lgkmcnt(0)
	v_add_f32_e32 v26, v26, v27
	ds_bpermute_b32 v27, v121, v26
	s_waitcnt lgkmcnt(0)
	v_add_f32_e32 v26, v26, v27
	ds_bpermute_b32 v27, v125, v26
	s_waitcnt lgkmcnt(0)
	v_add_f32_e32 v26, v26, v27
	ds_bpermute_b32 v27, v127, v26
	s_waitcnt lgkmcnt(0)
	v_add_f32_e32 v26, v26, v27
	ds_bpermute_b32 v27, v129, v26
	s_waitcnt lgkmcnt(0)
	v_add_f32_e32 v26, v26, v27
	v_fmamk_f32 v26, v26, 0x39800000, v131
	v_mul_f32_e32 v27, 0x4f800000, v26
	v_cmp_gt_f32_e32 vcc, s12, v26
	s_nop 1
	v_cndmask_b32_e32 v26, v26, v27, vcc
	v_sqrt_f32_e32 v27, v26
	s_nop 0
	v_add_u32_e32 v30, -1, v27
	v_add_u32_e32 v31, 1, v27
	v_fma_f32 v42, -v30, v27, v26
	v_fma_f32 v43, -v31, v27, v26
	v_cmp_ge_f32_e64 s[0:1], 0, v42
	s_nop 1
	v_cndmask_b32_e64 v27, v27, v30, s[0:1]
	v_cmp_lt_f32_e64 s[0:1], 0, v43
	s_nop 1
	v_cndmask_b32_e64 v27, v27, v31, s[0:1]
	v_mul_f32_e32 v30, 0x37800000, v27
	v_cndmask_b32_e32 v27, v27, v30, vcc
	v_cmp_class_f32_e32 vcc, v26, v138
	s_nop 1
	v_cndmask_b32_e32 v26, v27, v26, vcc
	v_div_scale_f32 v27, s[0:1], v26, v26, 1.0
	v_rcp_f32_e32 v31, v27
	v_div_scale_f32 v30, vcc, 1.0, v26, 1.0
	v_fma_f32 v42, -v27, v31, 1.0
	v_fmac_f32_e32 v31, v42, v31
	v_mul_f32_e32 v42, v30, v31
	v_fma_f32 v43, -v27, v42, v30
	v_fmac_f32_e32 v42, v43, v31
	v_fma_f32 v27, -v27, v42, v30
	v_div_fmas_f32 v27, v27, v31, v42
	v_div_fixup_f32 v26, v27, v26, 1.0
	v_pk_mul_f32 v[50:51], v[68:69], v[26:27] op_sel_hi:[1,0]
	v_pk_mul_f32 v[42:43], v[132:133], v[26:27] op_sel_hi:[1,0]
	v_pk_mul_f32 v[32:33], v[32:33], v[50:51]
	v_pk_mul_f32 v[104:105], v[34:35], v[26:27] op_sel_hi:[1,0]
	v_pk_mul_f32 v[34:35], v[102:103], v[42:43]
	v_and_b32_sdwa v43, v33, v139 dst_sel:DWORD dst_unused:UNUSED_PAD src0_sel:WORD_1 src1_sel:DWORD
	v_and_b32_sdwa v50, v32, v139 dst_sel:DWORD dst_unused:UNUSED_PAD src0_sel:WORD_1 src1_sel:DWORD
	v_pk_mul_f32 v[54:55], v[66:67], v[26:27] op_sel_hi:[1,0]
	v_pk_mul_f32 v[60:61], v[60:61], v[26:27] op_sel_hi:[1,0]
	v_pk_mul_f32 v[58:59], v[58:59], v[26:27] op_sel_hi:[1,0]
	v_pk_mul_f32 v[62:63], v[64:65], v[26:27] op_sel_hi:[1,0]
	v_pk_mul_f32 v[64:65], v[154:155], v[26:27] op_sel_hi:[1,0]
	v_pk_mul_f32 v[56:57], v[56:57], v[26:27] op_sel_hi:[1,0]
	v_pk_mul_f32 v[66:67], v[134:135], v[26:27] op_sel_hi:[1,0]
	v_pk_mul_f32 v[48:49], v[48:49], v[26:27] op_sel_hi:[1,0]
	v_pk_mul_f32 v[46:47], v[46:47], v[26:27] op_sel_hi:[1,0]
	v_pk_mul_f32 v[52:53], v[52:53], v[26:27] op_sel_hi:[1,0]
	v_pk_mul_f32 v[68:69], v[136:137], v[26:27] op_sel_hi:[1,0]
	v_pk_mul_f32 v[36:37], v[36:37], v[26:27] op_sel_hi:[1,0]
	v_pk_mul_f32 v[40:41], v[40:41], v[26:27] op_sel_hi:[1,0]
	v_pk_mul_f32 v[38:39], v[38:39], v[26:27] op_sel_hi:[1,0]
	v_pk_mul_f32 v[44:45], v[44:45], v[26:27] op_sel_hi:[1,0]
	v_pk_mul_f32 v[30:31], v[156:157], v[26:27] op_sel_hi:[1,0]
	v_and_b32_sdwa v27, v35, v139 dst_sel:DWORD dst_unused:UNUSED_PAD src0_sel:WORD_1 src1_sel:DWORD
	v_and_b32_sdwa v42, v34, v139 dst_sel:DWORD dst_unused:UNUSED_PAD src0_sel:WORD_1 src1_sel:DWORD
	v_add3_u32 v33, v33, v43, s13
	v_add3_u32 v32, v32, v50, s13
	v_add3_u32 v34, v34, v42, s13
	v_add3_u32 v27, v35, v27, s13
	v_and_b32_e32 v33, 0xffff0000, v33
	v_and_b32_e32 v32, 0xffff0000, v32
	v_or_b32_sdwa v33, v33, v27 dst_sel:DWORD dst_unused:UNUSED_PAD src0_sel:DWORD src1_sel:WORD_1
	v_or_b32_sdwa v32, v32, v34 dst_sel:DWORD dst_unused:UNUSED_PAD src0_sel:DWORD src1_sel:WORD_1
	global_store_dwordx2 v[92:93], v[32:33], off offset:-3584
	global_load_dwordx4 v[32:35], v[70:71], off offset:1024
	s_waitcnt vmcnt(0)
	v_mov_b32_e32 v42, v32
	v_mov_b32_e32 v43, v34
	v_mov_b32_e32 v34, v33
	v_pk_mul_f32 v[32:33], v[42:43], v[54:55]
	v_pk_mul_f32 v[34:35], v[34:35], v[60:61]
	v_and_b32_sdwa v27, v33, v139 dst_sel:DWORD dst_unused:UNUSED_PAD src0_sel:WORD_1 src1_sel:DWORD
	v_and_b32_sdwa v43, v35, v139 dst_sel:DWORD dst_unused:UNUSED_PAD src0_sel:WORD_1 src1_sel:DWORD
	v_and_b32_sdwa v50, v34, v139 dst_sel:DWORD dst_unused:UNUSED_PAD src0_sel:WORD_1 src1_sel:DWORD
	v_and_b32_sdwa v42, v32, v139 dst_sel:DWORD dst_unused:UNUSED_PAD src0_sel:WORD_1 src1_sel:DWORD
	v_add3_u32 v27, v33, v27, s13
	v_add3_u32 v33, v35, v43, s13
	v_add3_u32 v34, v34, v50, s13
	v_add3_u32 v32, v32, v42, s13
	v_and_b32_e32 v33, 0xffff0000, v33
	v_and_b32_e32 v34, 0xffff0000, v34
	v_or_b32_sdwa v33, v33, v27 dst_sel:DWORD dst_unused:UNUSED_PAD src0_sel:DWORD src1_sel:WORD_1
	v_or_b32_sdwa v32, v34, v32 dst_sel:DWORD dst_unused:UNUSED_PAD src0_sel:DWORD src1_sel:WORD_1
	global_store_dwordx2 v[92:93], v[32:33], off offset:-3072
	global_load_dwordx4 v[32:35], v[70:71], off offset:2048
	s_waitcnt vmcnt(0)
	v_mov_b32_e32 v42, v32
	v_mov_b32_e32 v43, v34
	v_mov_b32_e32 v34, v33
	v_pk_mul_f32 v[32:33], v[42:43], v[58:59]
	v_pk_mul_f32 v[34:35], v[34:35], v[62:63]
	v_and_b32_sdwa v27, v33, v139 dst_sel:DWORD dst_unused:UNUSED_PAD src0_sel:WORD_1 src1_sel:DWORD
	v_and_b32_sdwa v43, v35, v139 dst_sel:DWORD dst_unused:UNUSED_PAD src0_sel:WORD_1 src1_sel:DWORD
	v_and_b32_sdwa v50, v34, v139 dst_sel:DWORD dst_unused:UNUSED_PAD src0_sel:WORD_1 src1_sel:DWORD
	v_and_b32_sdwa v42, v32, v139 dst_sel:DWORD dst_unused:UNUSED_PAD src0_sel:WORD_1 src1_sel:DWORD
	v_add3_u32 v27, v33, v27, s13
	v_add3_u32 v33, v35, v43, s13
	v_add3_u32 v34, v34, v50, s13
	v_add3_u32 v32, v32, v42, s13
	v_and_b32_e32 v33, 0xffff0000, v33
	v_and_b32_e32 v34, 0xffff0000, v34
	v_or_b32_sdwa v33, v33, v27 dst_sel:DWORD dst_unused:UNUSED_PAD src0_sel:DWORD src1_sel:WORD_1
	v_or_b32_sdwa v32, v34, v32 dst_sel:DWORD dst_unused:UNUSED_PAD src0_sel:DWORD src1_sel:WORD_1
	global_store_dwordx2 v[92:93], v[32:33], off offset:-2560
	global_load_dwordx4 v[32:35], v[70:71], off offset:3072
	s_waitcnt vmcnt(0)
	v_mov_b32_e32 v42, v32
	v_mov_b32_e32 v43, v34
	v_mov_b32_e32 v34, v33
	v_pk_mul_f32 v[32:33], v[42:43], v[64:65]
	v_pk_mul_f32 v[34:35], v[34:35], v[56:57]
	v_and_b32_sdwa v27, v33, v139 dst_sel:DWORD dst_unused:UNUSED_PAD src0_sel:WORD_1 src1_sel:DWORD
	v_and_b32_sdwa v43, v35, v139 dst_sel:DWORD dst_unused:UNUSED_PAD src0_sel:WORD_1 src1_sel:DWORD
	v_and_b32_sdwa v50, v34, v139 dst_sel:DWORD dst_unused:UNUSED_PAD src0_sel:WORD_1 src1_sel:DWORD
	v_and_b32_sdwa v42, v32, v139 dst_sel:DWORD dst_unused:UNUSED_PAD src0_sel:WORD_1 src1_sel:DWORD
	v_add3_u32 v27, v33, v27, s13
	v_add3_u32 v33, v35, v43, s13
	v_add3_u32 v34, v34, v50, s13
	v_add3_u32 v32, v32, v42, s13
	v_and_b32_e32 v33, 0xffff0000, v33
	v_and_b32_e32 v34, 0xffff0000, v34
	v_or_b32_sdwa v33, v33, v27 dst_sel:DWORD dst_unused:UNUSED_PAD src0_sel:DWORD src1_sel:WORD_1
	v_or_b32_sdwa v32, v34, v32 dst_sel:DWORD dst_unused:UNUSED_PAD src0_sel:DWORD src1_sel:WORD_1
	global_store_dwordx2 v[92:93], v[32:33], off offset:-2048
	global_load_dwordx4 v[32:35], v[72:73], off
	s_waitcnt vmcnt(0)
	v_mov_b32_e32 v42, v32
	v_mov_b32_e32 v43, v34
	v_mov_b32_e32 v34, v33
	v_pk_mul_f32 v[32:33], v[66:67], v[42:43]
	v_pk_mul_f32 v[34:35], v[48:49], v[34:35]
	v_and_b32_sdwa v27, v33, v139 dst_sel:DWORD dst_unused:UNUSED_PAD src0_sel:WORD_1 src1_sel:DWORD
	v_and_b32_sdwa v43, v35, v139 dst_sel:DWORD dst_unused:UNUSED_PAD src0_sel:WORD_1 src1_sel:DWORD
	v_and_b32_sdwa v48, v34, v139 dst_sel:DWORD dst_unused:UNUSED_PAD src0_sel:WORD_1 src1_sel:DWORD
	v_and_b32_sdwa v42, v32, v139 dst_sel:DWORD dst_unused:UNUSED_PAD src0_sel:WORD_1 src1_sel:DWORD
	v_add3_u32 v27, v33, v27, s13
	v_add3_u32 v33, v35, v43, s13
	v_add3_u32 v34, v34, v48, s13
	v_add3_u32 v32, v32, v42, s13
	v_and_b32_e32 v33, 0xffff0000, v33
	v_and_b32_e32 v34, 0xffff0000, v34
	v_or_b32_sdwa v33, v33, v27 dst_sel:DWORD dst_unused:UNUSED_PAD src0_sel:DWORD src1_sel:WORD_1
	v_or_b32_sdwa v32, v34, v32 dst_sel:DWORD dst_unused:UNUSED_PAD src0_sel:DWORD src1_sel:WORD_1
	global_store_dwordx2 v[92:93], v[32:33], off offset:-1536
	global_load_dwordx4 v[32:35], v[74:75], off
	s_waitcnt vmcnt(0)
	v_mov_b32_e32 v42, v32
	v_mov_b32_e32 v43, v34
	v_mov_b32_e32 v34, v33
	v_pk_mul_f32 v[32:33], v[46:47], v[42:43]
	v_pk_mul_f32 v[34:35], v[52:53], v[34:35]
	v_and_b32_sdwa v27, v33, v139 dst_sel:DWORD dst_unused:UNUSED_PAD src0_sel:WORD_1 src1_sel:DWORD
	v_and_b32_sdwa v43, v35, v139 dst_sel:DWORD dst_unused:UNUSED_PAD src0_sel:WORD_1 src1_sel:DWORD
	v_and_b32_sdwa v46, v34, v139 dst_sel:DWORD dst_unused:UNUSED_PAD src0_sel:WORD_1 src1_sel:DWORD
	v_and_b32_sdwa v42, v32, v139 dst_sel:DWORD dst_unused:UNUSED_PAD src0_sel:WORD_1 src1_sel:DWORD
	v_add3_u32 v27, v33, v27, s13
	v_add3_u32 v33, v35, v43, s13
	v_add3_u32 v34, v34, v46, s13
	v_add3_u32 v32, v32, v42, s13
	v_and_b32_e32 v33, 0xffff0000, v33
	v_and_b32_e32 v34, 0xffff0000, v34
	v_or_b32_sdwa v33, v33, v27 dst_sel:DWORD dst_unused:UNUSED_PAD src0_sel:DWORD src1_sel:WORD_1
	v_or_b32_sdwa v32, v34, v32 dst_sel:DWORD dst_unused:UNUSED_PAD src0_sel:DWORD src1_sel:WORD_1
	global_store_dwordx2 v[92:93], v[32:33], off offset:-1024
	global_load_dwordx4 v[32:35], v[76:77], off
	s_waitcnt vmcnt(0)
	v_mov_b32_e32 v42, v32
	v_mov_b32_e32 v43, v34
	v_mov_b32_e32 v34, v33
	v_pk_mul_f32 v[32:33], v[68:69], v[42:43]
	v_pk_mul_f32 v[34:35], v[36:37], v[34:35]
	v_and_b32_sdwa v27, v33, v139 dst_sel:DWORD dst_unused:UNUSED_PAD src0_sel:WORD_1 src1_sel:DWORD
	v_and_b32_sdwa v37, v35, v139 dst_sel:DWORD dst_unused:UNUSED_PAD src0_sel:WORD_1 src1_sel:DWORD
	v_and_b32_sdwa v42, v34, v139 dst_sel:DWORD dst_unused:UNUSED_PAD src0_sel:WORD_1 src1_sel:DWORD
	v_and_b32_sdwa v36, v32, v139 dst_sel:DWORD dst_unused:UNUSED_PAD src0_sel:WORD_1 src1_sel:DWORD
	v_add3_u32 v27, v33, v27, s13
	v_add3_u32 v33, v35, v37, s13
	v_add3_u32 v34, v34, v42, s13
	v_add3_u32 v32, v32, v36, s13
	v_and_b32_e32 v33, 0xffff0000, v33
	v_and_b32_e32 v34, 0xffff0000, v34
	v_or_b32_sdwa v33, v33, v27 dst_sel:DWORD dst_unused:UNUSED_PAD src0_sel:DWORD src1_sel:WORD_1
	v_or_b32_sdwa v32, v34, v32 dst_sel:DWORD dst_unused:UNUSED_PAD src0_sel:DWORD src1_sel:WORD_1
	global_store_dwordx2 v[92:93], v[32:33], off offset:-512
	global_load_dwordx4 v[32:35], v[78:79], off
	s_waitcnt vmcnt(0)
	v_mov_b32_e32 v36, v32
	v_mov_b32_e32 v37, v34
	v_mov_b32_e32 v34, v33
	v_pk_mul_f32 v[32:33], v[104:105], v[36:37]
	v_pk_mul_f32 v[34:35], v[40:41], v[34:35]
	v_and_b32_sdwa v27, v33, v139 dst_sel:DWORD dst_unused:UNUSED_PAD src0_sel:WORD_1 src1_sel:DWORD
	v_and_b32_sdwa v37, v35, v139 dst_sel:DWORD dst_unused:UNUSED_PAD src0_sel:WORD_1 src1_sel:DWORD
	v_and_b32_sdwa v40, v34, v139 dst_sel:DWORD dst_unused:UNUSED_PAD src0_sel:WORD_1 src1_sel:DWORD
	v_and_b32_sdwa v36, v32, v139 dst_sel:DWORD dst_unused:UNUSED_PAD src0_sel:WORD_1 src1_sel:DWORD
	v_add3_u32 v27, v33, v27, s13
	v_add3_u32 v33, v35, v37, s13
	v_add3_u32 v34, v34, v40, s13
	v_add3_u32 v32, v32, v36, s13
	v_and_b32_e32 v33, 0xffff0000, v33
	v_and_b32_e32 v34, 0xffff0000, v34
	v_or_b32_sdwa v33, v33, v27 dst_sel:DWORD dst_unused:UNUSED_PAD src0_sel:DWORD src1_sel:WORD_1
	v_or_b32_sdwa v32, v34, v32 dst_sel:DWORD dst_unused:UNUSED_PAD src0_sel:DWORD src1_sel:WORD_1
	global_store_dwordx2 v[90:91], v[32:33], off offset:-4096
	global_load_dwordx4 v[32:35], v[80:81], off
	s_waitcnt vmcnt(0)
	v_mov_b32_e32 v36, v32
	v_mov_b32_e32 v37, v34
	v_mov_b32_e32 v34, v33
	v_pk_mul_f32 v[32:33], v[38:39], v[36:37]
	v_pk_mul_f32 v[34:35], v[44:45], v[34:35]
	v_and_b32_sdwa v27, v33, v139 dst_sel:DWORD dst_unused:UNUSED_PAD src0_sel:WORD_1 src1_sel:DWORD
	v_and_b32_sdwa v37, v35, v139 dst_sel:DWORD dst_unused:UNUSED_PAD src0_sel:WORD_1 src1_sel:DWORD
	v_and_b32_sdwa v38, v34, v139 dst_sel:DWORD dst_unused:UNUSED_PAD src0_sel:WORD_1 src1_sel:DWORD
	v_and_b32_sdwa v36, v32, v139 dst_sel:DWORD dst_unused:UNUSED_PAD src0_sel:WORD_1 src1_sel:DWORD
	v_add3_u32 v27, v33, v27, s13
	v_add3_u32 v33, v35, v37, s13
	v_add3_u32 v34, v34, v38, s13
	v_add3_u32 v32, v32, v36, s13
	v_and_b32_e32 v33, 0xffff0000, v33
	v_and_b32_e32 v34, 0xffff0000, v34
	v_or_b32_sdwa v33, v33, v27 dst_sel:DWORD dst_unused:UNUSED_PAD src0_sel:DWORD src1_sel:WORD_1
	v_or_b32_sdwa v32, v34, v32 dst_sel:DWORD dst_unused:UNUSED_PAD src0_sel:DWORD src1_sel:WORD_1
	global_store_dwordx2 v[90:91], v[32:33], off offset:-3584
	global_load_dwordx4 v[32:35], v[82:83], off
	v_pk_mul_f32 v[28:29], v[28:29], v[26:27] op_sel_hi:[1,0]
	s_waitcnt vmcnt(0)
	v_mov_b32_e32 v37, v34
	v_mov_b32_e32 v34, v33
	v_mov_b32_e32 v36, v32
	v_pk_mul_f32 v[28:29], v[28:29], v[34:35]
	v_pk_mul_f32 v[30:31], v[30:31], v[36:37]
	v_and_b32_sdwa v33, v29, v139 dst_sel:DWORD dst_unused:UNUSED_PAD src0_sel:WORD_1 src1_sel:DWORD
	v_and_b32_sdwa v34, v28, v139 dst_sel:DWORD dst_unused:UNUSED_PAD src0_sel:WORD_1 src1_sel:DWORD
	v_and_b32_sdwa v27, v31, v139 dst_sel:DWORD dst_unused:UNUSED_PAD src0_sel:WORD_1 src1_sel:DWORD
	v_and_b32_sdwa v32, v30, v139 dst_sel:DWORD dst_unused:UNUSED_PAD src0_sel:WORD_1 src1_sel:DWORD
	v_add3_u32 v29, v29, v33, s13
	v_add3_u32 v28, v28, v34, s13
	v_add3_u32 v30, v30, v32, s13
	v_add3_u32 v27, v31, v27, s13
	v_and_b32_e32 v29, 0xffff0000, v29
	v_and_b32_e32 v28, 0xffff0000, v28
	v_or_b32_sdwa v29, v29, v27 dst_sel:DWORD dst_unused:UNUSED_PAD src0_sel:DWORD src1_sel:WORD_1
	v_or_b32_sdwa v28, v28, v30 dst_sel:DWORD dst_unused:UNUSED_PAD src0_sel:DWORD src1_sel:WORD_1
	global_store_dwordx2 v[90:91], v[28:29], off offset:-3072
	global_load_dwordx4 v[28:31], v[84:85], off
	v_mov_b32_e32 v32, v22
	v_mov_b32_e32 v33, v24
	v_mov_b32_e32 v24, v23
	v_pk_mul_f32 v[22:23], v[32:33], v[26:27] op_sel_hi:[1,0]
	v_pk_mul_f32 v[24:25], v[24:25], v[26:27] op_sel_hi:[1,0]
	s_waitcnt vmcnt(0)
	v_mov_b32_e32 v33, v30
	v_mov_b32_e32 v30, v29
	v_mov_b32_e32 v32, v28
	v_pk_mul_f32 v[24:25], v[24:25], v[30:31]
	v_pk_mul_f32 v[22:23], v[22:23], v[32:33]
	v_and_b32_sdwa v29, v25, v139 dst_sel:DWORD dst_unused:UNUSED_PAD src0_sel:WORD_1 src1_sel:DWORD
	v_and_b32_sdwa v30, v24, v139 dst_sel:DWORD dst_unused:UNUSED_PAD src0_sel:WORD_1 src1_sel:DWORD
	v_and_b32_sdwa v27, v23, v139 dst_sel:DWORD dst_unused:UNUSED_PAD src0_sel:WORD_1 src1_sel:DWORD
	v_and_b32_sdwa v28, v22, v139 dst_sel:DWORD dst_unused:UNUSED_PAD src0_sel:WORD_1 src1_sel:DWORD
	v_add3_u32 v25, v25, v29, s13
	v_add3_u32 v24, v24, v30, s13
	v_add3_u32 v22, v22, v28, s13
	v_add3_u32 v23, v23, v27, s13
	v_and_b32_e32 v25, 0xffff0000, v25
	v_and_b32_e32 v24, 0xffff0000, v24
	v_or_b32_sdwa v23, v25, v23 dst_sel:DWORD dst_unused:UNUSED_PAD src0_sel:DWORD src1_sel:WORD_1
	v_or_b32_sdwa v22, v24, v22 dst_sel:DWORD dst_unused:UNUSED_PAD src0_sel:DWORD src1_sel:WORD_1
	global_store_dwordx2 v[90:91], v[22:23], off offset:-2560
	global_load_dwordx4 v[22:25], v[86:87], off
	v_mov_b32_e32 v28, v18
	v_mov_b32_e32 v29, v20
	v_mov_b32_e32 v20, v19
	v_pk_mul_f32 v[18:19], v[28:29], v[26:27] op_sel_hi:[1,0]
	v_pk_mul_f32 v[20:21], v[20:21], v[26:27] op_sel_hi:[1,0]
	s_waitcnt vmcnt(0)
	v_mov_b32_e32 v29, v24
	v_mov_b32_e32 v24, v23
	v_mov_b32_e32 v28, v22
	v_pk_mul_f32 v[20:21], v[20:21], v[24:25]
	v_pk_mul_f32 v[18:19], v[18:19], v[28:29]
	v_and_b32_sdwa v24, v21, v139 dst_sel:DWORD dst_unused:UNUSED_PAD src0_sel:WORD_1 src1_sel:DWORD
	v_and_b32_sdwa v25, v20, v139 dst_sel:DWORD dst_unused:UNUSED_PAD src0_sel:WORD_1 src1_sel:DWORD
	v_and_b32_sdwa v22, v19, v139 dst_sel:DWORD dst_unused:UNUSED_PAD src0_sel:WORD_1 src1_sel:DWORD
	v_and_b32_sdwa v23, v18, v139 dst_sel:DWORD dst_unused:UNUSED_PAD src0_sel:WORD_1 src1_sel:DWORD
	v_add3_u32 v21, v21, v24, s13
	v_add3_u32 v20, v20, v25, s13
	v_add3_u32 v18, v18, v23, s13
	v_add3_u32 v19, v19, v22, s13
	v_and_b32_e32 v21, 0xffff0000, v21
	v_and_b32_e32 v20, 0xffff0000, v20
	v_or_b32_sdwa v19, v21, v19 dst_sel:DWORD dst_unused:UNUSED_PAD src0_sel:DWORD src1_sel:WORD_1
	v_or_b32_sdwa v18, v20, v18 dst_sel:DWORD dst_unused:UNUSED_PAD src0_sel:DWORD src1_sel:WORD_1
	global_store_dwordx2 v[90:91], v[18:19], off offset:-2048
	global_load_dwordx4 v[18:21], v[88:89], off
	v_mov_b32_e32 v22, v14
	v_mov_b32_e32 v23, v16
	v_mov_b32_e32 v16, v15
	v_pk_mul_f32 v[14:15], v[22:23], v[26:27] op_sel_hi:[1,0]
	v_pk_mul_f32 v[16:17], v[16:17], v[26:27] op_sel_hi:[1,0]
	s_waitcnt vmcnt(0)
	v_mov_b32_e32 v23, v20
	v_mov_b32_e32 v20, v19
	v_mov_b32_e32 v22, v18
	v_pk_mul_f32 v[16:17], v[16:17], v[20:21]
	v_pk_mul_f32 v[14:15], v[14:15], v[22:23]
	v_and_b32_sdwa v20, v17, v139 dst_sel:DWORD dst_unused:UNUSED_PAD src0_sel:WORD_1 src1_sel:DWORD
	v_and_b32_sdwa v21, v16, v139 dst_sel:DWORD dst_unused:UNUSED_PAD src0_sel:WORD_1 src1_sel:DWORD
	v_and_b32_sdwa v18, v15, v139 dst_sel:DWORD dst_unused:UNUSED_PAD src0_sel:WORD_1 src1_sel:DWORD
	v_and_b32_sdwa v19, v14, v139 dst_sel:DWORD dst_unused:UNUSED_PAD src0_sel:WORD_1 src1_sel:DWORD
	v_add3_u32 v17, v17, v20, s13
	v_add3_u32 v16, v16, v21, s13
	v_add3_u32 v14, v14, v19, s13
	v_add3_u32 v15, v15, v18, s13
	v_and_b32_e32 v17, 0xffff0000, v17
	v_and_b32_e32 v16, 0xffff0000, v16
	v_or_b32_sdwa v15, v17, v15 dst_sel:DWORD dst_unused:UNUSED_PAD src0_sel:DWORD src1_sel:WORD_1
	v_or_b32_sdwa v14, v16, v14 dst_sel:DWORD dst_unused:UNUSED_PAD src0_sel:DWORD src1_sel:WORD_1
	global_store_dwordx2 v[90:91], v[14:15], off offset:-1536
	global_load_dwordx4 v[14:17], v[94:95], off
	v_mov_b32_e32 v18, v10
	v_mov_b32_e32 v19, v12
	v_mov_b32_e32 v12, v11
	v_pk_mul_f32 v[10:11], v[18:19], v[26:27] op_sel_hi:[1,0]
	v_pk_mul_f32 v[12:13], v[12:13], v[26:27] op_sel_hi:[1,0]
	s_waitcnt vmcnt(0)
	v_mov_b32_e32 v19, v16
	v_mov_b32_e32 v16, v15
	v_mov_b32_e32 v18, v14
	v_pk_mul_f32 v[12:13], v[12:13], v[16:17]
	v_pk_mul_f32 v[10:11], v[10:11], v[18:19]
	v_and_b32_sdwa v16, v13, v139 dst_sel:DWORD dst_unused:UNUSED_PAD src0_sel:WORD_1 src1_sel:DWORD
	v_and_b32_sdwa v17, v12, v139 dst_sel:DWORD dst_unused:UNUSED_PAD src0_sel:WORD_1 src1_sel:DWORD
	v_and_b32_sdwa v14, v11, v139 dst_sel:DWORD dst_unused:UNUSED_PAD src0_sel:WORD_1 src1_sel:DWORD
	v_and_b32_sdwa v15, v10, v139 dst_sel:DWORD dst_unused:UNUSED_PAD src0_sel:WORD_1 src1_sel:DWORD
	v_add3_u32 v13, v13, v16, s13
	v_add3_u32 v12, v12, v17, s13
	v_add3_u32 v10, v10, v15, s13
	v_add3_u32 v11, v11, v14, s13
	v_and_b32_e32 v13, 0xffff0000, v13
	v_and_b32_e32 v12, 0xffff0000, v12
	v_or_b32_sdwa v11, v13, v11 dst_sel:DWORD dst_unused:UNUSED_PAD src0_sel:DWORD src1_sel:WORD_1
	v_or_b32_sdwa v10, v12, v10 dst_sel:DWORD dst_unused:UNUSED_PAD src0_sel:DWORD src1_sel:WORD_1
	global_store_dwordx2 v[90:91], v[10:11], off offset:-1024
	global_load_dwordx4 v[10:13], v[96:97], off
	v_mov_b32_e32 v14, v6
	v_mov_b32_e32 v15, v8
	v_mov_b32_e32 v8, v7
	v_pk_mul_f32 v[6:7], v[14:15], v[26:27] op_sel_hi:[1,0]
	v_pk_mul_f32 v[8:9], v[8:9], v[26:27] op_sel_hi:[1,0]
	s_waitcnt vmcnt(0)
	v_mov_b32_e32 v15, v12
	v_mov_b32_e32 v12, v11
	v_mov_b32_e32 v14, v10
	v_pk_mul_f32 v[8:9], v[8:9], v[12:13]
	v_pk_mul_f32 v[6:7], v[6:7], v[14:15]
	v_and_b32_sdwa v12, v9, v139 dst_sel:DWORD dst_unused:UNUSED_PAD src0_sel:WORD_1 src1_sel:DWORD
	v_and_b32_sdwa v13, v8, v139 dst_sel:DWORD dst_unused:UNUSED_PAD src0_sel:WORD_1 src1_sel:DWORD
	v_and_b32_sdwa v10, v7, v139 dst_sel:DWORD dst_unused:UNUSED_PAD src0_sel:WORD_1 src1_sel:DWORD
	v_and_b32_sdwa v11, v6, v139 dst_sel:DWORD dst_unused:UNUSED_PAD src0_sel:WORD_1 src1_sel:DWORD
	v_add3_u32 v9, v9, v12, s13
	v_add3_u32 v8, v8, v13, s13
	v_add3_u32 v6, v6, v11, s13
	v_add3_u32 v7, v7, v10, s13
	v_and_b32_e32 v9, 0xffff0000, v9
	v_and_b32_e32 v8, 0xffff0000, v8
	v_or_b32_sdwa v7, v9, v7 dst_sel:DWORD dst_unused:UNUSED_PAD src0_sel:DWORD src1_sel:WORD_1
	v_or_b32_sdwa v6, v8, v6 dst_sel:DWORD dst_unused:UNUSED_PAD src0_sel:DWORD src1_sel:WORD_1
	global_store_dwordx2 v[90:91], v[6:7], off offset:-512
	global_load_dwordx4 v[6:9], v[98:99], off
	v_mov_b32_e32 v10, v2
	v_mov_b32_e32 v11, v4
	v_mov_b32_e32 v4, v3
	v_pk_mul_f32 v[2:3], v[10:11], v[26:27] op_sel_hi:[1,0]
	v_pk_mul_f32 v[4:5], v[4:5], v[26:27] op_sel_hi:[1,0]
	s_waitcnt vmcnt(0)
	v_mov_b32_e32 v11, v8
	v_mov_b32_e32 v8, v7
	v_mov_b32_e32 v10, v6
	v_pk_mul_f32 v[4:5], v[4:5], v[8:9]
	v_pk_mul_f32 v[2:3], v[2:3], v[10:11]
	v_and_b32_sdwa v8, v5, v139 dst_sel:DWORD dst_unused:UNUSED_PAD src0_sel:WORD_1 src1_sel:DWORD
	v_and_b32_sdwa v9, v4, v139 dst_sel:DWORD dst_unused:UNUSED_PAD src0_sel:WORD_1 src1_sel:DWORD
	v_and_b32_sdwa v6, v3, v139 dst_sel:DWORD dst_unused:UNUSED_PAD src0_sel:WORD_1 src1_sel:DWORD
	v_and_b32_sdwa v7, v2, v139 dst_sel:DWORD dst_unused:UNUSED_PAD src0_sel:WORD_1 src1_sel:DWORD
	v_add3_u32 v5, v5, v8, s13
	v_add3_u32 v4, v4, v9, s13
	v_add3_u32 v2, v2, v7, s13
	v_add3_u32 v3, v3, v6, s13
	v_and_b32_e32 v5, 0xffff0000, v5
	v_and_b32_e32 v4, 0xffff0000, v4
	v_or_b32_sdwa v3, v5, v3 dst_sel:DWORD dst_unused:UNUSED_PAD src0_sel:DWORD src1_sel:WORD_1
	v_or_b32_sdwa v2, v4, v2 dst_sel:DWORD dst_unused:UNUSED_PAD src0_sel:DWORD src1_sel:WORD_1
	global_store_dwordx2 v[90:91], v[2:3], off
	v_lshl_add_u64 v[90:91], v[90:91], 0, s[10:11]
	s_cbranch_scc0 .LBB0_146

.LBB0_321:
	v_lshl_add_u32 v6, s18, 8, v182
	v_lshl_or_b32 v4, s19, 8, v184
	v_ashrrev_i32_e32 v7, 31, v6
	v_ashrrev_i32_e32 v5, 31, v4
	v_lshlrev_b64 v[2:3], 12, v[6:7]
	v_readlane_b32 s68, v247, 6
	v_lshl_add_u64 v[2:3], v[2:3], 0, v[4:5]
	v_readlane_b32 s69, v247, 7
	v_lshlrev_b64 v[2:3], 2, v[2:3]
	s_mov_b64 s[40:41], s[68:69]
	v_lshl_add_u64 v[20:21], s[40:41], 0, v[2:3]
	global_load_dwordx4 v[8:11], v[20:21], off
	global_load_dwordx4 v[12:15], v[20:21], off offset:64
	global_load_dwordx4 v[16:19], v[20:21], off offset:512
	global_load_dwordx4 v[20:23], v[20:21], off offset:576
	v_readlane_b32 s24, v247, 2
	v_readlane_b32 s26, v247, 4
	v_readlane_b32 s27, v247, 5
	s_mov_b64 s[18:19], 0x200000
	s_and_b64 vcc, exec, s[0:1]
	v_lshl_add_u64 v[24:25], s[26:27], 0, v[2:3]
	v_readlane_b32 s70, v247, 8
	v_readlane_b32 s71, v247, 9
	v_readlane_b32 s72, v247, 10
	v_readlane_b32 s73, v247, 11
	v_readlane_b32 s74, v247, 12
	v_readlane_b32 s75, v247, 13
	v_readlane_b32 s76, v247, 14
	v_readlane_b32 s77, v247, 15
	v_readlane_b32 s78, v247, 16
	v_readlane_b32 s79, v247, 17
	v_readlane_b32 s80, v247, 18
	v_readlane_b32 s81, v247, 19
	v_readlane_b32 s82, v247, 20
	v_readlane_b32 s83, v247, 21
	v_readlane_b32 s25, v247, 3
	s_waitcnt vmcnt(0)
	v_pk_fma_f32 v[10:11], v[160:161], s[16:17], v[10:11] op_sel_hi:[1,0,1]
	v_pk_fma_f32 v[8:9], v[158:159], s[16:17], v[8:9] op_sel_hi:[1,0,1]
	global_store_dwordx4 v[24:25], v[8:11], off
	s_nop 1
	v_pk_fma_f32 v[10:11], v[156:157], s[16:17], v[14:15] op_sel_hi:[1,0,1]
	v_pk_fma_f32 v[8:9], v[154:155], s[16:17], v[12:13] op_sel_hi:[1,0,1]
	global_store_dwordx4 v[24:25], v[8:11], off offset:64
	s_nop 1
	v_pk_fma_f32 v[10:11], v[152:153], s[16:17], v[18:19] op_sel_hi:[1,0,1]
	v_pk_fma_f32 v[8:9], v[150:151], s[16:17], v[16:17] op_sel_hi:[1,0,1]
	global_store_dwordx4 v[24:25], v[8:11], off offset:512
	s_nop 1
	v_pk_fma_f32 v[10:11], v[148:149], s[16:17], v[22:23] op_sel_hi:[1,0,1]
	v_pk_fma_f32 v[8:9], v[146:147], s[16:17], v[20:21] op_sel_hi:[1,0,1]
	global_store_dwordx4 v[24:25], v[8:11], off offset:576
	s_nop 1
	v_or_b32_e32 v8, 16, v6
	v_ashrrev_i32_e32 v9, 31, v8
	v_lshlrev_b64 v[8:9], 12, v[8:9]
	v_lshl_add_u64 v[8:9], v[8:9], 0, v[4:5]
	v_lshlrev_b64 v[24:25], 2, v[8:9]
	v_lshl_add_u64 v[20:21], s[40:41], 0, v[24:25]
	global_load_dwordx4 v[8:11], v[20:21], off
	global_load_dwordx4 v[12:15], v[20:21], off offset:64
	global_load_dwordx4 v[16:19], v[20:21], off offset:512
	global_load_dwordx4 v[20:23], v[20:21], off offset:576
	v_lshl_add_u64 v[24:25], s[26:27], 0, v[24:25]
	s_waitcnt vmcnt(3)
	v_pk_fma_f32 v[10:11], v[144:145], s[16:17], v[10:11] op_sel_hi:[1,0,1]
	v_pk_fma_f32 v[8:9], v[142:143], s[16:17], v[8:9] op_sel_hi:[1,0,1]
	global_store_dwordx4 v[24:25], v[8:11], off
	s_waitcnt vmcnt(3)
	s_nop 0
	v_pk_fma_f32 v[10:11], v[140:141], s[16:17], v[14:15] op_sel_hi:[1,0,1]
	v_pk_fma_f32 v[8:9], v[138:139], s[16:17], v[12:13] op_sel_hi:[1,0,1]
	global_store_dwordx4 v[24:25], v[8:11], off offset:64
	s_waitcnt vmcnt(3)
	s_nop 0
	v_pk_fma_f32 v[10:11], v[136:137], s[16:17], v[18:19] op_sel_hi:[1,0,1]
	v_pk_fma_f32 v[8:9], v[134:135], s[16:17], v[16:17] op_sel_hi:[1,0,1]
	global_store_dwordx4 v[24:25], v[8:11], off offset:512
	s_waitcnt vmcnt(3)
	s_nop 0
	v_pk_fma_f32 v[10:11], v[132:133], s[16:17], v[22:23] op_sel_hi:[1,0,1]
	v_pk_fma_f32 v[8:9], v[130:131], s[16:17], v[20:21] op_sel_hi:[1,0,1]
	global_store_dwordx4 v[24:25], v[8:11], off offset:576
	s_nop 1
	v_or_b32_e32 v8, 32, v6
	v_ashrrev_i32_e32 v9, 31, v8
	v_lshlrev_b64 v[8:9], 12, v[8:9]
	v_lshl_add_u64 v[8:9], v[8:9], 0, v[4:5]
	v_lshlrev_b64 v[24:25], 2, v[8:9]
	v_lshl_add_u64 v[20:21], s[40:41], 0, v[24:25]
	global_load_dwordx4 v[8:11], v[20:21], off
	global_load_dwordx4 v[12:15], v[20:21], off offset:64
	global_load_dwordx4 v[16:19], v[20:21], off offset:512
	global_load_dwordx4 v[20:23], v[20:21], off offset:576
	v_lshl_add_u64 v[24:25], s[26:27], 0, v[24:25]
	v_or_b32_e32 v6, 48, v6
	v_ashrrev_i32_e32 v7, 31, v6
	v_lshlrev_b64 v[6:7], 12, v[6:7]
	v_lshl_add_u64 v[4:5], v[6:7], 0, v[4:5]
	s_waitcnt vmcnt(3)
	v_pk_fma_f32 v[10:11], v[128:129], s[16:17], v[10:11] op_sel_hi:[1,0,1]
	v_pk_fma_f32 v[8:9], v[126:127], s[16:17], v[8:9] op_sel_hi:[1,0,1]
	global_store_dwordx4 v[24:25], v[8:11], off
	s_waitcnt vmcnt(3)
	s_nop 0
	v_pk_fma_f32 v[10:11], v[124:125], s[16:17], v[14:15] op_sel_hi:[1,0,1]
	v_pk_fma_f32 v[8:9], v[122:123], s[16:17], v[12:13] op_sel_hi:[1,0,1]
	global_store_dwordx4 v[24:25], v[8:11], off offset:64
	s_waitcnt vmcnt(3)
	s_nop 0
	v_pk_fma_f32 v[10:11], v[120:121], s[16:17], v[18:19] op_sel_hi:[1,0,1]
	v_pk_fma_f32 v[8:9], v[118:119], s[16:17], v[16:17] op_sel_hi:[1,0,1]
	global_store_dwordx4 v[24:25], v[8:11], off offset:512
	s_waitcnt vmcnt(3)
	s_nop 0
	v_pk_fma_f32 v[10:11], v[116:117], s[16:17], v[22:23] op_sel_hi:[1,0,1]
	v_pk_fma_f32 v[8:9], v[114:115], s[16:17], v[20:21] op_sel_hi:[1,0,1]
	global_store_dwordx4 v[24:25], v[8:11], off offset:576
	v_lshlrev_b64 v[20:21], 2, v[4:5]
	v_lshl_add_u64 v[16:17], s[40:41], 0, v[20:21]
	global_load_dwordx4 v[4:7], v[16:17], off
	global_load_dwordx4 v[8:11], v[16:17], off offset:64
	global_load_dwordx4 v[12:15], v[16:17], off offset:512
	global_load_dwordx4 v[16:19], v[16:17], off offset:576
	v_lshl_add_u64 v[20:21], s[26:27], 0, v[20:21]
	s_waitcnt vmcnt(3)
	v_pk_fma_f32 v[6:7], v[112:113], s[16:17], v[6:7] op_sel_hi:[1,0,1]
	v_pk_fma_f32 v[4:5], v[110:111], s[16:17], v[4:5] op_sel_hi:[1,0,1]
	global_store_dwordx4 v[20:21], v[4:7], off
	s_waitcnt vmcnt(3)
	s_nop 0
	v_pk_fma_f32 v[6:7], v[108:109], s[16:17], v[10:11] op_sel_hi:[1,0,1]
	v_pk_fma_f32 v[4:5], v[106:107], s[16:17], v[8:9] op_sel_hi:[1,0,1]
	global_store_dwordx4 v[20:21], v[4:7], off offset:64
	s_waitcnt vmcnt(3)
	s_nop 0
	v_pk_fma_f32 v[6:7], v[104:105], s[16:17], v[14:15] op_sel_hi:[1,0,1]
	v_pk_fma_f32 v[4:5], v[102:103], s[16:17], v[12:13] op_sel_hi:[1,0,1]
	global_store_dwordx4 v[20:21], v[4:7], off offset:512
	s_waitcnt vmcnt(3)
	s_nop 0
	v_pk_fma_f32 v[6:7], v[100:101], s[16:17], v[18:19] op_sel_hi:[1,0,1]
	v_pk_fma_f32 v[4:5], v[98:99], s[16:17], v[16:17] op_sel_hi:[1,0,1]
	global_store_dwordx4 v[20:21], v[4:7], off offset:576
	v_lshl_add_u64 v[20:21], v[2:3], 0, s[18:19]
	v_lshl_add_u64 v[16:17], s[40:41], 0, v[20:21]
	global_load_dwordx4 v[4:7], v[16:17], off
	global_load_dwordx4 v[8:11], v[16:17], off offset:64
	global_load_dwordx4 v[12:15], v[16:17], off offset:512
	global_load_dwordx4 v[16:19], v[16:17], off offset:576
	v_lshl_add_u64 v[20:21], s[26:27], 0, v[20:21]
	s_mov_b64 s[18:19], 0x240000
	s_waitcnt vmcnt(3)
	v_pk_fma_f32 v[6:7], v[96:97], s[16:17], v[6:7] op_sel_hi:[1,0,1]
	v_pk_fma_f32 v[4:5], v[94:95], s[16:17], v[4:5] op_sel_hi:[1,0,1]
	global_store_dwordx4 v[20:21], v[4:7], off
	s_waitcnt vmcnt(3)
	s_nop 0
	v_pk_fma_f32 v[6:7], v[92:93], s[16:17], v[10:11] op_sel_hi:[1,0,1]
	v_pk_fma_f32 v[4:5], v[90:91], s[16:17], v[8:9] op_sel_hi:[1,0,1]
	global_store_dwordx4 v[20:21], v[4:7], off offset:64
	s_waitcnt vmcnt(3)
	s_nop 0
	v_pk_fma_f32 v[6:7], v[88:89], s[16:17], v[14:15] op_sel_hi:[1,0,1]
	v_pk_fma_f32 v[4:5], v[86:87], s[16:17], v[12:13] op_sel_hi:[1,0,1]
	global_store_dwordx4 v[20:21], v[4:7], off offset:512
	s_waitcnt vmcnt(3)
	s_nop 0
	v_pk_fma_f32 v[6:7], v[84:85], s[16:17], v[18:19] op_sel_hi:[1,0,1]
	v_pk_fma_f32 v[4:5], v[82:83], s[16:17], v[16:17] op_sel_hi:[1,0,1]
	global_store_dwordx4 v[20:21], v[4:7], off offset:576
	v_lshl_add_u64 v[20:21], v[2:3], 0, s[18:19]
	v_lshl_add_u64 v[16:17], s[40:41], 0, v[20:21]
	global_load_dwordx4 v[4:7], v[16:17], off
	global_load_dwordx4 v[8:11], v[16:17], off offset:64
	global_load_dwordx4 v[12:15], v[16:17], off offset:512
	global_load_dwordx4 v[16:19], v[16:17], off offset:576
	v_lshl_add_u64 v[20:21], s[26:27], 0, v[20:21]
	s_mov_b64 s[18:19], 0x280000
	s_waitcnt vmcnt(3)
	v_pk_fma_f32 v[6:7], v[80:81], s[16:17], v[6:7] op_sel_hi:[1,0,1]
	v_pk_fma_f32 v[4:5], v[78:79], s[16:17], v[4:5] op_sel_hi:[1,0,1]
	global_store_dwordx4 v[20:21], v[4:7], off
	s_waitcnt vmcnt(3)
	s_nop 0
	v_pk_fma_f32 v[6:7], v[76:77], s[16:17], v[10:11] op_sel_hi:[1,0,1]
	v_pk_fma_f32 v[4:5], v[74:75], s[16:17], v[8:9] op_sel_hi:[1,0,1]
	global_store_dwordx4 v[20:21], v[4:7], off offset:64
	s_waitcnt vmcnt(3)
	s_nop 0
	v_pk_fma_f32 v[6:7], v[72:73], s[16:17], v[14:15] op_sel_hi:[1,0,1]
	v_pk_fma_f32 v[4:5], v[70:71], s[16:17], v[12:13] op_sel_hi:[1,0,1]
	global_store_dwordx4 v[20:21], v[4:7], off offset:512
	s_waitcnt vmcnt(3)
	s_nop 0
	v_pk_fma_f32 v[6:7], v[68:69], s[16:17], v[18:19] op_sel_hi:[1,0,1]
	v_pk_fma_f32 v[4:5], v[66:67], s[16:17], v[16:17] op_sel_hi:[1,0,1]
	global_store_dwordx4 v[20:21], v[4:7], off offset:576
	v_lshl_add_u64 v[20:21], v[2:3], 0, s[18:19]
	v_lshl_add_u64 v[16:17], s[40:41], 0, v[20:21]
	global_load_dwordx4 v[4:7], v[16:17], off
	global_load_dwordx4 v[8:11], v[16:17], off offset:64
	global_load_dwordx4 v[12:15], v[16:17], off offset:512
	global_load_dwordx4 v[16:19], v[16:17], off offset:576
	v_lshl_add_u64 v[20:21], s[26:27], 0, v[20:21]
	s_mov_b64 s[18:19], 0x2c0000
	s_waitcnt vmcnt(3)
	v_pk_fma_f32 v[6:7], v[64:65], s[16:17], v[6:7] op_sel_hi:[1,0,1]
	v_pk_fma_f32 v[4:5], v[62:63], s[16:17], v[4:5] op_sel_hi:[1,0,1]
	global_store_dwordx4 v[20:21], v[4:7], off
	s_waitcnt vmcnt(3)
	s_nop 0
	v_pk_fma_f32 v[6:7], v[60:61], s[16:17], v[10:11] op_sel_hi:[1,0,1]
	v_pk_fma_f32 v[4:5], v[58:59], s[16:17], v[8:9] op_sel_hi:[1,0,1]
	global_store_dwordx4 v[20:21], v[4:7], off offset:64
	s_waitcnt vmcnt(3)
	s_nop 0
	v_pk_fma_f32 v[6:7], v[56:57], s[16:17], v[14:15] op_sel_hi:[1,0,1]
	v_pk_fma_f32 v[4:5], v[54:55], s[16:17], v[12:13] op_sel_hi:[1,0,1]
	global_store_dwordx4 v[20:21], v[4:7], off offset:512
	s_waitcnt vmcnt(3)
	s_nop 0
	v_pk_fma_f32 v[6:7], v[52:53], s[16:17], v[18:19] op_sel_hi:[1,0,1]
	v_pk_fma_f32 v[4:5], v[50:51], s[16:17], v[16:17] op_sel_hi:[1,0,1]
	global_store_dwordx4 v[20:21], v[4:7], off offset:576
	v_lshl_add_u64 v[18:19], v[2:3], 0, s[18:19]
	v_lshl_add_u64 v[14:15], s[40:41], 0, v[18:19]
	global_load_dwordx4 v[2:5], v[14:15], off
	global_load_dwordx4 v[6:9], v[14:15], off offset:64
	global_load_dwordx4 v[10:13], v[14:15], off offset:512
	global_load_dwordx4 v[14:17], v[14:15], off offset:576
	v_lshl_add_u64 v[18:19], s[26:27], 0, v[18:19]
	s_mov_b64 s[18:19], -1
	s_waitcnt vmcnt(3)
	v_pk_fma_f32 v[4:5], v[48:49], s[16:17], v[4:5] op_sel_hi:[1,0,1]
	v_pk_fma_f32 v[2:3], v[46:47], s[16:17], v[2:3] op_sel_hi:[1,0,1]
	global_store_dwordx4 v[18:19], v[2:5], off
	s_waitcnt vmcnt(3)
	s_nop 0
	v_pk_fma_f32 v[4:5], v[44:45], s[16:17], v[8:9] op_sel_hi:[1,0,1]
	v_pk_fma_f32 v[2:3], v[42:43], s[16:17], v[6:7] op_sel_hi:[1,0,1]
	global_store_dwordx4 v[18:19], v[2:5], off offset:64
	s_waitcnt vmcnt(3)
	s_nop 0
	v_pk_fma_f32 v[4:5], v[40:41], s[16:17], v[12:13] op_sel_hi:[1,0,1]
	v_pk_fma_f32 v[2:3], v[38:39], s[16:17], v[10:11] op_sel_hi:[1,0,1]
	global_store_dwordx4 v[18:19], v[2:5], off offset:512
	s_waitcnt vmcnt(3)
	s_nop 0
	v_pk_fma_f32 v[4:5], v[36:37], s[16:17], v[16:17] op_sel_hi:[1,0,1]
	v_pk_fma_f32 v[2:3], v[34:35], s[16:17], v[14:15] op_sel_hi:[1,0,1]
	global_store_dwordx4 v[18:19], v[2:5], off offset:576
	s_cbranch_vccnz .LBB0_306
	s_andn2_b64 vcc, exec, s[10:11]
	s_cbranch_vccnz .LBB0_305
	s_barrier
	s_branch .LBB0_305

.LBB0_335:
	s_lshl_b32 s93, s10, 8
	v_lshrrev_b32_e32 v2, 2, v186
	s_lshl_b32 s94, s16, 5
	v_and_b32_e32 v168, 12, v2
	v_add_u32_e32 v26, s93, v184
	v_or_b32_e32 v170, s94, v168
	v_ashrrev_i32_e32 v27, 31, v26
	v_or_b32_e32 v162, s60, v170
	v_lshlrev_b64 v[166:167], 12, v[26:27]
	v_readlane_b32 s40, v247, 6
	v_or_b32_e32 v166, v166, v162
	v_readlane_b32 s41, v247, 7
	s_barrier
	v_lshl_add_u64 v[14:15], v[166:167], 1, s[56:57]
	v_lshl_add_u64 v[10:11], v[166:167], 2, s[40:41]
	global_load_dwordx4 v[2:5], v[10:11], off
	global_load_dwordx4 v[6:9], v[10:11], off offset:64
	s_mov_b64 s[0:1], 0x80000
	v_and_b32_e32 v171, 63, v186
	v_readlane_b32 s42, v247, 8
	v_readlane_b32 s43, v247, 9
	v_readlane_b32 s44, v247, 10
	v_readlane_b32 s45, v247, 11
	v_readlane_b32 s46, v247, 12
	v_readlane_b32 s47, v247, 13
	v_readlane_b32 s48, v247, 14
	v_readlane_b32 s49, v247, 15
	v_readlane_b32 s50, v247, 16
	v_readlane_b32 s51, v247, 17
	v_readlane_b32 s52, v247, 18
	v_readlane_b32 s53, v247, 19
	v_readlane_b32 s54, v247, 20
	v_readlane_b32 s55, v247, 21
	s_waitcnt vmcnt(0)
	v_pk_fma_f32 v[72:73], v[72:73], s[58:59], v[4:5] op_sel_hi:[1,0,1]
	v_pk_fma_f32 v[70:71], v[70:71], s[58:59], v[2:3] op_sel_hi:[1,0,1]
	v_pk_fma_f32 v[68:69], v[68:69], s[58:59], v[8:9] op_sel_hi:[1,0,1]
	v_pk_fma_f32 v[66:67], v[66:67], s[58:59], v[6:7] op_sel_hi:[1,0,1]
	v_cvt_pk_bf16_f32 v2, v70, v71
	v_cvt_pk_bf16_f32 v3, v72, v73
	s_nop 0
	v_cvt_pk_bf16_f32 v4, v66, v67
	v_cvt_pk_bf16_f32 v5, v68, v69
	global_store_dwordx2 v[14:15], v[2:3], off
	global_store_dwordx2 v[14:15], v[4:5], off offset:32
	global_load_dwordx4 v[2:5], v[10:11], off offset:512
	global_load_dwordx4 v[10:13], v[10:11], off offset:576
	s_waitcnt vmcnt(1)
	v_pk_fma_f32 v[8:9], v[160:161], s[58:59], v[4:5] op_sel_hi:[1,0,1]
	v_pk_fma_f32 v[6:7], v[158:159], s[58:59], v[2:3] op_sel_hi:[1,0,1]
	s_waitcnt vmcnt(0)
	v_pk_fma_f32 v[2:3], v[154:155], s[58:59], v[10:11] op_sel_hi:[1,0,1]
	v_cvt_pk_bf16_f32 v10, v6, v7
	v_cvt_pk_bf16_f32 v11, v8, v9
	v_pk_fma_f32 v[4:5], v[156:157], s[58:59], v[12:13] op_sel_hi:[1,0,1]
	v_cvt_pk_bf16_f32 v12, v2, v3
	s_nop 0
	v_cvt_pk_bf16_f32 v13, v4, v5
	global_store_dwordx2 v[14:15], v[10:11], off offset:256
	global_store_dwordx2 v[14:15], v[12:13], off offset:288
	v_or_b32_e32 v10, 16, v26
	v_ashrrev_i32_e32 v11, 31, v10
	v_lshlrev_b64 v[18:19], 12, v[10:11]
	v_or_b32_e32 v18, v18, v162
	v_lshl_add_u64 v[20:21], v[18:19], 2, s[40:41]
	global_load_dwordx4 v[10:13], v[20:21], off
	global_load_dwordx4 v[14:17], v[20:21], off offset:64
	v_lshl_add_u64 v[22:23], v[18:19], 1, s[56:57]
	s_waitcnt vmcnt(1)
	v_pk_fma_f32 v[80:81], v[80:81], s[58:59], v[12:13] op_sel_hi:[1,0,1]
	v_pk_fma_f32 v[78:79], v[78:79], s[58:59], v[10:11] op_sel_hi:[1,0,1]
	s_waitcnt vmcnt(0)
	v_pk_fma_f32 v[76:77], v[76:77], s[58:59], v[16:17] op_sel_hi:[1,0,1]
	v_pk_fma_f32 v[74:75], v[74:75], s[58:59], v[14:15] op_sel_hi:[1,0,1]
	v_cvt_pk_bf16_f32 v10, v78, v79
	v_cvt_pk_bf16_f32 v11, v80, v81
	s_nop 0
	v_cvt_pk_bf16_f32 v12, v74, v75
	v_cvt_pk_bf16_f32 v13, v76, v77
	global_store_dwordx2 v[22:23], v[10:11], off
	global_store_dwordx2 v[22:23], v[12:13], off offset:32
	global_load_dwordx4 v[10:13], v[20:21], off offset:512
	global_load_dwordx4 v[18:21], v[20:21], off offset:576
	s_waitcnt vmcnt(1)
	v_pk_fma_f32 v[16:17], v[152:153], s[58:59], v[12:13] op_sel_hi:[1,0,1]
	v_pk_fma_f32 v[14:15], v[150:151], s[58:59], v[10:11] op_sel_hi:[1,0,1]
	s_waitcnt vmcnt(0)
	v_pk_fma_f32 v[10:11], v[146:147], s[58:59], v[18:19] op_sel_hi:[1,0,1]
	v_cvt_pk_bf16_f32 v18, v14, v15
	v_cvt_pk_bf16_f32 v19, v16, v17
	v_pk_fma_f32 v[12:13], v[148:149], s[58:59], v[20:21] op_sel_hi:[1,0,1]
	v_cvt_pk_bf16_f32 v20, v10, v11
	s_nop 0
	v_cvt_pk_bf16_f32 v21, v12, v13
	global_store_dwordx2 v[22:23], v[18:19], off offset:256
	global_store_dwordx2 v[22:23], v[20:21], off offset:288
	v_or_b32_e32 v18, 32, v26
	v_ashrrev_i32_e32 v19, 31, v18
	v_lshlrev_b64 v[28:29], 12, v[18:19]
	v_or_b32_e32 v28, v28, v162
	v_lshl_add_u64 v[30:31], v[28:29], 2, s[40:41]
	global_load_dwordx4 v[18:21], v[30:31], off
	global_load_dwordx4 v[22:25], v[30:31], off offset:64
	v_lshl_add_u64 v[32:33], v[28:29], 1, s[56:57]
	v_or_b32_e32 v26, 48, v26
	v_ashrrev_i32_e32 v27, 31, v26
	s_waitcnt vmcnt(1)
	v_pk_fma_f32 v[88:89], v[88:89], s[58:59], v[20:21] op_sel_hi:[1,0,1]
	v_pk_fma_f32 v[86:87], v[86:87], s[58:59], v[18:19] op_sel_hi:[1,0,1]
	s_waitcnt vmcnt(0)
	v_pk_fma_f32 v[84:85], v[84:85], s[58:59], v[24:25] op_sel_hi:[1,0,1]
	v_pk_fma_f32 v[82:83], v[82:83], s[58:59], v[22:23] op_sel_hi:[1,0,1]
	v_cvt_pk_bf16_f32 v18, v86, v87
	v_cvt_pk_bf16_f32 v19, v88, v89
	s_nop 0
	v_cvt_pk_bf16_f32 v20, v82, v83
	v_cvt_pk_bf16_f32 v21, v84, v85
	global_store_dwordx2 v[32:33], v[18:19], off
	global_store_dwordx2 v[32:33], v[20:21], off offset:32
	global_load_dwordx4 v[18:21], v[30:31], off offset:512
	global_load_dwordx4 v[28:31], v[30:31], off offset:576
	s_waitcnt vmcnt(1)
	v_pk_fma_f32 v[22:23], v[142:143], s[58:59], v[18:19] op_sel_hi:[1,0,1]
	s_waitcnt vmcnt(0)
	v_pk_fma_f32 v[18:19], v[138:139], s[58:59], v[28:29] op_sel_hi:[1,0,1]
	v_lshlrev_b64 v[138:139], 12, v[26:27]
	v_pk_fma_f32 v[24:25], v[144:145], s[58:59], v[20:21] op_sel_hi:[1,0,1]
	v_pk_fma_f32 v[20:21], v[140:141], s[58:59], v[30:31] op_sel_hi:[1,0,1]
	v_cvt_pk_bf16_f32 v28, v22, v23
	v_cvt_pk_bf16_f32 v29, v24, v25
	v_or_b32_e32 v138, v138, v162
	v_cvt_pk_bf16_f32 v30, v18, v19
	v_cvt_pk_bf16_f32 v31, v20, v21
	global_store_dwordx2 v[32:33], v[28:29], off offset:256
	global_store_dwordx2 v[32:33], v[30:31], off offset:288
	v_lshl_add_u64 v[140:141], v[138:139], 2, s[40:41]
	global_load_dwordx4 v[26:29], v[140:141], off
	global_load_dwordx4 v[30:33], v[140:141], off offset:64
	v_lshl_add_u64 v[142:143], v[138:139], 1, s[56:57]
	s_waitcnt vmcnt(1)
	v_pk_fma_f32 v[96:97], v[96:97], s[58:59], v[28:29] op_sel_hi:[1,0,1]
	v_pk_fma_f32 v[94:95], v[94:95], s[58:59], v[26:27] op_sel_hi:[1,0,1]
	s_waitcnt vmcnt(0)
	v_pk_fma_f32 v[92:93], v[92:93], s[58:59], v[32:33] op_sel_hi:[1,0,1]
	v_pk_fma_f32 v[90:91], v[90:91], s[58:59], v[30:31] op_sel_hi:[1,0,1]
	v_cvt_pk_bf16_f32 v26, v94, v95
	v_cvt_pk_bf16_f32 v27, v96, v97
	s_nop 0
	v_cvt_pk_bf16_f32 v28, v90, v91
	v_cvt_pk_bf16_f32 v29, v92, v93
	global_store_dwordx2 v[142:143], v[26:27], off
	global_store_dwordx2 v[142:143], v[28:29], off offset:32
	global_load_dwordx4 v[26:29], v[140:141], off offset:512
	global_load_dwordx4 v[138:141], v[140:141], off offset:576
	s_waitcnt vmcnt(1)
	v_pk_fma_f32 v[32:33], v[136:137], s[58:59], v[28:29] op_sel_hi:[1,0,1]
	v_pk_fma_f32 v[30:31], v[134:135], s[58:59], v[26:27] op_sel_hi:[1,0,1]
	s_waitcnt vmcnt(0)
	v_pk_fma_f32 v[28:29], v[132:133], s[58:59], v[140:141] op_sel_hi:[1,0,1]
	v_pk_fma_f32 v[26:27], v[130:131], s[58:59], v[138:139] op_sel_hi:[1,0,1]
	v_cvt_pk_bf16_f32 v130, v30, v31
	v_cvt_pk_bf16_f32 v131, v32, v33
	v_lshl_add_u64 v[138:139], v[166:167], 0, s[0:1]
	v_cvt_pk_bf16_f32 v132, v26, v27
	v_cvt_pk_bf16_f32 v133, v28, v29
	global_store_dwordx2 v[142:143], v[130:131], off offset:256
	global_store_dwordx2 v[142:143], v[132:133], off offset:288
	v_lshl_add_u64 v[140:141], v[138:139], 2, s[40:41]
	global_load_dwordx4 v[130:133], v[140:141], off
	global_load_dwordx4 v[134:137], v[140:141], off offset:64
	v_lshl_add_u64 v[138:139], v[138:139], 1, s[56:57]
	s_mov_b64 s[0:1], 0x90000
	s_waitcnt vmcnt(1)
	v_pk_fma_f32 v[104:105], v[104:105], s[58:59], v[132:133] op_sel_hi:[1,0,1]
	v_pk_fma_f32 v[102:103], v[102:103], s[58:59], v[130:131] op_sel_hi:[1,0,1]
	s_waitcnt vmcnt(0)
	v_pk_fma_f32 v[100:101], v[100:101], s[58:59], v[136:137] op_sel_hi:[1,0,1]
	v_pk_fma_f32 v[98:99], v[98:99], s[58:59], v[134:135] op_sel_hi:[1,0,1]
	v_cvt_pk_bf16_f32 v130, v102, v103
	v_cvt_pk_bf16_f32 v131, v104, v105
	s_nop 0
	v_cvt_pk_bf16_f32 v132, v98, v99
	v_cvt_pk_bf16_f32 v133, v100, v101
	global_store_dwordx2 v[138:139], v[130:131], off
	global_store_dwordx2 v[138:139], v[132:133], off offset:32
	global_load_dwordx4 v[130:133], v[140:141], off offset:512
	global_load_dwordx4 v[134:137], v[140:141], off offset:576
	s_waitcnt vmcnt(1)
	v_pk_fma_f32 v[40:41], v[40:41], s[58:59], v[132:133] op_sel_hi:[1,0,1]
	v_pk_fma_f32 v[38:39], v[38:39], s[58:59], v[130:131] op_sel_hi:[1,0,1]
	s_waitcnt vmcnt(0)
	v_pk_fma_f32 v[36:37], v[36:37], s[58:59], v[136:137] op_sel_hi:[1,0,1]
	v_cvt_pk_bf16_f32 v130, v38, v39
	v_cvt_pk_bf16_f32 v131, v40, v41
	v_pk_fma_f32 v[34:35], v[34:35], s[58:59], v[134:135] op_sel_hi:[1,0,1]
	s_nop 0
	v_cvt_pk_bf16_f32 v132, v34, v35
	v_cvt_pk_bf16_f32 v133, v36, v37
	global_store_dwordx2 v[138:139], v[130:131], off offset:256
	global_store_dwordx2 v[138:139], v[132:133], off offset:288
	v_lshl_add_u64 v[138:139], v[166:167], 0, s[0:1]
	v_lshl_add_u64 v[140:141], v[138:139], 2, s[40:41]
	global_load_dwordx4 v[130:133], v[140:141], off
	global_load_dwordx4 v[134:137], v[140:141], off offset:64
	v_lshl_add_u64 v[138:139], v[138:139], 1, s[56:57]
	s_mov_b64 s[0:1], 0xa0000
	s_waitcnt vmcnt(1)
	v_pk_fma_f32 v[112:113], v[112:113], s[58:59], v[132:133] op_sel_hi:[1,0,1]
	v_pk_fma_f32 v[110:111], v[110:111], s[58:59], v[130:131] op_sel_hi:[1,0,1]
	s_waitcnt vmcnt(0)
	v_pk_fma_f32 v[108:109], v[108:109], s[58:59], v[136:137] op_sel_hi:[1,0,1]
	v_pk_fma_f32 v[106:107], v[106:107], s[58:59], v[134:135] op_sel_hi:[1,0,1]
	v_cvt_pk_bf16_f32 v130, v110, v111
	v_cvt_pk_bf16_f32 v131, v112, v113
	s_nop 0
	v_cvt_pk_bf16_f32 v132, v106, v107
	v_cvt_pk_bf16_f32 v133, v108, v109
	global_store_dwordx2 v[138:139], v[130:131], off
	global_store_dwordx2 v[138:139], v[132:133], off offset:32
	global_load_dwordx4 v[130:133], v[140:141], off offset:512
	global_load_dwordx4 v[134:137], v[140:141], off offset:576
	s_waitcnt vmcnt(1)
	v_pk_fma_f32 v[48:49], v[48:49], s[58:59], v[132:133] op_sel_hi:[1,0,1]
	v_pk_fma_f32 v[46:47], v[46:47], s[58:59], v[130:131] op_sel_hi:[1,0,1]
	s_waitcnt vmcnt(0)
	v_pk_fma_f32 v[44:45], v[44:45], s[58:59], v[136:137] op_sel_hi:[1,0,1]
	v_cvt_pk_bf16_f32 v130, v46, v47
	v_cvt_pk_bf16_f32 v131, v48, v49
	v_pk_fma_f32 v[42:43], v[42:43], s[58:59], v[134:135] op_sel_hi:[1,0,1]
	s_nop 0
	v_cvt_pk_bf16_f32 v132, v42, v43
	v_cvt_pk_bf16_f32 v133, v44, v45
	global_store_dwordx2 v[138:139], v[130:131], off offset:256
	global_store_dwordx2 v[138:139], v[132:133], off offset:288
	v_lshl_add_u64 v[138:139], v[166:167], 0, s[0:1]
	v_lshl_add_u64 v[140:141], v[138:139], 2, s[40:41]
	global_load_dwordx4 v[130:133], v[140:141], off
	global_load_dwordx4 v[134:137], v[140:141], off offset:64
	v_lshl_add_u64 v[138:139], v[138:139], 1, s[56:57]
	s_mov_b64 s[0:1], 0xb0000
	s_waitcnt vmcnt(1)
	v_pk_fma_f32 v[120:121], v[120:121], s[58:59], v[132:133] op_sel_hi:[1,0,1]
	v_pk_fma_f32 v[118:119], v[118:119], s[58:59], v[130:131] op_sel_hi:[1,0,1]
	s_waitcnt vmcnt(0)
	v_pk_fma_f32 v[116:117], v[116:117], s[58:59], v[136:137] op_sel_hi:[1,0,1]
	v_pk_fma_f32 v[114:115], v[114:115], s[58:59], v[134:135] op_sel_hi:[1,0,1]
	v_cvt_pk_bf16_f32 v130, v118, v119
	v_cvt_pk_bf16_f32 v131, v120, v121
	s_nop 0
	v_cvt_pk_bf16_f32 v132, v114, v115
	v_cvt_pk_bf16_f32 v133, v116, v117
	global_store_dwordx2 v[138:139], v[130:131], off
	global_store_dwordx2 v[138:139], v[132:133], off offset:32
	global_load_dwordx4 v[130:133], v[140:141], off offset:512
	global_load_dwordx4 v[134:137], v[140:141], off offset:576
	s_waitcnt vmcnt(1)
	v_pk_fma_f32 v[56:57], v[56:57], s[58:59], v[132:133] op_sel_hi:[1,0,1]
	v_pk_fma_f32 v[54:55], v[54:55], s[58:59], v[130:131] op_sel_hi:[1,0,1]
	s_waitcnt vmcnt(0)
	v_pk_fma_f32 v[52:53], v[52:53], s[58:59], v[136:137] op_sel_hi:[1,0,1]
	v_cvt_pk_bf16_f32 v130, v54, v55
	v_cvt_pk_bf16_f32 v131, v56, v57
	v_pk_fma_f32 v[50:51], v[50:51], s[58:59], v[134:135] op_sel_hi:[1,0,1]
	s_nop 0
	v_cvt_pk_bf16_f32 v132, v50, v51
	v_cvt_pk_bf16_f32 v133, v52, v53
	global_store_dwordx2 v[138:139], v[130:131], off offset:256
	global_store_dwordx2 v[138:139], v[132:133], off offset:288
	v_lshl_add_u64 v[138:139], v[166:167], 0, s[0:1]
	v_lshl_add_u64 v[140:141], v[138:139], 2, s[40:41]
	global_load_dwordx4 v[130:133], v[140:141], off
	global_load_dwordx4 v[134:137], v[140:141], off offset:64
	v_lshl_add_u64 v[138:139], v[138:139], 1, s[56:57]
	s_lshl_b32 s0, s16, 2
	s_add_i32 s4, s0, 0
	s_waitcnt vmcnt(1)
	v_pk_fma_f32 v[128:129], v[128:129], s[58:59], v[132:133] op_sel_hi:[1,0,1]
	v_pk_fma_f32 v[126:127], v[126:127], s[58:59], v[130:131] op_sel_hi:[1,0,1]
	s_waitcnt vmcnt(0)
	v_pk_fma_f32 v[124:125], v[124:125], s[58:59], v[136:137] op_sel_hi:[1,0,1]
	v_pk_fma_f32 v[122:123], v[122:123], s[58:59], v[134:135] op_sel_hi:[1,0,1]
	v_cvt_pk_bf16_f32 v130, v126, v127
	v_cvt_pk_bf16_f32 v131, v128, v129
	s_nop 0
	v_cvt_pk_bf16_f32 v132, v122, v123
	v_cvt_pk_bf16_f32 v133, v124, v125
	global_store_dwordx2 v[138:139], v[130:131], off
	global_store_dwordx2 v[138:139], v[132:133], off offset:32
	global_load_dwordx4 v[130:133], v[140:141], off offset:512
	global_load_dwordx4 v[134:137], v[140:141], off offset:576
	s_waitcnt vmcnt(1)
	v_pk_fma_f32 v[64:65], v[64:65], s[58:59], v[132:133] op_sel_hi:[1,0,1]
	v_pk_fma_f32 v[62:63], v[62:63], s[58:59], v[130:131] op_sel_hi:[1,0,1]
	s_waitcnt vmcnt(0)
	v_pk_fma_f32 v[60:61], v[60:61], s[58:59], v[136:137] op_sel_hi:[1,0,1]
	v_pk_fma_f32 v[58:59], v[58:59], s[58:59], v[134:135] op_sel_hi:[1,0,1]
	v_cvt_pk_bf16_f32 v130, v62, v63
	v_cvt_pk_bf16_f32 v131, v64, v65
	v_mul_f32_e32 v134, v69, v69
	v_cvt_pk_bf16_f32 v132, v58, v59
	v_cvt_pk_bf16_f32 v133, v60, v61
	global_store_dwordx2 v[138:139], v[130:131], off offset:256
	global_store_dwordx2 v[138:139], v[132:133], off offset:288
	v_mul_f32_e32 v132, v71, v71
	v_mul_f32_e32 v133, v73, v73
	v_fmac_f32_e32 v132, v70, v70
	v_fmac_f32_e32 v133, v72, v72
	v_add_f32_e32 v132, v132, v133
	v_mul_f32_e32 v133, v67, v67
	v_fmac_f32_e32 v133, v66, v66
	v_fmac_f32_e32 v134, v68, v68
	v_add_f32_e32 v133, v133, v134
	v_add_f32_e32 v132, v132, v133
	v_mul_f32_e32 v133, v7, v7
	v_mul_f32_e32 v134, v9, v9
	v_fmac_f32_e32 v133, v6, v6
	v_fmac_f32_e32 v134, v8, v8
	v_and_b32_e32 v131, 64, v1
	v_add_f32_e32 v133, v133, v134
	v_xor_b32_e32 v130, 16, v1
	v_add_u32_e32 v155, 64, v131
	v_add_f32_e32 v132, v132, v133
	v_mul_f32_e32 v133, v3, v3
	v_mul_f32_e32 v134, v5, v5
	v_cmp_lt_i32_e32 vcc, v130, v155
	v_fmac_f32_e32 v133, v2, v2
	v_fmac_f32_e32 v134, v4, v4
	v_cndmask_b32_e32 v130, v1, v130, vcc
	v_add_f32_e32 v133, v133, v134
	v_lshlrev_b32_e32 v130, 2, v130
	v_add_f32_e32 v132, v133, v132
	ds_bpermute_b32 v133, v130, v132
	v_xor_b32_e32 v131, 32, v1
	v_cmp_lt_i32_e32 vcc, v131, v155
	s_waitcnt lgkmcnt(0)
	v_add_f32_e32 v132, v132, v133
	v_cndmask_b32_e32 v131, v1, v131, vcc
	v_lshlrev_b32_e32 v131, 2, v131
	ds_bpermute_b32 v133, v131, v132
	v_cmp_gt_u32_e32 vcc, 16, v171
	s_and_saveexec_b64 s[0:1], vcc
	s_cbranch_execz .LBB0_337
	s_lshl_b32 s5, s15, 10
	s_add_i32 s5, s4, s5
	v_lshl_add_u32 v134, v185, 4, s5
	s_waitcnt lgkmcnt(0)
	v_add_f32_e32 v132, v132, v133
	ds_write_b32 v134, v132

.LBB0_534:
	v_add_co_u32_e64 v22, s[0:1], s14, v96
	v_add_co_u32_e32 v62, vcc, 0xffffd000, v96
	s_nop 0
	v_addc_co_u32_e64 v23, s[0:1], -1, v97, s[0:1]
	v_add_co_u32_e64 v24, s[0:1], s15, v96
	v_lshl_add_u64 v[54:55], s[52:53], 0, v[100:101]
	v_addc_co_u32_e32 v63, vcc, -1, v97, vcc
	v_addc_co_u32_e64 v25, s[0:1], -1, v97, s[0:1]
	v_add_co_u32_e32 v106, vcc, s18, v54
	global_load_dwordx4 v[10:13], v[96:97], off offset:-3072
	global_load_dwordx4 v[14:17], v[96:97], off offset:-2048
	global_load_dwordx4 v[2:5], v[96:97], off
	global_load_dwordx4 v[6:9], v[96:97], off offset:-1024
	global_load_dwordx4 v[18:21], v[70:71], off
	global_load_dwordx4 v[46:49], v[22:23], off offset:-3072
	global_load_dwordx4 v[34:37], v[22:23], off offset:-1024
	global_load_dwordx4 v[50:53], v[22:23], off offset:-2048
	global_load_dwordx4 v[38:41], v[22:23], off
	global_load_dwordx4 v[26:29], v[24:25], off offset:-2048
	global_load_dwordx4 v[42:45], v[24:25], off offset:-3072
	global_load_dwordx4 v[30:33], v[24:25], off offset:-1024
	global_load_dwordx4 v[22:25], v[96:97], off offset:-4096
	v_addc_co_u32_e32 v107, vcc, 0, v55, vcc
	v_add_co_u32_e32 v104, vcc, s21, v54
	v_lshl_add_u64 v[102:103], s[52:53], 0, v[98:99]
	s_nop 0
	v_addc_co_u32_e32 v105, vcc, 0, v55, vcc
	global_load_dwordx4 v[66:69], v[62:63], off offset:-3072
	global_load_dwordx4 v[58:61], v[62:63], off offset:-2048
	global_load_dwordx4 v[54:57], v[62:63], off
	global_load_dwordx4 v[62:65], v[62:63], off offset:-1024
	s_add_i32 s3, s3, s92
	v_lshl_add_u64 v[98:99], v[98:99], 0, s[10:11]
	v_lshl_add_u64 v[100:101], v[100:101], 0, s[12:13]
	v_lshl_add_u64 v[96:97], v[96:97], 0, s[6:7]
	s_cmpk_lt_i32 s3, 0x4000
	s_waitcnt vmcnt(0)
	v_mov_b32_e32 v160, v46
	v_mul_f32_e32 v176, v34, v34
	v_mul_f32_e32 v125, v10, v10
	v_mul_f32_e32 v127, v11, v11
	v_mul_f32_e32 v129, v12, v12
	v_pk_mul_f32 v[112:113], v[16:17], v[16:17]
	v_pk_mul_f32 v[110:111], v[14:15], v[14:15]
	v_mov_b32_e32 v108, v18
	v_mov_b32_e32 v109, v20
	v_mov_b32_e32 v20, v19
	v_mov_b32_e32 v18, v10
	v_mov_b32_e32 v19, v12
	v_mov_b32_e32 v12, v11
	v_mov_b32_e32 v134, v14
	v_mov_b32_e32 v135, v16
	v_mov_b32_e32 v16, v15
	v_pk_mul_f32 v[10:11], v[48:49], v[48:49]
	v_pk_mul_f32 v[14:15], v[46:47], v[46:47]
	v_mul_f32_e32 v136, v51, v51
	v_mul_f32_e32 v138, v53, v53
	v_pk_mul_f32 v[140:141], v[40:41], v[40:41]
	v_pk_mul_f32 v[142:143], v[38:39], v[38:39]
	v_mul_f32_e32 v180, v26, v26
	v_mul_f32_e32 v181, v27, v27
	v_mul_f32_e32 v182, v28, v28
	v_mul_f32_e32 v144, v43, v43
	v_mul_f32_e32 v146, v45, v45
	v_pk_mul_f32 v[148:149], v[32:33], v[32:33]
	v_pk_mul_f32 v[150:151], v[30:31], v[30:31]
	v_mul_f32_e32 v152, v23, v23
	v_mul_f32_e32 v154, v25, v25
	v_mov_b32_e32 v164, v26
	v_mov_b32_e32 v165, v28
	v_mov_b32_e32 v28, v27
	v_mov_b32_e32 v26, v30
	v_mov_b32_e32 v27, v32
	v_mov_b32_e32 v32, v31
	v_pk_mul_f32 v[30:31], v[68:69], v[68:69]
	v_pk_mul_f32 v[168:169], v[66:67], v[66:67]
	v_pk_mul_f32 v[170:171], v[60:61], v[60:61]
	v_pk_mul_f32 v[172:173], v[58:59], v[58:59]
	v_mul_f32_e32 v114, v7, v7
	v_mul_f32_e32 v116, v9, v9
	v_mov_b32_e32 v166, v22
	v_mov_b32_e32 v167, v24
	v_pk_mov_b32 v[174:175], v[14:15], v[10:11] op_sel:[1,0]
	v_mov_b32_e32 v15, v11
	v_pk_fma_f32 v[10:11], v[50:51], v[50:51], v[136:137] op_sel_hi:[1,1,0]
	v_pk_fma_f32 v[136:137], v[52:53], v[52:53], v[138:139] op_sel_hi:[1,1,0]
	v_pk_mov_b32 v[138:139], v[142:143], v[140:141] op_sel:[1,0]
	v_mov_b32_e32 v143, v141
	v_pk_fma_f32 v[140:141], v[42:43], v[42:43], v[144:145] op_sel_hi:[1,1,0]
	v_pk_fma_f32 v[144:145], v[44:45], v[44:45], v[146:147] op_sel_hi:[1,1,0]
	v_pk_mov_b32 v[146:147], v[150:151], v[148:149] op_sel:[1,0]
	v_mov_b32_e32 v151, v149
	v_pk_fma_f32 v[148:149], v[22:23], v[22:23], v[152:153] op_sel_hi:[1,1,0]
	v_pk_fma_f32 v[152:153], v[24:25], v[24:25], v[154:155] op_sel_hi:[1,1,0]
	v_mov_b32_e32 v24, v23
	v_pk_mov_b32 v[22:23], v[168:169], v[30:31] op_sel:[1,0]
	v_mov_b32_e32 v169, v31
	v_pk_mov_b32 v[30:31], v[172:173], v[170:171] op_sel:[1,0]
	v_mov_b32_e32 v173, v171
	v_pk_mov_b32 v[156:157], v[110:111], v[112:113] op_sel:[1,0]
	v_mov_b32_e32 v111, v113
	v_pk_fma_f32 v[112:113], v[6:7], v[6:7], v[114:115] op_sel_hi:[1,1,0]
	v_pk_fma_f32 v[158:159], v[8:9], v[8:9], v[116:117] op_sel_hi:[1,1,0]
	v_mul_f32_e32 v114, v63, v63
	v_mul_f32_e32 v116, v65, v65
	v_pk_add_f32 v[22:23], v[22:23], v[168:169]
	v_pk_add_f32 v[30:31], v[30:31], v[172:173]
	v_mul_f32_e32 v177, v35, v35
	v_mul_f32_e32 v178, v36, v36
	v_mov_b32_e32 v161, v48
	v_mov_b32_e32 v48, v47
	v_mov_b32_e32 v46, v50
	v_mov_b32_e32 v47, v52
	v_mov_b32_e32 v162, v34
	v_mov_b32_e32 v163, v36
	v_mov_b32_e32 v36, v35
	v_mov_b32_e32 v34, v38
	v_mov_b32_e32 v35, v40
	v_mov_b32_e32 v40, v39
	v_mov_b32_e32 v38, v42
	v_mov_b32_e32 v39, v44
	v_mul_f32_e32 v184, v54, v54
	v_mul_f32_e32 v185, v55, v55
	v_mul_f32_e32 v186, v56, v56
	v_mul_f32_e32 v187, v57, v57
	v_mov_b32_e32 v52, v51
	v_mov_b32_e32 v44, v43
	v_pk_fma_f32 v[42:43], v[62:63], v[62:63], v[114:115] op_sel_hi:[1,1,0]
	v_pk_fma_f32 v[50:51], v[64:65], v[64:65], v[116:117] op_sel_hi:[1,1,0]
	v_pk_add_f32 v[22:23], v[22:23], v[22:23] op_sel:[0,1] op_sel_hi:[1,0]
	v_pk_add_f32 v[30:31], v[30:31], v[30:31] op_sel:[0,1] op_sel_hi:[1,0]
	v_mov_b32_e32 v43, v186
	v_mov_b32_e32 v51, v187
	v_mov_b32_e32 v23, v184
	v_mov_b32_e32 v31, v185
	v_pk_add_f32 v[42:43], v[42:43], v[50:51]
	v_pk_add_f32 v[22:23], v[22:23], v[30:31]
	v_pk_add_f32 v[14:15], v[174:175], v[14:15]
	v_pk_add_f32 v[22:23], v[22:23], v[42:43]
	v_mul_f32_e32 v179, v37, v37
	v_pk_add_f32 v[14:15], v[14:15], v[14:15] op_sel:[0,1] op_sel_hi:[1,0]
	v_pk_add_f32 v[22:23], v[22:23], v[22:23] op_sel:[0,1] op_sel_hi:[1,0]
	v_mov_b32_e32 v11, v178
	v_mov_b32_e32 v137, v179
	v_mov_b32_e32 v15, v177
	v_mov_b32_e32 v23, v176
	v_pk_add_f32 v[10:11], v[10:11], v[136:137]
	v_pk_add_f32 v[14:15], v[22:23], v[14:15]
	v_mov_b32_e32 v154, v54
	v_mov_b32_e32 v155, v56
	v_mov_b32_e32 v56, v55
	v_pk_add_f32 v[54:55], v[138:139], v[142:143]
	v_pk_add_f32 v[10:11], v[14:15], v[10:11]
	v_mul_f32_e32 v183, v29, v29
	v_pk_add_f32 v[54:55], v[54:55], v[54:55] op_sel:[0,1] op_sel_hi:[1,0]
	v_pk_add_f32 v[10:11], v[10:11], v[10:11] op_sel:[0,1] op_sel_hi:[1,0]
	v_mul_f32_e32 v132, v5, v5
	v_mov_b32_e32 v141, v182
	v_mov_b32_e32 v145, v183
	v_mov_b32_e32 v55, v181
	v_mov_b32_e32 v11, v180
	v_mov_b32_e32 v159, v132
	v_mov_b32_e32 v132, v66
	v_mov_b32_e32 v133, v68
	v_mov_b32_e32 v68, v67
	v_mov_b32_e32 v66, v58
	v_mov_b32_e32 v67, v60
	v_mov_b32_e32 v60, v59
	v_mov_b32_e32 v58, v62
	v_mov_b32_e32 v59, v64
	v_mov_b32_e32 v64, v63
	v_pk_add_f32 v[62:63], v[140:141], v[144:145]
	v_pk_add_f32 v[10:11], v[10:11], v[54:55]
	v_mul_f32_e32 v130, v13, v13
	v_mul_f32_e32 v131, v4, v4
	v_pk_add_f32 v[138:139], v[146:147], v[150:151]
	v_pk_add_f32 v[10:11], v[10:11], v[62:63]
	v_mov_b32_e32 v113, v131
	v_mov_b32_e32 v153, v130
	v_pk_add_f32 v[130:131], v[138:139], v[138:139] op_sel:[0,1] op_sel_hi:[1,0]
	v_pk_add_f32 v[10:11], v[10:11], v[10:11] op_sel:[0,1] op_sel_hi:[1,0]
	v_mov_b32_e32 v149, v129
	v_mov_b32_e32 v131, v127
	v_mov_b32_e32 v11, v125
	v_pk_add_f32 v[136:137], v[148:149], v[152:153]
	v_pk_add_f32 v[10:11], v[10:11], v[130:131]
	v_pk_add_f32 v[110:111], v[156:157], v[110:111]
	v_pk_add_f32 v[10:11], v[10:11], v[136:137]
	v_mul_f32_e32 v126, v2, v2
	v_mul_f32_e32 v128, v3, v3
	v_pk_add_f32 v[110:111], v[110:111], v[110:111] op_sel:[0,1] op_sel_hi:[1,0]
	v_pk_add_f32 v[10:11], v[10:11], v[10:11] op_sel:[0,1] op_sel_hi:[1,0]
	v_mov_b32_e32 v111, v128
	v_mov_b32_e32 v11, v126
	v_pk_add_f32 v[112:113], v[112:113], v[158:159]
	v_pk_add_f32 v[10:11], v[10:11], v[110:111]
	s_nop 0
	v_pk_add_f32 v[10:11], v[10:11], v[112:113]
	s_nop 0
	v_add_f32_e32 v10, v10, v11
	ds_bpermute_b32 v11, v1, v10
	s_waitcnt lgkmcnt(0)
	v_add_f32_e32 v10, v10, v11
	ds_bpermute_b32 v11, v115, v10
	s_waitcnt lgkmcnt(0)
	v_add_f32_e32 v10, v10, v11
	ds_bpermute_b32 v11, v117, v10
	s_waitcnt lgkmcnt(0)
	v_add_f32_e32 v10, v10, v11
	ds_bpermute_b32 v11, v118, v10
	s_waitcnt lgkmcnt(0)
	v_add_f32_e32 v10, v10, v11
	ds_bpermute_b32 v11, v119, v10
	s_waitcnt lgkmcnt(0)
	v_add_f32_e32 v10, v10, v11
	ds_bpermute_b32 v11, v120, v10
	s_waitcnt lgkmcnt(0)
	v_add_f32_e32 v10, v10, v11
	v_fmamk_f32 v10, v10, 0x39800000, v121
	v_mul_f32_e32 v11, 0x4f800000, v10
	v_cmp_gt_f32_e32 vcc, s16, v10
	s_nop 1
	v_cndmask_b32_e32 v10, v10, v11, vcc
	v_sqrt_f32_e32 v11, v10
	s_nop 0
	v_add_u32_e32 v14, -1, v11
	v_add_u32_e32 v15, 1, v11
	v_fma_f32 v22, -v14, v11, v10
	v_fma_f32 v23, -v15, v11, v10
	v_cmp_ge_f32_e64 s[0:1], 0, v22
	s_nop 1
	v_cndmask_b32_e64 v11, v11, v14, s[0:1]
	v_cmp_lt_f32_e64 s[0:1], 0, v23
	s_nop 1
	v_cndmask_b32_e64 v11, v11, v15, s[0:1]
	v_mul_f32_e32 v14, 0x37800000, v11
	v_cndmask_b32_e32 v11, v11, v14, vcc
	v_cmp_class_f32_e32 vcc, v10, v122
	s_nop 1
	v_cndmask_b32_e32 v10, v11, v10, vcc
	v_div_scale_f32 v11, s[0:1], v10, v10, 1.0
	v_rcp_f32_e32 v15, v11
	v_div_scale_f32 v14, vcc, 1.0, v10, 1.0
	v_fma_f32 v22, -v11, v15, 1.0
	v_fmac_f32_e32 v15, v22, v15
	v_mul_f32_e32 v22, v14, v15
	v_fma_f32 v23, -v11, v22, v14
	v_fmac_f32_e32 v22, v23, v15
	v_fma_f32 v11, -v11, v22, v14
	v_div_fmas_f32 v11, v11, v15, v22
	v_div_fixup_f32 v10, v11, v10, 1.0
	v_pk_mul_f32 v[54:55], v[132:133], v[10:11] op_sel_hi:[1,0]
	v_pk_mul_f32 v[62:63], v[68:69], v[10:11] op_sel_hi:[1,0]
	v_pk_mul_f32 v[14:15], v[16:17], v[10:11] op_sel_hi:[1,0]
	v_pk_mul_f32 v[16:17], v[108:109], v[54:55]
	v_pk_mul_f32 v[20:21], v[20:21], v[62:63]
	v_pk_mul_f32 v[126:127], v[46:47], v[10:11] op_sel_hi:[1,0]
	v_pk_mul_f32 v[128:129], v[52:53], v[10:11] op_sel_hi:[1,0]
	v_pk_mul_f32 v[46:47], v[40:41], v[10:11] op_sel_hi:[1,0]
	v_pk_mul_f32 v[40:41], v[44:45], v[10:11] op_sel_hi:[1,0]
	v_pk_mul_f32 v[30:31], v[32:33], v[10:11] op_sel_hi:[1,0]
	v_and_b32_sdwa v32, v16, v124 dst_sel:DWORD dst_unused:UNUSED_PAD src0_sel:WORD_1 src1_sel:DWORD
	v_and_b32_sdwa v44, v20, v124 dst_sel:DWORD dst_unused:UNUSED_PAD src0_sel:WORD_1 src1_sel:DWORD
	v_mul_f32_e32 v52, 0x417e0000, v20
	v_pk_mul_f32 v[66:67], v[66:67], v[10:11] op_sel_hi:[1,0]
	v_pk_mul_f32 v[60:61], v[60:61], v[10:11] op_sel_hi:[1,0]
	v_pk_mul_f32 v[58:59], v[58:59], v[10:11] op_sel_hi:[1,0]
	v_pk_mul_f32 v[64:65], v[64:65], v[10:11] op_sel_hi:[1,0]
	v_pk_mul_f32 v[68:69], v[154:155], v[10:11] op_sel_hi:[1,0]
	v_pk_mul_f32 v[56:57], v[56:57], v[10:11] op_sel_hi:[1,0]
	v_pk_mul_f32 v[110:111], v[160:161], v[10:11] op_sel_hi:[1,0]
	v_pk_mul_f32 v[112:113], v[48:49], v[10:11] op_sel_hi:[1,0]
	v_pk_mul_f32 v[48:49], v[162:163], v[10:11] op_sel_hi:[1,0]
	v_pk_mul_f32 v[50:51], v[36:37], v[10:11] op_sel_hi:[1,0]
	v_pk_mul_f32 v[42:43], v[34:35], v[10:11] op_sel_hi:[1,0]
	v_pk_mul_f32 v[38:39], v[38:39], v[10:11] op_sel_hi:[1,0]
	v_pk_mul_f32 v[34:35], v[164:165], v[10:11] op_sel_hi:[1,0]
	v_pk_mul_f32 v[36:37], v[28:29], v[10:11] op_sel_hi:[1,0]
	v_pk_mul_f32 v[28:29], v[26:27], v[10:11] op_sel_hi:[1,0]
	v_pk_mul_f32 v[26:27], v[166:167], v[10:11] op_sel_hi:[1,0]
	v_pk_mul_f32 v[24:25], v[24:25], v[10:11] op_sel_hi:[1,0]
	v_pk_mul_f32 v[18:19], v[18:19], v[10:11] op_sel_hi:[1,0]
	v_pk_mul_f32 v[22:23], v[12:13], v[10:11] op_sel_hi:[1,0]
	v_pk_mul_f32 v[12:13], v[134:135], v[10:11] op_sel_hi:[1,0]
	v_and_b32_sdwa v11, v17, v124 dst_sel:DWORD dst_unused:UNUSED_PAD src0_sel:WORD_1 src1_sel:DWORD
	v_and_b32_sdwa v33, v21, v124 dst_sel:DWORD dst_unused:UNUSED_PAD src0_sel:WORD_1 src1_sel:DWORD
	v_mul_f32_e32 v45, 0x417e0000, v16
	v_mul_f32_e32 v53, 0x417e0000, v17
	v_mul_f32_e32 v54, 0x417e0000, v21
	v_add3_u32 v16, v16, v32, s17
	v_add3_u32 v20, v20, v44, s17
	v_med3_f32 v32, v52, s19, v123
	v_add3_u32 v11, v17, v11, s17
	v_add3_u32 v17, v21, v33, s17
	v_med3_f32 v21, v45, s19, v123
	v_med3_f32 v33, v53, s19, v123
	v_med3_f32 v44, v54, s19, v123
	v_and_b32_e32 v20, 0xffff0000, v20
	v_rndne_f32_e32 v32, v32
	v_and_b32_e32 v17, 0xffff0000, v17
	v_rndne_f32_e32 v21, v21
	v_rndne_f32_e32 v33, v33
	v_rndne_f32_e32 v44, v44
	v_or_b32_sdwa v16, v20, v16 dst_sel:DWORD dst_unused:UNUSED_PAD src0_sel:DWORD src1_sel:WORD_1
	v_cvt_i32_f32_e32 v20, v32
	v_or_b32_sdwa v17, v17, v11 dst_sel:DWORD dst_unused:UNUSED_PAD src0_sel:DWORD src1_sel:WORD_1
	v_cvt_i32_f32_e32 v11, v21
	v_cvt_i32_f32_sdwa v21, v33 dst_sel:WORD_1 dst_unused:UNUSED_PAD src0_sel:DWORD
	v_cvt_i32_f32_e32 v32, v44
	global_store_dwordx2 v[104:105], v[16:17], off offset:-4096
	v_lshlrev_b32_e32 v16, 8, v20
	v_and_b32_e32 v17, 0xff0000, v21
	v_perm_b32 v11, v32, v11, s20
	v_and_b32_e32 v16, 0xff00, v16
	v_or3_b32 v11, v11, v16, v17
	global_store_dword v[102:103], v11, off offset:-2048
	global_load_dwordx4 v[52:55], v[70:71], off offset:1024
	s_waitcnt vmcnt(0)
	v_mov_b32_e32 v16, v52
	v_mov_b32_e32 v17, v54
	v_mov_b32_e32 v54, v53
	v_pk_mul_f32 v[16:17], v[16:17], v[66:67]
	v_pk_mul_f32 v[20:21], v[54:55], v[60:61]
	v_and_b32_sdwa v32, v16, v124 dst_sel:DWORD dst_unused:UNUSED_PAD src0_sel:WORD_1 src1_sel:DWORD
	v_and_b32_sdwa v44, v20, v124 dst_sel:DWORD dst_unused:UNUSED_PAD src0_sel:WORD_1 src1_sel:DWORD
	v_mul_f32_e32 v52, 0x417e0000, v20
	v_and_b32_sdwa v11, v17, v124 dst_sel:DWORD dst_unused:UNUSED_PAD src0_sel:WORD_1 src1_sel:DWORD
	v_and_b32_sdwa v33, v21, v124 dst_sel:DWORD dst_unused:UNUSED_PAD src0_sel:WORD_1 src1_sel:DWORD
	v_mul_f32_e32 v45, 0x417e0000, v16
	v_mul_f32_e32 v53, 0x417e0000, v17
	v_mul_f32_e32 v54, 0x417e0000, v21
	v_add3_u32 v16, v16, v32, s17
	v_add3_u32 v20, v20, v44, s17
	v_med3_f32 v32, v52, s19, v123
	v_add3_u32 v11, v17, v11, s17
	v_add3_u32 v17, v21, v33, s17
	v_med3_f32 v21, v45, s19, v123
	v_med3_f32 v33, v53, s19, v123
	v_med3_f32 v44, v54, s19, v123
	v_and_b32_e32 v20, 0xffff0000, v20
	v_rndne_f32_e32 v32, v32
	v_and_b32_e32 v17, 0xffff0000, v17
	v_rndne_f32_e32 v21, v21
	v_rndne_f32_e32 v33, v33
	v_rndne_f32_e32 v44, v44
	v_or_b32_sdwa v16, v20, v16 dst_sel:DWORD dst_unused:UNUSED_PAD src0_sel:DWORD src1_sel:WORD_1
	v_cvt_i32_f32_e32 v20, v32
	v_or_b32_sdwa v17, v17, v11 dst_sel:DWORD dst_unused:UNUSED_PAD src0_sel:DWORD src1_sel:WORD_1
	v_cvt_i32_f32_e32 v11, v21
	v_cvt_i32_f32_sdwa v21, v33 dst_sel:WORD_1 dst_unused:UNUSED_PAD src0_sel:DWORD
	v_cvt_i32_f32_e32 v32, v44
	global_store_dwordx2 v[106:107], v[16:17], off offset:512
	v_lshlrev_b32_e32 v16, 8, v20
	v_and_b32_e32 v17, 0xff0000, v21
	v_perm_b32 v11, v32, v11, s20
	v_and_b32_e32 v16, 0xff00, v16
	v_or3_b32 v11, v11, v16, v17
	global_store_dword v[102:103], v11, off offset:-1792
	global_load_dwordx4 v[52:55], v[70:71], off offset:2048
	s_waitcnt vmcnt(0)
	v_mov_b32_e32 v16, v52
	v_mov_b32_e32 v17, v54
	v_mov_b32_e32 v54, v53
	v_pk_mul_f32 v[16:17], v[16:17], v[58:59]
	v_pk_mul_f32 v[20:21], v[54:55], v[64:65]
	v_and_b32_sdwa v32, v16, v124 dst_sel:DWORD dst_unused:UNUSED_PAD src0_sel:WORD_1 src1_sel:DWORD
	v_and_b32_sdwa v44, v20, v124 dst_sel:DWORD dst_unused:UNUSED_PAD src0_sel:WORD_1 src1_sel:DWORD
	v_mul_f32_e32 v52, 0x417e0000, v20
	v_and_b32_sdwa v11, v17, v124 dst_sel:DWORD dst_unused:UNUSED_PAD src0_sel:WORD_1 src1_sel:DWORD
	v_and_b32_sdwa v33, v21, v124 dst_sel:DWORD dst_unused:UNUSED_PAD src0_sel:WORD_1 src1_sel:DWORD
	v_mul_f32_e32 v45, 0x417e0000, v16
	v_mul_f32_e32 v53, 0x417e0000, v17
	v_mul_f32_e32 v54, 0x417e0000, v21
	v_add3_u32 v16, v16, v32, s17
	v_add3_u32 v20, v20, v44, s17
	v_med3_f32 v32, v52, s19, v123
	v_add3_u32 v11, v17, v11, s17
	v_add3_u32 v17, v21, v33, s17
	v_med3_f32 v21, v45, s19, v123
	v_med3_f32 v33, v53, s19, v123
	v_med3_f32 v44, v54, s19, v123
	v_and_b32_e32 v20, 0xffff0000, v20
	v_rndne_f32_e32 v32, v32
	v_and_b32_e32 v17, 0xffff0000, v17
	v_rndne_f32_e32 v21, v21
	v_rndne_f32_e32 v33, v33
	v_rndne_f32_e32 v44, v44
	v_or_b32_sdwa v16, v20, v16 dst_sel:DWORD dst_unused:UNUSED_PAD src0_sel:DWORD src1_sel:WORD_1
	v_cvt_i32_f32_e32 v20, v32
	v_or_b32_sdwa v17, v17, v11 dst_sel:DWORD dst_unused:UNUSED_PAD src0_sel:DWORD src1_sel:WORD_1
	v_cvt_i32_f32_e32 v11, v21
	v_cvt_i32_f32_sdwa v21, v33 dst_sel:WORD_1 dst_unused:UNUSED_PAD src0_sel:DWORD
	v_cvt_i32_f32_e32 v32, v44
	global_store_dwordx2 v[106:107], v[16:17], off offset:1024
	v_lshlrev_b32_e32 v16, 8, v20
	v_and_b32_e32 v17, 0xff0000, v21
	v_perm_b32 v11, v32, v11, s20
	v_and_b32_e32 v16, 0xff00, v16
	v_or3_b32 v11, v11, v16, v17
	global_store_dword v[102:103], v11, off offset:-1536
	global_load_dwordx4 v[52:55], v[70:71], off offset:3072
	s_waitcnt vmcnt(0)
	v_mov_b32_e32 v16, v52
	v_mov_b32_e32 v17, v54
	v_mov_b32_e32 v54, v53
	v_pk_mul_f32 v[16:17], v[68:69], v[16:17]
	v_pk_mul_f32 v[20:21], v[56:57], v[54:55]
	v_and_b32_sdwa v32, v16, v124 dst_sel:DWORD dst_unused:UNUSED_PAD src0_sel:WORD_1 src1_sel:DWORD
	v_and_b32_sdwa v44, v20, v124 dst_sel:DWORD dst_unused:UNUSED_PAD src0_sel:WORD_1 src1_sel:DWORD
	v_mul_f32_e32 v52, 0x417e0000, v20
	v_and_b32_sdwa v11, v17, v124 dst_sel:DWORD dst_unused:UNUSED_PAD src0_sel:WORD_1 src1_sel:DWORD
	v_and_b32_sdwa v33, v21, v124 dst_sel:DWORD dst_unused:UNUSED_PAD src0_sel:WORD_1 src1_sel:DWORD
	v_mul_f32_e32 v45, 0x417e0000, v16
	v_mul_f32_e32 v53, 0x417e0000, v17
	v_mul_f32_e32 v54, 0x417e0000, v21
	v_add3_u32 v16, v16, v32, s17
	v_add3_u32 v20, v20, v44, s17
	v_med3_f32 v32, v52, s19, v123
	v_add3_u32 v11, v17, v11, s17
	v_add3_u32 v17, v21, v33, s17
	v_med3_f32 v21, v45, s19, v123
	v_med3_f32 v33, v53, s19, v123
	v_med3_f32 v44, v54, s19, v123
	v_and_b32_e32 v20, 0xffff0000, v20
	v_rndne_f32_e32 v32, v32
	v_and_b32_e32 v17, 0xffff0000, v17
	v_rndne_f32_e32 v21, v21
	v_rndne_f32_e32 v33, v33
	v_rndne_f32_e32 v44, v44
	v_or_b32_sdwa v16, v20, v16 dst_sel:DWORD dst_unused:UNUSED_PAD src0_sel:DWORD src1_sel:WORD_1
	v_cvt_i32_f32_e32 v20, v32
	v_or_b32_sdwa v17, v17, v11 dst_sel:DWORD dst_unused:UNUSED_PAD src0_sel:DWORD src1_sel:WORD_1
	v_cvt_i32_f32_e32 v11, v21
	v_cvt_i32_f32_sdwa v21, v33 dst_sel:WORD_1 dst_unused:UNUSED_PAD src0_sel:DWORD
	v_cvt_i32_f32_e32 v32, v44
	global_store_dwordx2 v[106:107], v[16:17], off offset:1536
	v_lshlrev_b32_e32 v16, 8, v20
	v_and_b32_e32 v17, 0xff0000, v21
	v_perm_b32 v11, v32, v11, s20
	v_and_b32_e32 v16, 0xff00, v16
	v_or3_b32 v11, v11, v16, v17
	global_store_dword v[102:103], v11, off offset:-1280
	global_load_dwordx4 v[52:55], v[72:73], off
	s_waitcnt vmcnt(0)
	v_mov_b32_e32 v16, v52
	v_mov_b32_e32 v17, v54
	v_mov_b32_e32 v54, v53
	v_pk_mul_f32 v[16:17], v[110:111], v[16:17]
	v_pk_mul_f32 v[20:21], v[112:113], v[54:55]
	v_and_b32_sdwa v32, v16, v124 dst_sel:DWORD dst_unused:UNUSED_PAD src0_sel:WORD_1 src1_sel:DWORD
	v_and_b32_sdwa v44, v20, v124 dst_sel:DWORD dst_unused:UNUSED_PAD src0_sel:WORD_1 src1_sel:DWORD
	v_mul_f32_e32 v52, 0x417e0000, v20
	v_and_b32_sdwa v11, v17, v124 dst_sel:DWORD dst_unused:UNUSED_PAD src0_sel:WORD_1 src1_sel:DWORD
	v_and_b32_sdwa v33, v21, v124 dst_sel:DWORD dst_unused:UNUSED_PAD src0_sel:WORD_1 src1_sel:DWORD
	v_mul_f32_e32 v45, 0x417e0000, v16
	v_mul_f32_e32 v53, 0x417e0000, v17
	v_mul_f32_e32 v54, 0x417e0000, v21
	v_add3_u32 v16, v16, v32, s17
	v_add3_u32 v20, v20, v44, s17
	v_med3_f32 v32, v52, s19, v123
	v_add3_u32 v11, v17, v11, s17
	v_add3_u32 v17, v21, v33, s17
	v_med3_f32 v21, v45, s19, v123
	v_med3_f32 v33, v53, s19, v123
	v_med3_f32 v44, v54, s19, v123
	v_and_b32_e32 v20, 0xffff0000, v20
	v_rndne_f32_e32 v32, v32
	v_and_b32_e32 v17, 0xffff0000, v17
	v_rndne_f32_e32 v21, v21
	v_rndne_f32_e32 v33, v33
	v_rndne_f32_e32 v44, v44
	v_or_b32_sdwa v16, v20, v16 dst_sel:DWORD dst_unused:UNUSED_PAD src0_sel:DWORD src1_sel:WORD_1
	v_cvt_i32_f32_e32 v20, v32
	v_or_b32_sdwa v17, v17, v11 dst_sel:DWORD dst_unused:UNUSED_PAD src0_sel:DWORD src1_sel:WORD_1
	v_cvt_i32_f32_e32 v11, v21
	v_cvt_i32_f32_sdwa v21, v33 dst_sel:WORD_1 dst_unused:UNUSED_PAD src0_sel:DWORD
	v_cvt_i32_f32_e32 v32, v44
	global_store_dwordx2 v[106:107], v[16:17], off offset:2048
	v_lshlrev_b32_e32 v16, 8, v20
	v_and_b32_e32 v17, 0xff0000, v21
	v_perm_b32 v11, v32, v11, s20
	v_and_b32_e32 v16, 0xff00, v16
	v_or3_b32 v11, v11, v16, v17
	global_store_dword v[102:103], v11, off offset:-1024
	global_load_dwordx4 v[52:55], v[74:75], off
	s_waitcnt vmcnt(0)
	v_mov_b32_e32 v16, v52
	v_mov_b32_e32 v17, v54
	v_mov_b32_e32 v54, v53
	v_pk_mul_f32 v[16:17], v[126:127], v[16:17]
	v_pk_mul_f32 v[20:21], v[128:129], v[54:55]
	v_and_b32_sdwa v32, v16, v124 dst_sel:DWORD dst_unused:UNUSED_PAD src0_sel:WORD_1 src1_sel:DWORD
	v_and_b32_sdwa v44, v20, v124 dst_sel:DWORD dst_unused:UNUSED_PAD src0_sel:WORD_1 src1_sel:DWORD
	v_mul_f32_e32 v52, 0x417e0000, v20
	v_and_b32_sdwa v11, v17, v124 dst_sel:DWORD dst_unused:UNUSED_PAD src0_sel:WORD_1 src1_sel:DWORD
	v_and_b32_sdwa v33, v21, v124 dst_sel:DWORD dst_unused:UNUSED_PAD src0_sel:WORD_1 src1_sel:DWORD
	v_mul_f32_e32 v45, 0x417e0000, v16
	v_mul_f32_e32 v53, 0x417e0000, v17
	v_mul_f32_e32 v54, 0x417e0000, v21
	v_add3_u32 v16, v16, v32, s17
	v_add3_u32 v20, v20, v44, s17
	v_med3_f32 v32, v52, s19, v123
	v_add3_u32 v11, v17, v11, s17
	v_add3_u32 v17, v21, v33, s17
	v_med3_f32 v21, v45, s19, v123
	v_med3_f32 v33, v53, s19, v123
	v_med3_f32 v44, v54, s19, v123
	v_and_b32_e32 v20, 0xffff0000, v20
	v_rndne_f32_e32 v32, v32
	v_and_b32_e32 v17, 0xffff0000, v17
	v_rndne_f32_e32 v21, v21
	v_rndne_f32_e32 v33, v33
	v_rndne_f32_e32 v44, v44
	v_or_b32_sdwa v16, v20, v16 dst_sel:DWORD dst_unused:UNUSED_PAD src0_sel:DWORD src1_sel:WORD_1
	v_cvt_i32_f32_e32 v20, v32
	v_or_b32_sdwa v17, v17, v11 dst_sel:DWORD dst_unused:UNUSED_PAD src0_sel:DWORD src1_sel:WORD_1
	v_cvt_i32_f32_e32 v11, v21
	v_cvt_i32_f32_sdwa v21, v33 dst_sel:WORD_1 dst_unused:UNUSED_PAD src0_sel:DWORD
	v_cvt_i32_f32_e32 v32, v44
	global_store_dwordx2 v[106:107], v[16:17], off offset:2560
	v_lshlrev_b32_e32 v16, 8, v20
	v_and_b32_e32 v17, 0xff0000, v21
	v_perm_b32 v11, v32, v11, s20
	v_and_b32_e32 v16, 0xff00, v16
	v_or3_b32 v11, v11, v16, v17
	global_store_dword v[102:103], v11, off offset:-768
	global_load_dwordx4 v[52:55], v[76:77], off
	s_waitcnt vmcnt(0)
	v_mov_b32_e32 v16, v52
	v_mov_b32_e32 v17, v54
	v_mov_b32_e32 v54, v53
	v_pk_mul_f32 v[16:17], v[48:49], v[16:17]
	v_pk_mul_f32 v[20:21], v[50:51], v[54:55]
	v_and_b32_sdwa v32, v16, v124 dst_sel:DWORD dst_unused:UNUSED_PAD src0_sel:WORD_1 src1_sel:DWORD
	v_and_b32_sdwa v44, v20, v124 dst_sel:DWORD dst_unused:UNUSED_PAD src0_sel:WORD_1 src1_sel:DWORD
	v_mul_f32_e32 v48, 0x417e0000, v20
	v_and_b32_sdwa v11, v17, v124 dst_sel:DWORD dst_unused:UNUSED_PAD src0_sel:WORD_1 src1_sel:DWORD
	v_and_b32_sdwa v33, v21, v124 dst_sel:DWORD dst_unused:UNUSED_PAD src0_sel:WORD_1 src1_sel:DWORD
	v_mul_f32_e32 v45, 0x417e0000, v16
	v_mul_f32_e32 v49, 0x417e0000, v17
	v_mul_f32_e32 v50, 0x417e0000, v21
	v_add3_u32 v16, v16, v32, s17
	v_add3_u32 v20, v20, v44, s17
	v_med3_f32 v32, v48, s19, v123
	v_add3_u32 v11, v17, v11, s17
	v_add3_u32 v17, v21, v33, s17
	v_med3_f32 v21, v45, s19, v123
	v_med3_f32 v33, v49, s19, v123
	v_med3_f32 v44, v50, s19, v123
	v_and_b32_e32 v20, 0xffff0000, v20
	v_rndne_f32_e32 v32, v32
	v_and_b32_e32 v17, 0xffff0000, v17
	v_rndne_f32_e32 v21, v21
	v_rndne_f32_e32 v33, v33
	v_rndne_f32_e32 v44, v44
	v_or_b32_sdwa v16, v20, v16 dst_sel:DWORD dst_unused:UNUSED_PAD src0_sel:DWORD src1_sel:WORD_1
	v_cvt_i32_f32_e32 v20, v32
	v_or_b32_sdwa v17, v17, v11 dst_sel:DWORD dst_unused:UNUSED_PAD src0_sel:DWORD src1_sel:WORD_1
	v_cvt_i32_f32_e32 v11, v21
	v_cvt_i32_f32_sdwa v21, v33 dst_sel:WORD_1 dst_unused:UNUSED_PAD src0_sel:DWORD
	v_cvt_i32_f32_e32 v32, v44
	global_store_dwordx2 v[106:107], v[16:17], off offset:3072
	v_lshlrev_b32_e32 v16, 8, v20
	v_and_b32_e32 v17, 0xff0000, v21
	v_perm_b32 v11, v32, v11, s20
	v_and_b32_e32 v16, 0xff00, v16
	v_or3_b32 v11, v11, v16, v17
	global_store_dword v[102:103], v11, off offset:-512
	global_load_dwordx4 v[48:51], v[78:79], off
	s_waitcnt vmcnt(0)
	v_mov_b32_e32 v16, v48
	v_mov_b32_e32 v17, v50
	v_mov_b32_e32 v50, v49
	v_pk_mul_f32 v[16:17], v[42:43], v[16:17]
	v_pk_mul_f32 v[20:21], v[46:47], v[50:51]
	v_and_b32_sdwa v32, v16, v124 dst_sel:DWORD dst_unused:UNUSED_PAD src0_sel:WORD_1 src1_sel:DWORD
	v_and_b32_sdwa v42, v20, v124 dst_sel:DWORD dst_unused:UNUSED_PAD src0_sel:WORD_1 src1_sel:DWORD
	v_mul_f32_e32 v44, 0x417e0000, v20
	v_and_b32_sdwa v11, v17, v124 dst_sel:DWORD dst_unused:UNUSED_PAD src0_sel:WORD_1 src1_sel:DWORD
	v_and_b32_sdwa v33, v21, v124 dst_sel:DWORD dst_unused:UNUSED_PAD src0_sel:WORD_1 src1_sel:DWORD
	v_mul_f32_e32 v43, 0x417e0000, v16
	v_mul_f32_e32 v45, 0x417e0000, v17
	v_mul_f32_e32 v46, 0x417e0000, v21
	v_add3_u32 v16, v16, v32, s17
	v_add3_u32 v20, v20, v42, s17
	v_med3_f32 v32, v44, s19, v123
	v_add3_u32 v11, v17, v11, s17
	v_add3_u32 v17, v21, v33, s17
	v_med3_f32 v21, v43, s19, v123
	v_med3_f32 v33, v45, s19, v123
	v_med3_f32 v42, v46, s19, v123
	v_and_b32_e32 v20, 0xffff0000, v20
	v_rndne_f32_e32 v32, v32
	v_and_b32_e32 v17, 0xffff0000, v17
	v_rndne_f32_e32 v21, v21
	v_rndne_f32_e32 v33, v33
	v_rndne_f32_e32 v42, v42
	v_or_b32_sdwa v16, v20, v16 dst_sel:DWORD dst_unused:UNUSED_PAD src0_sel:DWORD src1_sel:WORD_1
	v_cvt_i32_f32_e32 v20, v32
	v_or_b32_sdwa v17, v17, v11 dst_sel:DWORD dst_unused:UNUSED_PAD src0_sel:DWORD src1_sel:WORD_1
	v_cvt_i32_f32_e32 v11, v21
	v_cvt_i32_f32_sdwa v21, v33 dst_sel:WORD_1 dst_unused:UNUSED_PAD src0_sel:DWORD
	v_cvt_i32_f32_e32 v32, v42
	global_store_dwordx2 v[106:107], v[16:17], off offset:3584
	v_lshlrev_b32_e32 v16, 8, v20
	v_and_b32_e32 v17, 0xff0000, v21
	v_perm_b32 v11, v32, v11, s20
	v_and_b32_e32 v16, 0xff00, v16
	v_or3_b32 v11, v11, v16, v17
	global_store_dword v[102:103], v11, off offset:-256
	global_load_dwordx4 v[42:45], v[80:81], off
	s_waitcnt vmcnt(0)
	v_mov_b32_e32 v16, v42
	v_mov_b32_e32 v17, v44
	v_mov_b32_e32 v44, v43
	v_pk_mul_f32 v[16:17], v[38:39], v[16:17]
	v_pk_mul_f32 v[20:21], v[40:41], v[44:45]
	v_and_b32_sdwa v32, v16, v124 dst_sel:DWORD dst_unused:UNUSED_PAD src0_sel:WORD_1 src1_sel:DWORD
	v_and_b32_sdwa v38, v20, v124 dst_sel:DWORD dst_unused:UNUSED_PAD src0_sel:WORD_1 src1_sel:DWORD
	v_mul_f32_e32 v40, 0x417e0000, v20
	v_and_b32_sdwa v11, v17, v124 dst_sel:DWORD dst_unused:UNUSED_PAD src0_sel:WORD_1 src1_sel:DWORD
	v_and_b32_sdwa v33, v21, v124 dst_sel:DWORD dst_unused:UNUSED_PAD src0_sel:WORD_1 src1_sel:DWORD
	v_mul_f32_e32 v39, 0x417e0000, v16
	v_mul_f32_e32 v41, 0x417e0000, v17
	v_mul_f32_e32 v42, 0x417e0000, v21
	v_add3_u32 v16, v16, v32, s17
	v_add3_u32 v20, v20, v38, s17
	v_med3_f32 v32, v40, s19, v123
	v_add3_u32 v11, v17, v11, s17
	v_add3_u32 v17, v21, v33, s17
	v_med3_f32 v21, v39, s19, v123
	v_med3_f32 v33, v41, s19, v123
	v_med3_f32 v38, v42, s19, v123
	v_and_b32_e32 v20, 0xffff0000, v20
	v_rndne_f32_e32 v32, v32
	v_and_b32_e32 v17, 0xffff0000, v17
	v_rndne_f32_e32 v21, v21
	v_rndne_f32_e32 v33, v33
	v_rndne_f32_e32 v38, v38
	v_or_b32_sdwa v16, v20, v16 dst_sel:DWORD dst_unused:UNUSED_PAD src0_sel:DWORD src1_sel:WORD_1
	v_cvt_i32_f32_e32 v20, v32
	v_or_b32_sdwa v17, v17, v11 dst_sel:DWORD dst_unused:UNUSED_PAD src0_sel:DWORD src1_sel:WORD_1
	v_cvt_i32_f32_e32 v11, v21
	v_cvt_i32_f32_sdwa v21, v33 dst_sel:WORD_1 dst_unused:UNUSED_PAD src0_sel:DWORD
	v_cvt_i32_f32_e32 v32, v38
	global_store_dwordx2 v[104:105], v[16:17], off
	v_lshlrev_b32_e32 v16, 8, v20
	v_and_b32_e32 v17, 0xff0000, v21
	v_perm_b32 v11, v32, v11, s20
	v_and_b32_e32 v16, 0xff00, v16
	v_or3_b32 v11, v11, v16, v17
	global_store_dword v[102:103], v11, off
	global_load_dwordx4 v[38:41], v[82:83], off
	s_waitcnt vmcnt(0)
	v_mov_b32_e32 v16, v38
	v_mov_b32_e32 v17, v40
	v_mov_b32_e32 v40, v39
	v_pk_mul_f32 v[16:17], v[34:35], v[16:17]
	v_pk_mul_f32 v[20:21], v[36:37], v[40:41]
	v_and_b32_sdwa v32, v16, v124 dst_sel:DWORD dst_unused:UNUSED_PAD src0_sel:WORD_1 src1_sel:DWORD
	v_and_b32_sdwa v34, v20, v124 dst_sel:DWORD dst_unused:UNUSED_PAD src0_sel:WORD_1 src1_sel:DWORD
	v_mul_f32_e32 v36, 0x417e0000, v20
	v_and_b32_sdwa v11, v17, v124 dst_sel:DWORD dst_unused:UNUSED_PAD src0_sel:WORD_1 src1_sel:DWORD
	v_and_b32_sdwa v33, v21, v124 dst_sel:DWORD dst_unused:UNUSED_PAD src0_sel:WORD_1 src1_sel:DWORD
	v_mul_f32_e32 v35, 0x417e0000, v16
	v_mul_f32_e32 v37, 0x417e0000, v17
	v_mul_f32_e32 v38, 0x417e0000, v21
	v_add3_u32 v16, v16, v32, s17
	v_add3_u32 v20, v20, v34, s17
	v_med3_f32 v32, v36, s19, v123
	v_add3_u32 v11, v17, v11, s17
	v_add3_u32 v17, v21, v33, s17
	v_med3_f32 v21, v35, s19, v123
	v_med3_f32 v33, v37, s19, v123
	v_med3_f32 v34, v38, s19, v123
	v_and_b32_e32 v20, 0xffff0000, v20
	v_rndne_f32_e32 v32, v32
	v_and_b32_e32 v17, 0xffff0000, v17
	v_rndne_f32_e32 v21, v21
	v_rndne_f32_e32 v33, v33
	v_rndne_f32_e32 v34, v34
	v_or_b32_sdwa v16, v20, v16 dst_sel:DWORD dst_unused:UNUSED_PAD src0_sel:DWORD src1_sel:WORD_1
	v_cvt_i32_f32_e32 v20, v32
	v_or_b32_sdwa v17, v17, v11 dst_sel:DWORD dst_unused:UNUSED_PAD src0_sel:DWORD src1_sel:WORD_1
	v_cvt_i32_f32_e32 v11, v21
	v_cvt_i32_f32_sdwa v21, v33 dst_sel:WORD_1 dst_unused:UNUSED_PAD src0_sel:DWORD
	v_cvt_i32_f32_e32 v32, v34
	global_store_dwordx2 v[104:105], v[16:17], off offset:512
	v_lshlrev_b32_e32 v16, 8, v20
	v_and_b32_e32 v17, 0xff0000, v21
	v_perm_b32 v11, v32, v11, s20
	v_and_b32_e32 v16, 0xff00, v16
	v_or3_b32 v11, v11, v16, v17
	global_store_dword v[102:103], v11, off offset:256
	global_load_dwordx4 v[32:35], v[84:85], off
	s_waitcnt vmcnt(0)
	v_mov_b32_e32 v16, v32
	v_mov_b32_e32 v17, v34
	v_mov_b32_e32 v34, v33
	v_pk_mul_f32 v[16:17], v[28:29], v[16:17]
	v_pk_mul_f32 v[20:21], v[30:31], v[34:35]
	v_and_b32_sdwa v28, v16, v124 dst_sel:DWORD dst_unused:UNUSED_PAD src0_sel:WORD_1 src1_sel:DWORD
	v_and_b32_sdwa v30, v20, v124 dst_sel:DWORD dst_unused:UNUSED_PAD src0_sel:WORD_1 src1_sel:DWORD
	v_mul_f32_e32 v32, 0x417e0000, v20
	v_and_b32_sdwa v11, v17, v124 dst_sel:DWORD dst_unused:UNUSED_PAD src0_sel:WORD_1 src1_sel:DWORD
	v_and_b32_sdwa v29, v21, v124 dst_sel:DWORD dst_unused:UNUSED_PAD src0_sel:WORD_1 src1_sel:DWORD
	v_mul_f32_e32 v31, 0x417e0000, v16
	v_mul_f32_e32 v33, 0x417e0000, v17
	v_mul_f32_e32 v34, 0x417e0000, v21
	v_add3_u32 v16, v16, v28, s17
	v_add3_u32 v20, v20, v30, s17
	v_med3_f32 v28, v32, s19, v123
	v_add3_u32 v11, v17, v11, s17
	v_add3_u32 v17, v21, v29, s17
	v_med3_f32 v21, v31, s19, v123
	v_med3_f32 v29, v33, s19, v123
	v_med3_f32 v30, v34, s19, v123
	v_and_b32_e32 v20, 0xffff0000, v20
	v_rndne_f32_e32 v28, v28
	v_and_b32_e32 v17, 0xffff0000, v17
	v_rndne_f32_e32 v21, v21
	v_rndne_f32_e32 v29, v29
	v_rndne_f32_e32 v30, v30
	v_or_b32_sdwa v16, v20, v16 dst_sel:DWORD dst_unused:UNUSED_PAD src0_sel:DWORD src1_sel:WORD_1
	v_cvt_i32_f32_e32 v20, v28
	v_or_b32_sdwa v17, v17, v11 dst_sel:DWORD dst_unused:UNUSED_PAD src0_sel:DWORD src1_sel:WORD_1
	v_cvt_i32_f32_e32 v11, v21
	v_cvt_i32_f32_sdwa v21, v29 dst_sel:WORD_1 dst_unused:UNUSED_PAD src0_sel:DWORD
	v_cvt_i32_f32_e32 v28, v30
	global_store_dwordx2 v[104:105], v[16:17], off offset:1024
	v_lshlrev_b32_e32 v16, 8, v20
	v_and_b32_e32 v17, 0xff0000, v21
	v_perm_b32 v11, v28, v11, s20
	v_and_b32_e32 v16, 0xff00, v16
	v_or3_b32 v11, v11, v16, v17
	global_store_dword v[102:103], v11, off offset:512
	global_load_dwordx4 v[28:31], v[86:87], off
	s_waitcnt vmcnt(0)
	v_mov_b32_e32 v16, v28
	v_mov_b32_e32 v17, v30
	v_mov_b32_e32 v30, v29
	v_pk_mul_f32 v[16:17], v[26:27], v[16:17]
	v_pk_mul_f32 v[20:21], v[24:25], v[30:31]
	v_and_b32_sdwa v24, v16, v124 dst_sel:DWORD dst_unused:UNUSED_PAD src0_sel:WORD_1 src1_sel:DWORD
	v_and_b32_sdwa v26, v20, v124 dst_sel:DWORD dst_unused:UNUSED_PAD src0_sel:WORD_1 src1_sel:DWORD
	v_mul_f32_e32 v28, 0x417e0000, v20
	v_and_b32_sdwa v11, v17, v124 dst_sel:DWORD dst_unused:UNUSED_PAD src0_sel:WORD_1 src1_sel:DWORD
	v_and_b32_sdwa v25, v21, v124 dst_sel:DWORD dst_unused:UNUSED_PAD src0_sel:WORD_1 src1_sel:DWORD
	v_mul_f32_e32 v27, 0x417e0000, v16
	v_mul_f32_e32 v29, 0x417e0000, v17
	v_mul_f32_e32 v30, 0x417e0000, v21
	v_add3_u32 v16, v16, v24, s17
	v_add3_u32 v20, v20, v26, s17
	v_med3_f32 v24, v28, s19, v123
	v_add3_u32 v11, v17, v11, s17
	v_add3_u32 v17, v21, v25, s17
	v_med3_f32 v21, v27, s19, v123
	v_med3_f32 v25, v29, s19, v123
	v_med3_f32 v26, v30, s19, v123
	v_and_b32_e32 v20, 0xffff0000, v20
	v_rndne_f32_e32 v24, v24
	v_and_b32_e32 v17, 0xffff0000, v17
	v_rndne_f32_e32 v21, v21
	v_rndne_f32_e32 v25, v25
	v_rndne_f32_e32 v26, v26
	v_or_b32_sdwa v16, v20, v16 dst_sel:DWORD dst_unused:UNUSED_PAD src0_sel:DWORD src1_sel:WORD_1
	v_cvt_i32_f32_e32 v20, v24
	v_or_b32_sdwa v17, v17, v11 dst_sel:DWORD dst_unused:UNUSED_PAD src0_sel:DWORD src1_sel:WORD_1
	v_cvt_i32_f32_e32 v11, v21
	v_cvt_i32_f32_sdwa v21, v25 dst_sel:WORD_1 dst_unused:UNUSED_PAD src0_sel:DWORD
	v_cvt_i32_f32_e32 v24, v26
	global_store_dwordx2 v[104:105], v[16:17], off offset:1536
	v_lshlrev_b32_e32 v16, 8, v20
	v_and_b32_e32 v17, 0xff0000, v21
	v_perm_b32 v11, v24, v11, s20
	v_and_b32_e32 v16, 0xff00, v16
	v_or3_b32 v11, v11, v16, v17
	global_store_dword v[102:103], v11, off offset:768
	global_load_dwordx4 v[24:27], v[88:89], off
	s_waitcnt vmcnt(0)
	v_mov_b32_e32 v16, v24
	v_mov_b32_e32 v17, v26
	v_mov_b32_e32 v26, v25
	v_pk_mul_f32 v[16:17], v[18:19], v[16:17]
	v_pk_mul_f32 v[18:19], v[22:23], v[26:27]
	v_and_b32_sdwa v20, v16, v124 dst_sel:DWORD dst_unused:UNUSED_PAD src0_sel:WORD_1 src1_sel:DWORD
	v_and_b32_sdwa v22, v18, v124 dst_sel:DWORD dst_unused:UNUSED_PAD src0_sel:WORD_1 src1_sel:DWORD
	v_mul_f32_e32 v24, 0x417e0000, v18
	v_and_b32_sdwa v11, v17, v124 dst_sel:DWORD dst_unused:UNUSED_PAD src0_sel:WORD_1 src1_sel:DWORD
	v_and_b32_sdwa v21, v19, v124 dst_sel:DWORD dst_unused:UNUSED_PAD src0_sel:WORD_1 src1_sel:DWORD
	v_mul_f32_e32 v23, 0x417e0000, v16
	v_mul_f32_e32 v25, 0x417e0000, v17
	v_mul_f32_e32 v26, 0x417e0000, v19
	v_add3_u32 v16, v16, v20, s17
	v_add3_u32 v18, v18, v22, s17
	v_med3_f32 v20, v24, s19, v123
	v_add3_u32 v11, v17, v11, s17
	v_add3_u32 v17, v19, v21, s17
	v_med3_f32 v19, v23, s19, v123
	v_med3_f32 v21, v25, s19, v123
	v_med3_f32 v22, v26, s19, v123
	v_and_b32_e32 v18, 0xffff0000, v18
	v_rndne_f32_e32 v20, v20
	v_and_b32_e32 v17, 0xffff0000, v17
	v_rndne_f32_e32 v19, v19
	v_rndne_f32_e32 v21, v21
	v_rndne_f32_e32 v22, v22
	v_or_b32_sdwa v16, v18, v16 dst_sel:DWORD dst_unused:UNUSED_PAD src0_sel:DWORD src1_sel:WORD_1
	v_cvt_i32_f32_e32 v18, v20
	v_or_b32_sdwa v17, v17, v11 dst_sel:DWORD dst_unused:UNUSED_PAD src0_sel:DWORD src1_sel:WORD_1
	v_cvt_i32_f32_e32 v11, v19
	v_cvt_i32_f32_sdwa v19, v21 dst_sel:WORD_1 dst_unused:UNUSED_PAD src0_sel:DWORD
	v_cvt_i32_f32_e32 v20, v22
	global_store_dwordx2 v[104:105], v[16:17], off offset:2048
	v_lshlrev_b32_e32 v16, 8, v18
	v_and_b32_e32 v17, 0xff0000, v19
	v_perm_b32 v11, v20, v11, s20
	v_and_b32_e32 v16, 0xff00, v16
	v_or3_b32 v11, v11, v16, v17
	global_store_dword v[102:103], v11, off offset:1024
	global_load_dwordx4 v[16:19], v[90:91], off
	s_waitcnt vmcnt(0)
	v_mov_b32_e32 v20, v16
	v_mov_b32_e32 v21, v18
	v_mov_b32_e32 v18, v17
	v_pk_mul_f32 v[12:13], v[12:13], v[20:21]
	v_pk_mul_f32 v[14:15], v[14:15], v[18:19]
	v_and_b32_sdwa v16, v12, v124 dst_sel:DWORD dst_unused:UNUSED_PAD src0_sel:WORD_1 src1_sel:DWORD
	v_and_b32_sdwa v18, v14, v124 dst_sel:DWORD dst_unused:UNUSED_PAD src0_sel:WORD_1 src1_sel:DWORD
	v_mul_f32_e32 v20, 0x417e0000, v14
	v_and_b32_sdwa v11, v13, v124 dst_sel:DWORD dst_unused:UNUSED_PAD src0_sel:WORD_1 src1_sel:DWORD
	v_and_b32_sdwa v17, v15, v124 dst_sel:DWORD dst_unused:UNUSED_PAD src0_sel:WORD_1 src1_sel:DWORD
	v_mul_f32_e32 v19, 0x417e0000, v12
	v_mul_f32_e32 v21, 0x417e0000, v13
	v_mul_f32_e32 v22, 0x417e0000, v15
	v_add3_u32 v12, v12, v16, s17
	v_add3_u32 v14, v14, v18, s17
	v_med3_f32 v16, v20, s19, v123
	v_add3_u32 v11, v13, v11, s17
	v_add3_u32 v13, v15, v17, s17
	v_med3_f32 v15, v19, s19, v123
	v_med3_f32 v17, v21, s19, v123
	v_med3_f32 v18, v22, s19, v123
	v_and_b32_e32 v14, 0xffff0000, v14
	v_rndne_f32_e32 v16, v16
	v_and_b32_e32 v13, 0xffff0000, v13
	v_rndne_f32_e32 v15, v15
	v_rndne_f32_e32 v17, v17
	v_rndne_f32_e32 v18, v18
	v_or_b32_sdwa v12, v14, v12 dst_sel:DWORD dst_unused:UNUSED_PAD src0_sel:DWORD src1_sel:WORD_1
	v_cvt_i32_f32_e32 v14, v16
	v_or_b32_sdwa v13, v13, v11 dst_sel:DWORD dst_unused:UNUSED_PAD src0_sel:DWORD src1_sel:WORD_1
	v_cvt_i32_f32_e32 v11, v15
	v_cvt_i32_f32_sdwa v15, v17 dst_sel:WORD_1 dst_unused:UNUSED_PAD src0_sel:DWORD
	v_cvt_i32_f32_e32 v16, v18
	global_store_dwordx2 v[104:105], v[12:13], off offset:2560
	v_lshlrev_b32_e32 v12, 8, v14
	v_and_b32_e32 v13, 0xff0000, v15
	v_perm_b32 v11, v16, v11, s20
	v_and_b32_e32 v12, 0xff00, v12
	v_or3_b32 v11, v11, v12, v13
	global_store_dword v[102:103], v11, off offset:1280
	global_load_dwordx4 v[12:15], v[92:93], off
	v_mov_b32_e32 v16, v6
	v_mov_b32_e32 v17, v8
	v_mov_b32_e32 v8, v7
	v_pk_mul_f32 v[6:7], v[16:17], v[10:11] op_sel_hi:[1,0]
	v_pk_mul_f32 v[8:9], v[8:9], v[10:11] op_sel_hi:[1,0]
	s_waitcnt vmcnt(0)
	v_mov_b32_e32 v16, v12
	v_mov_b32_e32 v17, v14
	v_mov_b32_e32 v14, v13
	v_pk_mul_f32 v[6:7], v[6:7], v[16:17]
	v_pk_mul_f32 v[8:9], v[8:9], v[14:15]
	v_and_b32_sdwa v12, v6, v124 dst_sel:DWORD dst_unused:UNUSED_PAD src0_sel:WORD_1 src1_sel:DWORD
	v_and_b32_sdwa v13, v9, v124 dst_sel:DWORD dst_unused:UNUSED_PAD src0_sel:WORD_1 src1_sel:DWORD
	v_mul_f32_e32 v16, 0x417e0000, v8
	v_and_b32_sdwa v11, v7, v124 dst_sel:DWORD dst_unused:UNUSED_PAD src0_sel:WORD_1 src1_sel:DWORD
	v_and_b32_sdwa v14, v8, v124 dst_sel:DWORD dst_unused:UNUSED_PAD src0_sel:WORD_1 src1_sel:DWORD
	v_mul_f32_e32 v15, 0x417e0000, v6
	v_mul_f32_e32 v17, 0x417e0000, v7
	v_mul_f32_e32 v18, 0x417e0000, v9
	v_add3_u32 v6, v6, v12, s17
	v_add3_u32 v9, v9, v13, s17
	v_med3_f32 v12, v16, s19, v123
	v_add3_u32 v7, v7, v11, s17
	v_add3_u32 v8, v8, v14, s17
	v_med3_f32 v11, v15, s19, v123
	v_med3_f32 v13, v17, s19, v123
	v_med3_f32 v14, v18, s19, v123
	v_and_b32_e32 v9, 0xffff0000, v9
	v_rndne_f32_e32 v12, v12
	v_and_b32_e32 v8, 0xffff0000, v8
	v_rndne_f32_e32 v11, v11
	v_rndne_f32_e32 v13, v13
	v_rndne_f32_e32 v14, v14
	v_or_b32_sdwa v7, v9, v7 dst_sel:DWORD dst_unused:UNUSED_PAD src0_sel:DWORD src1_sel:WORD_1
	v_cvt_i32_f32_e32 v9, v12
	v_or_b32_sdwa v6, v8, v6 dst_sel:DWORD dst_unused:UNUSED_PAD src0_sel:DWORD src1_sel:WORD_1
	v_cvt_i32_f32_e32 v8, v11
	v_cvt_i32_f32_sdwa v11, v13 dst_sel:WORD_1 dst_unused:UNUSED_PAD src0_sel:DWORD
	v_cvt_i32_f32_e32 v12, v14
	global_store_dwordx2 v[104:105], v[6:7], off offset:3072
	v_lshlrev_b32_e32 v6, 8, v9
	v_and_b32_e32 v7, 0xff0000, v11
	v_perm_b32 v8, v12, v8, s20
	v_and_b32_e32 v6, 0xff00, v6
	v_or3_b32 v6, v8, v6, v7
	global_store_dword v[102:103], v6, off offset:1536
	global_load_dwordx4 v[6:9], v[94:95], off
	v_mov_b32_e32 v12, v2
	v_mov_b32_e32 v13, v4
	v_mov_b32_e32 v4, v3
	v_pk_mul_f32 v[2:3], v[12:13], v[10:11] op_sel_hi:[1,0]
	v_pk_mul_f32 v[4:5], v[4:5], v[10:11] op_sel_hi:[1,0]
	s_waitcnt vmcnt(0)
	v_mov_b32_e32 v10, v6
	v_mov_b32_e32 v11, v8
	v_mov_b32_e32 v8, v7
	v_pk_mul_f32 v[2:3], v[2:3], v[10:11]
	v_pk_mul_f32 v[4:5], v[4:5], v[8:9]
	v_and_b32_sdwa v7, v2, v124 dst_sel:DWORD dst_unused:UNUSED_PAD src0_sel:WORD_1 src1_sel:DWORD
	v_and_b32_sdwa v8, v5, v124 dst_sel:DWORD dst_unused:UNUSED_PAD src0_sel:WORD_1 src1_sel:DWORD
	v_mul_f32_e32 v11, 0x417e0000, v4
	v_and_b32_sdwa v6, v3, v124 dst_sel:DWORD dst_unused:UNUSED_PAD src0_sel:WORD_1 src1_sel:DWORD
	v_and_b32_sdwa v9, v4, v124 dst_sel:DWORD dst_unused:UNUSED_PAD src0_sel:WORD_1 src1_sel:DWORD
	v_mul_f32_e32 v10, 0x417e0000, v2
	v_mul_f32_e32 v12, 0x417e0000, v3
	v_mul_f32_e32 v13, 0x417e0000, v5
	v_add3_u32 v2, v2, v7, s17
	v_add3_u32 v5, v5, v8, s17
	v_med3_f32 v7, v11, s19, v123
	v_add3_u32 v3, v3, v6, s17
	v_add3_u32 v4, v4, v9, s17
	v_med3_f32 v6, v10, s19, v123
	v_med3_f32 v8, v12, s19, v123
	v_med3_f32 v9, v13, s19, v123
	v_and_b32_e32 v5, 0xffff0000, v5
	v_rndne_f32_e32 v7, v7
	v_and_b32_e32 v4, 0xffff0000, v4
	v_rndne_f32_e32 v6, v6
	v_rndne_f32_e32 v8, v8
	v_rndne_f32_e32 v9, v9
	v_or_b32_sdwa v3, v5, v3 dst_sel:DWORD dst_unused:UNUSED_PAD src0_sel:DWORD src1_sel:WORD_1
	v_cvt_i32_f32_e32 v5, v7
	v_or_b32_sdwa v2, v4, v2 dst_sel:DWORD dst_unused:UNUSED_PAD src0_sel:DWORD src1_sel:WORD_1
	v_cvt_i32_f32_e32 v4, v6
	v_cvt_i32_f32_sdwa v6, v8 dst_sel:WORD_1 dst_unused:UNUSED_PAD src0_sel:DWORD
	v_cvt_i32_f32_e32 v7, v9
	global_store_dwordx2 v[104:105], v[2:3], off offset:3584
	v_lshlrev_b32_e32 v2, 8, v5
	v_and_b32_e32 v3, 0xff0000, v6
	v_perm_b32 v4, v7, v4, s20
	v_and_b32_e32 v2, 0xff00, v2
	v_or3_b32 v2, v4, v2, v3
	global_store_dword v[102:103], v2, off offset:1792
	s_cbranch_scc1 .LBB0_534
	v_readlane_b32 s93, v246, 7

.LBB0_697:
	v_mov_b32_e32 v35, v0
	s_ashr_i32 s61, s60, 6
	s_lshl_b32 s67, s61, 4
	v_and_b32_e32 v34, 15, v35
	v_or_b32_e32 v2, s67, v34
	v_ashrrev_i32_e32 v3, 31, v2
	s_bfe_u32 s65, s60, 0x40002
	v_lshlrev_b64 v[2:3], 13, v[2:3]
	v_bfe_u32 v36, v35, 4, 2
	v_lshl_add_u64 v[2:3], s[12:13], 0, v[2:3]
	s_lshl_b32 s14, s65, 9
	v_lshl_add_u64 v[2:3], v[2:3], 0, s[14:15]
	v_lshlrev_b32_e32 v46, 5, v36
	v_lshl_add_u64 v[30:31], v[2:3], 0, v[46:47]
	global_load_dwordx4 v[2:5], v[30:31], off offset:16
	global_load_dwordx4 v[6:9], v[30:31], off
	global_load_dwordx4 v[10:13], v[30:31], off offset:144
	global_load_dwordx4 v[14:17], v[30:31], off offset:128
	global_load_dwordx4 v[18:21], v[30:31], off offset:272
	global_load_dwordx4 v[22:25], v[30:31], off offset:256
	global_load_dwordx4 v[26:29], v[30:31], off offset:400
	global_load_dwordx4 v[30:33], v[30:31], off offset:384
	s_lshl_b32 s64, s65, 7
	s_and_b32 s0, s60, 3
	v_readfirstlane_b32 s14, v35
	s_cmp_eq_u32 s0, 0
	s_cselect_b64 s[0:1], -1, 0
	s_cmp_lt_u32 s14, 64
	s_cselect_b64 s[94:95], -1, 0
	v_lshlrev_b32_e32 v37, 3, v36
	s_and_b64 s[0:1], s[0:1], s[94:95]
	s_andn2_b64 vcc, exec, s[0:1]
	v_lshlrev_b32_e32 v46, 2, v37
	s_cbranch_vccnz .LBB0_701
	v_readlane_b32 s72, v247, 22
	s_lshl_b32 s0, s64, 2
	v_readlane_b32 s76, v247, 26
	v_readlane_b32 s77, v247, 27
	s_add_u32 vcc_lo, s76, s0
	s_addc_u32 vcc_hi, s77, 0
	global_load_dwordx4 v[38:41], v46, vcc offset:16
	global_load_dwordx4 v[42:45], v46, vcc
	v_readlane_b32 s73, v247, 23
	v_readlane_b32 s74, v247, 24
	v_readlane_b32 s75, v247, 25
	v_readlane_b32 s78, v247, 28
	v_readlane_b32 s79, v247, 29
	v_readlane_b32 s80, v247, 30
	v_readlane_b32 s81, v247, 31
	v_readlane_b32 s82, v247, 32
	v_readlane_b32 s83, v247, 33
	v_readlane_b32 s84, v247, 34
	v_readlane_b32 s85, v247, 35
	v_readlane_b32 s86, v247, 36
	v_readlane_b32 s87, v247, 37
	s_waitcnt vmcnt(0)
	v_mul_f32_e32 v37, v7, v43
	v_fmac_f32_e32 v37, v6, v42
	v_fmac_f32_e32 v37, v8, v44
	v_fmac_f32_e32 v37, v9, v45
	v_fmac_f32_e32 v37, v2, v38
	v_fmac_f32_e32 v37, v3, v39
	v_fmac_f32_e32 v37, v4, v40
	v_fmac_f32_e32 v37, v5, v41
	global_load_dwordx4 v[38:41], v46, vcc offset:144
	global_load_dwordx4 v[42:45], v46, vcc offset:128
	v_add_f32_e32 v37, 0, v37
	s_waitcnt vmcnt(0)
	v_mul_f32_e32 v43, v15, v43
	v_fmac_f32_e32 v43, v14, v42
	v_fmac_f32_e32 v43, v16, v44
	v_fmac_f32_e32 v43, v17, v45
	v_fmac_f32_e32 v43, v10, v38
	v_fmac_f32_e32 v43, v11, v39
	v_fmac_f32_e32 v43, v12, v40
	v_fmac_f32_e32 v43, v13, v41
	v_add_f32_e32 v37, v37, v43
	global_load_dwordx4 v[38:41], v46, vcc offset:272
	global_load_dwordx4 v[42:45], v46, vcc offset:256
	s_waitcnt vmcnt(0)
	v_mul_f32_e32 v43, v23, v43
	v_fmac_f32_e32 v43, v22, v42
	v_fmac_f32_e32 v43, v24, v44
	v_fmac_f32_e32 v43, v25, v45
	v_fmac_f32_e32 v43, v18, v38
	v_fmac_f32_e32 v43, v19, v39
	v_fmac_f32_e32 v43, v20, v40
	v_fmac_f32_e32 v43, v21, v41
	v_add_f32_e32 v37, v37, v43
	global_load_dwordx4 v[38:41], v46, vcc offset:400
	global_load_dwordx4 v[42:45], v46, vcc offset:384
	s_waitcnt vmcnt(0)
	v_mul_f32_e32 v43, v31, v43
	v_fmac_f32_e32 v43, v30, v42
	v_fmac_f32_e32 v43, v32, v44
	v_fmac_f32_e32 v43, v33, v45
	v_fmac_f32_e32 v43, v26, v38
	v_fmac_f32_e32 v43, v27, v39
	v_and_b32_e32 v39, 64, v1
	v_xor_b32_e32 v38, 16, v1
	v_add_u32_e32 v39, 64, v39
	v_fmac_f32_e32 v43, v28, v40
	v_cmp_lt_i32_e32 vcc, v38, v39
	v_fmac_f32_e32 v43, v29, v41
	v_add_f32_e32 v37, v37, v43
	v_cndmask_b32_e32 v38, v1, v38, vcc
	v_lshlrev_b32_e32 v38, 2, v38
	ds_bpermute_b32 v38, v38, v37
	s_waitcnt lgkmcnt(0)
	v_add_f32_e32 v37, v37, v38
	v_xor_b32_e32 v38, 32, v1
	v_cmp_lt_i32_e32 vcc, v38, v39
	s_nop 1
	v_cndmask_b32_e32 v38, v1, v38, vcc
	v_lshlrev_b32_e32 v38, 2, v38
	ds_bpermute_b32 v38, v38, v37
	v_cmp_eq_u32_e32 vcc, 0, v36
	s_and_saveexec_b64 s[0:1], vcc
	s_cbranch_execz .LBB0_700
	s_or_b32 s65, s67, s65
	v_lshl_or_b32 v40, s65, 4, v34
	v_ashrrev_i32_e32 v41, 31, v40
	s_waitcnt lgkmcnt(0)
	v_add_f32_e32 v36, v37, v38
	v_lshl_add_u64 v[40:41], v[40:41], 2, s[44:45]
	v_mul_f32_e32 v36, 0x3b800000, v36
	global_store_dword v[40:41], v36, off

.LBB0_862:
	s_or_b64 exec, exec, s[4:5]
	v_cmp_eq_u32_e32 vcc, s19, v102
	s_and_saveexec_b64 s[4:5], vcc
	v_mov_b32_e32 v1, s38
	ds_write_b32 v1, v178
	s_or_b64 exec, exec, s[4:5]
	s_lshl_b32 s4, s74, 8
	s_add_i32 s30, s4, s51
	s_mul_i32 s4, s30, 0x4800
	s_mul_hi_i32 s5, s30, 0x4800
	s_add_u32 s4, s69, s4
	s_mul_i32 s10, s74, 0x240000
	s_addc_u32 s5, s70, s5
	s_lshl_b64 s[6:7], s[10:11], 1
	s_add_u32 s64, s12, s6
	s_addc_u32 s65, s13, s7
	v_lshlrev_b32_e32 v1, 3, v102
	s_add_u32 s6, s24, s6
	v_and_b32_e32 v1, 0x78, v1
	s_addc_u32 s7, s25, s7
	v_lshlrev_b32_e32 v180, 1, v1
	v_ashrrev_i32_e32 v1, 4, v102
	v_lshl_add_u64 v[4:5], s[6:7], 0, v[180:181]
	v_mad_i64_i32 v[6:7], s[6:7], v1, s39, 0
	v_lshl_add_u64 v[2:3], s[64:65], 0, v[180:181]
	v_lshlrev_b64 v[188:189], 1, v[6:7]
	v_lshl_add_u64 v[6:7], v[2:3], 0, v[188:189]
	v_lshl_add_u64 v[8:9], v[4:5], 0, v[188:189]
	global_load_dwordx4 v[50:53], v[6:7], off
	global_load_dwordx4 v[54:57], v[8:9], off
	v_add_u32_e32 v6, 0x200, v102
	v_ashrrev_i32_e32 v10, 4, v6
	v_mad_i64_i32 v[6:7], s[6:7], v10, s39, 0
	v_lshlrev_b64 v[190:191], 1, v[6:7]
	v_lshl_add_u64 v[6:7], v[2:3], 0, v[190:191]
	v_lshl_add_u64 v[8:9], v[4:5], 0, v[190:191]
	global_load_dwordx4 v[58:61], v[6:7], off
	global_load_dwordx4 v[62:65], v[8:9], off
	s_ashr_i32 s76, s8, 1
	v_and_b32_e32 v202, 15, v102
	v_lshlrev_b32_e32 v6, 4, v102
	s_and_b32 s10, s76, 0xffffffe0
	v_and_b32_e32 v192, 48, v102
	v_mov_b32_e32 v193, v181
	v_and_b32_e32 v6, 0xf0, v6
	v_lshl_add_u64 v[2:3], v[2:3], 0, s[16:17]
	v_or_b32_e32 v186, s10, v202
	s_add_i32 s6, s10, s30
	v_mul_lo_u32 v203, v1, s40
	v_add_u32_e32 v204, 0, v6
	v_mul_lo_u32 v205, v10, s40
	v_lshl_add_u64 v[18:19], s[4:5], 0, v[192:193]
	v_lshl_add_u64 v[20:21], v[2:3], 0, v[188:189]
	v_lshl_add_u64 v[26:27], v[2:3], 0, v[190:191]
	v_lshl_add_u64 v[2:3], v[4:5], 0, s[16:17]
	v_or_b32_e32 v184, 16, v186
	v_or_b32_e32 v68, s6, v202
	v_bfe_u32 v103, v102, 4, 2
	v_add_u32_e32 v1, v204, v203
	v_add_u32_e32 v71, v204, v205
	v_mad_i64_i32 v[14:15], s[4:5], v186, s18, v[18:19]
	v_lshl_add_u64 v[22:23], v[2:3], 0, v[188:189]
	v_lshl_add_u64 v[30:31], v[2:3], 0, v[190:191]
	v_mad_i64_i32 v[42:43], s[4:5], v184, s18, v[18:19]
	v_or_b32_e32 v70, 16, v68
	v_mov_b32_e32 v67, v181
	v_lshlrev_b32_e32 v66, 14, v103
	global_load_dwordx4 v[2:5], v[14:15], off
	global_load_dwordx4 v[6:9], v[14:15], off offset:64
	global_load_dwordx4 v[10:13], v[14:15], off offset:128
	global_load_dwordx4 v[14:17], v[14:15], off offset:192
	global_load_dwordx4 v[18:21], v[20:21], off
	global_load_dwordx4 v[22:25], v[22:23], off
	global_load_dwordx4 v[26:29], v[26:27], off
	global_load_dwordx4 v[46:49], v[30:31], off
	v_ashrrev_i32_e32 v69, 31, v68
	global_load_dwordx4 v[30:33], v[42:43], off
	global_load_dwordx4 v[34:37], v[42:43], off offset:64
	global_load_dwordx4 v[38:41], v[42:43], off offset:128
	global_load_dwordx4 v[42:45], v[42:43], off offset:192
	v_lshl_add_u64 v[68:69], v[68:69], 0, v[66:67]
	v_lshlrev_b64 v[68:69], 10, v[68:69]
	v_lshl_add_u64 v[68:69], s[26:27], 0, v[68:69]
	s_cmp_eq_u32 s74, 0
	s_waitcnt vmcnt(15)
	ds_write_b128 v1, v[50:53]
	s_waitcnt vmcnt(14)
	ds_write_b128 v1, v[54:57] offset:18432
	s_waitcnt vmcnt(13)
	ds_write_b128 v71, v[58:61]
	s_waitcnt vmcnt(12)
	ds_write_b128 v71, v[62:65] offset:18432
	v_ashrrev_i32_e32 v71, 31, v70
	v_lshl_add_u64 v[50:51], v[70:71], 0, v[66:67]
	v_lshlrev_b64 v[50:51], 10, v[50:51]
	v_lshl_add_u64 v[54:55], s[26:27], 0, v[50:51]
	s_waitcnt lgkmcnt(0)
	s_barrier
	global_load_dwordx4 v[58:61], v[68:69], off offset:48
	global_load_dwordx4 v[62:65], v[68:69], off offset:32
	global_load_dwordx4 v[74:77], v[68:69], off offset:16
	global_load_dwordx4 v[86:89], v[68:69], off
	global_load_dwordx4 v[50:53], v[54:55], off offset:48
	global_load_dwordx4 v[70:73], v[54:55], off offset:32
	global_load_dwordx4 v[82:85], v[54:55], off offset:16
	global_load_dwordx4 v[94:97], v[54:55], off
	global_load_dwordx4 v[54:57], v181, s[28:29] offset:48
	global_load_dwordx4 v[66:69], v181, s[28:29] offset:32
	global_load_dwordx4 v[78:81], v181, s[28:29] offset:16
	global_load_dwordx4 v[90:93], v181, s[28:29]
	s_cbranch_scc1 .LBB0_868
	s_waitcnt vmcnt(7)
	v_and_b32_e32 v53, 64, v200
	v_xor_b32_e32 v1, 16, v200
	v_add_u32_e32 v53, 64, v53
	v_cmp_lt_i32_e32 vcc, v1, v53
	s_waitcnt vmcnt(3)
	v_xor_b32_e32 v57, 32, v200
	v_mov_b32_e32 v100, v86
	v_cndmask_b32_e32 v1, v200, v1, vcc
	v_lshlrev_b32_e32 v1, 2, v1
	ds_bpermute_b32 v98, v1, v86
	ds_bpermute_b32 v99, v1, v94
	v_cmp_lt_i32_e32 vcc, v57, v53
	v_mov_b32_e32 v101, v94
	s_waitcnt lgkmcnt(0)
	v_pk_add_f32 v[98:99], v[100:101], v[98:99]
	v_cndmask_b32_e32 v1, v200, v57, vcc
	v_lshlrev_b32_e32 v1, 2, v1
	ds_bpermute_b32 v100, v1, v98
	ds_bpermute_b32 v101, v1, v99
	s_waitcnt lgkmcnt(0)
	v_pk_add_f32 v[98:99], v[98:99], v[100:101]
	s_waitcnt vmcnt(0)
	v_pk_add_f32 v[98:99], v[90:91], v[98:99] op_sel_hi:[0,1]
	v_cmp_nlg_f32_e32 vcc, s41, v99
	v_cmp_nlg_f32_e64 s[4:5], s41, v98
	s_nop 0
	v_cndmask_b32_e32 v101, v99, v178, vcc
	v_cndmask_b32_e64 v100, v98, v178, s[4:5]
	v_cndmask_b32_e64 v99, 0, -1, vcc
	v_cndmask_b32_e64 v98, 0, -1, s[4:5]
	s_cmp_lt_u32 s74, 2
	s_cbranch_scc1 .LBB0_869

.LBB0_904:
	s_add_i32 s4, s64, 2
	s_cmp_ge_u32 s4, s75
	s_cbranch_scc1 .LBB0_906
	s_waitcnt vmcnt(3)
	v_sub_co_u32_e64 v19, vcc, s64, 2
	v_mov_b32_e32 v18, s74
	v_lshrrev_b32_e32 v20, 2, v19
	v_cndmask_b32_e32 v18, v20, v18, vcc
	v_and_b32_e32 v19, 3, v19
	v_mov_b32_e32 v20, s4
	v_cndmask_b32_e32 v19, v19, v20, vcc
	v_lshlrev_b32_e32 v18, 8, v18
	v_lshlrev_b32_e32 v19, 6, v19
	v_add_u32_e32 v18, v18, v19
	s_waitcnt vmcnt(1)
	v_mad_i64_i32 v[26:27], s[4:5], v18, s18, v[196:197]
	v_mad_i64_i32 v[28:29], s[4:5], v18, s18, v[198:199]
	v_lshl_add_u64 v[18:19], v[26:27], 0, v[188:189]
	v_lshl_add_u64 v[22:23], v[28:29], 0, v[188:189]
	v_lshl_add_u64 v[26:27], v[26:27], 0, v[190:191]
	s_waitcnt vmcnt(0)
	v_lshl_add_u64 v[46:47], v[28:29], 0, v[190:191]
	global_load_dwordx4 v[18:21], v[18:19], off
	global_load_dwordx4 v[22:25], v[22:23], off
	global_load_dwordx4 v[26:29], v[26:27], off
	global_load_dwordx4 v[46:49], v[46:47], off

.LBB0_928:
	s_or_b64 exec, exec, s[4:5]
	s_lshr_b32 s4, s31, 1
	s_or_b32 s5, s4, s13
	s_lshl_b32 s64, s5, 7
	s_ashr_i32 s60, s58, 8
	s_or_b32 s6, s64, s51
	s_lshl_b32 s59, s4, 7
	s_add_i32 s4, s60, s10
	s_ashr_i32 s7, s6, 31
	s_mul_i32 s9, s6, 0x4800
	s_mul_hi_i32 s8, s6, 0x4800
	s_add_u32 s10, s96, s9
	s_addc_u32 s61, s97, s8
	s_lshl_b32 s8, s4, 7
	s_ashr_i32 s9, s8, 31
	s_lshl_b64 s[8:9], s[8:9], 1
	s_add_u32 s62, s10, s8
	s_addc_u32 s63, s61, s9
	s_cmp_eq_u32 s5, 0
	s_cselect_b32 s10, 2, 0
	s_lshl_b32 s61, s10, 6
	s_add_i32 s5, s64, s61
	s_mulk_i32 s5, 0x2400
	s_add_i32 s64, s5, 0xffee0000
	s_ashr_i32 s65, s64, 31
	s_lshl_b64 s[64:65], s[64:65], 1
	s_add_u32 s66, s25, s64
	s_addc_u32 s67, s26, s65
	s_add_u32 s64, s27, s64
	v_lshlrev_b32_e32 v2, 4, v3
	s_addc_u32 s65, s28, s65
	v_and_b32_e32 v180, 0xf0, v2
	v_add_u32_e32 v2, 0x200, v3
	v_lshl_add_u64 v[12:13], s[66:67], 0, v[180:181]
	v_lshl_add_u64 v[14:15], s[64:65], 0, v[180:181]
	v_ashrrev_i32_e32 v112, 4, v3
	v_ashrrev_i32_e32 v113, 4, v2
	v_mad_i64_i32 v[4:5], s[64:65], v112, s18, v[12:13]
	v_mad_i64_i32 v[8:9], s[64:65], v112, s18, v[14:15]
	v_mad_i64_i32 v[12:13], s[64:65], v113, s18, v[12:13]
	v_mad_i64_i32 v[16:17], s[64:65], v113, s18, v[14:15]
	global_load_dwordx4 v[4:7], v[4:5], off
	global_load_dwordx4 v[8:11], v[8:9], off
	global_load_dwordx4 v[12:15], v[12:13], off
	global_load_dwordx4 v[16:19], v[16:17], off
	v_and_b32_e32 v136, 48, v3
	v_mov_b32_e32 v137, v181
	s_waitcnt vmcnt(23)
	v_lshl_add_u64 v[20:21], s[62:63], 0, v[136:137]
	s_mov_b64 s[62:63], 0x3000
	s_lshr_b32 s58, s58, 1
	v_and_b32_e32 v110, 15, v3
	v_lshl_add_u64 v[20:21], v[20:21], 0, s[62:63]
	s_add_i32 s62, s5, 0xfff70000
	s_and_b32 s68, s58, 0x60
	s_ashr_i32 s63, s62, 31
	v_or_b32_e32 v144, s68, v110
	s_lshl_b64 s[62:63], s[62:63], 1
	s_waitcnt vmcnt(22)
	v_mad_u64_u32 v[22:23], s[64:65], v144, s18, v[20:21]
	s_add_u32 s64, s25, s62
	s_addc_u32 s65, s26, s63
	s_add_u32 s62, s27, s62
	s_addc_u32 s63, s28, s63
	v_lshl_add_u64 v[24:25], s[62:63], 0, v[180:181]
	v_readlane_b32 s72, v247, 22
	v_or_b32_e32 v137, 16, v144
	s_ashr_i32 s5, s4, 31
	s_waitcnt vmcnt(21)
	v_mad_i64_i32 v[26:27], s[62:63], v112, s18, v[24:25]
	v_mad_i64_i32 v[24:25], s[62:63], v113, s18, v[24:25]
	v_readlane_b32 s78, v247, 28
	v_readlane_b32 s79, v247, 29
	v_mad_u64_u32 v[20:21], s[66:67], v137, s18, v[20:21]
	s_lshl_b64 s[4:5], s[4:5], 2
	s_mov_b64 s[62:63], s[78:79]
	v_mul_lo_u32 v143, v112, s40
	v_add_u32_e32 v145, 0, v180
	global_load_dwordx4 v[34:37], v[22:23], off
	global_load_dwordx4 v[38:41], v[22:23], off offset:64
	global_load_dwordx4 v[42:45], v[22:23], off offset:128
	global_load_dwordx4 v[46:49], v[22:23], off offset:192
	global_load_dwordx4 v[50:53], v[20:21], off
	global_load_dwordx4 v[54:57], v[20:21], off offset:64
	global_load_dwordx4 v[58:61], v[20:21], off offset:128
	global_load_dwordx4 v[62:65], v[20:21], off offset:192
	v_lshl_add_u64 v[20:21], s[64:65], 0, v[180:181]
	s_add_u32 s4, s62, s4
	v_mul_lo_u32 v146, v113, s40
	v_add_u32_e32 v2, v145, v143
	v_mad_i64_i32 v[22:23], s[64:65], v112, s18, v[20:21]
	s_addc_u32 s5, s63, s5
	v_add_u32_e32 v28, v145, v146
	v_mad_i64_i32 v[20:21], s[64:65], v113, s18, v[20:21]
	global_load_dwordx4 v[74:77], v[22:23], off
	global_load_dwordx4 v[78:81], v[26:27], off
	global_load_dwordx4 v[82:85], v[20:21], off
	global_load_dwordx4 v[90:93], v[24:25], off
	s_mulk_i32 s60, 0x210
	v_mul_u32_u24_e32 v148, 0x120, v110
	v_lshlrev_b32_e32 v180, 4, v110
	s_mov_b32 s58, 0
	v_readlane_b32 s73, v247, 23
	v_readlane_b32 s74, v247, 24
	v_readlane_b32 s75, v247, 25
	v_readlane_b32 s76, v247, 26
	v_readlane_b32 s77, v247, 27
	v_readlane_b32 s80, v247, 30
	v_readlane_b32 s81, v247, 31
	v_readlane_b32 s82, v247, 32
	s_waitcnt vmcnt(15)
	ds_write_b128 v2, v[4:7]
	s_waitcnt vmcnt(14)
	ds_write_b128 v2, v[8:11] offset:18432
	s_waitcnt vmcnt(13)
	ds_write_b128 v28, v[12:15]
	s_waitcnt vmcnt(12)
	ds_write_b128 v28, v[16:19] offset:18432
	s_waitcnt lgkmcnt(0)
	s_barrier
	global_load_dword v114, v181, s[4:5]
	s_add_i32 s4, s60, 0
	s_add_i32 s5, s12, s59
	s_add_i32 s59, s4, 0x14000
	s_add_i32 s4, s5, s61
	v_bfe_u32 v8, v3, 2, 4
	s_mul_hi_u32 s5, s4, 0x4800
	s_mulk_i32 s4, 0x4800
	v_and_b32_e32 v147, 12, v8
	s_add_u32 s4, s29, s4
	v_and_b32_e32 v6, 63, v3
	v_sub_u32_e32 v111, v144, v147
	s_addc_u32 s5, s30, s5
	v_lshlrev_b32_e32 v7, 3, v3
	v_mov_b32_e32 v4, v181
	v_mov_b32_e32 v5, v181
	v_cmp_gt_u32_e32 vcc, 16, v6
	v_subrev_u32_e32 v151, s61, v111
	v_mov_b64_e32 v[110:111], s[4:5]
	v_mov_b32_e32 v2, v181
	v_mov_b32_e32 v3, v181
	v_cndmask_b32_e64 v134, 0, 1.0, vcc
	v_mul_u32_u24_e32 v149, 0x120, v8
	v_and_b32_e32 v150, 24, v7
	v_mov_b64_e32 v[8:9], v[4:5]
	v_mov_b64_e32 v[12:13], v[4:5]
	v_mov_b64_e32 v[16:17], v[4:5]
	v_mov_b64_e32 v[20:21], v[4:5]
	v_mov_b64_e32 v[24:25], v[4:5]
	v_mov_b64_e32 v[28:29], v[4:5]
	v_mov_b64_e32 v[32:33], v[4:5]
	v_mov_b64_e32 v[68:69], v[4:5]
	v_mov_b64_e32 v[72:73], v[4:5]
	v_mov_b64_e32 v[88:89], v[4:5]
	v_mov_b64_e32 v[96:97], v[4:5]
	v_mov_b64_e32 v[100:101], v[4:5]
	v_mov_b64_e32 v[104:105], v[4:5]
	v_mov_b64_e32 v[108:109], v[4:5]
	v_mad_i64_i32 v[138:139], s[4:5], v112, s18, v[110:111]
	v_mad_i64_i32 v[140:141], s[4:5], v113, s18, v[110:111]
	v_mov_b64_e32 v[112:113], v[4:5]
	v_mov_b64_e32 v[6:7], v[2:3]
	v_mov_b64_e32 v[10:11], v[2:3]
	v_mov_b64_e32 v[14:15], v[2:3]
	v_mov_b64_e32 v[18:19], v[2:3]
	v_mov_b64_e32 v[22:23], v[2:3]
	v_mov_b64_e32 v[26:27], v[2:3]
	v_mov_b64_e32 v[30:31], v[2:3]
	v_mov_b64_e32 v[66:67], v[2:3]
	v_mov_b64_e32 v[70:71], v[2:3]
	v_mov_b64_e32 v[86:87], v[2:3]
	v_mov_b64_e32 v[94:95], v[2:3]
	v_mov_b64_e32 v[98:99], v[2:3]
	v_mov_b64_e32 v[102:103], v[2:3]
	v_mov_b64_e32 v[106:107], v[2:3]
	v_mov_b32_e32 v135, v134
	s_sub_i32 s60, s68, s61
	s_or_b32 s61, s61, 0xffffff40
	v_mov_b64_e32 v[110:111], v[2:3]
	v_readlane_b32 s83, v247, 33
	v_readlane_b32 s84, v247, 34
	v_readlane_b32 s85, v247, 35
	v_readlane_b32 s86, v247, 36
	v_readlane_b32 s87, v247, 37
	s_waitcnt vmcnt(0)
	v_mul_f32_e32 v153, 0x3fb8aa3b, v114
	v_mov_b32_e32 v152, v153
	s_add_i32 s62, s10, 1
	s_cmp_eq_u32 s61, s58
	s_cbranch_scc0 .LBB0_931

.LBB0_932:
	s_waitcnt vmcnt(3)
	v_lshl_add_u64 v[74:75], v[138:139], 0, v[180:181]
	s_waitcnt vmcnt(2)
	v_add_co_u32_e32 v78, vcc, 0x32804000, v74
	s_waitcnt vmcnt(1)
	v_lshl_add_u64 v[82:83], v[140:141], 0, v[180:181]
	v_addc_co_u32_e32 v79, vcc, 0, v75, vcc
	s_waitcnt vmcnt(0)
	v_add_co_u32_e32 v90, vcc, 0x32804000, v82
	global_load_dwordx4 v[74:77], v[78:79], off
	global_load_dwordx4 v[78:81], v[78:79], off offset:1024
	v_addc_co_u32_e32 v91, vcc, 0, v83, vcc
	global_load_dwordx4 v[82:85], v[90:91], off
	global_load_dwordx4 v[90:93], v[90:91], off offset:1024
	s_add_i32 s4, s60, s58
	s_addk_i32 s4, 0x80
	s_cmpk_gt_u32 s4, 0xbe
	s_cbranch_scc1 .LBB0_936

.LBB0_1092:
	s_waitcnt vmcnt(0) lgkmcnt(0)
	s_barrier
	ds_read_b32 v136, v163 offset:10240
	s_and_saveexec_b64 s[6:7], s[4:5]
	s_cbranch_execz .LBB0_1094
	v_lshlrev_b64 v[130:131], 6, v[130:131]
	v_lshl_add_u64 v[130:131], s[12:13], 0, v[130:131]
	global_load_dword v133, v[130:131], off sc1
	global_load_dword v138, v[130:131], off offset:4 sc1
	global_load_dword v139, v[130:131], off offset:8 sc1
	global_load_dword v140, v[130:131], off offset:12 sc1
	global_load_dword v141, v[130:131], off offset:16 sc1
	global_load_dword v142, v[130:131], off offset:20 sc1
	global_load_dword v143, v[130:131], off offset:24 sc1
	global_load_dword v144, v[130:131], off offset:28 sc1
	global_load_dword v145, v[130:131], off offset:32 sc1
	global_load_dword v146, v[130:131], off offset:36 sc1
	global_load_dword v147, v[130:131], off offset:40 sc1
	global_load_dword v148, v[130:131], off offset:44 sc1
	global_load_dword v149, v[130:131], off offset:48 sc1
	global_load_dword v150, v[130:131], off offset:52 sc1
	global_load_dword v151, v[130:131], off offset:56 sc1
	global_load_dword v130, v[130:131], off offset:60 sc1
	s_mov_b32 s4, 0xf800000
	s_waitcnt vmcnt(15)
	v_add_f32_e32 v131, 0, v133
	s_waitcnt vmcnt(14)
	v_add_f32_e32 v131, v131, v138
	s_waitcnt vmcnt(13)
	v_add_f32_e32 v131, v131, v139
	s_waitcnt vmcnt(12)
	v_add_f32_e32 v131, v131, v140
	s_waitcnt vmcnt(11)
	v_add_f32_e32 v131, v131, v141
	s_waitcnt vmcnt(10)
	v_add_f32_e32 v131, v131, v142
	s_waitcnt vmcnt(9)
	v_add_f32_e32 v131, v131, v143
	s_waitcnt vmcnt(8)
	v_add_f32_e32 v131, v131, v144
	s_waitcnt vmcnt(7)
	v_add_f32_e32 v131, v131, v145
	s_waitcnt vmcnt(6)
	v_add_f32_e32 v131, v131, v146
	s_waitcnt vmcnt(5)
	v_add_f32_e32 v131, v131, v147
	s_waitcnt vmcnt(4)
	v_add_f32_e32 v131, v131, v148
	s_waitcnt vmcnt(3)
	v_add_f32_e32 v131, v131, v149
	s_waitcnt vmcnt(2)
	v_add_f32_e32 v131, v131, v150
	s_waitcnt vmcnt(1)
	v_add_f32_e32 v131, v131, v151
	s_waitcnt vmcnt(0)
	v_add_f32_e32 v130, v131, v130
	v_fmamk_f32 v130, v130, 0x39800000, v181
	v_mul_f32_e32 v131, 0x4f800000, v130
	v_cmp_gt_f32_e32 vcc, s4, v130
	s_nop 1
	v_cndmask_b32_e32 v130, v130, v131, vcc
	v_sqrt_f32_e32 v131, v130
	s_nop 0
	v_add_u32_e32 v133, -1, v131
	v_add_u32_e32 v138, 1, v131
	v_fma_f32 v139, -v133, v131, v130
	v_fma_f32 v140, -v138, v131, v130
	v_cmp_ge_f32_e64 s[4:5], 0, v139
	s_nop 1
	v_cndmask_b32_e64 v131, v131, v133, s[4:5]
	v_cmp_lt_f32_e64 s[4:5], 0, v140
	s_nop 1
	v_cndmask_b32_e64 v131, v131, v138, s[4:5]
	v_mul_f32_e32 v133, 0x37800000, v131
	v_cndmask_b32_e32 v131, v131, v133, vcc
	v_cmp_class_f32_e32 vcc, v130, v182
	s_nop 1
	v_cndmask_b32_e32 v130, v131, v130, vcc
	v_div_scale_f32 v131, s[4:5], v130, v130, 1.0
	v_rcp_f32_e32 v133, v131
	v_div_scale_f32 v138, vcc, 1.0, v130, 1.0
	v_fma_f32 v139, -v131, v133, 1.0
	v_fmac_f32_e32 v133, v139, v133
	v_mul_f32_e32 v139, v138, v133
	v_fma_f32 v140, -v131, v139, v138
	v_fmac_f32_e32 v139, v140, v133
	v_fma_f32 v131, -v131, v139, v138
	v_div_fmas_f32 v131, v131, v133, v139
	v_div_fixup_f32 v130, v131, v130, 1.0
	v_lshl_add_u32 v131, v132, 2, 0
	ds_write_b32 v131, v130 offset:8192

.LBB0_1176:
	v_lshl_add_u32 v136, s34, 8, v1
	v_lshl_or_b32 v130, s62, 8, v183
	v_readlane_b32 s36, v247, 2
	v_ashrrev_i32_e32 v131, 31, v130
	v_ashrrev_i32_e32 v137, 31, v136
	v_readlane_b32 s38, v247, 4
	v_readlane_b32 s39, v247, 5
	v_readlane_b32 s22, v246, 3
	v_lshlrev_b64 v[132:133], 14, v[136:137]
	s_mov_b64 s[18:19], s[38:39]
	v_lshlrev_b64 v[134:135], 2, v[130:131]
	v_readlane_b32 s23, v246, 4
	v_lshl_add_u64 v[132:133], s[18:19], 0, v[132:133]
	v_lshl_add_u64 v[132:133], v[132:133], 0, v[134:135]
	v_lshl_add_u64 v[130:131], s[22:23], 0, v[134:135]
	global_load_dwordx4 v[138:141], v[130:131], off
	global_load_dwordx4 v[142:145], v[132:133], off
	v_cvt_f32_i32_e32 v147, v127
	v_cvt_f32_i32_e32 v146, v126
	v_cvt_f32_i32_e32 v149, v129
	v_cvt_f32_i32_e32 v148, v128
	global_load_dwordx4 v[126:129], v[132:133], off offset:64
	v_cvt_f32_i32_e32 v123, v123
	v_cvt_f32_i32_e32 v125, v125
	v_cvt_f32_i32_e32 v124, v124
	v_cvt_f32_i32_e32 v122, v122
	v_cvt_f32_i32_e32 v115, v115
	v_cvt_f32_i32_e32 v114, v114
	v_cvt_f32_i32_e32 v117, v117
	v_cvt_f32_i32_e32 v116, v116
	v_cvt_f32_i32_e32 v107, v107
	v_cvt_f32_i32_e32 v109, v109
	v_cvt_f32_i32_e32 v108, v108
	v_cvt_f32_i32_e32 v106, v106
	v_cvt_f32_i32_e32 v99, v99
	v_cvt_f32_i32_e32 v98, v98
	v_cvt_f32_i32_e32 v101, v101
	v_cvt_f32_i32_e32 v100, v100
	v_cvt_f32_i32_e32 v91, v91
	v_cvt_f32_i32_e32 v93, v93
	v_cvt_f32_i32_e32 v92, v92
	v_cvt_f32_i32_e32 v90, v90
	v_cvt_f32_i32_e32 v83, v83
	v_cvt_f32_i32_e32 v82, v82
	v_cvt_f32_i32_e32 v85, v85
	v_cvt_f32_i32_e32 v84, v84
	v_cvt_f32_i32_e32 v75, v75
	v_cvt_f32_i32_e32 v77, v77
	v_cvt_f32_i32_e32 v76, v76
	v_cvt_f32_i32_e32 v74, v74
	v_cvt_f32_i32_e32 v67, v67
	v_cvt_f32_i32_e32 v69, v69
	v_cvt_f32_i32_e32 v68, v68
	v_cvt_f32_i32_e32 v66, v66
	v_cvt_f32_i32_e32 v55, v55
	v_cvt_f32_i32_e32 v57, v57
	v_cvt_f32_i32_e32 v56, v56
	v_cvt_f32_i32_e32 v54, v54
	v_cvt_f32_i32_e32 v51, v51
	v_cvt_f32_i32_e32 v53, v53
	v_cvt_f32_i32_e32 v52, v52
	v_cvt_f32_i32_e32 v50, v50
	v_cvt_f32_i32_e32 v39, v39
	v_cvt_f32_i32_e32 v41, v41
	v_cvt_f32_i32_e32 v40, v40
	v_cvt_f32_i32_e32 v38, v38
	v_cvt_f32_i32_e32 v35, v35
	v_cvt_f32_i32_e32 v37, v37
	v_cvt_f32_i32_e32 v36, v36
	v_cvt_f32_i32_e32 v34, v34
	v_cvt_f32_i32_e32 v23, v23
	v_cvt_f32_i32_e32 v25, v25
	v_cvt_f32_i32_e32 v24, v24
	v_cvt_f32_i32_e32 v22, v22
	v_cvt_f32_i32_e32 v19, v19
	v_cvt_f32_i32_e32 v21, v21
	v_cvt_f32_i32_e32 v20, v20
	v_cvt_f32_i32_e32 v18, v18
	v_cvt_f32_i32_e32 v7, v7
	v_cvt_f32_i32_e32 v9, v9
	v_cvt_f32_i32_e32 v8, v8
	v_cvt_f32_i32_e32 v6, v6
	v_cvt_f32_i32_e32 v3, v3
	v_cvt_f32_i32_e32 v5, v5
	v_cvt_f32_i32_e32 v4, v4
	v_cvt_f32_i32_e32 v2, v2
	v_readlane_b32 s37, v247, 3
	s_waitcnt vmcnt(0)
	v_pk_mul_f32 v[140:141], v[140:141], s[14:15] op_sel_hi:[1,0]
	v_pk_mul_f32 v[138:139], v[138:139], s[14:15] op_sel_hi:[1,0]
	v_pk_fma_f32 v[140:141], v[140:141], v[148:149], v[144:145]
	v_pk_fma_f32 v[138:139], v[138:139], v[146:147], v[142:143]
	global_store_dwordx4 v[132:133], v[138:141], off
	global_load_dwordx4 v[138:141], v[130:131], off offset:64
	s_waitcnt vmcnt(0)
	v_pk_mul_f32 v[140:141], v[140:141], s[14:15] op_sel_hi:[1,0]
	v_pk_mul_f32 v[138:139], v[138:139], s[14:15] op_sel_hi:[1,0]
	v_pk_fma_f32 v[124:125], v[140:141], v[124:125], v[128:129]
	v_pk_fma_f32 v[122:123], v[138:139], v[122:123], v[126:127]
	global_store_dwordx4 v[132:133], v[122:125], off offset:64
	global_load_dwordx4 v[122:125], v[130:131], off offset:512
	global_load_dwordx4 v[126:129], v[132:133], off offset:512
	v_cvt_f32_i32_e32 v139, v119
	v_cvt_f32_i32_e32 v138, v118
	v_cvt_f32_i32_e32 v141, v121
	v_cvt_f32_i32_e32 v140, v120
	global_load_dwordx4 v[118:121], v[132:133], off offset:576
	s_waitcnt vmcnt(2)
	v_pk_mul_f32 v[124:125], v[124:125], s[14:15] op_sel_hi:[1,0]
	v_pk_mul_f32 v[122:123], v[122:123], s[14:15] op_sel_hi:[1,0]
	s_waitcnt vmcnt(1)
	v_pk_fma_f32 v[124:125], v[124:125], v[140:141], v[128:129]
	v_pk_fma_f32 v[122:123], v[122:123], v[138:139], v[126:127]
	global_store_dwordx4 v[132:133], v[122:125], off offset:512
	global_load_dwordx4 v[122:125], v[130:131], off offset:576
	v_or_b32_e32 v126, 16, v136
	v_ashrrev_i32_e32 v127, 31, v126
	v_lshlrev_b64 v[126:127], 14, v[126:127]
	v_lshl_add_u64 v[126:127], s[18:19], 0, v[126:127]
	s_waitcnt vmcnt(0)
	v_pk_mul_f32 v[124:125], v[124:125], s[14:15] op_sel_hi:[1,0]
	v_pk_mul_f32 v[122:123], v[122:123], s[14:15] op_sel_hi:[1,0]
	v_pk_fma_f32 v[116:117], v[124:125], v[116:117], v[120:121]
	v_pk_fma_f32 v[114:115], v[122:123], v[114:115], v[118:119]
	global_store_dwordx4 v[132:133], v[114:117], off offset:576
	global_load_dwordx4 v[114:117], v[130:131], off
	v_lshl_add_u64 v[122:123], v[126:127], 0, v[134:135]
	global_load_dwordx4 v[118:121], v[122:123], off
	v_cvt_f32_i32_e32 v125, v111
	v_cvt_f32_i32_e32 v124, v110
	v_cvt_f32_i32_e32 v127, v113
	v_cvt_f32_i32_e32 v126, v112
	global_load_dwordx4 v[110:113], v[122:123], off offset:64
	s_waitcnt vmcnt(2)
	v_pk_mul_f32 v[116:117], v[116:117], s[14:15] op_sel_hi:[1,0]
	v_pk_mul_f32 v[114:115], v[114:115], s[14:15] op_sel_hi:[1,0]
	s_waitcnt vmcnt(1)
	v_pk_fma_f32 v[116:117], v[116:117], v[126:127], v[120:121]
	v_pk_fma_f32 v[114:115], v[114:115], v[124:125], v[118:119]
	global_store_dwordx4 v[122:123], v[114:117], off
	global_load_dwordx4 v[114:117], v[130:131], off offset:64
	s_waitcnt vmcnt(0)
	v_pk_mul_f32 v[116:117], v[116:117], s[14:15] op_sel_hi:[1,0]
	v_pk_mul_f32 v[114:115], v[114:115], s[14:15] op_sel_hi:[1,0]
	v_pk_fma_f32 v[108:109], v[116:117], v[108:109], v[112:113]
	v_pk_fma_f32 v[106:107], v[114:115], v[106:107], v[110:111]
	global_store_dwordx4 v[122:123], v[106:109], off offset:64
	global_load_dwordx4 v[106:109], v[130:131], off offset:512
	global_load_dwordx4 v[110:113], v[122:123], off offset:512
	v_cvt_f32_i32_e32 v115, v103
	v_cvt_f32_i32_e32 v114, v102
	v_cvt_f32_i32_e32 v117, v105
	v_cvt_f32_i32_e32 v116, v104
	global_load_dwordx4 v[102:105], v[122:123], off offset:576
	s_waitcnt vmcnt(2)
	v_pk_mul_f32 v[108:109], v[108:109], s[14:15] op_sel_hi:[1,0]
	v_pk_mul_f32 v[106:107], v[106:107], s[14:15] op_sel_hi:[1,0]
	s_waitcnt vmcnt(1)
	v_pk_fma_f32 v[108:109], v[108:109], v[116:117], v[112:113]
	v_pk_fma_f32 v[106:107], v[106:107], v[114:115], v[110:111]
	global_store_dwordx4 v[122:123], v[106:109], off offset:512
	global_load_dwordx4 v[106:109], v[130:131], off offset:576
	v_or_b32_e32 v110, 32, v136
	v_ashrrev_i32_e32 v111, 31, v110
	v_lshlrev_b64 v[110:111], 14, v[110:111]
	v_lshl_add_u64 v[110:111], s[18:19], 0, v[110:111]
	s_waitcnt vmcnt(0)
	v_pk_mul_f32 v[108:109], v[108:109], s[14:15] op_sel_hi:[1,0]
	v_pk_mul_f32 v[106:107], v[106:107], s[14:15] op_sel_hi:[1,0]
	v_pk_fma_f32 v[100:101], v[108:109], v[100:101], v[104:105]
	v_pk_fma_f32 v[98:99], v[106:107], v[98:99], v[102:103]
	global_store_dwordx4 v[122:123], v[98:101], off offset:576
	global_load_dwordx4 v[98:101], v[130:131], off
	v_lshl_add_u64 v[106:107], v[110:111], 0, v[134:135]
	global_load_dwordx4 v[102:105], v[106:107], off
	v_cvt_f32_i32_e32 v109, v95
	v_cvt_f32_i32_e32 v108, v94
	v_cvt_f32_i32_e32 v111, v97
	v_cvt_f32_i32_e32 v110, v96
	global_load_dwordx4 v[94:97], v[106:107], off offset:64
	s_waitcnt vmcnt(2)
	v_pk_mul_f32 v[100:101], v[100:101], s[14:15] op_sel_hi:[1,0]
	v_pk_mul_f32 v[98:99], v[98:99], s[14:15] op_sel_hi:[1,0]
	s_waitcnt vmcnt(1)
	v_pk_fma_f32 v[100:101], v[100:101], v[110:111], v[104:105]
	v_pk_fma_f32 v[98:99], v[98:99], v[108:109], v[102:103]
	global_store_dwordx4 v[106:107], v[98:101], off
	global_load_dwordx4 v[98:101], v[130:131], off offset:64
	s_waitcnt vmcnt(0)
	v_pk_mul_f32 v[100:101], v[100:101], s[14:15] op_sel_hi:[1,0]
	v_pk_mul_f32 v[98:99], v[98:99], s[14:15] op_sel_hi:[1,0]
	v_pk_fma_f32 v[92:93], v[100:101], v[92:93], v[96:97]
	v_pk_fma_f32 v[90:91], v[98:99], v[90:91], v[94:95]
	global_store_dwordx4 v[106:107], v[90:93], off offset:64
	global_load_dwordx4 v[90:93], v[130:131], off offset:512
	global_load_dwordx4 v[94:97], v[106:107], off offset:512
	v_cvt_f32_i32_e32 v99, v87
	v_cvt_f32_i32_e32 v98, v86
	v_cvt_f32_i32_e32 v101, v89
	v_cvt_f32_i32_e32 v100, v88
	global_load_dwordx4 v[86:89], v[106:107], off offset:576
	s_waitcnt vmcnt(2)
	v_pk_mul_f32 v[92:93], v[92:93], s[14:15] op_sel_hi:[1,0]
	v_pk_mul_f32 v[90:91], v[90:91], s[14:15] op_sel_hi:[1,0]
	s_waitcnt vmcnt(1)
	v_pk_fma_f32 v[92:93], v[92:93], v[100:101], v[96:97]
	v_pk_fma_f32 v[90:91], v[90:91], v[98:99], v[94:95]
	global_store_dwordx4 v[106:107], v[90:93], off offset:512
	global_load_dwordx4 v[90:93], v[130:131], off offset:576
	v_or_b32_e32 v94, 48, v136
	v_ashrrev_i32_e32 v95, 31, v94
	v_lshlrev_b64 v[94:95], 14, v[94:95]
	v_lshl_add_u64 v[94:95], s[18:19], 0, v[94:95]
	s_mov_b32 s18, 0x200000
	s_waitcnt vmcnt(0)
	v_pk_mul_f32 v[92:93], v[92:93], s[14:15] op_sel_hi:[1,0]
	v_pk_mul_f32 v[90:91], v[90:91], s[14:15] op_sel_hi:[1,0]
	v_pk_fma_f32 v[84:85], v[92:93], v[84:85], v[88:89]
	v_pk_fma_f32 v[82:83], v[90:91], v[82:83], v[86:87]
	global_store_dwordx4 v[106:107], v[82:85], off offset:576
	global_load_dwordx4 v[82:85], v[130:131], off
	v_lshl_add_u64 v[90:91], v[94:95], 0, v[134:135]
	global_load_dwordx4 v[86:89], v[90:91], off
	v_cvt_f32_i32_e32 v93, v79
	v_cvt_f32_i32_e32 v92, v78
	v_cvt_f32_i32_e32 v95, v81
	v_cvt_f32_i32_e32 v94, v80
	global_load_dwordx4 v[78:81], v[90:91], off offset:64
	s_waitcnt vmcnt(2)
	v_pk_mul_f32 v[84:85], v[84:85], s[14:15] op_sel_hi:[1,0]
	v_pk_mul_f32 v[82:83], v[82:83], s[14:15] op_sel_hi:[1,0]
	s_waitcnt vmcnt(1)
	v_pk_fma_f32 v[84:85], v[84:85], v[94:95], v[88:89]
	v_pk_fma_f32 v[82:83], v[82:83], v[92:93], v[86:87]
	global_store_dwordx4 v[90:91], v[82:85], off
	global_load_dwordx4 v[82:85], v[130:131], off offset:64
	s_waitcnt vmcnt(0)
	v_pk_mul_f32 v[84:85], v[84:85], s[14:15] op_sel_hi:[1,0]
	v_pk_mul_f32 v[82:83], v[82:83], s[14:15] op_sel_hi:[1,0]
	v_pk_fma_f32 v[76:77], v[84:85], v[76:77], v[80:81]
	v_pk_fma_f32 v[74:75], v[82:83], v[74:75], v[78:79]
	global_store_dwordx4 v[90:91], v[74:77], off offset:64
	global_load_dwordx4 v[74:77], v[130:131], off offset:512
	global_load_dwordx4 v[78:81], v[90:91], off offset:512
	v_cvt_f32_i32_e32 v83, v71
	v_cvt_f32_i32_e32 v82, v70
	v_cvt_f32_i32_e32 v85, v73
	v_cvt_f32_i32_e32 v84, v72
	global_load_dwordx4 v[70:73], v[90:91], off offset:576
	s_waitcnt vmcnt(2)
	v_pk_mul_f32 v[76:77], v[76:77], s[14:15] op_sel_hi:[1,0]
	v_pk_mul_f32 v[74:75], v[74:75], s[14:15] op_sel_hi:[1,0]
	s_waitcnt vmcnt(1)
	v_pk_fma_f32 v[76:77], v[76:77], v[84:85], v[80:81]
	v_pk_fma_f32 v[74:75], v[74:75], v[82:83], v[78:79]
	global_store_dwordx4 v[90:91], v[74:77], off offset:512
	global_load_dwordx4 v[74:77], v[130:131], off offset:576
	v_cvt_f32_i32_e32 v79, v65
	v_cvt_f32_i32_e32 v78, v64
	s_waitcnt vmcnt(0)
	v_pk_mul_f32 v[76:77], v[76:77], s[14:15] op_sel_hi:[1,0]
	v_pk_mul_f32 v[74:75], v[74:75], s[14:15] op_sel_hi:[1,0]
	v_pk_fma_f32 v[68:69], v[76:77], v[68:69], v[72:73]
	v_pk_fma_f32 v[66:67], v[74:75], v[66:67], v[70:71]
	global_store_dwordx4 v[90:91], v[66:69], off offset:576
	v_add_co_u32_e32 v74, vcc, s18, v132
	global_load_dwordx4 v[66:69], v[130:131], off
	s_nop 0
	v_addc_co_u32_e32 v75, vcc, 0, v133, vcc
	global_load_dwordx4 v[70:73], v[74:75], off
	v_cvt_f32_i32_e32 v77, v63
	v_cvt_f32_i32_e32 v76, v62
	s_mov_b64 s[18:19], 0x200000
	v_lshl_add_u64 v[80:81], v[132:133], 0, s[18:19]
	global_load_dwordx4 v[62:65], v[80:81], off offset:576
	s_mov_b64 s[18:19], 0x240000
	s_waitcnt vmcnt(2)
	v_pk_mul_f32 v[68:69], v[68:69], s[14:15] op_sel_hi:[1,0]
	v_pk_mul_f32 v[66:67], v[66:67], s[14:15] op_sel_hi:[1,0]
	s_waitcnt vmcnt(1)
	v_pk_fma_f32 v[68:69], v[68:69], v[78:79], v[72:73]
	v_pk_fma_f32 v[66:67], v[66:67], v[76:77], v[70:71]
	global_store_dwordx4 v[74:75], v[66:69], off
	global_load_dwordx4 v[66:69], v[130:131], off offset:64
	global_load_dwordx4 v[70:73], v[80:81], off offset:64
	v_cvt_f32_i32_e32 v75, v59
	v_cvt_f32_i32_e32 v74, v58
	v_cvt_f32_i32_e32 v77, v61
	v_cvt_f32_i32_e32 v76, v60
	global_load_dwordx4 v[58:61], v[80:81], off offset:512
	s_waitcnt vmcnt(2)
	v_pk_mul_f32 v[68:69], v[68:69], s[14:15] op_sel_hi:[1,0]
	v_pk_mul_f32 v[66:67], v[66:67], s[14:15] op_sel_hi:[1,0]
	s_waitcnt vmcnt(1)
	v_pk_fma_f32 v[68:69], v[68:69], v[76:77], v[72:73]
	v_pk_fma_f32 v[66:67], v[66:67], v[74:75], v[70:71]
	global_store_dwordx4 v[80:81], v[66:69], off offset:64
	global_load_dwordx4 v[66:69], v[130:131], off offset:512
	s_waitcnt vmcnt(0)
	v_pk_mul_f32 v[68:69], v[68:69], s[14:15] op_sel_hi:[1,0]
	v_pk_mul_f32 v[66:67], v[66:67], s[14:15] op_sel_hi:[1,0]
	v_pk_fma_f32 v[56:57], v[68:69], v[56:57], v[60:61]
	v_pk_fma_f32 v[54:55], v[66:67], v[54:55], v[58:59]
	global_store_dwordx4 v[80:81], v[54:57], off offset:512
	global_load_dwordx4 v[54:57], v[130:131], off offset:576
	v_add_co_u32_e32 v58, vcc, s59, v132
	v_cvt_f32_i32_e32 v61, v47
	s_nop 0
	v_addc_co_u32_e32 v59, vcc, 0, v133, vcc
	v_cvt_f32_i32_e32 v60, v46
	s_waitcnt vmcnt(0)
	v_pk_mul_f32 v[56:57], v[56:57], s[14:15] op_sel_hi:[1,0]
	v_pk_mul_f32 v[54:55], v[54:55], s[14:15] op_sel_hi:[1,0]
	v_pk_fma_f32 v[52:53], v[56:57], v[52:53], v[64:65]
	v_pk_fma_f32 v[50:51], v[54:55], v[50:51], v[62:63]
	global_store_dwordx4 v[80:81], v[50:53], off offset:576
	global_load_dwordx4 v[50:53], v[130:131], off
	global_load_dwordx4 v[54:57], v[58:59], off
	v_cvt_f32_i32_e32 v63, v49
	v_cvt_f32_i32_e32 v62, v48
	v_lshl_add_u64 v[64:65], v[132:133], 0, s[18:19]
	global_load_dwordx4 v[46:49], v[64:65], off offset:576
	s_waitcnt vmcnt(2)
	v_pk_mul_f32 v[52:53], v[52:53], s[14:15] op_sel_hi:[1,0]
	v_pk_mul_f32 v[50:51], v[50:51], s[14:15] op_sel_hi:[1,0]
	s_waitcnt vmcnt(1)
	v_pk_fma_f32 v[52:53], v[52:53], v[62:63], v[56:57]
	v_pk_fma_f32 v[50:51], v[50:51], v[60:61], v[54:55]
	global_store_dwordx4 v[58:59], v[50:53], off
	global_load_dwordx4 v[50:53], v[130:131], off offset:64
	global_load_dwordx4 v[54:57], v[64:65], off offset:64
	v_cvt_f32_i32_e32 v59, v43
	v_cvt_f32_i32_e32 v58, v42
	v_cvt_f32_i32_e32 v61, v45
	v_cvt_f32_i32_e32 v60, v44
	global_load_dwordx4 v[42:45], v[64:65], off offset:512
	s_waitcnt vmcnt(2)
	v_pk_mul_f32 v[52:53], v[52:53], s[14:15] op_sel_hi:[1,0]
	v_pk_mul_f32 v[50:51], v[50:51], s[14:15] op_sel_hi:[1,0]
	s_waitcnt vmcnt(1)
	v_pk_fma_f32 v[52:53], v[52:53], v[60:61], v[56:57]
	v_pk_fma_f32 v[50:51], v[50:51], v[58:59], v[54:55]
	global_store_dwordx4 v[64:65], v[50:53], off offset:64
	global_load_dwordx4 v[50:53], v[130:131], off offset:512
	s_waitcnt vmcnt(0)
	v_pk_mul_f32 v[52:53], v[52:53], s[14:15] op_sel_hi:[1,0]
	v_pk_mul_f32 v[50:51], v[50:51], s[14:15] op_sel_hi:[1,0]
	v_pk_fma_f32 v[40:41], v[52:53], v[40:41], v[44:45]
	v_pk_fma_f32 v[38:39], v[50:51], v[38:39], v[42:43]
	global_store_dwordx4 v[64:65], v[38:41], off offset:512
	global_load_dwordx4 v[38:41], v[130:131], off offset:576
	v_add_co_u32_e32 v42, vcc, s60, v132
	v_cvt_f32_i32_e32 v45, v31
	s_nop 0
	v_addc_co_u32_e32 v43, vcc, 0, v133, vcc
	v_cvt_f32_i32_e32 v44, v30
	s_waitcnt vmcnt(0)
	v_pk_mul_f32 v[40:41], v[40:41], s[14:15] op_sel_hi:[1,0]
	v_pk_mul_f32 v[38:39], v[38:39], s[14:15] op_sel_hi:[1,0]
	v_pk_fma_f32 v[36:37], v[40:41], v[36:37], v[48:49]
	v_pk_fma_f32 v[34:35], v[38:39], v[34:35], v[46:47]
	global_store_dwordx4 v[64:65], v[34:37], off offset:576
	global_load_dwordx4 v[34:37], v[130:131], off
	global_load_dwordx4 v[38:41], v[42:43], off
	v_cvt_f32_i32_e32 v47, v33
	v_cvt_f32_i32_e32 v46, v32
	v_lshl_add_u64 v[48:49], v[132:133], 0, s[16:17]
	global_load_dwordx4 v[30:33], v[48:49], off offset:576
	s_waitcnt vmcnt(2)
	v_pk_mul_f32 v[36:37], v[36:37], s[14:15] op_sel_hi:[1,0]
	v_pk_mul_f32 v[34:35], v[34:35], s[14:15] op_sel_hi:[1,0]
	s_waitcnt vmcnt(1)
	v_pk_fma_f32 v[36:37], v[36:37], v[46:47], v[40:41]
	v_pk_fma_f32 v[34:35], v[34:35], v[44:45], v[38:39]
	global_store_dwordx4 v[42:43], v[34:37], off
	global_load_dwordx4 v[34:37], v[130:131], off offset:64
	global_load_dwordx4 v[38:41], v[48:49], off offset:64
	v_cvt_f32_i32_e32 v43, v27
	v_cvt_f32_i32_e32 v42, v26
	v_cvt_f32_i32_e32 v45, v29
	v_cvt_f32_i32_e32 v44, v28
	global_load_dwordx4 v[26:29], v[48:49], off offset:512
	s_waitcnt vmcnt(2)
	v_pk_mul_f32 v[36:37], v[36:37], s[14:15] op_sel_hi:[1,0]
	v_pk_mul_f32 v[34:35], v[34:35], s[14:15] op_sel_hi:[1,0]
	s_waitcnt vmcnt(1)
	v_pk_fma_f32 v[36:37], v[36:37], v[44:45], v[40:41]
	v_pk_fma_f32 v[34:35], v[34:35], v[42:43], v[38:39]
	global_store_dwordx4 v[48:49], v[34:37], off offset:64
	global_load_dwordx4 v[34:37], v[130:131], off offset:512
	s_waitcnt vmcnt(0)
	v_pk_mul_f32 v[36:37], v[36:37], s[14:15] op_sel_hi:[1,0]
	v_pk_mul_f32 v[34:35], v[34:35], s[14:15] op_sel_hi:[1,0]
	v_pk_fma_f32 v[24:25], v[36:37], v[24:25], v[28:29]
	v_pk_fma_f32 v[22:23], v[34:35], v[22:23], v[26:27]
	global_store_dwordx4 v[48:49], v[22:25], off offset:512
	global_load_dwordx4 v[22:25], v[130:131], off offset:576
	v_add_co_u32_e32 v26, vcc, s61, v132
	v_cvt_f32_i32_e32 v29, v15
	s_nop 0
	v_addc_co_u32_e32 v27, vcc, 0, v133, vcc
	v_cvt_f32_i32_e32 v28, v14
	s_andn2_b64 vcc, exec, s[4:5]
	s_mov_b64 s[4:5], -1
	s_waitcnt vmcnt(0)
	v_pk_mul_f32 v[24:25], v[24:25], s[14:15] op_sel_hi:[1,0]
	v_pk_mul_f32 v[22:23], v[22:23], s[14:15] op_sel_hi:[1,0]
	v_pk_fma_f32 v[20:21], v[24:25], v[20:21], v[32:33]
	v_pk_fma_f32 v[18:19], v[22:23], v[18:19], v[30:31]
	global_store_dwordx4 v[48:49], v[18:21], off offset:576
	global_load_dwordx4 v[18:21], v[130:131], off
	global_load_dwordx4 v[22:25], v[26:27], off
	v_cvt_f32_i32_e32 v31, v17
	v_cvt_f32_i32_e32 v30, v16
	v_lshl_add_u64 v[32:33], v[132:133], 0, s[20:21]
	global_load_dwordx4 v[14:17], v[32:33], off offset:576
	s_waitcnt vmcnt(2)
	v_pk_mul_f32 v[20:21], v[20:21], s[14:15] op_sel_hi:[1,0]
	v_pk_mul_f32 v[18:19], v[18:19], s[14:15] op_sel_hi:[1,0]
	s_waitcnt vmcnt(1)
	v_pk_fma_f32 v[20:21], v[20:21], v[30:31], v[24:25]
	v_pk_fma_f32 v[18:19], v[18:19], v[28:29], v[22:23]
	global_store_dwordx4 v[26:27], v[18:21], off
	global_load_dwordx4 v[18:21], v[130:131], off offset:64
	global_load_dwordx4 v[22:25], v[32:33], off offset:64
	v_cvt_f32_i32_e32 v27, v11
	v_cvt_f32_i32_e32 v26, v10
	v_cvt_f32_i32_e32 v29, v13
	v_cvt_f32_i32_e32 v28, v12
	global_load_dwordx4 v[10:13], v[32:33], off offset:512
	s_waitcnt vmcnt(2)
	v_pk_mul_f32 v[20:21], v[20:21], s[14:15] op_sel_hi:[1,0]
	v_pk_mul_f32 v[18:19], v[18:19], s[14:15] op_sel_hi:[1,0]
	s_waitcnt vmcnt(1)
	v_pk_fma_f32 v[20:21], v[20:21], v[28:29], v[24:25]
	v_pk_fma_f32 v[18:19], v[18:19], v[26:27], v[22:23]
	global_store_dwordx4 v[32:33], v[18:21], off offset:64
	global_load_dwordx4 v[18:21], v[130:131], off offset:512
	s_waitcnt vmcnt(0)
	v_pk_mul_f32 v[20:21], v[20:21], s[14:15] op_sel_hi:[1,0]
	v_pk_mul_f32 v[18:19], v[18:19], s[14:15] op_sel_hi:[1,0]
	v_pk_fma_f32 v[8:9], v[20:21], v[8:9], v[12:13]
	v_pk_fma_f32 v[6:7], v[18:19], v[6:7], v[10:11]
	global_store_dwordx4 v[32:33], v[6:9], off offset:512
	global_load_dwordx4 v[6:9], v[130:131], off offset:576
	s_waitcnt vmcnt(0)
	v_pk_mul_f32 v[8:9], v[8:9], s[14:15] op_sel_hi:[1,0]
	v_pk_mul_f32 v[6:7], v[6:7], s[14:15] op_sel_hi:[1,0]
	v_pk_fma_f32 v[4:5], v[8:9], v[4:5], v[16:17]
	v_pk_fma_f32 v[2:3], v[6:7], v[2:3], v[14:15]
	global_store_dwordx4 v[32:33], v[2:5], off offset:576
	s_cbranch_vccnz .LBB0_1165
	s_andn2_b64 vcc, exec, s[6:7]
	s_cbranch_vccnz .LBB0_1164
	s_barrier
	s_branch .LBB0_1164

.LBB0_1234:
	v_add_co_u32_e64 v18, s[4:5], s12, v72
	v_add_co_u32_e32 v76, vcc, 0xffffd000, v72
	s_nop 0
	v_addc_co_u32_e64 v19, s[4:5], -1, v73, s[4:5]
	v_add_co_u32_e64 v20, s[4:5], s13, v72
	global_load_dwordx4 v[14:17], v[72:73], off offset:-3072
	global_load_dwordx4 v[10:13], v[72:73], off offset:-2048
	global_load_dwordx4 v[6:9], v[72:73], off offset:-1024
	global_load_dwordx4 v[2:5], v[72:73], off
	global_load_dwordx4 v[86:89], v[46:47], off
	v_addc_co_u32_e64 v21, s[4:5], -1, v73, s[4:5]
	v_addc_co_u32_e32 v77, vcc, -1, v73, vcc
	global_load_dwordx4 v[90:93], v[18:19], off offset:-3072
	global_load_dwordx4 v[42:45], v[18:19], off offset:-2048
	global_load_dwordx4 v[38:41], v[18:19], off offset:-1024
	global_load_dwordx4 v[34:37], v[18:19], off
	global_load_dwordx4 v[30:33], v[20:21], off offset:-3072
	global_load_dwordx4 v[26:29], v[20:21], off offset:-2048
	global_load_dwordx4 v[22:25], v[20:21], off offset:-1024
	global_load_dwordx4 v[18:21], v[72:73], off offset:-4096
	global_load_dwordx4 v[94:97], v[76:77], off offset:-3072
	global_load_dwordx4 v[98:101], v[76:77], off offset:-2048
	global_load_dwordx4 v[102:105], v[76:77], off offset:-1024
	global_load_dwordx4 v[106:109], v[76:77], off
	v_mov_b32_e32 v111, 0
	v_mov_b32_e32 v112, 0
	v_mov_b32_e32 v113, 0
	s_add_i32 s3, s3, s92
	v_lshl_add_u64 v[72:73], v[72:73], 0, s[6:7]
	s_cmpk_lt_i32 s3, 0x4000
	s_waitcnt vmcnt(0)
	v_mul_f32_e32 v76, v15, v15
	v_mul_f32_e32 v77, v17, v17
	v_mul_f32_e32 v114, v11, v11
	v_mul_f32_e32 v115, v13, v13
	v_mul_f32_e32 v118, v3, v3
	v_mul_f32_e32 v119, v5, v5
	v_mul_f32_e32 v124, v39, v39
	v_mul_f32_e32 v125, v41, v41
	v_mul_f32_e32 v136, v95, v95
	v_mul_f32_e32 v137, v97, v97
	v_mul_f32_e32 v138, v99, v99
	v_mul_f32_e32 v139, v101, v101
	v_mul_f32_e32 v126, v35, v35
	v_mul_f32_e32 v127, v37, v37
	v_fmac_f32_e32 v76, v14, v14
	v_fmac_f32_e32 v77, v16, v16
	v_fmac_f32_e32 v114, v10, v10
	v_fmac_f32_e32 v115, v12, v12
	v_fmac_f32_e32 v118, v2, v2
	v_fmac_f32_e32 v119, v4, v4
	v_mul_f32_e32 v140, v103, v103
	v_mul_f32_e32 v141, v105, v105
	v_fmac_f32_e32 v124, v38, v38
	v_fmac_f32_e32 v125, v40, v40
	v_fmac_f32_e32 v136, v94, v94
	v_fmac_f32_e32 v137, v96, v96
	v_fmac_f32_e32 v138, v98, v98
	v_fmac_f32_e32 v139, v100, v100
	v_mul_f32_e32 v142, v107, v107
	v_mul_f32_e32 v143, v109, v109
	v_fmac_f32_e32 v126, v34, v34
	v_fmac_f32_e32 v127, v36, v36
	v_add_f32_e32 v76, v76, v77
	v_add_f32_e32 v77, v114, v115
	v_add_f32_e32 v115, v118, v119
	v_fmac_f32_e32 v140, v102, v102
	v_fmac_f32_e32 v141, v104, v104
	v_add_f32_e32 v118, v124, v125
	v_add_f32_e32 v124, v136, v137
	v_add_f32_e32 v125, v138, v139
	v_mul_f32_e32 v116, v7, v7
	v_mul_f32_e32 v117, v9, v9
	v_mul_f32_e32 v120, v91, v91
	v_mul_f32_e32 v121, v93, v93
	v_fmac_f32_e32 v142, v106, v106
	v_fmac_f32_e32 v143, v108, v108
	v_add_f32_e32 v119, v126, v127
	v_add_f32_e32 v126, v140, v141
	v_add_f32_e32 v124, v124, v125
	v_mul_f32_e32 v122, v43, v43
	v_mul_f32_e32 v123, v45, v45
	v_fmac_f32_e32 v116, v6, v6
	v_fmac_f32_e32 v117, v8, v8
	v_fmac_f32_e32 v120, v90, v90
	v_fmac_f32_e32 v121, v92, v92
	v_add_f32_e32 v127, v142, v143
	v_add_f32_e32 v124, v124, v126
	v_fmac_f32_e32 v122, v42, v42
	v_fmac_f32_e32 v123, v44, v44
	v_add_f32_e32 v114, v116, v117
	v_add_f32_e32 v116, v120, v121
	v_add_f32_e32 v124, v124, v127
	v_add_f32_e32 v117, v122, v123
	v_add_f32_e32 v116, v124, v116
	v_mul_f32_e32 v128, v31, v31
	v_mul_f32_e32 v129, v33, v33
	v_add_f32_e32 v116, v116, v117
	v_mul_f32_e32 v130, v27, v27
	v_mul_f32_e32 v131, v29, v29
	v_fmac_f32_e32 v128, v30, v30
	v_fmac_f32_e32 v129, v32, v32
	v_add_f32_e32 v116, v116, v118
	v_mul_f32_e32 v132, v23, v23
	v_mul_f32_e32 v133, v25, v25
	v_fmac_f32_e32 v130, v26, v26
	v_fmac_f32_e32 v131, v28, v28
	v_add_f32_e32 v120, v128, v129
	v_add_f32_e32 v116, v116, v119
	v_mul_f32_e32 v134, v19, v19
	v_mul_f32_e32 v135, v21, v21
	v_fmac_f32_e32 v132, v22, v22
	v_fmac_f32_e32 v133, v24, v24
	v_add_f32_e32 v121, v130, v131
	v_add_f32_e32 v116, v116, v120
	v_fmac_f32_e32 v134, v18, v18
	v_fmac_f32_e32 v135, v20, v20
	v_add_f32_e32 v122, v132, v133
	v_add_f32_e32 v116, v116, v121
	v_add_f32_e32 v123, v134, v135
	v_add_f32_e32 v116, v116, v122
	v_add_f32_e32 v116, v116, v123
	v_add_f32_e32 v76, v116, v76
	v_add_f32_e32 v76, v76, v77
	v_add_f32_e32 v76, v76, v114
	v_add_f32_e32 v76, v76, v115
	ds_bpermute_b32 v77, v1, v76
	s_waitcnt lgkmcnt(0)
	v_add_f32_e32 v76, v76, v77
	ds_bpermute_b32 v77, v78, v76
	s_waitcnt lgkmcnt(0)
	v_add_f32_e32 v76, v76, v77
	ds_bpermute_b32 v77, v79, v76
	s_waitcnt lgkmcnt(0)
	v_add_f32_e32 v76, v76, v77
	ds_bpermute_b32 v77, v80, v76
	s_waitcnt lgkmcnt(0)
	v_add_f32_e32 v76, v76, v77
	ds_bpermute_b32 v77, v81, v76
	s_waitcnt lgkmcnt(0)
	v_add_f32_e32 v76, v76, v77
	ds_bpermute_b32 v77, v82, v76
	s_waitcnt lgkmcnt(0)
	v_add_f32_e32 v76, v76, v77
	v_fmamk_f32 v76, v76, 0x39800000, v83
	v_mul_f32_e32 v77, 0x4f800000, v76
	v_cmp_gt_f32_e32 vcc, s14, v76
	s_nop 1
	v_cndmask_b32_e32 v76, v76, v77, vcc
	v_sqrt_f32_e32 v77, v76
	s_nop 0
	v_add_u32_e32 v114, -1, v77
	v_add_u32_e32 v115, 1, v77
	v_fma_f32 v116, -v114, v77, v76
	v_fma_f32 v117, -v115, v77, v76
	v_cmp_ge_f32_e64 s[4:5], 0, v116
	s_nop 1
	v_cndmask_b32_e64 v77, v77, v114, s[4:5]
	v_cmp_lt_f32_e64 s[4:5], 0, v117
	s_nop 1
	v_cndmask_b32_e64 v77, v77, v115, s[4:5]
	v_mul_f32_e32 v114, 0x37800000, v77
	v_cndmask_b32_e32 v77, v77, v114, vcc
	v_cmp_class_f32_e32 vcc, v76, v84
	s_nop 1
	v_cndmask_b32_e32 v76, v77, v76, vcc
	v_div_scale_f32 v77, s[4:5], v76, v76, 1.0
	v_rcp_f32_e32 v115, v77
	v_div_scale_f32 v114, vcc, 1.0, v76, 1.0
	v_fma_f32 v116, -v77, v115, 1.0
	v_fmac_f32_e32 v115, v116, v115
	v_mul_f32_e32 v116, v114, v115
	v_fma_f32 v117, -v77, v116, v114
	v_fmac_f32_e32 v116, v117, v115
	v_fma_f32 v77, -v77, v116, v114
	v_div_fmas_f32 v77, v77, v115, v116
	v_div_fixup_f32 v76, v77, v76, 1.0
	v_mul_f32_e32 v77, v94, v76
	v_mul_f32_e32 v94, v95, v76
	v_mul_f32_e32 v77, v86, v77
	v_mul_f32_e32 v86, v87, v94
	v_med3_f32 v77, v77, s15, v85
	v_med3_f32 v86, v86, s15, v85
	v_cvt_pk_fp8_f32 v110, v77, v86
	v_mul_f32_e32 v95, v96, v76
	v_mul_f32_e32 v96, v97, v76
	v_mul_f32_e32 v87, v88, v95
	v_mul_f32_e32 v88, v89, v96
	v_med3_f32 v87, v87, s15, v85
	v_med3_f32 v88, v88, s15, v85
	v_cvt_pk_fp8_f32 v110, v87, v88 op_sel:[0,0,1]
	v_mul_f32_e32 v97, v98, v76
	v_mul_f32_e32 v98, v99, v76
	v_mul_f32_e32 v99, v100, v76
	global_store_dword v[74:75], v110, off offset:-2048
	global_load_dwordx4 v[86:89], v[46:47], off offset:1024
	v_mul_f32_e32 v100, v101, v76
	v_mul_f32_e32 v101, v102, v76
	v_mul_f32_e32 v102, v103, v76
	v_mul_f32_e32 v103, v104, v76
	v_mul_f32_e32 v104, v105, v76
	v_mul_f32_e32 v105, v106, v76
	v_mul_f32_e32 v106, v107, v76
	v_mul_f32_e32 v94, v109, v76
	v_mul_f32_e32 v90, v90, v76
	v_mul_f32_e32 v91, v91, v76
	v_mul_f32_e32 v92, v92, v76
	v_mul_f32_e32 v93, v93, v76
	v_mul_f32_e32 v42, v42, v76
	v_mul_f32_e32 v43, v43, v76
	v_mul_f32_e32 v44, v44, v76
	v_mul_f32_e32 v45, v45, v76
	v_mul_f32_e32 v38, v38, v76
	v_mul_f32_e32 v39, v39, v76
	v_mul_f32_e32 v40, v40, v76
	v_mul_f32_e32 v41, v41, v76
	v_mul_f32_e32 v34, v34, v76
	v_mul_f32_e32 v35, v35, v76
	v_mul_f32_e32 v36, v36, v76
	v_mul_f32_e32 v37, v37, v76
	v_mul_f32_e32 v30, v30, v76
	v_mul_f32_e32 v31, v31, v76
	v_mul_f32_e32 v32, v32, v76
	v_mul_f32_e32 v33, v33, v76
	v_mul_f32_e32 v26, v26, v76
	v_mul_f32_e32 v27, v27, v76
	v_mul_f32_e32 v28, v28, v76
	v_mul_f32_e32 v29, v29, v76
	v_mul_f32_e32 v22, v22, v76
	v_mul_f32_e32 v23, v23, v76
	v_mul_f32_e32 v24, v24, v76
	v_mul_f32_e32 v25, v25, v76
	v_mul_f32_e32 v18, v18, v76
	v_mul_f32_e32 v19, v19, v76
	v_mul_f32_e32 v20, v20, v76
	v_mul_f32_e32 v21, v21, v76
	v_mul_f32_e32 v14, v14, v76
	v_mul_f32_e32 v15, v15, v76
	v_mul_f32_e32 v16, v16, v76
	v_mul_f32_e32 v17, v17, v76
	v_mul_f32_e32 v10, v10, v76
	v_mul_f32_e32 v11, v11, v76
	v_mul_f32_e32 v12, v12, v76
	v_mul_f32_e32 v13, v13, v76
	v_mul_f32_e32 v6, v6, v76
	v_mul_f32_e32 v7, v7, v76
	v_mul_f32_e32 v8, v8, v76
	v_mul_f32_e32 v9, v9, v76
	v_mul_f32_e32 v2, v2, v76
	v_mul_f32_e32 v3, v3, v76
	v_mul_f32_e32 v4, v4, v76
	v_mul_f32_e32 v5, v5, v76
	s_waitcnt vmcnt(0)
	v_mul_f32_e32 v77, v86, v97
	v_mul_f32_e32 v86, v87, v98
	v_med3_f32 v77, v77, s15, v85
	v_med3_f32 v86, v86, s15, v85
	v_cvt_pk_fp8_f32 v111, v77, v86
	v_mul_f32_e32 v87, v88, v99
	v_mul_f32_e32 v88, v89, v100
	v_med3_f32 v87, v87, s15, v85
	v_med3_f32 v88, v88, s15, v85
	v_cvt_pk_fp8_f32 v111, v87, v88 op_sel:[0,0,1]
	global_store_dword v[74:75], v111, off offset:-1792
	global_load_dwordx4 v[86:89], v[46:47], off offset:2048
	s_waitcnt vmcnt(0)
	v_mul_f32_e32 v77, v101, v86
	v_mul_f32_e32 v86, v102, v87
	v_med3_f32 v77, v77, s15, v85
	v_med3_f32 v86, v86, s15, v85
	v_cvt_pk_fp8_f32 v112, v77, v86
	v_mul_f32_e32 v87, v103, v88
	v_mul_f32_e32 v88, v104, v89
	v_med3_f32 v87, v87, s15, v85
	v_med3_f32 v88, v88, s15, v85
	v_cvt_pk_fp8_f32 v112, v87, v88 op_sel:[0,0,1]
	v_mul_f32_e32 v77, v108, v76
	global_store_dword v[74:75], v112, off offset:-1536
	global_load_dwordx4 v[86:89], v[46:47], off offset:3072
	s_waitcnt vmcnt(0)
	v_mul_f32_e32 v86, v105, v86
	v_mul_f32_e32 v87, v106, v87
	v_med3_f32 v86, v86, s15, v85
	v_med3_f32 v87, v87, s15, v85
	v_cvt_pk_fp8_f32 v113, v86, v87
	v_mul_f32_e32 v77, v77, v88
	v_mul_f32_e32 v88, v94, v89
	v_med3_f32 v77, v77, s15, v85
	v_med3_f32 v88, v88, s15, v85
	v_cvt_pk_fp8_f32 v113, v77, v88 op_sel:[0,0,1]
	global_store_dword v[74:75], v113, off offset:-1280
	global_load_dwordx4 v[86:89], v[48:49], off
	s_waitcnt vmcnt(0)
	v_mul_f32_e32 v86, v90, v86
	v_mul_f32_e32 v87, v91, v87
	v_med3_f32 v86, v86, s15, v85
	v_med3_f32 v87, v87, s15, v85
	v_cvt_pk_fp8_f32 v77, v86, v87
	v_mul_f32_e32 v88, v92, v88
	v_mul_f32_e32 v89, v93, v89
	v_med3_f32 v88, v88, s15, v85
	v_med3_f32 v89, v89, s15, v85
	v_cvt_pk_fp8_f32 v77, v88, v89 op_sel:[0,0,1]
	global_store_dword v[74:75], v77, off offset:-1024
	global_load_dwordx4 v[86:89], v[50:51], off
	s_waitcnt vmcnt(0)
	v_mul_f32_e32 v42, v42, v86
	v_mul_f32_e32 v43, v43, v87
	v_med3_f32 v42, v42, s15, v85
	v_med3_f32 v43, v43, s15, v85
	v_cvt_pk_fp8_f32 v77, v42, v43
	v_mul_f32_e32 v44, v44, v88
	v_mul_f32_e32 v45, v45, v89
	v_med3_f32 v44, v44, s15, v85
	v_med3_f32 v45, v45, s15, v85
	v_cvt_pk_fp8_f32 v77, v44, v45 op_sel:[0,0,1]
	global_store_dword v[74:75], v77, off offset:-768
	global_load_dwordx4 v[42:45], v[52:53], off
	s_waitcnt vmcnt(0)
	v_mul_f32_e32 v38, v38, v42
	v_mul_f32_e32 v39, v39, v43
	v_med3_f32 v38, v38, s15, v85
	v_med3_f32 v39, v39, s15, v85
	v_cvt_pk_fp8_f32 v77, v38, v39
	v_mul_f32_e32 v40, v40, v44
	v_mul_f32_e32 v41, v41, v45
	v_med3_f32 v40, v40, s15, v85
	v_med3_f32 v41, v41, s15, v85
	v_cvt_pk_fp8_f32 v77, v40, v41 op_sel:[0,0,1]
	global_store_dword v[74:75], v77, off offset:-512
	global_load_dwordx4 v[38:41], v[54:55], off
	s_waitcnt vmcnt(0)
	v_mul_f32_e32 v34, v34, v38
	v_mul_f32_e32 v35, v35, v39
	v_med3_f32 v34, v34, s15, v85
	v_med3_f32 v35, v35, s15, v85
	v_cvt_pk_fp8_f32 v42, v34, v35
	v_mul_f32_e32 v36, v36, v40
	v_mul_f32_e32 v37, v37, v41
	v_med3_f32 v36, v36, s15, v85
	v_med3_f32 v37, v37, s15, v85
	v_cvt_pk_fp8_f32 v42, v36, v37 op_sel:[0,0,1]
	global_store_dword v[74:75], v42, off offset:-256
	global_load_dwordx4 v[34:37], v[56:57], off
	s_waitcnt vmcnt(0)
	v_mul_f32_e32 v30, v30, v34
	v_mul_f32_e32 v31, v31, v35
	v_med3_f32 v30, v30, s15, v85
	v_med3_f32 v31, v31, s15, v85
	v_cvt_pk_fp8_f32 v38, v30, v31
	v_mul_f32_e32 v32, v32, v36
	v_mul_f32_e32 v33, v33, v37
	v_med3_f32 v32, v32, s15, v85
	v_med3_f32 v33, v33, s15, v85
	v_cvt_pk_fp8_f32 v38, v32, v33 op_sel:[0,0,1]
	global_store_dword v[74:75], v38, off
	global_load_dwordx4 v[30:33], v[58:59], off
	s_waitcnt vmcnt(0)
	v_mul_f32_e32 v26, v26, v30
	v_mul_f32_e32 v27, v27, v31
	v_med3_f32 v26, v26, s15, v85
	v_med3_f32 v27, v27, s15, v85
	v_cvt_pk_fp8_f32 v34, v26, v27
	v_mul_f32_e32 v28, v28, v32
	v_mul_f32_e32 v29, v29, v33
	v_med3_f32 v28, v28, s15, v85
	v_med3_f32 v29, v29, s15, v85
	v_cvt_pk_fp8_f32 v34, v28, v29 op_sel:[0,0,1]
	global_store_dword v[74:75], v34, off offset:256
	global_load_dwordx4 v[26:29], v[60:61], off
	s_waitcnt vmcnt(0)
	v_mul_f32_e32 v22, v22, v26
	v_mul_f32_e32 v23, v23, v27
	v_med3_f32 v22, v22, s15, v85
	v_med3_f32 v23, v23, s15, v85
	v_cvt_pk_fp8_f32 v30, v22, v23
	v_mul_f32_e32 v24, v24, v28
	v_mul_f32_e32 v25, v25, v29
	v_med3_f32 v24, v24, s15, v85
	v_med3_f32 v25, v25, s15, v85
	v_cvt_pk_fp8_f32 v30, v24, v25 op_sel:[0,0,1]
	global_store_dword v[74:75], v30, off offset:512
	global_load_dwordx4 v[22:25], v[62:63], off
	s_waitcnt vmcnt(0)
	v_mul_f32_e32 v18, v18, v22
	v_mul_f32_e32 v19, v19, v23
	v_med3_f32 v18, v18, s15, v85
	v_med3_f32 v19, v19, s15, v85
	v_cvt_pk_fp8_f32 v26, v18, v19
	v_mul_f32_e32 v20, v20, v24
	v_mul_f32_e32 v21, v21, v25
	v_med3_f32 v20, v20, s15, v85
	v_med3_f32 v21, v21, s15, v85
	v_cvt_pk_fp8_f32 v26, v20, v21 op_sel:[0,0,1]
	global_store_dword v[74:75], v26, off offset:768
	global_load_dwordx4 v[18:21], v[64:65], off
	s_waitcnt vmcnt(0)
	v_mul_f32_e32 v14, v14, v18
	v_mul_f32_e32 v15, v15, v19
	v_med3_f32 v14, v14, s15, v85
	v_med3_f32 v15, v15, s15, v85
	v_cvt_pk_fp8_f32 v22, v14, v15
	v_mul_f32_e32 v16, v16, v20
	v_mul_f32_e32 v17, v17, v21
	v_med3_f32 v16, v16, s15, v85
	v_med3_f32 v17, v17, s15, v85
	v_cvt_pk_fp8_f32 v22, v16, v17 op_sel:[0,0,1]
	global_store_dword v[74:75], v22, off offset:1024
	global_load_dwordx4 v[14:17], v[66:67], off
	s_waitcnt vmcnt(0)
	v_mul_f32_e32 v10, v10, v14
	v_mul_f32_e32 v11, v11, v15
	v_med3_f32 v10, v10, s15, v85
	v_med3_f32 v11, v11, s15, v85
	v_cvt_pk_fp8_f32 v18, v10, v11
	v_mul_f32_e32 v12, v12, v16
	v_mul_f32_e32 v13, v13, v17
	v_med3_f32 v12, v12, s15, v85
	v_med3_f32 v13, v13, s15, v85
	v_cvt_pk_fp8_f32 v18, v12, v13 op_sel:[0,0,1]
	global_store_dword v[74:75], v18, off offset:1280
	global_load_dwordx4 v[10:13], v[68:69], off
	s_waitcnt vmcnt(0)
	v_mul_f32_e32 v6, v6, v10
	v_mul_f32_e32 v7, v7, v11
	v_med3_f32 v6, v6, s15, v85
	v_med3_f32 v7, v7, s15, v85
	v_cvt_pk_fp8_f32 v14, v6, v7
	v_mul_f32_e32 v8, v8, v12
	v_mul_f32_e32 v9, v9, v13
	v_med3_f32 v8, v8, s15, v85
	v_med3_f32 v9, v9, s15, v85
	v_cvt_pk_fp8_f32 v14, v8, v9 op_sel:[0,0,1]
	global_store_dword v[74:75], v14, off offset:1536
	global_load_dwordx4 v[6:9], v[70:71], off
	s_waitcnt vmcnt(0)
	v_mul_f32_e32 v2, v2, v6
	v_mul_f32_e32 v3, v3, v7
	v_med3_f32 v2, v2, s15, v85
	v_med3_f32 v3, v3, s15, v85
	v_cvt_pk_fp8_f32 v10, v2, v3
	v_mul_f32_e32 v4, v4, v8
	v_mul_f32_e32 v5, v5, v9
	v_med3_f32 v2, v4, s15, v85
	v_med3_f32 v3, v5, s15, v85
	v_cvt_pk_fp8_f32 v10, v2, v3 op_sel:[0,0,1]
	global_store_dword v[74:75], v10, off offset:1792
	v_lshl_add_u64 v[74:75], v[74:75], 0, s[8:9]
	s_cbranch_scc1 .LBB0_1234
	v_readlane_b32 s93, v246, 7

.LBB0_1370:
	s_ashr_i32 s6, s30, 6
	s_lshl_b32 s18, s30, 8
	s_lshl_b32 s7, s6, 12
	s_and_b32 s18, s18, 0xf00
	s_or_b32 s20, s18, s7
	s_ashr_i32 s21, s20, 31
	s_lshl_b64 s[18:19], s[20:21], 10
	s_add_u32 s7, s0, s18
	s_addc_u32 s22, s1, s19
	s_lshl_b32 s23, s30, 3
	s_and_b32 s31, s23, 0x180
	s_lshl_b32 s34, s31, 1
	s_add_u32 s36, s7, s34
	s_addc_u32 s37, s22, 0
	s_lshl_b32 s6, s6, 8
	s_ashr_i32 s7, s6, 31
	s_lshl_b64 s[6:7], s[6:7], 11
	v_readlane_b32 s22, v246, 8
	v_mov_b32_e32 v87, v0
	v_readlane_b32 s23, v246, 9
	s_add_u32 s22, s22, s6
	s_addc_u32 s23, s23, s7
	v_lshlrev_b32_e32 v2, 3, v87
	s_add_u32 s22, s22, s34
	v_and_b32_e32 v2, 0x78, v2
	v_ashrrev_i32_e32 v70, 4, v87
	s_addc_u32 s23, s23, 0
	v_lshlrev_b32_e32 v114, 1, v2
	v_ashrrev_i32_e32 v71, 31, v70
	v_lshl_add_u64 v[2:3], s[22:23], 0, v[114:115]
	v_lshlrev_b64 v[66:67], 11, v[70:71]
	v_readfirstlane_b32 s35, v87
	v_lshl_add_u64 v[4:5], v[2:3], 0, v[66:67]
	s_waitcnt vmcnt(0)
	s_barrier
	global_load_dwordx4 v[34:37], v[4:5], off
	global_load_dwordx4 v[38:41], v[4:5], off offset:1024
	v_add_u32_e32 v4, 0x200, v87
	s_ashr_i32 s35, s35, 1
	v_and_b32_e32 v86, 15, v87
	v_ashrrev_i32_e32 v72, 4, v4
	s_andn2_b32 s35, s35, 31
	v_ashrrev_i32_e32 v73, 31, v72
	v_or_b32_e32 v50, s35, v86
	v_lshlrev_b64 v[68:69], 11, v[72:73]
	v_or_b32_e32 v52, 16, v50
	v_lshl_add_u64 v[2:3], v[2:3], 0, v[68:69]
	v_and_b32_e32 v120, 48, v87
	v_mov_b32_e32 v121, v115
	v_ashrrev_i32_e32 v51, 31, v50
	v_ashrrev_i32_e32 v53, 31, v52
	global_load_dwordx4 v[42:45], v[2:3], off
	global_load_dwordx4 v[46:49], v[2:3], off offset:1024
	v_lshl_add_u64 v[18:19], s[36:37], 0, v[120:121]
	v_lshlrev_b64 v[2:3], 10, v[50:51]
	v_lshlrev_b64 v[20:21], 10, v[52:53]
	v_lshl_add_u64 v[14:15], v[18:19], 0, v[2:3]
	v_lshl_add_u64 v[30:31], v[18:19], 0, v[20:21]
	global_load_dwordx4 v[2:5], v[14:15], off
	global_load_dwordx4 v[6:9], v[14:15], off offset:64
	global_load_dwordx4 v[10:13], v[14:15], off offset:128
	global_load_dwordx4 v[14:17], v[14:15], off offset:192
	global_load_dwordx4 v[18:21], v[30:31], off
	global_load_dwordx4 v[22:25], v[30:31], off offset:64
	global_load_dwordx4 v[26:29], v[30:31], off offset:128
	global_load_dwordx4 v[30:33], v[30:31], off offset:192
	v_bfe_u32 v121, v87, 4, 2
	v_lshlrev_b64 v[118:119], 9, v[50:51]
	s_and_b64 vcc, exec, s[4:5]
	v_lshlrev_b64 v[116:117], 9, v[52:53]
	s_cbranch_vccnz .LBB0_1372
	s_add_u32 s18, s60, s18
	s_addc_u32 s19, s61, s19
	v_lshlrev_b32_e32 v50, 3, v121
	s_add_u32 s18, s18, s34
	s_addc_u32 s19, s19, 0
	v_lshlrev_b32_e32 v50, 1, v50
	v_mov_b32_e32 v51, v115
	v_lshl_add_u64 v[50:51], s[18:19], 0, v[50:51]
	v_lshl_add_u64 v[52:53], v[118:119], 1, v[50:51]
	global_load_dwordx4 v[74:77], v[52:53], off
	global_load_dwordx4 v[78:81], v[52:53], off offset:64
	v_lshl_add_u64 v[50:51], v[116:117], 1, v[50:51]
	global_load_dwordx4 v[82:85], v[52:53], off offset:128
	global_load_dwordx4 v[88:91], v[52:53], off offset:192
	global_load_dwordx4 v[62:65], v[50:51], off
	global_load_dwordx4 v[58:61], v[50:51], off offset:64
	global_load_dwordx4 v[54:57], v[50:51], off offset:128
	global_load_dwordx4 v[50:53], v[50:51], off offset:192
	s_waitcnt vmcnt(15)
	v_lshlrev_b32_e32 v93, 16, v3
	v_lshlrev_b32_e32 v92, 16, v2
	v_and_b32_e32 v3, 0xffff0000, v3
	v_and_b32_e32 v2, 0xffff0000, v2
	v_and_b32_e32 v94, 0xffff0000, v4
	v_lshlrev_b32_e32 v95, 16, v4
	v_and_b32_e32 v4, 0xffff0000, v5
	v_lshlrev_b32_e32 v5, 16, v5
	s_waitcnt vmcnt(14)
	v_lshlrev_b32_e32 v97, 16, v7
	v_lshlrev_b32_e32 v96, 16, v6
	v_and_b32_e32 v7, 0xffff0000, v7
	v_and_b32_e32 v6, 0xffff0000, v6
	v_and_b32_e32 v98, 0xffff0000, v8
	v_lshlrev_b32_e32 v99, 16, v8
	s_waitcnt vmcnt(7)
	v_lshlrev_b32_e32 v101, 16, v75
	v_lshlrev_b32_e32 v100, 16, v74
	v_and_b32_e32 v75, 0xffff0000, v75
	v_and_b32_e32 v74, 0xffff0000, v74
	v_and_b32_e32 v102, 0xffff0000, v76
	v_lshlrev_b32_e32 v103, 16, v76
	v_and_b32_e32 v76, 0xffff0000, v77
	v_lshlrev_b32_e32 v77, 16, v77
	s_waitcnt vmcnt(6)
	v_lshlrev_b32_e32 v105, 16, v79
	v_lshlrev_b32_e32 v104, 16, v78
	v_and_b32_e32 v79, 0xffff0000, v79
	v_and_b32_e32 v78, 0xffff0000, v78
	v_and_b32_e32 v106, 0xffff0000, v80
	v_lshlrev_b32_e32 v107, 16, v80
	v_pk_add_f32 v[92:93], v[92:93], v[100:101]
	v_pk_add_f32 v[2:3], v[2:3], v[74:75]
	v_pk_add_f32 v[74:75], v[94:95], v[102:103]
	v_pk_add_f32 v[4:5], v[4:5], v[76:77]
	v_pk_add_f32 v[6:7], v[6:7], v[78:79]
	v_pk_add_f32 v[76:77], v[96:97], v[104:105]
	v_pk_add_f32 v[78:79], v[98:99], v[106:107]
	v_and_b32_sdwa v80, v92, v1 dst_sel:DWORD dst_unused:UNUSED_PAD src0_sel:WORD_1 src1_sel:DWORD
	v_and_b32_sdwa v96, v75, v1 dst_sel:DWORD dst_unused:UNUSED_PAD src0_sel:WORD_1 src1_sel:DWORD
	v_and_b32_sdwa v98, v5, v1 dst_sel:DWORD dst_unused:UNUSED_PAD src0_sel:WORD_1 src1_sel:DWORD
	v_and_b32_sdwa v99, v4, v1 dst_sel:DWORD dst_unused:UNUSED_PAD src0_sel:WORD_1 src1_sel:DWORD
	v_and_b32_sdwa v102, v7, v1 dst_sel:DWORD dst_unused:UNUSED_PAD src0_sel:WORD_1 src1_sel:DWORD
	v_and_b32_sdwa v103, v6, v1 dst_sel:DWORD dst_unused:UNUSED_PAD src0_sel:WORD_1 src1_sel:DWORD
	v_and_b32_sdwa v8, v93, v1 dst_sel:DWORD dst_unused:UNUSED_PAD src0_sel:WORD_1 src1_sel:DWORD
	v_and_b32_sdwa v97, v74, v1 dst_sel:DWORD dst_unused:UNUSED_PAD src0_sel:WORD_1 src1_sel:DWORD
	v_and_b32_sdwa v100, v77, v1 dst_sel:DWORD dst_unused:UNUSED_PAD src0_sel:WORD_1 src1_sel:DWORD
	v_and_b32_sdwa v101, v76, v1 dst_sel:DWORD dst_unused:UNUSED_PAD src0_sel:WORD_1 src1_sel:DWORD
	v_add3_u32 v80, v92, v80, s25
	v_add3_u32 v75, v75, v96, s25
	v_add3_u32 v92, v4, v99, s25
	v_add3_u32 v4, v5, v98, s25
	v_add3_u32 v5, v7, v102, s25
	v_add3_u32 v6, v6, v103, s25
	v_add3_u32 v8, v93, v8, s25
	v_add3_u32 v74, v74, v97, s25
	v_add3_u32 v76, v76, v101, s25
	v_add3_u32 v77, v77, v100, s25
	v_lshrrev_b32_e32 v7, 16, v75
	v_lshrrev_b32_e32 v75, 16, v4
	v_and_b32_e32 v93, 0xffff0000, v5
	v_and_b32_e32 v6, 0xffff0000, v6
	v_and_or_b32 v4, v74, s24, v7
	v_and_or_b32 v5, v92, s24, v75
	v_or_b32_sdwa v7, v93, v77 dst_sel:DWORD dst_unused:UNUSED_PAD src0_sel:DWORD src1_sel:WORD_1
	v_or_b32_sdwa v6, v6, v76 dst_sel:DWORD dst_unused:UNUSED_PAD src0_sel:DWORD src1_sel:WORD_1
	v_and_b32_e32 v74, 0xffff0000, v9
	v_lshlrev_b32_e32 v75, 16, v9
	v_and_b32_e32 v76, 0xffff0000, v81
	v_lshlrev_b32_e32 v77, 16, v81
	v_pk_add_f32 v[74:75], v[74:75], v[76:77]
	s_waitcnt vmcnt(5)
	v_lshlrev_b32_e32 v77, 16, v83
	v_and_b32_sdwa v9, v75, v1 dst_sel:DWORD dst_unused:UNUSED_PAD src0_sel:WORD_1 src1_sel:DWORD
	v_and_b32_sdwa v76, v74, v1 dst_sel:DWORD dst_unused:UNUSED_PAD src0_sel:WORD_1 src1_sel:DWORD
	v_add3_u32 v9, v75, v9, s25
	v_add3_u32 v74, v74, v76, s25
	v_lshrrev_b32_e32 v9, 16, v9
	v_and_or_b32 v9, v74, s24, v9
	v_lshlrev_b32_e32 v75, 16, v11
	v_lshlrev_b32_e32 v74, 16, v10
	v_lshlrev_b32_e32 v76, 16, v82
	v_pk_add_f32 v[74:75], v[74:75], v[76:77]
	v_and_b32_e32 v11, 0xffff0000, v11
	v_and_b32_e32 v10, 0xffff0000, v10
	v_and_b32_e32 v77, 0xffff0000, v83
	v_and_b32_e32 v76, 0xffff0000, v82
	v_pk_add_f32 v[10:11], v[10:11], v[76:77]
	v_and_b32_sdwa v76, v75, v1 dst_sel:DWORD dst_unused:UNUSED_PAD src0_sel:WORD_1 src1_sel:DWORD
	v_and_b32_sdwa v77, v74, v1 dst_sel:DWORD dst_unused:UNUSED_PAD src0_sel:WORD_1 src1_sel:DWORD
	v_add3_u32 v74, v74, v77, s25
	v_add3_u32 v75, v75, v76, s25
	v_and_b32_sdwa v76, v11, v1 dst_sel:DWORD dst_unused:UNUSED_PAD src0_sel:WORD_1 src1_sel:DWORD
	v_and_b32_sdwa v77, v10, v1 dst_sel:DWORD dst_unused:UNUSED_PAD src0_sel:WORD_1 src1_sel:DWORD
	v_add3_u32 v11, v11, v76, s25
	v_add3_u32 v10, v10, v77, s25
	v_and_b32_e32 v11, 0xffff0000, v11
	v_and_b32_e32 v10, 0xffff0000, v10
	v_or_b32_sdwa v11, v11, v75 dst_sel:DWORD dst_unused:UNUSED_PAD src0_sel:DWORD src1_sel:WORD_1
	v_or_b32_sdwa v10, v10, v74 dst_sel:DWORD dst_unused:UNUSED_PAD src0_sel:DWORD src1_sel:WORD_1
	v_and_b32_e32 v74, 0xffff0000, v12
	v_lshlrev_b32_e32 v75, 16, v12
	v_and_b32_e32 v76, 0xffff0000, v84
	v_lshlrev_b32_e32 v77, 16, v84
	v_pk_add_f32 v[74:75], v[74:75], v[76:77]
	v_lshlrev_b32_e32 v77, 16, v85
	v_and_b32_sdwa v12, v75, v1 dst_sel:DWORD dst_unused:UNUSED_PAD src0_sel:WORD_1 src1_sel:DWORD
	v_and_b32_sdwa v76, v74, v1 dst_sel:DWORD dst_unused:UNUSED_PAD src0_sel:WORD_1 src1_sel:DWORD
	v_add3_u32 v12, v75, v12, s25
	v_add3_u32 v74, v74, v76, s25
	v_lshrrev_b32_e32 v12, 16, v12
	v_and_or_b32 v12, v74, s24, v12
	v_and_b32_e32 v74, 0xffff0000, v13
	v_lshlrev_b32_e32 v75, 16, v13
	v_and_b32_e32 v76, 0xffff0000, v85
	v_pk_add_f32 v[74:75], v[74:75], v[76:77]
	s_waitcnt vmcnt(4)
	v_lshlrev_b32_e32 v77, 16, v89
	v_and_b32_sdwa v13, v75, v1 dst_sel:DWORD dst_unused:UNUSED_PAD src0_sel:WORD_1 src1_sel:DWORD
	v_and_b32_sdwa v76, v74, v1 dst_sel:DWORD dst_unused:UNUSED_PAD src0_sel:WORD_1 src1_sel:DWORD
	v_add3_u32 v13, v75, v13, s25
	v_add3_u32 v74, v74, v76, s25
	v_lshrrev_b32_e32 v13, 16, v13
	v_and_or_b32 v13, v74, s24, v13
	v_lshlrev_b32_e32 v75, 16, v15
	v_lshlrev_b32_e32 v74, 16, v14
	v_lshlrev_b32_e32 v76, 16, v88
	v_pk_add_f32 v[74:75], v[74:75], v[76:77]
	v_and_b32_e32 v15, 0xffff0000, v15
	v_and_b32_e32 v14, 0xffff0000, v14
	v_and_b32_e32 v77, 0xffff0000, v89
	v_and_b32_e32 v76, 0xffff0000, v88
	v_pk_add_f32 v[14:15], v[14:15], v[76:77]
	v_and_b32_sdwa v76, v75, v1 dst_sel:DWORD dst_unused:UNUSED_PAD src0_sel:WORD_1 src1_sel:DWORD
	v_and_b32_sdwa v77, v74, v1 dst_sel:DWORD dst_unused:UNUSED_PAD src0_sel:WORD_1 src1_sel:DWORD
	v_add3_u32 v74, v74, v77, s25
	v_add3_u32 v75, v75, v76, s25
	v_and_b32_sdwa v76, v15, v1 dst_sel:DWORD dst_unused:UNUSED_PAD src0_sel:WORD_1 src1_sel:DWORD
	v_and_b32_sdwa v77, v14, v1 dst_sel:DWORD dst_unused:UNUSED_PAD src0_sel:WORD_1 src1_sel:DWORD
	v_add3_u32 v15, v15, v76, s25
	v_add3_u32 v14, v14, v77, s25
	v_and_b32_e32 v15, 0xffff0000, v15
	v_and_b32_e32 v14, 0xffff0000, v14
	v_or_b32_sdwa v15, v15, v75 dst_sel:DWORD dst_unused:UNUSED_PAD src0_sel:DWORD src1_sel:WORD_1
	v_or_b32_sdwa v14, v14, v74 dst_sel:DWORD dst_unused:UNUSED_PAD src0_sel:DWORD src1_sel:WORD_1
	v_and_b32_e32 v74, 0xffff0000, v16
	v_lshlrev_b32_e32 v75, 16, v16
	v_and_b32_e32 v76, 0xffff0000, v90
	v_lshlrev_b32_e32 v77, 16, v90
	v_pk_add_f32 v[74:75], v[74:75], v[76:77]
	v_lshlrev_b32_e32 v77, 16, v91
	v_and_b32_sdwa v16, v75, v1 dst_sel:DWORD dst_unused:UNUSED_PAD src0_sel:WORD_1 src1_sel:DWORD
	v_and_b32_sdwa v76, v74, v1 dst_sel:DWORD dst_unused:UNUSED_PAD src0_sel:WORD_1 src1_sel:DWORD
	v_add3_u32 v16, v75, v16, s25
	v_add3_u32 v74, v74, v76, s25
	v_lshrrev_b32_e32 v16, 16, v16
	v_and_or_b32 v16, v74, s24, v16
	v_and_b32_e32 v74, 0xffff0000, v17
	v_lshlrev_b32_e32 v75, 16, v17
	v_and_b32_e32 v76, 0xffff0000, v91
	v_pk_add_f32 v[74:75], v[74:75], v[76:77]
	s_waitcnt vmcnt(3)
	v_lshlrev_b32_e32 v77, 16, v63
	v_and_b32_sdwa v17, v75, v1 dst_sel:DWORD dst_unused:UNUSED_PAD src0_sel:WORD_1 src1_sel:DWORD
	v_and_b32_sdwa v76, v74, v1 dst_sel:DWORD dst_unused:UNUSED_PAD src0_sel:WORD_1 src1_sel:DWORD
	v_add3_u32 v17, v75, v17, s25
	v_add3_u32 v74, v74, v76, s25
	v_lshrrev_b32_e32 v17, 16, v17
	v_and_or_b32 v17, v74, s24, v17
	v_lshlrev_b32_e32 v75, 16, v19
	v_lshlrev_b32_e32 v74, 16, v18
	v_lshlrev_b32_e32 v76, 16, v62
	v_pk_add_f32 v[74:75], v[74:75], v[76:77]
	v_and_b32_e32 v19, 0xffff0000, v19
	v_and_b32_e32 v18, 0xffff0000, v18
	v_and_b32_e32 v63, 0xffff0000, v63
	v_and_b32_e32 v62, 0xffff0000, v62
	v_pk_add_f32 v[18:19], v[18:19], v[62:63]
	v_and_b32_sdwa v62, v75, v1 dst_sel:DWORD dst_unused:UNUSED_PAD src0_sel:WORD_1 src1_sel:DWORD
	v_and_b32_sdwa v63, v74, v1 dst_sel:DWORD dst_unused:UNUSED_PAD src0_sel:WORD_1 src1_sel:DWORD
	v_add3_u32 v63, v74, v63, s25
	v_add3_u32 v62, v75, v62, s25
	v_and_b32_sdwa v74, v19, v1 dst_sel:DWORD dst_unused:UNUSED_PAD src0_sel:WORD_1 src1_sel:DWORD
	v_and_b32_sdwa v75, v18, v1 dst_sel:DWORD dst_unused:UNUSED_PAD src0_sel:WORD_1 src1_sel:DWORD
	v_add3_u32 v19, v19, v74, s25
	v_add3_u32 v18, v18, v75, s25
	v_and_b32_e32 v19, 0xffff0000, v19
	v_and_b32_e32 v18, 0xffff0000, v18
	v_or_b32_sdwa v19, v19, v62 dst_sel:DWORD dst_unused:UNUSED_PAD src0_sel:DWORD src1_sel:WORD_1
	v_or_b32_sdwa v18, v18, v63 dst_sel:DWORD dst_unused:UNUSED_PAD src0_sel:DWORD src1_sel:WORD_1
	v_and_b32_e32 v62, 0xffff0000, v20
	v_lshlrev_b32_e32 v63, 16, v20
	v_and_b32_e32 v74, 0xffff0000, v64
	v_lshlrev_b32_e32 v75, 16, v64
	v_pk_add_f32 v[62:63], v[62:63], v[74:75]
	v_and_b32_sdwa v94, v3, v1 dst_sel:DWORD dst_unused:UNUSED_PAD src0_sel:WORD_1 src1_sel:DWORD
	v_and_b32_sdwa v20, v63, v1 dst_sel:DWORD dst_unused:UNUSED_PAD src0_sel:WORD_1 src1_sel:DWORD
	v_and_b32_sdwa v64, v62, v1 dst_sel:DWORD dst_unused:UNUSED_PAD src0_sel:WORD_1 src1_sel:DWORD
	v_add3_u32 v20, v63, v20, s25
	v_add3_u32 v62, v62, v64, s25
	v_lshrrev_b32_e32 v20, 16, v20
	v_and_or_b32 v20, v62, s24, v20
	v_and_b32_e32 v62, 0xffff0000, v21
	v_lshlrev_b32_e32 v63, 16, v21
	v_and_b32_e32 v64, 0xffff0000, v65
	v_lshlrev_b32_e32 v65, 16, v65
	v_pk_add_f32 v[62:63], v[62:63], v[64:65]
	s_waitcnt vmcnt(2)
	v_lshlrev_b32_e32 v65, 16, v59
	v_and_b32_sdwa v21, v63, v1 dst_sel:DWORD dst_unused:UNUSED_PAD src0_sel:WORD_1 src1_sel:DWORD
	v_and_b32_sdwa v64, v62, v1 dst_sel:DWORD dst_unused:UNUSED_PAD src0_sel:WORD_1 src1_sel:DWORD
	v_add3_u32 v21, v63, v21, s25
	v_add3_u32 v62, v62, v64, s25
	v_lshrrev_b32_e32 v21, 16, v21
	v_and_or_b32 v21, v62, s24, v21
	v_lshlrev_b32_e32 v63, 16, v23
	v_lshlrev_b32_e32 v62, 16, v22
	v_lshlrev_b32_e32 v64, 16, v58
	v_pk_add_f32 v[62:63], v[62:63], v[64:65]
	v_and_b32_e32 v23, 0xffff0000, v23
	v_and_b32_e32 v22, 0xffff0000, v22
	v_and_b32_e32 v59, 0xffff0000, v59
	v_and_b32_e32 v58, 0xffff0000, v58
	v_pk_add_f32 v[22:23], v[22:23], v[58:59]
	v_and_b32_sdwa v58, v63, v1 dst_sel:DWORD dst_unused:UNUSED_PAD src0_sel:WORD_1 src1_sel:DWORD
	v_and_b32_sdwa v59, v62, v1 dst_sel:DWORD dst_unused:UNUSED_PAD src0_sel:WORD_1 src1_sel:DWORD
	v_add3_u32 v59, v62, v59, s25
	v_add3_u32 v58, v63, v58, s25
	v_and_b32_sdwa v62, v23, v1 dst_sel:DWORD dst_unused:UNUSED_PAD src0_sel:WORD_1 src1_sel:DWORD
	v_and_b32_sdwa v63, v22, v1 dst_sel:DWORD dst_unused:UNUSED_PAD src0_sel:WORD_1 src1_sel:DWORD
	v_add3_u32 v23, v23, v62, s25
	v_add3_u32 v22, v22, v63, s25
	v_and_b32_e32 v23, 0xffff0000, v23
	v_and_b32_e32 v22, 0xffff0000, v22
	v_or_b32_sdwa v23, v23, v58 dst_sel:DWORD dst_unused:UNUSED_PAD src0_sel:DWORD src1_sel:WORD_1
	v_or_b32_sdwa v22, v22, v59 dst_sel:DWORD dst_unused:UNUSED_PAD src0_sel:DWORD src1_sel:WORD_1
	v_and_b32_e32 v58, 0xffff0000, v24
	v_lshlrev_b32_e32 v59, 16, v24
	v_and_b32_e32 v62, 0xffff0000, v60
	v_lshlrev_b32_e32 v63, 16, v60
	v_pk_add_f32 v[58:59], v[58:59], v[62:63]
	v_add3_u32 v3, v3, v94, s25
	v_and_b32_sdwa v24, v59, v1 dst_sel:DWORD dst_unused:UNUSED_PAD src0_sel:WORD_1 src1_sel:DWORD
	v_and_b32_sdwa v60, v58, v1 dst_sel:DWORD dst_unused:UNUSED_PAD src0_sel:WORD_1 src1_sel:DWORD
	v_add3_u32 v24, v59, v24, s25
	v_add3_u32 v58, v58, v60, s25
	v_lshrrev_b32_e32 v24, 16, v24
	v_and_or_b32 v24, v58, s24, v24
	v_and_b32_e32 v58, 0xffff0000, v25
	v_lshlrev_b32_e32 v59, 16, v25
	v_and_b32_e32 v60, 0xffff0000, v61
	v_lshlrev_b32_e32 v61, 16, v61
	v_pk_add_f32 v[58:59], v[58:59], v[60:61]
	s_waitcnt vmcnt(1)
	v_lshlrev_b32_e32 v61, 16, v55
	v_and_b32_sdwa v25, v59, v1 dst_sel:DWORD dst_unused:UNUSED_PAD src0_sel:WORD_1 src1_sel:DWORD
	v_and_b32_sdwa v60, v58, v1 dst_sel:DWORD dst_unused:UNUSED_PAD src0_sel:WORD_1 src1_sel:DWORD
	v_add3_u32 v25, v59, v25, s25
	v_add3_u32 v58, v58, v60, s25
	v_lshrrev_b32_e32 v25, 16, v25
	v_and_or_b32 v25, v58, s24, v25
	v_lshlrev_b32_e32 v59, 16, v27
	v_lshlrev_b32_e32 v58, 16, v26
	v_lshlrev_b32_e32 v60, 16, v54
	v_pk_add_f32 v[58:59], v[58:59], v[60:61]
	v_and_b32_e32 v27, 0xffff0000, v27
	v_and_b32_e32 v26, 0xffff0000, v26
	v_and_b32_e32 v55, 0xffff0000, v55
	v_and_b32_e32 v54, 0xffff0000, v54
	v_pk_add_f32 v[26:27], v[26:27], v[54:55]
	v_and_b32_sdwa v54, v59, v1 dst_sel:DWORD dst_unused:UNUSED_PAD src0_sel:WORD_1 src1_sel:DWORD
	v_and_b32_sdwa v55, v58, v1 dst_sel:DWORD dst_unused:UNUSED_PAD src0_sel:WORD_1 src1_sel:DWORD
	v_add3_u32 v55, v58, v55, s25
	v_add3_u32 v54, v59, v54, s25
	v_and_b32_sdwa v58, v27, v1 dst_sel:DWORD dst_unused:UNUSED_PAD src0_sel:WORD_1 src1_sel:DWORD
	v_and_b32_sdwa v59, v26, v1 dst_sel:DWORD dst_unused:UNUSED_PAD src0_sel:WORD_1 src1_sel:DWORD
	v_add3_u32 v27, v27, v58, s25
	v_add3_u32 v26, v26, v59, s25
	v_and_b32_e32 v27, 0xffff0000, v27
	v_and_b32_e32 v26, 0xffff0000, v26
	v_or_b32_sdwa v27, v27, v54 dst_sel:DWORD dst_unused:UNUSED_PAD src0_sel:DWORD src1_sel:WORD_1
	v_or_b32_sdwa v26, v26, v55 dst_sel:DWORD dst_unused:UNUSED_PAD src0_sel:DWORD src1_sel:WORD_1
	v_and_b32_e32 v54, 0xffff0000, v28
	v_lshlrev_b32_e32 v55, 16, v28
	v_and_b32_e32 v58, 0xffff0000, v56
	v_lshlrev_b32_e32 v59, 16, v56
	v_pk_add_f32 v[54:55], v[54:55], v[58:59]
	v_and_b32_sdwa v95, v2, v1 dst_sel:DWORD dst_unused:UNUSED_PAD src0_sel:WORD_1 src1_sel:DWORD
	v_and_b32_sdwa v28, v55, v1 dst_sel:DWORD dst_unused:UNUSED_PAD src0_sel:WORD_1 src1_sel:DWORD
	v_and_b32_sdwa v56, v54, v1 dst_sel:DWORD dst_unused:UNUSED_PAD src0_sel:WORD_1 src1_sel:DWORD
	v_add3_u32 v28, v55, v28, s25
	v_add3_u32 v54, v54, v56, s25
	v_lshrrev_b32_e32 v28, 16, v28
	v_and_or_b32 v28, v54, s24, v28
	v_and_b32_e32 v54, 0xffff0000, v29
	v_lshlrev_b32_e32 v55, 16, v29
	v_and_b32_e32 v56, 0xffff0000, v57
	v_lshlrev_b32_e32 v57, 16, v57
	v_pk_add_f32 v[54:55], v[54:55], v[56:57]
	s_waitcnt vmcnt(0)
	v_lshlrev_b32_e32 v57, 16, v51
	v_and_b32_sdwa v29, v55, v1 dst_sel:DWORD dst_unused:UNUSED_PAD src0_sel:WORD_1 src1_sel:DWORD
	v_and_b32_sdwa v56, v54, v1 dst_sel:DWORD dst_unused:UNUSED_PAD src0_sel:WORD_1 src1_sel:DWORD
	v_add3_u32 v29, v55, v29, s25
	v_add3_u32 v54, v54, v56, s25
	v_lshrrev_b32_e32 v29, 16, v29
	v_and_or_b32 v29, v54, s24, v29
	v_lshlrev_b32_e32 v55, 16, v31
	v_lshlrev_b32_e32 v54, 16, v30
	v_lshlrev_b32_e32 v56, 16, v50
	v_pk_add_f32 v[54:55], v[54:55], v[56:57]
	v_and_b32_e32 v31, 0xffff0000, v31
	v_and_b32_e32 v30, 0xffff0000, v30
	v_and_b32_e32 v51, 0xffff0000, v51
	v_and_b32_e32 v50, 0xffff0000, v50
	v_pk_add_f32 v[30:31], v[30:31], v[50:51]
	v_and_b32_sdwa v50, v55, v1 dst_sel:DWORD dst_unused:UNUSED_PAD src0_sel:WORD_1 src1_sel:DWORD
	v_and_b32_sdwa v51, v54, v1 dst_sel:DWORD dst_unused:UNUSED_PAD src0_sel:WORD_1 src1_sel:DWORD
	v_add3_u32 v51, v54, v51, s25
	v_add3_u32 v50, v55, v50, s25
	v_and_b32_sdwa v54, v31, v1 dst_sel:DWORD dst_unused:UNUSED_PAD src0_sel:WORD_1 src1_sel:DWORD
	v_and_b32_sdwa v55, v30, v1 dst_sel:DWORD dst_unused:UNUSED_PAD src0_sel:WORD_1 src1_sel:DWORD
	v_add3_u32 v31, v31, v54, s25
	v_add3_u32 v30, v30, v55, s25
	v_and_b32_e32 v31, 0xffff0000, v31
	v_and_b32_e32 v30, 0xffff0000, v30
	v_or_b32_sdwa v31, v31, v50 dst_sel:DWORD dst_unused:UNUSED_PAD src0_sel:DWORD src1_sel:WORD_1
	v_or_b32_sdwa v30, v30, v51 dst_sel:DWORD dst_unused:UNUSED_PAD src0_sel:DWORD src1_sel:WORD_1
	v_and_b32_e32 v50, 0xffff0000, v32
	v_lshlrev_b32_e32 v51, 16, v32
	v_and_b32_e32 v54, 0xffff0000, v52
	v_lshlrev_b32_e32 v55, 16, v52
	v_pk_add_f32 v[50:51], v[50:51], v[54:55]
	v_and_b32_sdwa v104, v79, v1 dst_sel:DWORD dst_unused:UNUSED_PAD src0_sel:WORD_1 src1_sel:DWORD
	v_and_b32_sdwa v32, v51, v1 dst_sel:DWORD dst_unused:UNUSED_PAD src0_sel:WORD_1 src1_sel:DWORD
	v_and_b32_sdwa v52, v50, v1 dst_sel:DWORD dst_unused:UNUSED_PAD src0_sel:WORD_1 src1_sel:DWORD
	v_add3_u32 v32, v51, v32, s25
	v_add3_u32 v50, v50, v52, s25
	v_lshrrev_b32_e32 v32, 16, v32
	v_and_or_b32 v32, v50, s24, v32
	v_and_b32_e32 v50, 0xffff0000, v33
	v_lshlrev_b32_e32 v51, 16, v33
	v_and_b32_e32 v52, 0xffff0000, v53
	v_lshlrev_b32_e32 v53, 16, v53
	v_pk_add_f32 v[50:51], v[50:51], v[52:53]
	v_and_b32_e32 v3, 0xffff0000, v3
	v_and_b32_sdwa v33, v51, v1 dst_sel:DWORD dst_unused:UNUSED_PAD src0_sel:WORD_1 src1_sel:DWORD
	v_and_b32_sdwa v105, v78, v1 dst_sel:DWORD dst_unused:UNUSED_PAD src0_sel:WORD_1 src1_sel:DWORD
	v_add3_u32 v2, v2, v95, s25
	v_or_b32_sdwa v3, v3, v8 dst_sel:DWORD dst_unused:UNUSED_PAD src0_sel:DWORD src1_sel:WORD_1
	v_add3_u32 v8, v79, v104, s25
	v_and_b32_sdwa v52, v50, v1 dst_sel:DWORD dst_unused:UNUSED_PAD src0_sel:WORD_1 src1_sel:DWORD
	v_add3_u32 v33, v51, v33, s25
	v_add3_u32 v78, v78, v105, s25
	v_and_b32_e32 v2, 0xffff0000, v2
	v_lshrrev_b32_e32 v8, 16, v8
	v_add3_u32 v50, v50, v52, s25
	v_lshrrev_b32_e32 v33, 16, v33
	v_or_b32_sdwa v2, v2, v80 dst_sel:DWORD dst_unused:UNUSED_PAD src0_sel:DWORD src1_sel:WORD_1
	v_and_or_b32 v8, v78, s24, v8
	v_and_or_b32 v33, v50, s24, v33

.LBB0_1374:
	s_cmp_gt_u32 s19, 1
	s_cbranch_scc1 .LBB0_1376
	s_waitcnt vmcnt(3)
	v_lshl_add_u64 v[74:75], v[124:125], 0, s[22:23]
	s_waitcnt vmcnt(2)
	v_add_co_u32_e32 v78, vcc, 0x240000, v74
	s_waitcnt vmcnt(1)
	v_lshl_add_u64 v[82:83], v[126:127], 0, s[22:23]
	v_addc_co_u32_e32 v79, vcc, 0, v75, vcc
	s_waitcnt vmcnt(0)
	v_add_co_u32_e32 v90, vcc, 0x240000, v82
	global_load_dwordx4 v[74:77], v[78:79], off
	global_load_dwordx4 v[78:81], v[78:79], off offset:1024
	v_addc_co_u32_e32 v91, vcc, 0, v83, vcc
	global_load_dwordx4 v[82:85], v[90:91], off
	global_load_dwordx4 v[90:93], v[90:91], off offset:1024

.LBB0_1477:
	s_waitcnt vmcnt(0) lgkmcnt(0)
	s_barrier
	ds_read_b32 v138, v155 offset:10240
	s_and_saveexec_b64 s[6:7], s[4:5]
	s_cbranch_execz .LBB0_1479
	v_lshlrev_b64 v[58:59], 6, v[58:59]
	v_lshl_add_u64 v[58:59], s[16:17], 0, v[58:59]
	global_load_dword v61, v[58:59], off sc1
	global_load_dword v140, v[58:59], off offset:4 sc1
	global_load_dword v141, v[58:59], off offset:8 sc1
	global_load_dword v142, v[58:59], off offset:12 sc1
	global_load_dword v143, v[58:59], off offset:16 sc1
	global_load_dword v144, v[58:59], off offset:20 sc1
	global_load_dword v145, v[58:59], off offset:24 sc1
	global_load_dword v146, v[58:59], off offset:28 sc1
	global_load_dword v147, v[58:59], off offset:32 sc1
	global_load_dword v148, v[58:59], off offset:36 sc1
	global_load_dword v149, v[58:59], off offset:40 sc1
	global_load_dword v150, v[58:59], off offset:44 sc1
	global_load_dword v151, v[58:59], off offset:48 sc1
	global_load_dword v152, v[58:59], off offset:52 sc1
	global_load_dword v153, v[58:59], off offset:56 sc1
	global_load_dword v58, v[58:59], off offset:60 sc1
	s_waitcnt vmcnt(15)
	v_add_f32_e32 v59, 0, v61
	s_waitcnt vmcnt(14)
	v_add_f32_e32 v59, v59, v140
	s_waitcnt vmcnt(13)
	v_add_f32_e32 v59, v59, v141
	s_waitcnt vmcnt(12)
	v_add_f32_e32 v59, v59, v142
	s_waitcnt vmcnt(11)
	v_add_f32_e32 v59, v59, v143
	s_waitcnt vmcnt(10)
	v_add_f32_e32 v59, v59, v144
	s_waitcnt vmcnt(9)
	v_add_f32_e32 v59, v59, v145
	s_waitcnt vmcnt(8)
	v_add_f32_e32 v59, v59, v146
	s_waitcnt vmcnt(7)
	v_add_f32_e32 v59, v59, v147
	s_waitcnt vmcnt(6)
	v_add_f32_e32 v59, v59, v148
	s_waitcnt vmcnt(5)
	v_add_f32_e32 v59, v59, v149
	s_waitcnt vmcnt(4)
	v_add_f32_e32 v59, v59, v150
	s_waitcnt vmcnt(3)
	v_add_f32_e32 v59, v59, v151
	s_waitcnt vmcnt(2)
	v_add_f32_e32 v59, v59, v152
	s_waitcnt vmcnt(1)
	v_add_f32_e32 v59, v59, v153
	s_waitcnt vmcnt(0)
	v_add_f32_e32 v58, v59, v58
	v_fmamk_f32 v58, v58, 0x39800000, v185
	v_mul_f32_e32 v59, 0x4f800000, v58
	v_cmp_gt_f32_e32 vcc, s62, v58
	s_nop 1
	v_cndmask_b32_e32 v58, v58, v59, vcc
	v_sqrt_f32_e32 v59, v58
	s_nop 0
	v_add_u32_e32 v61, -1, v59
	v_add_u32_e32 v140, 1, v59
	v_fma_f32 v141, -v61, v59, v58
	v_fma_f32 v142, -v140, v59, v58
	v_cmp_ge_f32_e64 s[4:5], 0, v141
	s_nop 1
	v_cndmask_b32_e64 v59, v59, v61, s[4:5]
	v_cmp_lt_f32_e64 s[4:5], 0, v142
	s_nop 1
	v_cndmask_b32_e64 v59, v59, v140, s[4:5]
	v_mul_f32_e32 v61, 0x37800000, v59
	v_cndmask_b32_e32 v59, v59, v61, vcc
	v_cmp_class_f32_e32 vcc, v58, v186
	s_nop 1
	v_cndmask_b32_e32 v58, v59, v58, vcc
	v_div_scale_f32 v59, s[4:5], v58, v58, 1.0
	v_rcp_f32_e32 v61, v59
	v_div_scale_f32 v140, vcc, 1.0, v58, 1.0
	v_fma_f32 v141, -v59, v61, 1.0
	v_fmac_f32_e32 v61, v141, v61
	v_mul_f32_e32 v141, v140, v61
	v_fma_f32 v142, -v59, v141, v140
	v_fmac_f32_e32 v141, v142, v61
	v_fma_f32 v59, -v59, v141, v140
	v_div_fmas_f32 v59, v59, v61, v141
	v_div_fixup_f32 v58, v59, v58, 1.0
	v_lshl_add_u32 v59, v60, 2, 0
	ds_write_b32 v59, v58 offset:8192

.LBB0_1619:
	v_add_co_u32_e64 v94, s[4:5], s12, v72
	v_add_co_u32_e32 v76, vcc, 0xffffd000, v72
	s_nop 0
	v_addc_co_u32_e64 v95, s[4:5], -1, v73, s[4:5]
	v_add_co_u32_e64 v96, s[4:5], s13, v72
	global_load_dwordx4 v[14:17], v[72:73], off offset:-3072
	global_load_dwordx4 v[10:13], v[72:73], off offset:-2048
	global_load_dwordx4 v[6:9], v[72:73], off offset:-1024
	global_load_dwordx4 v[2:5], v[72:73], off
	global_load_dwordx4 v[86:89], v[46:47], off
	v_addc_co_u32_e64 v97, s[4:5], -1, v73, s[4:5]
	v_addc_co_u32_e32 v77, vcc, -1, v73, vcc
	global_load_dwordx4 v[90:93], v[94:95], off offset:-3072
	global_load_dwordx4 v[42:45], v[94:95], off offset:-2048
	global_load_dwordx4 v[38:41], v[94:95], off offset:-1024
	global_load_dwordx4 v[34:37], v[94:95], off
	global_load_dwordx4 v[30:33], v[96:97], off offset:-3072
	global_load_dwordx4 v[26:29], v[96:97], off offset:-2048
	global_load_dwordx4 v[22:25], v[96:97], off offset:-1024
	global_load_dwordx4 v[18:21], v[72:73], off offset:-4096
	global_load_dwordx4 v[94:97], v[76:77], off offset:-3072
	global_load_dwordx4 v[98:101], v[76:77], off offset:-2048
	global_load_dwordx4 v[102:105], v[76:77], off offset:-1024
	global_load_dwordx4 v[106:109], v[76:77], off
	v_mov_b32_e32 v111, 0
	v_mov_b32_e32 v112, 0
	v_mov_b32_e32 v113, 0
	s_add_i32 s3, s3, s92
	v_lshl_add_u64 v[72:73], v[72:73], 0, s[6:7]
	s_cmpk_lt_i32 s3, 0x4000
	s_waitcnt vmcnt(0)
	v_mul_f32_e32 v76, v15, v15
	v_mul_f32_e32 v77, v17, v17
	v_mul_f32_e32 v114, v11, v11
	v_mul_f32_e32 v115, v13, v13
	v_mul_f32_e32 v118, v3, v3
	v_mul_f32_e32 v119, v5, v5
	v_mul_f32_e32 v124, v39, v39
	v_mul_f32_e32 v125, v41, v41
	v_mul_f32_e32 v136, v95, v95
	v_mul_f32_e32 v137, v97, v97
	v_mul_f32_e32 v138, v99, v99
	v_mul_f32_e32 v139, v101, v101
	v_mul_f32_e32 v126, v35, v35
	v_mul_f32_e32 v127, v37, v37
	v_fmac_f32_e32 v76, v14, v14
	v_fmac_f32_e32 v77, v16, v16
	v_fmac_f32_e32 v114, v10, v10
	v_fmac_f32_e32 v115, v12, v12
	v_fmac_f32_e32 v118, v2, v2
	v_fmac_f32_e32 v119, v4, v4
	v_mul_f32_e32 v140, v103, v103
	v_mul_f32_e32 v141, v105, v105
	v_fmac_f32_e32 v124, v38, v38
	v_fmac_f32_e32 v125, v40, v40
	v_fmac_f32_e32 v136, v94, v94
	v_fmac_f32_e32 v137, v96, v96
	v_fmac_f32_e32 v138, v98, v98
	v_fmac_f32_e32 v139, v100, v100
	v_mul_f32_e32 v142, v107, v107
	v_mul_f32_e32 v143, v109, v109
	v_fmac_f32_e32 v126, v34, v34
	v_fmac_f32_e32 v127, v36, v36
	v_add_f32_e32 v76, v76, v77
	v_add_f32_e32 v77, v114, v115
	v_add_f32_e32 v115, v118, v119
	v_fmac_f32_e32 v140, v102, v102
	v_fmac_f32_e32 v141, v104, v104
	v_add_f32_e32 v118, v124, v125
	v_add_f32_e32 v124, v136, v137
	v_add_f32_e32 v125, v138, v139
	v_mul_f32_e32 v116, v7, v7
	v_mul_f32_e32 v117, v9, v9
	v_mul_f32_e32 v120, v91, v91
	v_mul_f32_e32 v121, v93, v93
	v_fmac_f32_e32 v142, v106, v106
	v_fmac_f32_e32 v143, v108, v108
	v_add_f32_e32 v119, v126, v127
	v_add_f32_e32 v126, v140, v141
	v_add_f32_e32 v124, v124, v125
	v_mul_f32_e32 v122, v43, v43
	v_mul_f32_e32 v123, v45, v45
	v_fmac_f32_e32 v116, v6, v6
	v_fmac_f32_e32 v117, v8, v8
	v_fmac_f32_e32 v120, v90, v90
	v_fmac_f32_e32 v121, v92, v92
	v_add_f32_e32 v127, v142, v143
	v_add_f32_e32 v124, v124, v126
	v_fmac_f32_e32 v122, v42, v42
	v_fmac_f32_e32 v123, v44, v44
	v_add_f32_e32 v114, v116, v117
	v_add_f32_e32 v116, v120, v121
	v_add_f32_e32 v124, v124, v127
	v_add_f32_e32 v117, v122, v123
	v_add_f32_e32 v116, v124, v116
	v_mul_f32_e32 v128, v31, v31
	v_mul_f32_e32 v129, v33, v33
	v_add_f32_e32 v116, v116, v117
	v_mul_f32_e32 v130, v27, v27
	v_mul_f32_e32 v131, v29, v29
	v_fmac_f32_e32 v128, v30, v30
	v_fmac_f32_e32 v129, v32, v32
	v_add_f32_e32 v116, v116, v118
	v_mul_f32_e32 v132, v23, v23
	v_mul_f32_e32 v133, v25, v25
	v_fmac_f32_e32 v130, v26, v26
	v_fmac_f32_e32 v131, v28, v28
	v_add_f32_e32 v120, v128, v129
	v_add_f32_e32 v116, v116, v119
	v_mul_f32_e32 v134, v19, v19
	v_mul_f32_e32 v135, v21, v21
	v_fmac_f32_e32 v132, v22, v22
	v_fmac_f32_e32 v133, v24, v24
	v_add_f32_e32 v121, v130, v131
	v_add_f32_e32 v116, v116, v120
	v_fmac_f32_e32 v134, v18, v18
	v_fmac_f32_e32 v135, v20, v20
	v_add_f32_e32 v122, v132, v133
	v_add_f32_e32 v116, v116, v121
	v_add_f32_e32 v123, v134, v135
	v_add_f32_e32 v116, v116, v122
	v_add_f32_e32 v116, v116, v123
	v_add_f32_e32 v76, v116, v76
	v_add_f32_e32 v76, v76, v77
	v_add_f32_e32 v76, v76, v114
	v_add_f32_e32 v76, v76, v115
	ds_bpermute_b32 v77, v1, v76
	s_waitcnt lgkmcnt(0)
	v_add_f32_e32 v76, v76, v77
	ds_bpermute_b32 v77, v78, v76
	s_waitcnt lgkmcnt(0)
	v_add_f32_e32 v76, v76, v77
	ds_bpermute_b32 v77, v79, v76
	s_waitcnt lgkmcnt(0)
	v_add_f32_e32 v76, v76, v77
	ds_bpermute_b32 v77, v80, v76
	s_waitcnt lgkmcnt(0)
	v_add_f32_e32 v76, v76, v77
	ds_bpermute_b32 v77, v81, v76
	s_waitcnt lgkmcnt(0)
	v_add_f32_e32 v76, v76, v77
	ds_bpermute_b32 v77, v82, v76
	s_waitcnt lgkmcnt(0)
	v_add_f32_e32 v76, v76, v77
	v_fmamk_f32 v76, v76, 0x39800000, v83
	v_mul_f32_e32 v77, 0x4f800000, v76
	v_cmp_gt_f32_e32 vcc, s14, v76
	s_nop 1
	v_cndmask_b32_e32 v76, v76, v77, vcc
	v_sqrt_f32_e32 v77, v76
	s_nop 0
	v_add_u32_e32 v114, -1, v77
	v_add_u32_e32 v115, 1, v77
	v_fma_f32 v116, -v114, v77, v76
	v_fma_f32 v117, -v115, v77, v76
	v_cmp_ge_f32_e64 s[4:5], 0, v116
	s_nop 1
	v_cndmask_b32_e64 v77, v77, v114, s[4:5]
	v_cmp_lt_f32_e64 s[4:5], 0, v117
	s_nop 1
	v_cndmask_b32_e64 v77, v77, v115, s[4:5]
	v_mul_f32_e32 v114, 0x37800000, v77
	v_cndmask_b32_e32 v77, v77, v114, vcc
	v_cmp_class_f32_e32 vcc, v76, v84
	s_nop 1
	v_cndmask_b32_e32 v76, v77, v76, vcc
	v_div_scale_f32 v77, s[4:5], v76, v76, 1.0
	v_rcp_f32_e32 v115, v77
	v_div_scale_f32 v114, vcc, 1.0, v76, 1.0
	v_fma_f32 v116, -v77, v115, 1.0
	v_fmac_f32_e32 v115, v116, v115
	v_mul_f32_e32 v116, v114, v115
	v_fma_f32 v117, -v77, v116, v114
	v_fmac_f32_e32 v116, v117, v115
	v_fma_f32 v77, -v77, v116, v114
	v_div_fmas_f32 v77, v77, v115, v116
	v_div_fixup_f32 v76, v77, v76, 1.0
	v_mul_f32_e32 v77, v94, v76
	v_mul_f32_e32 v94, v95, v76
	v_mul_f32_e32 v77, v86, v77
	v_mul_f32_e32 v86, v87, v94
	v_med3_f32 v77, v77, s15, v85
	v_med3_f32 v86, v86, s15, v85
	v_cvt_pk_fp8_f32 v110, v77, v86
	v_mul_f32_e32 v95, v96, v76
	v_mul_f32_e32 v96, v97, v76
	v_mul_f32_e32 v87, v88, v95
	v_mul_f32_e32 v88, v89, v96
	v_med3_f32 v87, v87, s15, v85
	v_med3_f32 v88, v88, s15, v85
	v_cvt_pk_fp8_f32 v110, v87, v88 op_sel:[0,0,1]
	v_mul_f32_e32 v97, v98, v76
	v_mul_f32_e32 v98, v99, v76
	v_mul_f32_e32 v99, v100, v76
	global_store_dword v[74:75], v110, off offset:-2048
	global_load_dwordx4 v[86:89], v[46:47], off offset:1024
	v_mul_f32_e32 v100, v101, v76
	v_mul_f32_e32 v101, v102, v76
	v_mul_f32_e32 v102, v103, v76
	v_mul_f32_e32 v103, v104, v76
	v_mul_f32_e32 v104, v105, v76
	v_mul_f32_e32 v105, v106, v76
	v_mul_f32_e32 v106, v107, v76
	v_mul_f32_e32 v94, v109, v76
	v_mul_f32_e32 v90, v90, v76
	v_mul_f32_e32 v91, v91, v76
	v_mul_f32_e32 v92, v92, v76
	v_mul_f32_e32 v93, v93, v76
	v_mul_f32_e32 v42, v42, v76
	v_mul_f32_e32 v43, v43, v76
	v_mul_f32_e32 v44, v44, v76
	v_mul_f32_e32 v45, v45, v76
	v_mul_f32_e32 v38, v38, v76
	v_mul_f32_e32 v39, v39, v76
	v_mul_f32_e32 v40, v40, v76
	v_mul_f32_e32 v41, v41, v76
	v_mul_f32_e32 v34, v34, v76
	v_mul_f32_e32 v35, v35, v76
	v_mul_f32_e32 v36, v36, v76
	v_mul_f32_e32 v37, v37, v76
	v_mul_f32_e32 v30, v30, v76
	v_mul_f32_e32 v31, v31, v76
	v_mul_f32_e32 v32, v32, v76
	v_mul_f32_e32 v33, v33, v76
	v_mul_f32_e32 v26, v26, v76
	v_mul_f32_e32 v27, v27, v76
	v_mul_f32_e32 v28, v28, v76
	v_mul_f32_e32 v29, v29, v76
	v_mul_f32_e32 v22, v22, v76
	v_mul_f32_e32 v23, v23, v76
	v_mul_f32_e32 v24, v24, v76
	v_mul_f32_e32 v25, v25, v76
	v_mul_f32_e32 v18, v18, v76
	v_mul_f32_e32 v19, v19, v76
	v_mul_f32_e32 v20, v20, v76
	v_mul_f32_e32 v21, v21, v76
	v_mul_f32_e32 v14, v14, v76
	v_mul_f32_e32 v15, v15, v76
	v_mul_f32_e32 v16, v16, v76
	v_mul_f32_e32 v17, v17, v76
	v_mul_f32_e32 v10, v10, v76
	v_mul_f32_e32 v11, v11, v76
	v_mul_f32_e32 v12, v12, v76
	v_mul_f32_e32 v13, v13, v76
	v_mul_f32_e32 v6, v6, v76
	v_mul_f32_e32 v7, v7, v76
	v_mul_f32_e32 v8, v8, v76
	v_mul_f32_e32 v9, v9, v76
	v_mul_f32_e32 v2, v2, v76
	v_mul_f32_e32 v3, v3, v76
	v_mul_f32_e32 v4, v4, v76
	v_mul_f32_e32 v5, v5, v76
	s_waitcnt vmcnt(0)
	v_mul_f32_e32 v77, v86, v97
	v_mul_f32_e32 v86, v87, v98
	v_med3_f32 v77, v77, s15, v85
	v_med3_f32 v86, v86, s15, v85
	v_cvt_pk_fp8_f32 v111, v77, v86
	v_mul_f32_e32 v87, v88, v99
	v_mul_f32_e32 v88, v89, v100
	v_med3_f32 v87, v87, s15, v85
	v_med3_f32 v88, v88, s15, v85
	v_cvt_pk_fp8_f32 v111, v87, v88 op_sel:[0,0,1]
	global_store_dword v[74:75], v111, off offset:-1792
	global_load_dwordx4 v[86:89], v[46:47], off offset:2048
	s_waitcnt vmcnt(0)
	v_mul_f32_e32 v77, v101, v86
	v_mul_f32_e32 v86, v102, v87
	v_med3_f32 v77, v77, s15, v85
	v_med3_f32 v86, v86, s15, v85
	v_cvt_pk_fp8_f32 v112, v77, v86
	v_mul_f32_e32 v87, v103, v88
	v_mul_f32_e32 v88, v104, v89
	v_med3_f32 v87, v87, s15, v85
	v_med3_f32 v88, v88, s15, v85
	v_cvt_pk_fp8_f32 v112, v87, v88 op_sel:[0,0,1]
	v_mul_f32_e32 v77, v108, v76
	global_store_dword v[74:75], v112, off offset:-1536
	global_load_dwordx4 v[86:89], v[46:47], off offset:3072
	s_waitcnt vmcnt(0)
	v_mul_f32_e32 v86, v105, v86
	v_mul_f32_e32 v87, v106, v87
	v_med3_f32 v86, v86, s15, v85
	v_med3_f32 v87, v87, s15, v85
	v_cvt_pk_fp8_f32 v113, v86, v87
	v_mul_f32_e32 v77, v77, v88
	v_mul_f32_e32 v88, v94, v89
	v_med3_f32 v77, v77, s15, v85
	v_med3_f32 v88, v88, s15, v85
	v_cvt_pk_fp8_f32 v113, v77, v88 op_sel:[0,0,1]
	global_store_dword v[74:75], v113, off offset:-1280
	global_load_dwordx4 v[86:89], v[48:49], off
	s_waitcnt vmcnt(0)
	v_mul_f32_e32 v86, v90, v86
	v_mul_f32_e32 v87, v91, v87
	v_med3_f32 v86, v86, s15, v85
	v_med3_f32 v87, v87, s15, v85
	v_cvt_pk_fp8_f32 v77, v86, v87
	v_mul_f32_e32 v88, v92, v88
	v_mul_f32_e32 v89, v93, v89
	v_med3_f32 v88, v88, s15, v85
	v_med3_f32 v89, v89, s15, v85
	v_cvt_pk_fp8_f32 v77, v88, v89 op_sel:[0,0,1]
	global_store_dword v[74:75], v77, off offset:-1024
	global_load_dwordx4 v[86:89], v[50:51], off
	s_waitcnt vmcnt(0)
	v_mul_f32_e32 v42, v42, v86
	v_mul_f32_e32 v43, v43, v87
	v_med3_f32 v42, v42, s15, v85
	v_med3_f32 v43, v43, s15, v85
	v_cvt_pk_fp8_f32 v77, v42, v43
	v_mul_f32_e32 v44, v44, v88
	v_mul_f32_e32 v45, v45, v89
	v_med3_f32 v44, v44, s15, v85
	v_med3_f32 v45, v45, s15, v85
	v_cvt_pk_fp8_f32 v77, v44, v45 op_sel:[0,0,1]
	global_store_dword v[74:75], v77, off offset:-768
	global_load_dwordx4 v[42:45], v[52:53], off
	s_waitcnt vmcnt(0)
	v_mul_f32_e32 v38, v38, v42
	v_mul_f32_e32 v39, v39, v43
	v_med3_f32 v38, v38, s15, v85
	v_med3_f32 v39, v39, s15, v85
	v_cvt_pk_fp8_f32 v77, v38, v39
	v_mul_f32_e32 v40, v40, v44
	v_mul_f32_e32 v41, v41, v45
	v_med3_f32 v40, v40, s15, v85
	v_med3_f32 v41, v41, s15, v85
	v_cvt_pk_fp8_f32 v77, v40, v41 op_sel:[0,0,1]
	global_store_dword v[74:75], v77, off offset:-512
	global_load_dwordx4 v[38:41], v[54:55], off
	s_waitcnt vmcnt(0)
	v_mul_f32_e32 v34, v34, v38
	v_mul_f32_e32 v35, v35, v39
	v_med3_f32 v34, v34, s15, v85
	v_med3_f32 v35, v35, s15, v85
	v_cvt_pk_fp8_f32 v42, v34, v35
	v_mul_f32_e32 v36, v36, v40
	v_mul_f32_e32 v37, v37, v41
	v_med3_f32 v36, v36, s15, v85
	v_med3_f32 v37, v37, s15, v85
	v_cvt_pk_fp8_f32 v42, v36, v37 op_sel:[0,0,1]
	global_store_dword v[74:75], v42, off offset:-256
	global_load_dwordx4 v[34:37], v[56:57], off
	s_waitcnt vmcnt(0)
	v_mul_f32_e32 v30, v30, v34
	v_mul_f32_e32 v31, v31, v35
	v_med3_f32 v30, v30, s15, v85
	v_med3_f32 v31, v31, s15, v85
	v_cvt_pk_fp8_f32 v38, v30, v31
	v_mul_f32_e32 v32, v32, v36
	v_mul_f32_e32 v33, v33, v37
	v_med3_f32 v32, v32, s15, v85
	v_med3_f32 v33, v33, s15, v85
	v_cvt_pk_fp8_f32 v38, v32, v33 op_sel:[0,0,1]
	global_store_dword v[74:75], v38, off
	global_load_dwordx4 v[30:33], v[58:59], off
	s_waitcnt vmcnt(0)
	v_mul_f32_e32 v26, v26, v30
	v_mul_f32_e32 v27, v27, v31
	v_med3_f32 v26, v26, s15, v85
	v_med3_f32 v27, v27, s15, v85
	v_cvt_pk_fp8_f32 v34, v26, v27
	v_mul_f32_e32 v28, v28, v32
	v_mul_f32_e32 v29, v29, v33
	v_med3_f32 v28, v28, s15, v85
	v_med3_f32 v29, v29, s15, v85
	v_cvt_pk_fp8_f32 v34, v28, v29 op_sel:[0,0,1]
	global_store_dword v[74:75], v34, off offset:256
	global_load_dwordx4 v[26:29], v[60:61], off
	s_waitcnt vmcnt(0)
	v_mul_f32_e32 v22, v22, v26
	v_mul_f32_e32 v23, v23, v27
	v_med3_f32 v22, v22, s15, v85
	v_med3_f32 v23, v23, s15, v85
	v_cvt_pk_fp8_f32 v30, v22, v23
	v_mul_f32_e32 v24, v24, v28
	v_mul_f32_e32 v25, v25, v29
	v_med3_f32 v24, v24, s15, v85
	v_med3_f32 v25, v25, s15, v85
	v_cvt_pk_fp8_f32 v30, v24, v25 op_sel:[0,0,1]
	global_store_dword v[74:75], v30, off offset:512
	global_load_dwordx4 v[22:25], v[62:63], off
	s_waitcnt vmcnt(0)
	v_mul_f32_e32 v18, v18, v22
	v_mul_f32_e32 v19, v19, v23
	v_med3_f32 v18, v18, s15, v85
	v_med3_f32 v19, v19, s15, v85
	v_cvt_pk_fp8_f32 v26, v18, v19
	v_mul_f32_e32 v20, v20, v24
	v_mul_f32_e32 v21, v21, v25
	v_med3_f32 v20, v20, s15, v85
	v_med3_f32 v21, v21, s15, v85
	v_cvt_pk_fp8_f32 v26, v20, v21 op_sel:[0,0,1]
	global_store_dword v[74:75], v26, off offset:768
	global_load_dwordx4 v[18:21], v[64:65], off
	s_waitcnt vmcnt(0)
	v_mul_f32_e32 v14, v14, v18
	v_mul_f32_e32 v15, v15, v19
	v_med3_f32 v14, v14, s15, v85
	v_med3_f32 v15, v15, s15, v85
	v_cvt_pk_fp8_f32 v22, v14, v15
	v_mul_f32_e32 v16, v16, v20
	v_mul_f32_e32 v17, v17, v21
	v_med3_f32 v16, v16, s15, v85
	v_med3_f32 v17, v17, s15, v85
	v_cvt_pk_fp8_f32 v22, v16, v17 op_sel:[0,0,1]
	global_store_dword v[74:75], v22, off offset:1024
	global_load_dwordx4 v[14:17], v[66:67], off
	s_waitcnt vmcnt(0)
	v_mul_f32_e32 v10, v10, v14
	v_mul_f32_e32 v11, v11, v15
	v_med3_f32 v10, v10, s15, v85
	v_med3_f32 v11, v11, s15, v85
	v_cvt_pk_fp8_f32 v18, v10, v11
	v_mul_f32_e32 v12, v12, v16
	v_mul_f32_e32 v13, v13, v17
	v_med3_f32 v12, v12, s15, v85
	v_med3_f32 v13, v13, s15, v85
	v_cvt_pk_fp8_f32 v18, v12, v13 op_sel:[0,0,1]
	global_store_dword v[74:75], v18, off offset:1280
	global_load_dwordx4 v[10:13], v[68:69], off
	s_waitcnt vmcnt(0)
	v_mul_f32_e32 v6, v6, v10
	v_mul_f32_e32 v7, v7, v11
	v_med3_f32 v6, v6, s15, v85
	v_med3_f32 v7, v7, s15, v85
	v_cvt_pk_fp8_f32 v14, v6, v7
	v_mul_f32_e32 v8, v8, v12
	v_mul_f32_e32 v9, v9, v13
	v_med3_f32 v8, v8, s15, v85
	v_med3_f32 v9, v9, s15, v85
	v_cvt_pk_fp8_f32 v14, v8, v9 op_sel:[0,0,1]
	global_store_dword v[74:75], v14, off offset:1536
	global_load_dwordx4 v[6:9], v[70:71], off
	s_waitcnt vmcnt(0)
	v_mul_f32_e32 v2, v2, v6
	v_mul_f32_e32 v3, v3, v7
	v_med3_f32 v2, v2, s15, v85
	v_med3_f32 v3, v3, s15, v85
	v_cvt_pk_fp8_f32 v10, v2, v3
	v_mul_f32_e32 v4, v4, v8
	v_mul_f32_e32 v5, v5, v9
	v_med3_f32 v2, v4, s15, v85
	v_med3_f32 v3, v5, s15, v85
	v_cvt_pk_fp8_f32 v10, v2, v3 op_sel:[0,0,1]
	global_store_dword v[74:75], v10, off offset:1792
	v_lshl_add_u64 v[74:75], v[74:75], 0, s[8:9]
	s_cbranch_scc1 .LBB0_1619
	v_readlane_b32 s93, v246, 7

.LBB0_1748:
	s_lshl_b32 s64, s41, 8
	s_add_i32 s68, s68, s64
	s_lshl_b32 s4, s42, 5
	v_or_b32_e32 v22, s68, v186
	s_or_b32 s4, s4, s48
	v_lshrrev_b32_e32 v2, 2, v185
	v_ashrrev_i32_e32 v23, 31, v22
	v_and_or_b32 v168, v2, 12, s4
	v_lshlrev_b64 v[2:3], 13, v[22:23]
	v_lshl_add_u64 v[2:3], s[56:57], 0, v[2:3]
	v_lshlrev_b32_e32 v162, 1, v168
	v_lshl_add_u64 v[166:167], v[2:3], 0, v[162:163]
	s_barrier
	global_load_dwordx2 v[2:3], v[166:167], off
	global_load_dwordx2 v[4:5], v[166:167], off offset:32
	global_load_dwordx2 v[6:7], v[166:167], off offset:256
	global_load_dwordx2 v[8:9], v[166:167], off offset:288
	v_or_b32_e32 v10, 16, v22
	v_ashrrev_i32_e32 v11, 31, v10
	v_lshlrev_b64 v[10:11], 13, v[10:11]
	v_lshl_add_u64 v[10:11], s[56:57], 0, v[10:11]
	v_lshl_add_u64 v[18:19], v[10:11], 0, v[162:163]
	v_or_b32_e32 v28, 32, v22
	v_ashrrev_i32_e32 v29, 31, v28
	v_lshlrev_b64 v[28:29], 13, v[28:29]
	v_lshl_add_u64 v[28:29], s[56:57], 0, v[28:29]
	v_lshl_add_u64 v[28:29], v[28:29], 0, v[162:163]
	v_or_b32_e32 v22, 48, v22
	v_ashrrev_i32_e32 v23, 31, v22
	v_lshlrev_b64 v[22:23], 13, v[22:23]
	v_lshl_add_u64 v[22:23], s[56:57], 0, v[22:23]
	s_lshl_b32 s4, s42, 2
	s_add_i32 s6, s4, 0
	s_waitcnt vmcnt(0)
	v_lshlrev_b32_e32 v10, 16, v2
	v_and_b32_e32 v11, 0xffff0000, v2
	v_lshlrev_b32_e32 v2, 16, v3
	v_and_b32_e32 v3, 0xffff0000, v3
	v_lshlrev_b32_e32 v12, 16, v4
	v_and_b32_e32 v13, 0xffff0000, v4
	v_lshlrev_b32_e32 v14, 16, v5
	v_and_b32_e32 v15, 0xffff0000, v5
	v_lshlrev_b32_e32 v16, 16, v6
	v_and_b32_e32 v17, 0xffff0000, v6
	v_lshlrev_b32_e32 v20, 16, v7
	v_and_b32_e32 v21, 0xffff0000, v7
	v_lshlrev_b32_e32 v24, 16, v8
	v_and_b32_e32 v25, 0xffff0000, v8
	v_lshlrev_b32_e32 v26, 16, v9
	v_and_b32_e32 v27, 0xffff0000, v9
	v_pk_fma_f32 v[4:5], v[160:161], s[24:25], v[2:3] op_sel_hi:[1,0,1]
	v_pk_fma_f32 v[2:3], v[158:159], s[24:25], v[10:11] op_sel_hi:[1,0,1]
	v_pk_fma_f32 v[8:9], v[156:157], s[24:25], v[14:15] op_sel_hi:[1,0,1]
	v_pk_fma_f32 v[6:7], v[154:155], s[24:25], v[12:13] op_sel_hi:[1,0,1]
	v_pk_fma_f32 v[12:13], v[152:153], s[24:25], v[20:21] op_sel_hi:[1,0,1]
	v_pk_fma_f32 v[10:11], v[150:151], s[24:25], v[16:17] op_sel_hi:[1,0,1]
	v_pk_fma_f32 v[16:17], v[148:149], s[24:25], v[26:27] op_sel_hi:[1,0,1]
	v_pk_fma_f32 v[14:15], v[146:147], s[24:25], v[24:25] op_sel_hi:[1,0,1]
	s_nop 0
	global_load_dwordx2 v[20:21], v[18:19], off
	global_load_dwordx2 v[24:25], v[18:19], off offset:32
	global_load_dwordx2 v[26:27], v[18:19], off offset:256
	global_load_dwordx2 v[18:19], v[18:19], off offset:288
	s_waitcnt vmcnt(3)
	v_lshlrev_b32_e32 v30, 16, v20
	v_and_b32_e32 v31, 0xffff0000, v20
	v_lshlrev_b32_e32 v20, 16, v21
	v_and_b32_e32 v21, 0xffff0000, v21
	s_waitcnt vmcnt(2)
	v_lshlrev_b32_e32 v32, 16, v24
	v_and_b32_e32 v33, 0xffff0000, v24
	v_lshlrev_b32_e32 v24, 16, v25
	v_and_b32_e32 v25, 0xffff0000, v25
	s_waitcnt vmcnt(1)
	v_lshlrev_b32_e32 v146, 16, v26
	v_and_b32_e32 v147, 0xffff0000, v26
	v_lshlrev_b32_e32 v26, 16, v27
	v_and_b32_e32 v27, 0xffff0000, v27
	s_waitcnt vmcnt(0)
	v_lshlrev_b32_e32 v148, 16, v18
	v_and_b32_e32 v149, 0xffff0000, v18
	v_lshlrev_b32_e32 v18, 16, v19
	v_and_b32_e32 v19, 0xffff0000, v19
	v_pk_fma_f32 v[124:125], v[124:125], s[24:25], v[20:21] op_sel_hi:[1,0,1]
	v_pk_fma_f32 v[122:123], v[122:123], s[24:25], v[30:31] op_sel_hi:[1,0,1]
	v_pk_fma_f32 v[120:121], v[120:121], s[24:25], v[24:25] op_sel_hi:[1,0,1]
	v_pk_fma_f32 v[118:119], v[118:119], s[24:25], v[32:33] op_sel_hi:[1,0,1]
	v_pk_fma_f32 v[32:33], v[144:145], s[24:25], v[26:27] op_sel_hi:[1,0,1]
	v_pk_fma_f32 v[30:31], v[142:143], s[24:25], v[146:147] op_sel_hi:[1,0,1]
	v_pk_fma_f32 v[20:21], v[140:141], s[24:25], v[18:19] op_sel_hi:[1,0,1]
	v_pk_fma_f32 v[18:19], v[138:139], s[24:25], v[148:149] op_sel_hi:[1,0,1]
	v_lshl_add_u64 v[140:141], v[22:23], 0, v[162:163]
	global_load_dwordx2 v[24:25], v[28:29], off
	global_load_dwordx2 v[26:27], v[28:29], off offset:32
	global_load_dwordx2 v[138:139], v[28:29], off offset:256
	global_load_dwordx2 v[28:29], v[28:29], off offset:288
	s_waitcnt vmcnt(3)
	v_lshlrev_b32_e32 v22, 16, v24
	v_and_b32_e32 v23, 0xffff0000, v24
	v_lshlrev_b32_e32 v24, 16, v25
	v_and_b32_e32 v25, 0xffff0000, v25
	s_waitcnt vmcnt(2)
	v_lshlrev_b32_e32 v142, 16, v26
	v_and_b32_e32 v143, 0xffff0000, v26
	v_lshlrev_b32_e32 v26, 16, v27
	v_and_b32_e32 v27, 0xffff0000, v27
	s_waitcnt vmcnt(1)
	v_lshlrev_b32_e32 v144, 16, v138
	v_and_b32_e32 v145, 0xffff0000, v138
	v_lshlrev_b32_e32 v138, 16, v139
	v_and_b32_e32 v139, 0xffff0000, v139
	s_waitcnt vmcnt(0)
	v_lshlrev_b32_e32 v146, 16, v28
	v_and_b32_e32 v147, 0xffff0000, v28
	v_lshlrev_b32_e32 v148, 16, v29
	v_and_b32_e32 v149, 0xffff0000, v29
	v_pk_fma_f32 v[128:129], v[128:129], s[24:25], v[24:25] op_sel_hi:[1,0,1]
	v_pk_fma_f32 v[126:127], v[126:127], s[24:25], v[22:23] op_sel_hi:[1,0,1]
	v_pk_fma_f32 v[116:117], v[116:117], s[24:25], v[26:27] op_sel_hi:[1,0,1]
	v_pk_fma_f32 v[114:115], v[114:115], s[24:25], v[142:143] op_sel_hi:[1,0,1]
	v_pk_fma_f32 v[28:29], v[136:137], s[24:25], v[138:139] op_sel_hi:[1,0,1]
	v_pk_fma_f32 v[26:27], v[134:135], s[24:25], v[144:145] op_sel_hi:[1,0,1]
	v_pk_fma_f32 v[24:25], v[132:133], s[24:25], v[148:149] op_sel_hi:[1,0,1]
	v_pk_fma_f32 v[22:23], v[130:131], s[24:25], v[146:147] op_sel_hi:[1,0,1]
	v_add_co_u32_e32 v138, vcc, s59, v166
	global_load_dwordx2 v[130:131], v[140:141], off
	global_load_dwordx2 v[132:133], v[140:141], off offset:32
	global_load_dwordx2 v[134:135], v[140:141], off offset:256
	global_load_dwordx2 v[136:137], v[140:141], off offset:288
	v_addc_co_u32_e32 v139, vcc, 0, v167, vcc
	v_mul_f32_e32 v148, v17, v17
	v_fmac_f32_e32 v148, v16, v16
	s_waitcnt vmcnt(3)
	v_lshlrev_b32_e32 v140, 16, v130
	v_and_b32_e32 v141, 0xffff0000, v130
	v_lshlrev_b32_e32 v130, 16, v131
	v_and_b32_e32 v131, 0xffff0000, v131
	s_waitcnt vmcnt(2)
	v_lshlrev_b32_e32 v142, 16, v132
	v_and_b32_e32 v143, 0xffff0000, v132
	v_lshlrev_b32_e32 v132, 16, v133
	v_and_b32_e32 v133, 0xffff0000, v133
	s_waitcnt vmcnt(1)
	v_lshlrev_b32_e32 v144, 16, v134
	v_and_b32_e32 v145, 0xffff0000, v134
	v_lshlrev_b32_e32 v134, 16, v135
	v_and_b32_e32 v135, 0xffff0000, v135
	s_waitcnt vmcnt(0)
	v_lshlrev_b32_e32 v146, 16, v136
	v_and_b32_e32 v147, 0xffff0000, v136
	v_lshlrev_b32_e32 v136, 16, v137
	v_and_b32_e32 v137, 0xffff0000, v137
	v_pk_fma_f32 v[112:113], v[112:113], s[24:25], v[130:131] op_sel_hi:[1,0,1]
	v_pk_fma_f32 v[110:111], v[110:111], s[24:25], v[140:141] op_sel_hi:[1,0,1]
	v_pk_fma_f32 v[108:109], v[108:109], s[24:25], v[132:133] op_sel_hi:[1,0,1]
	v_pk_fma_f32 v[106:107], v[106:107], s[24:25], v[142:143] op_sel_hi:[1,0,1]
	v_pk_fma_f32 v[104:105], v[104:105], s[24:25], v[134:135] op_sel_hi:[1,0,1]
	v_pk_fma_f32 v[102:103], v[102:103], s[24:25], v[144:145] op_sel_hi:[1,0,1]
	v_pk_fma_f32 v[100:101], v[100:101], s[24:25], v[136:137] op_sel_hi:[1,0,1]
	v_pk_fma_f32 v[98:99], v[98:99], s[24:25], v[146:147] op_sel_hi:[1,0,1]
	v_lshl_add_u64 v[132:133], v[166:167], 0, s[26:27]
	global_load_dwordx2 v[130:131], v[138:139], off
	global_load_dwordx2 v[134:135], v[132:133], off offset:32
	global_load_dwordx2 v[136:137], v[132:133], off offset:256
	global_load_dwordx2 v[132:133], v[132:133], off offset:288
	v_add_co_u32_e32 v138, vcc, s60, v166
	s_waitcnt vmcnt(2)
	v_lshlrev_b32_e32 v142, 16, v134
	v_lshlrev_b32_e32 v140, 16, v130
	v_and_b32_e32 v141, 0xffff0000, v130
	v_lshlrev_b32_e32 v130, 16, v131
	v_and_b32_e32 v131, 0xffff0000, v131
	v_and_b32_e32 v143, 0xffff0000, v134
	v_lshlrev_b32_e32 v134, 16, v135
	v_and_b32_e32 v135, 0xffff0000, v135
	s_waitcnt vmcnt(1)
	v_lshlrev_b32_e32 v144, 16, v136
	v_and_b32_e32 v145, 0xffff0000, v136
	v_lshlrev_b32_e32 v136, 16, v137
	v_and_b32_e32 v137, 0xffff0000, v137
	s_waitcnt vmcnt(0)
	v_lshlrev_b32_e32 v146, 16, v132
	v_and_b32_e32 v147, 0xffff0000, v132
	v_lshlrev_b32_e32 v132, 16, v133
	v_and_b32_e32 v133, 0xffff0000, v133
	v_pk_fma_f32 v[96:97], v[96:97], s[24:25], v[130:131] op_sel_hi:[1,0,1]
	v_pk_fma_f32 v[94:95], v[94:95], s[24:25], v[140:141] op_sel_hi:[1,0,1]
	v_pk_fma_f32 v[92:93], v[92:93], s[24:25], v[134:135] op_sel_hi:[1,0,1]
	v_pk_fma_f32 v[90:91], v[90:91], s[24:25], v[142:143] op_sel_hi:[1,0,1]
	v_pk_fma_f32 v[88:89], v[88:89], s[24:25], v[136:137] op_sel_hi:[1,0,1]
	v_pk_fma_f32 v[86:87], v[86:87], s[24:25], v[144:145] op_sel_hi:[1,0,1]
	v_pk_fma_f32 v[84:85], v[84:85], s[24:25], v[132:133] op_sel_hi:[1,0,1]
	v_pk_fma_f32 v[82:83], v[82:83], s[24:25], v[146:147] op_sel_hi:[1,0,1]
	v_addc_co_u32_e32 v139, vcc, 0, v167, vcc
	v_lshl_add_u64 v[132:133], v[166:167], 0, s[28:29]
	global_load_dwordx2 v[130:131], v[138:139], off
	global_load_dwordx2 v[134:135], v[132:133], off offset:32
	global_load_dwordx2 v[136:137], v[132:133], off offset:256
	global_load_dwordx2 v[132:133], v[132:133], off offset:288
	v_add_co_u32_e32 v138, vcc, s61, v166
	s_waitcnt vmcnt(2)
	v_lshlrev_b32_e32 v142, 16, v134
	v_lshlrev_b32_e32 v140, 16, v130
	v_and_b32_e32 v141, 0xffff0000, v130
	v_lshlrev_b32_e32 v130, 16, v131
	v_and_b32_e32 v131, 0xffff0000, v131
	v_and_b32_e32 v143, 0xffff0000, v134
	v_lshlrev_b32_e32 v134, 16, v135
	v_and_b32_e32 v135, 0xffff0000, v135
	s_waitcnt vmcnt(1)
	v_lshlrev_b32_e32 v144, 16, v136
	v_and_b32_e32 v145, 0xffff0000, v136
	v_lshlrev_b32_e32 v136, 16, v137
	v_and_b32_e32 v137, 0xffff0000, v137
	s_waitcnt vmcnt(0)
	v_lshlrev_b32_e32 v146, 16, v132
	v_and_b32_e32 v147, 0xffff0000, v132
	v_lshlrev_b32_e32 v132, 16, v133
	v_and_b32_e32 v133, 0xffff0000, v133
	v_pk_fma_f32 v[80:81], v[80:81], s[24:25], v[130:131] op_sel_hi:[1,0,1]
	v_pk_fma_f32 v[78:79], v[78:79], s[24:25], v[140:141] op_sel_hi:[1,0,1]
	v_pk_fma_f32 v[76:77], v[76:77], s[24:25], v[134:135] op_sel_hi:[1,0,1]
	v_pk_fma_f32 v[74:75], v[74:75], s[24:25], v[142:143] op_sel_hi:[1,0,1]
	v_pk_fma_f32 v[72:73], v[72:73], s[24:25], v[136:137] op_sel_hi:[1,0,1]
	v_pk_fma_f32 v[70:71], v[70:71], s[24:25], v[144:145] op_sel_hi:[1,0,1]
	v_pk_fma_f32 v[68:69], v[68:69], s[24:25], v[132:133] op_sel_hi:[1,0,1]
	v_pk_fma_f32 v[66:67], v[66:67], s[24:25], v[146:147] op_sel_hi:[1,0,1]
	v_addc_co_u32_e32 v139, vcc, 0, v167, vcc
	v_lshl_add_u64 v[132:133], v[166:167], 0, s[30:31]
	global_load_dwordx2 v[130:131], v[138:139], off
	global_load_dwordx2 v[134:135], v[132:133], off offset:32
	global_load_dwordx2 v[136:137], v[132:133], off offset:256
	global_load_dwordx2 v[132:133], v[132:133], off offset:288
	v_add_co_u32_e32 v138, vcc, s62, v166
	s_waitcnt vmcnt(2)
	v_lshlrev_b32_e32 v142, 16, v134
	v_lshlrev_b32_e32 v140, 16, v130
	v_and_b32_e32 v141, 0xffff0000, v130
	v_lshlrev_b32_e32 v130, 16, v131
	v_and_b32_e32 v131, 0xffff0000, v131
	v_and_b32_e32 v143, 0xffff0000, v134
	v_lshlrev_b32_e32 v134, 16, v135
	v_and_b32_e32 v135, 0xffff0000, v135
	s_waitcnt vmcnt(1)
	v_lshlrev_b32_e32 v144, 16, v136
	v_and_b32_e32 v145, 0xffff0000, v136
	v_lshlrev_b32_e32 v136, 16, v137
	v_and_b32_e32 v137, 0xffff0000, v137
	s_waitcnt vmcnt(0)
	v_lshlrev_b32_e32 v146, 16, v132
	v_and_b32_e32 v147, 0xffff0000, v132
	v_lshlrev_b32_e32 v132, 16, v133
	v_and_b32_e32 v133, 0xffff0000, v133
	v_pk_fma_f32 v[64:65], v[64:65], s[24:25], v[130:131] op_sel_hi:[1,0,1]
	v_pk_fma_f32 v[62:63], v[62:63], s[24:25], v[140:141] op_sel_hi:[1,0,1]
	v_pk_fma_f32 v[60:61], v[60:61], s[24:25], v[134:135] op_sel_hi:[1,0,1]
	v_pk_fma_f32 v[58:59], v[58:59], s[24:25], v[142:143] op_sel_hi:[1,0,1]
	v_pk_fma_f32 v[56:57], v[56:57], s[24:25], v[136:137] op_sel_hi:[1,0,1]
	v_pk_fma_f32 v[54:55], v[54:55], s[24:25], v[144:145] op_sel_hi:[1,0,1]
	v_pk_fma_f32 v[52:53], v[52:53], s[24:25], v[132:133] op_sel_hi:[1,0,1]
	v_pk_fma_f32 v[50:51], v[50:51], s[24:25], v[146:147] op_sel_hi:[1,0,1]
	v_addc_co_u32_e32 v139, vcc, 0, v167, vcc
	v_lshl_add_u64 v[130:131], v[166:167], 0, s[34:35]
	global_load_dwordx2 v[136:137], v[138:139], off
	global_load_dwordx2 v[138:139], v[130:131], off offset:32
	global_load_dwordx2 v[140:141], v[130:131], off offset:256
	global_load_dwordx2 v[142:143], v[130:131], off offset:288
	v_mul_f32_e32 v133, v3, v3
	v_mul_f32_e32 v134, v5, v5
	v_mul_f32_e32 v135, v7, v7
	v_mul_f32_e32 v144, v9, v9
	v_and_b32_e32 v131, 64, v1
	v_mul_f32_e32 v145, v11, v11
	v_mul_f32_e32 v146, v13, v13
	v_fmac_f32_e32 v133, v2, v2
	v_fmac_f32_e32 v134, v4, v4
	v_fmac_f32_e32 v135, v6, v6
	v_fmac_f32_e32 v144, v8, v8
	v_xor_b32_e32 v130, 16, v1
	v_add_u32_e32 v131, 64, v131
	v_mul_f32_e32 v147, v15, v15
	v_fmac_f32_e32 v145, v10, v10
	v_fmac_f32_e32 v146, v12, v12
	v_add_f32_e32 v133, v133, v134
	v_add_f32_e32 v134, v135, v144
	v_cmp_lt_i32_e32 vcc, v130, v131
	v_fmac_f32_e32 v147, v14, v14
	v_add_f32_e32 v135, v145, v146
	v_add_f32_e32 v133, v133, v134
	v_cndmask_b32_e32 v130, v1, v130, vcc
	v_add_f32_e32 v144, v147, v148
	v_add_f32_e32 v133, v135, v133
	v_lshlrev_b32_e32 v130, 2, v130
	v_add_f32_e32 v133, v144, v133
	ds_bpermute_b32 v134, v130, v133
	v_xor_b32_e32 v135, 32, v1
	v_cmp_lt_i32_e32 vcc, v135, v131
	v_and_b32_e32 v132, 63, v185
	s_waitcnt lgkmcnt(0)
	v_add_f32_e32 v133, v133, v134
	v_cndmask_b32_e32 v131, v1, v135, vcc
	v_lshlrev_b32_e32 v131, 2, v131
	ds_bpermute_b32 v134, v131, v133
	v_cmp_gt_u32_e32 vcc, 16, v132
	s_waitcnt vmcnt(2)
	v_lshlrev_b32_e32 v146, 16, v138
	v_lshlrev_b32_e32 v144, 16, v136
	v_and_b32_e32 v145, 0xffff0000, v136
	v_lshlrev_b32_e32 v136, 16, v137
	v_and_b32_e32 v137, 0xffff0000, v137
	v_and_b32_e32 v147, 0xffff0000, v138
	v_lshlrev_b32_e32 v138, 16, v139
	v_and_b32_e32 v139, 0xffff0000, v139
	s_waitcnt vmcnt(1)
	v_lshlrev_b32_e32 v148, 16, v140
	v_and_b32_e32 v149, 0xffff0000, v140
	v_lshlrev_b32_e32 v140, 16, v141
	v_and_b32_e32 v141, 0xffff0000, v141
	s_waitcnt vmcnt(0)
	v_lshlrev_b32_e32 v150, 16, v142
	v_and_b32_e32 v151, 0xffff0000, v142
	v_lshlrev_b32_e32 v142, 16, v143
	v_and_b32_e32 v143, 0xffff0000, v143
	v_pk_fma_f32 v[48:49], v[48:49], s[24:25], v[136:137] op_sel_hi:[1,0,1]
	v_pk_fma_f32 v[46:47], v[46:47], s[24:25], v[144:145] op_sel_hi:[1,0,1]
	v_pk_fma_f32 v[44:45], v[44:45], s[24:25], v[138:139] op_sel_hi:[1,0,1]
	v_pk_fma_f32 v[42:43], v[42:43], s[24:25], v[146:147] op_sel_hi:[1,0,1]
	v_pk_fma_f32 v[40:41], v[40:41], s[24:25], v[140:141] op_sel_hi:[1,0,1]
	v_pk_fma_f32 v[38:39], v[38:39], s[24:25], v[148:149] op_sel_hi:[1,0,1]
	v_pk_fma_f32 v[36:37], v[36:37], s[24:25], v[142:143] op_sel_hi:[1,0,1]
	v_pk_fma_f32 v[34:35], v[34:35], s[24:25], v[150:151] op_sel_hi:[1,0,1]
	s_nop 0
	s_and_saveexec_b64 s[4:5], vcc
	s_cbranch_execz .LBB0_1750
	s_lshl_b32 s7, s39, 10
	s_add_i32 s7, s6, s7
	v_lshl_add_u32 v135, v186, 4, s7
	s_waitcnt lgkmcnt(0)
	v_add_f32_e32 v133, v133, v134
	ds_write_b32 v135, v133

.LBB0_1786:
	s_waitcnt vmcnt(0) lgkmcnt(0)
	s_barrier
	ds_read_b32 v148, v163 offset:10240
	s_and_saveexec_b64 s[6:7], s[8:9]
	s_cbranch_execz .LBB0_1741
	v_lshlrev_b64 v[130:131], 6, v[130:131]
	v_lshl_add_u64 v[130:131], s[10:11], 0, v[130:131]
	global_load_dword v132, v[130:131], off sc1
	global_load_dword v134, v[130:131], off offset:4 sc1
	global_load_dword v135, v[130:131], off offset:8 sc1
	global_load_dword v136, v[130:131], off offset:12 sc1
	global_load_dword v137, v[130:131], off offset:16 sc1
	global_load_dword v138, v[130:131], off offset:20 sc1
	global_load_dword v139, v[130:131], off offset:24 sc1
	global_load_dword v140, v[130:131], off offset:28 sc1
	global_load_dword v141, v[130:131], off offset:32 sc1
	global_load_dword v142, v[130:131], off offset:36 sc1
	global_load_dword v143, v[130:131], off offset:40 sc1
	global_load_dword v144, v[130:131], off offset:44 sc1
	global_load_dword v145, v[130:131], off offset:48 sc1
	global_load_dword v146, v[130:131], off offset:52 sc1
	global_load_dword v147, v[130:131], off offset:56 sc1
	global_load_dword v130, v[130:131], off offset:60 sc1
	s_waitcnt vmcnt(15)
	v_add_f32_e32 v131, 0, v132
	s_waitcnt vmcnt(14)
	v_add_f32_e32 v131, v131, v134
	s_waitcnt vmcnt(13)
	v_add_f32_e32 v131, v131, v135
	s_waitcnt vmcnt(12)
	v_add_f32_e32 v131, v131, v136
	s_waitcnt vmcnt(11)
	v_add_f32_e32 v131, v131, v137
	s_waitcnt vmcnt(10)
	v_add_f32_e32 v131, v131, v138
	s_waitcnt vmcnt(9)
	v_add_f32_e32 v131, v131, v139
	s_waitcnt vmcnt(8)
	v_add_f32_e32 v131, v131, v140
	s_waitcnt vmcnt(7)
	v_add_f32_e32 v131, v131, v141
	s_waitcnt vmcnt(6)
	v_add_f32_e32 v131, v131, v142
	s_waitcnt vmcnt(5)
	v_add_f32_e32 v131, v131, v143
	s_waitcnt vmcnt(4)
	v_add_f32_e32 v131, v131, v144
	s_waitcnt vmcnt(3)
	v_add_f32_e32 v131, v131, v145
	s_waitcnt vmcnt(2)
	v_add_f32_e32 v131, v131, v146
	s_waitcnt vmcnt(1)
	v_add_f32_e32 v131, v131, v147
	s_waitcnt vmcnt(0)
	v_add_f32_e32 v130, v131, v130
	v_fmamk_f32 v130, v130, 0x39800000, v181
	v_mul_f32_e32 v131, 0x4f800000, v130
	v_cmp_gt_f32_e32 vcc, s63, v130
	s_nop 1
	v_cndmask_b32_e32 v130, v130, v131, vcc
	v_sqrt_f32_e32 v131, v130
	s_nop 0
	v_add_u32_e32 v132, -1, v131
	v_add_u32_e32 v134, 1, v131
	v_fma_f32 v135, -v132, v131, v130
	v_fma_f32 v136, -v134, v131, v130
	v_cmp_ge_f32_e64 s[4:5], 0, v135
	s_nop 1
	v_cndmask_b32_e64 v131, v131, v132, s[4:5]
	v_cmp_lt_f32_e64 s[4:5], 0, v136
	s_nop 1
	v_cndmask_b32_e64 v131, v131, v134, s[4:5]
	v_mul_f32_e32 v132, 0x37800000, v131
	v_cndmask_b32_e32 v131, v131, v132, vcc
	v_cmp_class_f32_e32 vcc, v130, v182
	s_nop 1
	v_cndmask_b32_e32 v130, v131, v130, vcc
	v_div_scale_f32 v131, s[4:5], v130, v130, 1.0
	v_rcp_f32_e32 v132, v131
	v_div_scale_f32 v134, vcc, 1.0, v130, 1.0
	v_fma_f32 v135, -v131, v132, 1.0
	v_fmac_f32_e32 v132, v135, v132
	v_mul_f32_e32 v135, v134, v132
	v_fma_f32 v136, -v131, v135, v134
	v_fmac_f32_e32 v135, v136, v132
	v_fma_f32 v131, -v131, v135, v134
	v_div_fmas_f32 v131, v131, v132, v135
	v_div_fixup_f32 v130, v131, v130, 1.0
	v_lshl_add_u32 v131, v133, 2, 0
	ds_write_b32 v131, v130 offset:8192
	s_branch .LBB0_1741
